# PEER down/up: table row gathers issued with sc0 (no L1 retention: rows are never reused within a CU, the L1 was holding in-flight lines only)
# baseline (speedup 1.0000x reference)
; DI int tidx() { int t = threadIdx.x & 255; asm volatile("" : "+v"(t)); return t; }
; DI int ftid() { int t = threadIdx.x; asm volatile("" : "+v"(t)); return t; }
; #define PD_E(t, E) do { const char* eb_ = eiu + (size_t)(t) * 512; _Pragma("unroll") for (int q = 0; q < 4; ++q) E[q] = *(const i32x4_t*)(eb_ + (eio + 16u * q)); } while (0)
; #define PD_H(t, H) do { const char* hb_ = h2u + (size_t)(t) * 2048; H[0] = *(const u32x4*)(hb_ + h2o); H[1] = *(const u32x4*)(hb_ + (h2o + 16u)); } while (0)
; #define PD_TAB(E, W) do { _Pragma("unroll") for (int q = 0; q < 16; ++q) W[q] = *(const u32x4*)(tabu + ((unsigned)E[q >> 2][q & 3] * 128u + tabo)); } while (0)
; DI void phase_peerdown(const Params& p, int bid, int nb) {
;   const int lane = tidx() & 63, wid = __builtin_amdgcn_readfirstlane(ftid() >> 6), e8 = lane >> 3, c = lane & 7;
;   const int x = bid & 7, gw = (bid >> 3) * 8 + wid, nw = (nb >> 3) * 8;
;   const char* h2u = p.ws + WS_H + 256 * x; const unsigned h2o = 32u * c;
;   const char* tabu = p.ws + WS_PU + (size_t)x * 16384 * 128; const unsigned tabo = 16u * c;
;   const char* eiu = p.ws + WS_EIDX; const unsigned eio = 64u * e8;
;   char* pdu = p.ws + WS_PD + (size_t)x * T_ * 256; const unsigned pdo = 32u * e8 + 4u * c;
;   const bool c0 = (lane & 1) != 0, c1 = (lane & 2) != 0, c2 = (lane & 4) != 0;
;     ...
;   i32x4_t eA[4], eB[4]; u32x4 hA[2], hB[2], wA[16], wB[16];
;   int t = gw; if (t >= T_) return;
;   int t1 = t + nw;
;   PD_E(t, eA); PD_H(t, hA); PD_TAB(eA, wA);
;   if (t1 < T_) { PD_E(t1, eB); PD_H(t1, hB); }
;   for (;;) {
;     if (t1 < T_) PD_TAB(eB, wB);
.LBB0_1735:
	s_or_b64 exec, exec, s[0:1]
	v_mov_b32_e32 v116, v206
	s_waitcnt lgkmcnt(0)
	v_mov_b32_e32 v0, v207
	s_barrier
	v_readlane_b32 s2, v250, 0
	v_readfirstlane_b32 s0, v0
	s_ashr_i32 s0, s0, 6
	s_and_b32 s19, s2, 7
	s_and_b32 s49, s2, -8
	s_add_i32 s12, s0, s49
	s_and_b32 s18, s86, -8
	s_lshl_b32 s48, s19, 21
	s_add_u32 s16, s84, 0x12000000
	s_addc_u32 s17, s85, 0
	s_cmpk_gt_i32 s12, 0x7fff
	v_readlane_b32 s3, v250, 1
	s_cbranch_scc1 .LBB0_1753
	s_lshl_b32 s0, s19, 8
	s_add_u32 s8, s56, s0
	s_addc_u32 s9, s57, 0
	s_add_u32 s0, s84, s48
	s_addc_u32 s1, s85, 0
	s_add_u32 s6, s0, 0xe000000
	s_addc_u32 s7, s1, 0
	v_bfe_u32 v117, v116, 3, 3
	v_and_b32_e32 v118, 7, v116
	v_lshlrev_b32_e32 v209, 4, v118
	v_lshlrev_b32_e32 v112, 6, v117
	v_lshlrev_b32_e32 v114, 5, v118
	v_mov_b32_e32 v113, 0
	v_mov_b32_e32 v115, 0
	v_lshl_add_u64 v[180:181], s[16:17], 0, v[112:113]
	v_lshl_add_u64 v[182:183], s[8:9], 0, v[114:115]
	s_lshl_b32 s0, s19, 23
	s_add_u32 s10, s84, s0
	s_addc_u32 s11, s85, 0
	s_add_u32 s10, s10, 0x14000000
	s_addc_u32 s11, s11, 0
	v_lshlrev_b32_e32 v118, 2, v118
	v_lshl_or_b32 v118, v117, 5, v118
	v_mov_b32_e32 v119, 0
	v_lshl_add_u64 v[178:179], s[10:11], 0, v[118:119]
	v_and_b32_e32 v117, 1, v116
	v_cmp_eq_u32_e64 s[0:1], 0, v117
	v_and_b32_e32 v117, 2, v116
	v_cmp_eq_u32_e64 s[2:3], 0, v117
	v_and_b32_e32 v117, 4, v116
	v_cmp_eq_u32_e64 s[4:5], 0, v117
	v_and_b32_e32 v117, 3, v116
	v_cmp_eq_u32_e64 s[22:23], 1, v117
	v_cmp_eq_u32_e64 s[24:25], 2, v117
	v_cmp_eq_u32_e64 s[26:27], 3, v117
	s_mov_b32 s21, 0
	s_add_u32 s20, s12, 0x0
	s_lshl_b32 s20, s20, 9
	v_lshl_add_u64 v[0:1], v[180:181], 0, s[20:21]
	global_load_dwordx4 v[12:15], v[0:1], off offset:48
	global_load_dwordx4 v[8:11], v[0:1], off offset:32
	global_load_dwordx4 v[4:7], v[0:1], off offset:16
	s_nop 0
	global_load_dwordx4 v[0:3], v[0:1], off
	s_add_u32 s20, s12, 0x100
	s_lshl_b32 s20, s20, 9
	v_lshl_add_u64 v[80:81], v[180:181], 0, s[20:21]
	global_load_dwordx4 v[64:67], v[80:81], off offset:48
	global_load_dwordx4 v[68:71], v[80:81], off offset:32
	global_load_dwordx4 v[72:75], v[80:81], off offset:16
	s_nop 0
	global_load_dwordx4 v[80:83], v[80:81], off
	s_add_u32 s20, s12, 0x0
	s_lshl_b32 s20, s20, 11
	v_lshl_add_u64 v[20:21], v[182:183], 0, s[20:21]
	global_load_dwordx4 v[16:19], v[20:21], off offset:16
	s_nop 0
	global_load_dwordx4 v[20:23], v[20:21], off
	s_add_u32 s20, s12, 0x100
	s_lshl_b32 s20, s20, 11
	v_lshl_add_u64 v[108:109], v[182:183], 0, s[20:21]
	global_load_dwordx4 v[100:103], v[108:109], off offset:16
	s_nop 0
	global_load_dwordx4 v[108:111], v[108:109], off
	s_waitcnt vmcnt(8)
	v_lshl_or_b32 v0, v0, 7, v209
	global_load_dwordx4 v[24:27], v0, s[6:7] sc0
	v_lshl_or_b32 v1, v1, 7, v209
	global_load_dwordx4 v[28:31], v1, s[6:7] sc0
	v_lshl_or_b32 v2, v2, 7, v209
	global_load_dwordx4 v[32:35], v2, s[6:7] sc0
	v_lshl_or_b32 v3, v3, 7, v209
	global_load_dwordx4 v[36:39], v3, s[6:7] sc0
	v_lshl_or_b32 v4, v4, 7, v209
	global_load_dwordx4 v[40:43], v4, s[6:7] sc0
	v_lshl_or_b32 v5, v5, 7, v209
	global_load_dwordx4 v[44:47], v5, s[6:7] sc0
	v_lshl_or_b32 v6, v6, 7, v209
	global_load_dwordx4 v[48:51], v6, s[6:7] sc0
	v_lshl_or_b32 v7, v7, 7, v209
	global_load_dwordx4 v[52:55], v7, s[6:7] sc0
	v_lshl_or_b32 v8, v8, 7, v209
	global_load_dwordx4 v[56:59], v8, s[6:7] sc0
	v_lshl_or_b32 v9, v9, 7, v209
	global_load_dwordx4 v[60:63], v9, s[6:7] sc0
	v_lshl_or_b32 v10, v10, 7, v209
	global_load_dwordx4 v[76:79], v10, s[6:7] sc0
	v_lshl_or_b32 v11, v11, 7, v209
	global_load_dwordx4 v[84:87], v11, s[6:7] sc0
	v_lshl_or_b32 v12, v12, 7, v209
	global_load_dwordx4 v[88:91], v12, s[6:7] sc0
	v_lshl_or_b32 v13, v13, 7, v209
	global_load_dwordx4 v[92:95], v13, s[6:7] sc0
	v_lshl_or_b32 v14, v14, 7, v209
	global_load_dwordx4 v[96:99], v14, s[6:7] sc0
	v_lshl_or_b32 v15, v15, 7, v209
	global_load_dwordx4 v[104:107], v15, s[6:7] sc0
	s_add_u32 s20, s12, 0x200
	s_lshl_b32 s20, s20, 9
	v_lshl_add_u64 v[0:1], v[180:181], 0, s[20:21]
	global_load_dwordx4 v[12:15], v[0:1], off offset:48
	global_load_dwordx4 v[8:11], v[0:1], off offset:32
	global_load_dwordx4 v[4:7], v[0:1], off offset:16
	s_nop 0
	global_load_dwordx4 v[0:3], v[0:1], off
	s_waitcnt vmcnt(24)
	v_lshl_or_b32 v80, v80, 7, v209
	global_load_dwordx4 v[112:115], v80, s[6:7] sc0
	v_lshl_or_b32 v81, v81, 7, v209
	global_load_dwordx4 v[116:119], v81, s[6:7] sc0
	v_lshl_or_b32 v82, v82, 7, v209
	global_load_dwordx4 v[120:123], v82, s[6:7] sc0
	v_lshl_or_b32 v83, v83, 7, v209
	global_load_dwordx4 v[124:127], v83, s[6:7] sc0
	v_lshl_or_b32 v72, v72, 7, v209
	global_load_dwordx4 v[128:131], v72, s[6:7] sc0
	v_lshl_or_b32 v73, v73, 7, v209
	global_load_dwordx4 v[132:135], v73, s[6:7] sc0
	v_lshl_or_b32 v74, v74, 7, v209
	global_load_dwordx4 v[136:139], v74, s[6:7] sc0
	v_lshl_or_b32 v75, v75, 7, v209
	global_load_dwordx4 v[140:143], v75, s[6:7] sc0
	v_lshl_or_b32 v68, v68, 7, v209
	global_load_dwordx4 v[144:147], v68, s[6:7] sc0
	v_lshl_or_b32 v69, v69, 7, v209
	global_load_dwordx4 v[148:151], v69, s[6:7] sc0
	v_lshl_or_b32 v70, v70, 7, v209
	global_load_dwordx4 v[152:155], v70, s[6:7] sc0
	v_lshl_or_b32 v71, v71, 7, v209
	global_load_dwordx4 v[156:159], v71, s[6:7] sc0
	v_lshl_or_b32 v64, v64, 7, v209
	global_load_dwordx4 v[160:163], v64, s[6:7] sc0
	v_lshl_or_b32 v65, v65, 7, v209
	global_load_dwordx4 v[164:167], v65, s[6:7] sc0
	v_lshl_or_b32 v66, v66, 7, v209
	global_load_dwordx4 v[168:171], v66, s[6:7] sc0
	v_lshl_or_b32 v67, v67, 7, v209
	global_load_dwordx4 v[172:175], v67, s[6:7] sc0
	s_add_u32 s20, s12, 0x300
	s_lshl_b32 s20, s20, 9
	v_lshl_add_u64 v[80:81], v[180:181], 0, s[20:21]
	global_load_dwordx4 v[64:67], v[80:81], off offset:48
	global_load_dwordx4 v[68:71], v[80:81], off offset:32
	global_load_dwordx4 v[72:75], v[80:81], off offset:16
	s_nop 0
	global_load_dwordx4 v[80:83], v[80:81], off
	s_mov_b32 s14, s12
	s_waitcnt vmcnt(20)
	v_cvt_scalef32_pk_bf16_fp8 v210, v24, 1.0
	v_cvt_scalef32_pk_bf16_fp8 v211, v24, 1.0 op_sel:[1,0,0]
	v_cvt_scalef32_pk_bf16_fp8 v212, v25, 1.0
	v_cvt_scalef32_pk_bf16_fp8 v213, v25, 1.0 op_sel:[1,0,0]
	v_mfma_f32_4x4x4_16b_bf16 v[228:231], v[210:211], v[20:21], 0
	v_cvt_scalef32_pk_bf16_fp8 v214, v26, 1.0
	v_cvt_scalef32_pk_bf16_fp8 v215, v26, 1.0 op_sel:[1,0,0]
	v_mfma_f32_4x4x4_16b_bf16 v[228:231], v[212:213], v[22:23], v[228:231]
	v_cvt_scalef32_pk_bf16_fp8 v216, v27, 1.0
	v_cvt_scalef32_pk_bf16_fp8 v217, v27, 1.0 op_sel:[1,0,0]
	v_lshl_or_b32 v0, v0, 7, v209
	global_load_dwordx4 v[24:27], v0, s[6:7] sc0
	v_mfma_f32_4x4x4_16b_bf16 v[228:231], v[214:215], v[16:17], v[228:231]
	v_cvt_scalef32_pk_bf16_fp8 v218, v28, 1.0
	v_cvt_scalef32_pk_bf16_fp8 v219, v28, 1.0 op_sel:[1,0,0]
	v_mfma_f32_4x4x4_16b_bf16 v[228:231], v[216:217], v[18:19], v[228:231]
	v_cvt_scalef32_pk_bf16_fp8 v220, v29, 1.0
	v_cvt_scalef32_pk_bf16_fp8 v221, v29, 1.0 op_sel:[1,0,0]
	v_mfma_f32_4x4x4_16b_bf16 v[232:235], v[218:219], v[20:21], 0
	v_cvt_scalef32_pk_bf16_fp8 v222, v30, 1.0
	v_cvt_scalef32_pk_bf16_fp8 v223, v30, 1.0 op_sel:[1,0,0]
	v_mfma_f32_4x4x4_16b_bf16 v[232:235], v[220:221], v[22:23], v[232:235]
	v_cvt_scalef32_pk_bf16_fp8 v224, v31, 1.0
	v_cvt_scalef32_pk_bf16_fp8 v225, v31, 1.0 op_sel:[1,0,0]
	v_lshl_or_b32 v1, v1, 7, v209
	global_load_dwordx4 v[28:31], v1, s[6:7] sc0
	v_mfma_f32_4x4x4_16b_bf16 v[232:235], v[222:223], v[16:17], v[232:235]
	v_cvt_scalef32_pk_bf16_fp8 v210, v32, 1.0
	v_cvt_scalef32_pk_bf16_fp8 v211, v32, 1.0 op_sel:[1,0,0]
	v_mfma_f32_4x4x4_16b_bf16 v[232:235], v[224:225], v[18:19], v[232:235]
	v_cvt_scalef32_pk_bf16_fp8 v212, v33, 1.0
	v_cvt_scalef32_pk_bf16_fp8 v213, v33, 1.0 op_sel:[1,0,0]
	v_cndmask_b32_e64 v184, v228, v229, s[22:23]
	v_cndmask_b32_e64 v184, v184, v230, s[24:25]
	v_cndmask_b32_e64 v184, v184, v231, s[26:27]
	v_mfma_f32_4x4x4_16b_bf16 v[228:231], v[210:211], v[20:21], 0
	v_cvt_scalef32_pk_bf16_fp8 v214, v34, 1.0
	v_cvt_scalef32_pk_bf16_fp8 v215, v34, 1.0 op_sel:[1,0,0]
	v_mfma_f32_4x4x4_16b_bf16 v[228:231], v[212:213], v[22:23], v[228:231]
	v_cvt_scalef32_pk_bf16_fp8 v216, v35, 1.0
	v_cvt_scalef32_pk_bf16_fp8 v217, v35, 1.0 op_sel:[1,0,0]
	v_lshl_or_b32 v2, v2, 7, v209
	global_load_dwordx4 v[32:35], v2, s[6:7] sc0
	v_mfma_f32_4x4x4_16b_bf16 v[228:231], v[214:215], v[16:17], v[228:231]
	v_cvt_scalef32_pk_bf16_fp8 v218, v36, 1.0
	v_cvt_scalef32_pk_bf16_fp8 v219, v36, 1.0 op_sel:[1,0,0]
	v_mfma_f32_4x4x4_16b_bf16 v[228:231], v[216:217], v[18:19], v[228:231]
	v_cvt_scalef32_pk_bf16_fp8 v220, v37, 1.0
	v_cvt_scalef32_pk_bf16_fp8 v221, v37, 1.0 op_sel:[1,0,0]
	v_cndmask_b32_e64 v185, v232, v233, s[22:23]
	v_cndmask_b32_e64 v185, v185, v234, s[24:25]
	v_cndmask_b32_e64 v185, v185, v235, s[26:27]
	v_mfma_f32_4x4x4_16b_bf16 v[232:235], v[218:219], v[20:21], 0
	v_cvt_scalef32_pk_bf16_fp8 v222, v38, 1.0
	v_cvt_scalef32_pk_bf16_fp8 v223, v38, 1.0 op_sel:[1,0,0]
	v_mfma_f32_4x4x4_16b_bf16 v[232:235], v[220:221], v[22:23], v[232:235]
	v_cvt_scalef32_pk_bf16_fp8 v224, v39, 1.0
	v_cvt_scalef32_pk_bf16_fp8 v225, v39, 1.0 op_sel:[1,0,0]
	v_lshl_or_b32 v3, v3, 7, v209
	global_load_dwordx4 v[36:39], v3, s[6:7] sc0
	v_mfma_f32_4x4x4_16b_bf16 v[232:235], v[222:223], v[16:17], v[232:235]
	v_cvt_scalef32_pk_bf16_fp8 v210, v40, 1.0
	v_cvt_scalef32_pk_bf16_fp8 v211, v40, 1.0 op_sel:[1,0,0]
	v_mfma_f32_4x4x4_16b_bf16 v[232:235], v[224:225], v[18:19], v[232:235]
	v_cvt_scalef32_pk_bf16_fp8 v212, v41, 1.0
	v_cvt_scalef32_pk_bf16_fp8 v213, v41, 1.0 op_sel:[1,0,0]
	v_cndmask_b32_e64 v186, v228, v229, s[22:23]
	v_cndmask_b32_e64 v186, v186, v230, s[24:25]
	v_cndmask_b32_e64 v186, v186, v231, s[26:27]
	v_mfma_f32_4x4x4_16b_bf16 v[228:231], v[210:211], v[20:21], 0
	v_cvt_scalef32_pk_bf16_fp8 v214, v42, 1.0
	v_cvt_scalef32_pk_bf16_fp8 v215, v42, 1.0 op_sel:[1,0,0]
	v_mfma_f32_4x4x4_16b_bf16 v[228:231], v[212:213], v[22:23], v[228:231]
	v_cvt_scalef32_pk_bf16_fp8 v216, v43, 1.0
	v_cvt_scalef32_pk_bf16_fp8 v217, v43, 1.0 op_sel:[1,0,0]
	v_lshl_or_b32 v4, v4, 7, v209
	global_load_dwordx4 v[40:43], v4, s[6:7] sc0
	v_mfma_f32_4x4x4_16b_bf16 v[228:231], v[214:215], v[16:17], v[228:231]
	v_cvt_scalef32_pk_bf16_fp8 v218, v44, 1.0
	v_cvt_scalef32_pk_bf16_fp8 v219, v44, 1.0 op_sel:[1,0,0]
	v_mfma_f32_4x4x4_16b_bf16 v[228:231], v[216:217], v[18:19], v[228:231]
	v_cvt_scalef32_pk_bf16_fp8 v220, v45, 1.0
	v_cvt_scalef32_pk_bf16_fp8 v221, v45, 1.0 op_sel:[1,0,0]
	v_cndmask_b32_e64 v187, v232, v233, s[22:23]
	v_cndmask_b32_e64 v187, v187, v234, s[24:25]
	v_cndmask_b32_e64 v187, v187, v235, s[26:27]
	v_mfma_f32_4x4x4_16b_bf16 v[232:235], v[218:219], v[20:21], 0
	v_cvt_scalef32_pk_bf16_fp8 v222, v46, 1.0
	v_cvt_scalef32_pk_bf16_fp8 v223, v46, 1.0 op_sel:[1,0,0]
	v_mfma_f32_4x4x4_16b_bf16 v[232:235], v[220:221], v[22:23], v[232:235]
	v_cvt_scalef32_pk_bf16_fp8 v224, v47, 1.0
	v_cvt_scalef32_pk_bf16_fp8 v225, v47, 1.0 op_sel:[1,0,0]
	v_lshl_or_b32 v5, v5, 7, v209
	global_load_dwordx4 v[44:47], v5, s[6:7] sc0
	v_mfma_f32_4x4x4_16b_bf16 v[232:235], v[222:223], v[16:17], v[232:235]
	v_cvt_scalef32_pk_bf16_fp8 v210, v48, 1.0
	v_cvt_scalef32_pk_bf16_fp8 v211, v48, 1.0 op_sel:[1,0,0]
	v_mfma_f32_4x4x4_16b_bf16 v[232:235], v[224:225], v[18:19], v[232:235]
	v_cvt_scalef32_pk_bf16_fp8 v212, v49, 1.0
	v_cvt_scalef32_pk_bf16_fp8 v213, v49, 1.0 op_sel:[1,0,0]
	v_cndmask_b32_e64 v188, v228, v229, s[22:23]
	v_cndmask_b32_e64 v188, v188, v230, s[24:25]
	v_cndmask_b32_e64 v188, v188, v231, s[26:27]
	v_mfma_f32_4x4x4_16b_bf16 v[228:231], v[210:211], v[20:21], 0
	v_cvt_scalef32_pk_bf16_fp8 v214, v50, 1.0
	v_cvt_scalef32_pk_bf16_fp8 v215, v50, 1.0 op_sel:[1,0,0]
	v_mfma_f32_4x4x4_16b_bf16 v[228:231], v[212:213], v[22:23], v[228:231]
	v_cvt_scalef32_pk_bf16_fp8 v216, v51, 1.0
	v_cvt_scalef32_pk_bf16_fp8 v217, v51, 1.0 op_sel:[1,0,0]
	v_lshl_or_b32 v6, v6, 7, v209
	global_load_dwordx4 v[48:51], v6, s[6:7] sc0
	v_mfma_f32_4x4x4_16b_bf16 v[228:231], v[214:215], v[16:17], v[228:231]
	v_cvt_scalef32_pk_bf16_fp8 v218, v52, 1.0
	v_cvt_scalef32_pk_bf16_fp8 v219, v52, 1.0 op_sel:[1,0,0]
	v_mfma_f32_4x4x4_16b_bf16 v[228:231], v[216:217], v[18:19], v[228:231]
	v_cvt_scalef32_pk_bf16_fp8 v220, v53, 1.0
	v_cvt_scalef32_pk_bf16_fp8 v221, v53, 1.0 op_sel:[1,0,0]
	v_cndmask_b32_e64 v189, v232, v233, s[22:23]
	v_cndmask_b32_e64 v189, v189, v234, s[24:25]
	v_cndmask_b32_e64 v189, v189, v235, s[26:27]
	v_mfma_f32_4x4x4_16b_bf16 v[232:235], v[218:219], v[20:21], 0
	v_cvt_scalef32_pk_bf16_fp8 v222, v54, 1.0
	v_cvt_scalef32_pk_bf16_fp8 v223, v54, 1.0 op_sel:[1,0,0]
	v_mfma_f32_4x4x4_16b_bf16 v[232:235], v[220:221], v[22:23], v[232:235]
	v_cvt_scalef32_pk_bf16_fp8 v224, v55, 1.0
	v_cvt_scalef32_pk_bf16_fp8 v225, v55, 1.0 op_sel:[1,0,0]
	v_lshl_or_b32 v7, v7, 7, v209
	global_load_dwordx4 v[52:55], v7, s[6:7] sc0
	v_mfma_f32_4x4x4_16b_bf16 v[232:235], v[222:223], v[16:17], v[232:235]
	v_cvt_scalef32_pk_bf16_fp8 v210, v56, 1.0
	v_cvt_scalef32_pk_bf16_fp8 v211, v56, 1.0 op_sel:[1,0,0]
	v_mfma_f32_4x4x4_16b_bf16 v[232:235], v[224:225], v[18:19], v[232:235]
	v_cvt_scalef32_pk_bf16_fp8 v212, v57, 1.0
	v_cvt_scalef32_pk_bf16_fp8 v213, v57, 1.0 op_sel:[1,0,0]
	v_cndmask_b32_e64 v190, v228, v229, s[22:23]
	v_cndmask_b32_e64 v190, v190, v230, s[24:25]
	v_cndmask_b32_e64 v190, v190, v231, s[26:27]
	v_mfma_f32_4x4x4_16b_bf16 v[228:231], v[210:211], v[20:21], 0
	v_cvt_scalef32_pk_bf16_fp8 v214, v58, 1.0
	v_cvt_scalef32_pk_bf16_fp8 v215, v58, 1.0 op_sel:[1,0,0]
	v_mfma_f32_4x4x4_16b_bf16 v[228:231], v[212:213], v[22:23], v[228:231]
	v_cvt_scalef32_pk_bf16_fp8 v216, v59, 1.0
	v_cvt_scalef32_pk_bf16_fp8 v217, v59, 1.0 op_sel:[1,0,0]
	v_lshl_or_b32 v8, v8, 7, v209
	global_load_dwordx4 v[56:59], v8, s[6:7] sc0
	v_mfma_f32_4x4x4_16b_bf16 v[228:231], v[214:215], v[16:17], v[228:231]
	v_cvt_scalef32_pk_bf16_fp8 v218, v60, 1.0
	v_cvt_scalef32_pk_bf16_fp8 v219, v60, 1.0 op_sel:[1,0,0]
	v_mfma_f32_4x4x4_16b_bf16 v[228:231], v[216:217], v[18:19], v[228:231]
	v_cvt_scalef32_pk_bf16_fp8 v220, v61, 1.0
	v_cvt_scalef32_pk_bf16_fp8 v221, v61, 1.0 op_sel:[1,0,0]
	v_cndmask_b32_e64 v191, v232, v233, s[22:23]
	v_cndmask_b32_e64 v191, v191, v234, s[24:25]
	v_cndmask_b32_e64 v191, v191, v235, s[26:27]
	v_mfma_f32_4x4x4_16b_bf16 v[232:235], v[218:219], v[20:21], 0
	v_cvt_scalef32_pk_bf16_fp8 v222, v62, 1.0
	v_cvt_scalef32_pk_bf16_fp8 v223, v62, 1.0 op_sel:[1,0,0]
	v_mfma_f32_4x4x4_16b_bf16 v[232:235], v[220:221], v[22:23], v[232:235]
	v_cvt_scalef32_pk_bf16_fp8 v224, v63, 1.0
	v_cvt_scalef32_pk_bf16_fp8 v225, v63, 1.0 op_sel:[1,0,0]
	v_lshl_or_b32 v9, v9, 7, v209
	global_load_dwordx4 v[60:63], v9, s[6:7] sc0
	v_mfma_f32_4x4x4_16b_bf16 v[232:235], v[222:223], v[16:17], v[232:235]
	v_cvt_scalef32_pk_bf16_fp8 v210, v76, 1.0
	v_cvt_scalef32_pk_bf16_fp8 v211, v76, 1.0 op_sel:[1,0,0]
	v_mfma_f32_4x4x4_16b_bf16 v[232:235], v[224:225], v[18:19], v[232:235]
	v_cvt_scalef32_pk_bf16_fp8 v212, v77, 1.0
	v_cvt_scalef32_pk_bf16_fp8 v213, v77, 1.0 op_sel:[1,0,0]
	v_cndmask_b32_e64 v192, v228, v229, s[22:23]
	v_cndmask_b32_e64 v192, v192, v230, s[24:25]
	v_cndmask_b32_e64 v192, v192, v231, s[26:27]
	v_mfma_f32_4x4x4_16b_bf16 v[228:231], v[210:211], v[20:21], 0
	v_cvt_scalef32_pk_bf16_fp8 v214, v78, 1.0
	v_cvt_scalef32_pk_bf16_fp8 v215, v78, 1.0 op_sel:[1,0,0]
	v_mfma_f32_4x4x4_16b_bf16 v[228:231], v[212:213], v[22:23], v[228:231]
	v_cvt_scalef32_pk_bf16_fp8 v216, v79, 1.0
	v_cvt_scalef32_pk_bf16_fp8 v217, v79, 1.0 op_sel:[1,0,0]
	v_lshl_or_b32 v10, v10, 7, v209
	global_load_dwordx4 v[76:79], v10, s[6:7] sc0
	v_mfma_f32_4x4x4_16b_bf16 v[228:231], v[214:215], v[16:17], v[228:231]
	v_cvt_scalef32_pk_bf16_fp8 v218, v84, 1.0
	v_cvt_scalef32_pk_bf16_fp8 v219, v84, 1.0 op_sel:[1,0,0]
	v_mfma_f32_4x4x4_16b_bf16 v[228:231], v[216:217], v[18:19], v[228:231]
	v_cvt_scalef32_pk_bf16_fp8 v220, v85, 1.0
	v_cvt_scalef32_pk_bf16_fp8 v221, v85, 1.0 op_sel:[1,0,0]
	v_cndmask_b32_e64 v193, v232, v233, s[22:23]
	v_cndmask_b32_e64 v193, v193, v234, s[24:25]
	v_cndmask_b32_e64 v193, v193, v235, s[26:27]
	v_mfma_f32_4x4x4_16b_bf16 v[232:235], v[218:219], v[20:21], 0
	v_cvt_scalef32_pk_bf16_fp8 v222, v86, 1.0
	v_cvt_scalef32_pk_bf16_fp8 v223, v86, 1.0 op_sel:[1,0,0]
	v_mfma_f32_4x4x4_16b_bf16 v[232:235], v[220:221], v[22:23], v[232:235]
	v_cvt_scalef32_pk_bf16_fp8 v224, v87, 1.0
	v_cvt_scalef32_pk_bf16_fp8 v225, v87, 1.0 op_sel:[1,0,0]
	v_lshl_or_b32 v11, v11, 7, v209
	global_load_dwordx4 v[84:87], v11, s[6:7] sc0
	v_mfma_f32_4x4x4_16b_bf16 v[232:235], v[222:223], v[16:17], v[232:235]
	v_cvt_scalef32_pk_bf16_fp8 v210, v88, 1.0
	v_cvt_scalef32_pk_bf16_fp8 v211, v88, 1.0 op_sel:[1,0,0]
	v_mfma_f32_4x4x4_16b_bf16 v[232:235], v[224:225], v[18:19], v[232:235]
	v_cvt_scalef32_pk_bf16_fp8 v212, v89, 1.0
	v_cvt_scalef32_pk_bf16_fp8 v213, v89, 1.0 op_sel:[1,0,0]
	v_cndmask_b32_e64 v194, v228, v229, s[22:23]
	v_cndmask_b32_e64 v194, v194, v230, s[24:25]
	v_cndmask_b32_e64 v194, v194, v231, s[26:27]
	v_mfma_f32_4x4x4_16b_bf16 v[228:231], v[210:211], v[20:21], 0
	v_cvt_scalef32_pk_bf16_fp8 v214, v90, 1.0
	v_cvt_scalef32_pk_bf16_fp8 v215, v90, 1.0 op_sel:[1,0,0]
	v_mfma_f32_4x4x4_16b_bf16 v[228:231], v[212:213], v[22:23], v[228:231]
	v_cvt_scalef32_pk_bf16_fp8 v216, v91, 1.0
	v_cvt_scalef32_pk_bf16_fp8 v217, v91, 1.0 op_sel:[1,0,0]
	v_lshl_or_b32 v12, v12, 7, v209
	global_load_dwordx4 v[88:91], v12, s[6:7] sc0
	v_mfma_f32_4x4x4_16b_bf16 v[228:231], v[214:215], v[16:17], v[228:231]
	v_cvt_scalef32_pk_bf16_fp8 v218, v92, 1.0
	v_cvt_scalef32_pk_bf16_fp8 v219, v92, 1.0 op_sel:[1,0,0]
	v_mfma_f32_4x4x4_16b_bf16 v[228:231], v[216:217], v[18:19], v[228:231]
	v_cvt_scalef32_pk_bf16_fp8 v220, v93, 1.0
	v_cvt_scalef32_pk_bf16_fp8 v221, v93, 1.0 op_sel:[1,0,0]
	v_cndmask_b32_e64 v195, v232, v233, s[22:23]
	v_cndmask_b32_e64 v195, v195, v234, s[24:25]
	v_cndmask_b32_e64 v195, v195, v235, s[26:27]
	v_mfma_f32_4x4x4_16b_bf16 v[232:235], v[218:219], v[20:21], 0
	v_cvt_scalef32_pk_bf16_fp8 v222, v94, 1.0
	v_cvt_scalef32_pk_bf16_fp8 v223, v94, 1.0 op_sel:[1,0,0]
	v_mfma_f32_4x4x4_16b_bf16 v[232:235], v[220:221], v[22:23], v[232:235]
	v_cvt_scalef32_pk_bf16_fp8 v224, v95, 1.0
	v_cvt_scalef32_pk_bf16_fp8 v225, v95, 1.0 op_sel:[1,0,0]
	v_lshl_or_b32 v13, v13, 7, v209
	global_load_dwordx4 v[92:95], v13, s[6:7] sc0
	v_mfma_f32_4x4x4_16b_bf16 v[232:235], v[222:223], v[16:17], v[232:235]
	v_cvt_scalef32_pk_bf16_fp8 v210, v96, 1.0
	v_cvt_scalef32_pk_bf16_fp8 v211, v96, 1.0 op_sel:[1,0,0]
	v_mfma_f32_4x4x4_16b_bf16 v[232:235], v[224:225], v[18:19], v[232:235]
	v_cvt_scalef32_pk_bf16_fp8 v212, v97, 1.0
	v_cvt_scalef32_pk_bf16_fp8 v213, v97, 1.0 op_sel:[1,0,0]
	v_cndmask_b32_e64 v196, v228, v229, s[22:23]
	v_cndmask_b32_e64 v196, v196, v230, s[24:25]
	v_cndmask_b32_e64 v196, v196, v231, s[26:27]
	v_mfma_f32_4x4x4_16b_bf16 v[228:231], v[210:211], v[20:21], 0
	v_cvt_scalef32_pk_bf16_fp8 v214, v98, 1.0
	v_cvt_scalef32_pk_bf16_fp8 v215, v98, 1.0 op_sel:[1,0,0]
	v_mfma_f32_4x4x4_16b_bf16 v[228:231], v[212:213], v[22:23], v[228:231]
	v_cvt_scalef32_pk_bf16_fp8 v216, v99, 1.0
	v_cvt_scalef32_pk_bf16_fp8 v217, v99, 1.0 op_sel:[1,0,0]
	v_lshl_or_b32 v14, v14, 7, v209
	global_load_dwordx4 v[96:99], v14, s[6:7] sc0
	v_mfma_f32_4x4x4_16b_bf16 v[228:231], v[214:215], v[16:17], v[228:231]
	v_cvt_scalef32_pk_bf16_fp8 v218, v104, 1.0
	v_cvt_scalef32_pk_bf16_fp8 v219, v104, 1.0 op_sel:[1,0,0]
	v_mfma_f32_4x4x4_16b_bf16 v[228:231], v[216:217], v[18:19], v[228:231]
	v_cvt_scalef32_pk_bf16_fp8 v220, v105, 1.0
	v_cvt_scalef32_pk_bf16_fp8 v221, v105, 1.0 op_sel:[1,0,0]
	v_cndmask_b32_e64 v197, v232, v233, s[22:23]
	v_cndmask_b32_e64 v197, v197, v234, s[24:25]
	v_cndmask_b32_e64 v197, v197, v235, s[26:27]
	v_mfma_f32_4x4x4_16b_bf16 v[232:235], v[218:219], v[20:21], 0
	v_cvt_scalef32_pk_bf16_fp8 v222, v106, 1.0
	v_cvt_scalef32_pk_bf16_fp8 v223, v106, 1.0 op_sel:[1,0,0]
	v_mfma_f32_4x4x4_16b_bf16 v[232:235], v[220:221], v[22:23], v[232:235]
	v_cvt_scalef32_pk_bf16_fp8 v224, v107, 1.0
	v_cvt_scalef32_pk_bf16_fp8 v225, v107, 1.0 op_sel:[1,0,0]
	v_lshl_or_b32 v15, v15, 7, v209
	global_load_dwordx4 v[104:107], v15, s[6:7] sc0
	v_mfma_f32_4x4x4_16b_bf16 v[232:235], v[222:223], v[16:17], v[232:235]
	s_nop 1
	v_mfma_f32_4x4x4_16b_bf16 v[232:235], v[224:225], v[18:19], v[232:235]
	v_cndmask_b32_e64 v198, v228, v229, s[22:23]
	v_cndmask_b32_e64 v198, v198, v230, s[24:25]
	v_cndmask_b32_e64 v198, v198, v231, s[26:27]
	s_nop 4
	v_cndmask_b32_e64 v199, v232, v233, s[22:23]
	v_cndmask_b32_e64 v199, v199, v234, s[24:25]
	v_cndmask_b32_e64 v199, v199, v235, s[26:27]
	v_cndmask_b32_e64 v200, v184, v192, s[4:5]
	v_cndmask_b32_e64 v201, v192, v184, s[4:5]
	v_cndmask_b32_e64 v202, v185, v193, s[4:5]
	v_cndmask_b32_e64 v203, v193, v185, s[4:5]
	v_cndmask_b32_e64 v204, v186, v194, s[4:5]
	v_cndmask_b32_e64 v205, v194, v186, s[4:5]
	v_cndmask_b32_e64 v236, v187, v195, s[4:5]
	v_cndmask_b32_e64 v237, v195, v187, s[4:5]
	v_cndmask_b32_e64 v238, v188, v196, s[4:5]
	v_cndmask_b32_e64 v239, v196, v188, s[4:5]
	v_cndmask_b32_e64 v240, v189, v197, s[4:5]
	v_cndmask_b32_e64 v241, v197, v189, s[4:5]
	v_cndmask_b32_e64 v242, v190, v198, s[4:5]
	v_cndmask_b32_e64 v243, v198, v190, s[4:5]
	v_cndmask_b32_e64 v244, v191, v199, s[4:5]
	v_cndmask_b32_e64 v245, v199, v191, s[4:5]
	v_add_f32_dpp v246, v200, v201 row_half_mirror row_mask:0xf bank_mask:0xf
	v_add_f32_dpp v247, v202, v203 row_half_mirror row_mask:0xf bank_mask:0xf
	v_add_f32_dpp v248, v204, v205 row_half_mirror row_mask:0xf bank_mask:0xf
	v_add_f32_dpp v249, v236, v237 row_half_mirror row_mask:0xf bank_mask:0xf
	v_add_f32_dpp v226, v238, v239 row_half_mirror row_mask:0xf bank_mask:0xf
	v_add_f32_dpp v227, v240, v241 row_half_mirror row_mask:0xf bank_mask:0xf
	v_add_f32_dpp v210, v242, v243 row_half_mirror row_mask:0xf bank_mask:0xf
	v_add_f32_dpp v211, v244, v245 row_half_mirror row_mask:0xf bank_mask:0xf
	v_cndmask_b32_e64 v200, v246, v226, s[2:3]
	v_cndmask_b32_e64 v201, v226, v246, s[2:3]
	v_cndmask_b32_e64 v202, v247, v227, s[2:3]
	v_cndmask_b32_e64 v203, v227, v247, s[2:3]
	v_cndmask_b32_e64 v204, v248, v210, s[2:3]
	v_cndmask_b32_e64 v205, v210, v248, s[2:3]
	v_cndmask_b32_e64 v236, v249, v211, s[2:3]
	v_cndmask_b32_e64 v237, v211, v249, s[2:3]
	v_add_f32_dpp v212, v200, v201 quad_perm:[2,3,0,1] row_mask:0xf bank_mask:0xf
	v_add_f32_dpp v213, v202, v203 quad_perm:[2,3,0,1] row_mask:0xf bank_mask:0xf
	v_add_f32_dpp v214, v204, v205 quad_perm:[2,3,0,1] row_mask:0xf bank_mask:0xf
	v_add_f32_dpp v215, v236, v237 quad_perm:[2,3,0,1] row_mask:0xf bank_mask:0xf
	v_cndmask_b32_e64 v200, v212, v214, s[0:1]
	v_cndmask_b32_e64 v201, v214, v212, s[0:1]
	v_cndmask_b32_e64 v202, v213, v215, s[0:1]
	v_cndmask_b32_e64 v203, v215, v213, s[0:1]
	s_nop 1
	v_add_f32_dpp v216, v200, v201 quad_perm:[1,0,3,2] row_mask:0xf bank_mask:0xf
	v_add_f32_dpp v217, v202, v203 quad_perm:[1,0,3,2] row_mask:0xf bank_mask:0xf
	s_ashr_i32 s15, s14, 31
	s_lshl_b64 s[14:15], s[14:15], 8
	v_cvt_pk_bf16_f32 v186, v216, v217
	v_lshl_add_u64 v[184:185], v[178:179], 0, s[14:15]
	global_store_dword v[184:185], v186, off
	s_add_u32 s20, s12, 0x200
	s_lshl_b32 s20, s20, 11
	v_lshl_add_u64 v[20:21], v[182:183], 0, s[20:21]
	global_load_dwordx4 v[16:19], v[20:21], off offset:16
	s_nop 0
	global_load_dwordx4 v[20:23], v[20:21], off
	s_add_u32 s20, s12, 0x400
	s_lshl_b32 s20, s20, 9
	v_lshl_add_u64 v[0:1], v[180:181], 0, s[20:21]
	global_load_dwordx4 v[12:15], v[0:1], off offset:48
	global_load_dwordx4 v[8:11], v[0:1], off offset:32
	global_load_dwordx4 v[4:7], v[0:1], off offset:16
	s_nop 0
	global_load_dwordx4 v[0:3], v[0:1], off
	s_add_u32 s10, s12, 0x100
	s_waitcnt vmcnt(23)
	v_cvt_scalef32_pk_bf16_fp8 v210, v112, 1.0
	v_cvt_scalef32_pk_bf16_fp8 v211, v112, 1.0 op_sel:[1,0,0]
	v_cvt_scalef32_pk_bf16_fp8 v212, v113, 1.0
	v_cvt_scalef32_pk_bf16_fp8 v213, v113, 1.0 op_sel:[1,0,0]
	v_mfma_f32_4x4x4_16b_bf16 v[228:231], v[210:211], v[108:109], 0
	v_cvt_scalef32_pk_bf16_fp8 v214, v114, 1.0
	v_cvt_scalef32_pk_bf16_fp8 v215, v114, 1.0 op_sel:[1,0,0]
	v_mfma_f32_4x4x4_16b_bf16 v[228:231], v[212:213], v[110:111], v[228:231]
	v_cvt_scalef32_pk_bf16_fp8 v216, v115, 1.0
	v_cvt_scalef32_pk_bf16_fp8 v217, v115, 1.0 op_sel:[1,0,0]
	v_lshl_or_b32 v80, v80, 7, v209
	global_load_dwordx4 v[112:115], v80, s[6:7] sc0
	v_mfma_f32_4x4x4_16b_bf16 v[228:231], v[214:215], v[100:101], v[228:231]
	v_cvt_scalef32_pk_bf16_fp8 v218, v116, 1.0
	v_cvt_scalef32_pk_bf16_fp8 v219, v116, 1.0 op_sel:[1,0,0]
	v_mfma_f32_4x4x4_16b_bf16 v[228:231], v[216:217], v[102:103], v[228:231]
	v_cvt_scalef32_pk_bf16_fp8 v220, v117, 1.0
	v_cvt_scalef32_pk_bf16_fp8 v221, v117, 1.0 op_sel:[1,0,0]
	v_mfma_f32_4x4x4_16b_bf16 v[232:235], v[218:219], v[108:109], 0
	v_cvt_scalef32_pk_bf16_fp8 v222, v118, 1.0
	v_cvt_scalef32_pk_bf16_fp8 v223, v118, 1.0 op_sel:[1,0,0]
	v_mfma_f32_4x4x4_16b_bf16 v[232:235], v[220:221], v[110:111], v[232:235]
	v_cvt_scalef32_pk_bf16_fp8 v224, v119, 1.0
	v_cvt_scalef32_pk_bf16_fp8 v225, v119, 1.0 op_sel:[1,0,0]
	v_lshl_or_b32 v81, v81, 7, v209
	global_load_dwordx4 v[116:119], v81, s[6:7] sc0
	v_mfma_f32_4x4x4_16b_bf16 v[232:235], v[222:223], v[100:101], v[232:235]
	v_cvt_scalef32_pk_bf16_fp8 v210, v120, 1.0
	v_cvt_scalef32_pk_bf16_fp8 v211, v120, 1.0 op_sel:[1,0,0]
	v_mfma_f32_4x4x4_16b_bf16 v[232:235], v[224:225], v[102:103], v[232:235]
	v_cvt_scalef32_pk_bf16_fp8 v212, v121, 1.0
	v_cvt_scalef32_pk_bf16_fp8 v213, v121, 1.0 op_sel:[1,0,0]
	v_cndmask_b32_e64 v184, v228, v229, s[22:23]
	v_cndmask_b32_e64 v184, v184, v230, s[24:25]
	v_cndmask_b32_e64 v184, v184, v231, s[26:27]
	v_mfma_f32_4x4x4_16b_bf16 v[228:231], v[210:211], v[108:109], 0
	v_cvt_scalef32_pk_bf16_fp8 v214, v122, 1.0
	v_cvt_scalef32_pk_bf16_fp8 v215, v122, 1.0 op_sel:[1,0,0]
	v_mfma_f32_4x4x4_16b_bf16 v[228:231], v[212:213], v[110:111], v[228:231]
	v_cvt_scalef32_pk_bf16_fp8 v216, v123, 1.0
	v_cvt_scalef32_pk_bf16_fp8 v217, v123, 1.0 op_sel:[1,0,0]
	v_lshl_or_b32 v82, v82, 7, v209
	global_load_dwordx4 v[120:123], v82, s[6:7] sc0
	v_mfma_f32_4x4x4_16b_bf16 v[228:231], v[214:215], v[100:101], v[228:231]
	v_cvt_scalef32_pk_bf16_fp8 v218, v124, 1.0
	v_cvt_scalef32_pk_bf16_fp8 v219, v124, 1.0 op_sel:[1,0,0]
	v_mfma_f32_4x4x4_16b_bf16 v[228:231], v[216:217], v[102:103], v[228:231]
	v_cvt_scalef32_pk_bf16_fp8 v220, v125, 1.0
	v_cvt_scalef32_pk_bf16_fp8 v221, v125, 1.0 op_sel:[1,0,0]
	v_cndmask_b32_e64 v185, v232, v233, s[22:23]
	v_cndmask_b32_e64 v185, v185, v234, s[24:25]
	v_cndmask_b32_e64 v185, v185, v235, s[26:27]
	v_mfma_f32_4x4x4_16b_bf16 v[232:235], v[218:219], v[108:109], 0
	v_cvt_scalef32_pk_bf16_fp8 v222, v126, 1.0
	v_cvt_scalef32_pk_bf16_fp8 v223, v126, 1.0 op_sel:[1,0,0]
	v_mfma_f32_4x4x4_16b_bf16 v[232:235], v[220:221], v[110:111], v[232:235]
	v_cvt_scalef32_pk_bf16_fp8 v224, v127, 1.0
	v_cvt_scalef32_pk_bf16_fp8 v225, v127, 1.0 op_sel:[1,0,0]
	v_lshl_or_b32 v83, v83, 7, v209
	global_load_dwordx4 v[124:127], v83, s[6:7] sc0
	v_mfma_f32_4x4x4_16b_bf16 v[232:235], v[222:223], v[100:101], v[232:235]
	v_cvt_scalef32_pk_bf16_fp8 v210, v128, 1.0
	v_cvt_scalef32_pk_bf16_fp8 v211, v128, 1.0 op_sel:[1,0,0]
	v_mfma_f32_4x4x4_16b_bf16 v[232:235], v[224:225], v[102:103], v[232:235]
	v_cvt_scalef32_pk_bf16_fp8 v212, v129, 1.0
	v_cvt_scalef32_pk_bf16_fp8 v213, v129, 1.0 op_sel:[1,0,0]
	v_cndmask_b32_e64 v186, v228, v229, s[22:23]
	v_cndmask_b32_e64 v186, v186, v230, s[24:25]
	v_cndmask_b32_e64 v186, v186, v231, s[26:27]
	v_mfma_f32_4x4x4_16b_bf16 v[228:231], v[210:211], v[108:109], 0
	v_cvt_scalef32_pk_bf16_fp8 v214, v130, 1.0
	v_cvt_scalef32_pk_bf16_fp8 v215, v130, 1.0 op_sel:[1,0,0]
	v_mfma_f32_4x4x4_16b_bf16 v[228:231], v[212:213], v[110:111], v[228:231]
	v_cvt_scalef32_pk_bf16_fp8 v216, v131, 1.0
	v_cvt_scalef32_pk_bf16_fp8 v217, v131, 1.0 op_sel:[1,0,0]
	v_lshl_or_b32 v72, v72, 7, v209
	global_load_dwordx4 v[128:131], v72, s[6:7] sc0
	v_mfma_f32_4x4x4_16b_bf16 v[228:231], v[214:215], v[100:101], v[228:231]
	v_cvt_scalef32_pk_bf16_fp8 v218, v132, 1.0
	v_cvt_scalef32_pk_bf16_fp8 v219, v132, 1.0 op_sel:[1,0,0]
	v_mfma_f32_4x4x4_16b_bf16 v[228:231], v[216:217], v[102:103], v[228:231]
	v_cvt_scalef32_pk_bf16_fp8 v220, v133, 1.0
	v_cvt_scalef32_pk_bf16_fp8 v221, v133, 1.0 op_sel:[1,0,0]
	v_cndmask_b32_e64 v187, v232, v233, s[22:23]
	v_cndmask_b32_e64 v187, v187, v234, s[24:25]
	v_cndmask_b32_e64 v187, v187, v235, s[26:27]
	v_mfma_f32_4x4x4_16b_bf16 v[232:235], v[218:219], v[108:109], 0
	v_cvt_scalef32_pk_bf16_fp8 v222, v134, 1.0
	v_cvt_scalef32_pk_bf16_fp8 v223, v134, 1.0 op_sel:[1,0,0]
	v_mfma_f32_4x4x4_16b_bf16 v[232:235], v[220:221], v[110:111], v[232:235]
	v_cvt_scalef32_pk_bf16_fp8 v224, v135, 1.0
	v_cvt_scalef32_pk_bf16_fp8 v225, v135, 1.0 op_sel:[1,0,0]
	v_lshl_or_b32 v73, v73, 7, v209
	global_load_dwordx4 v[132:135], v73, s[6:7] sc0
	v_mfma_f32_4x4x4_16b_bf16 v[232:235], v[222:223], v[100:101], v[232:235]
	v_cvt_scalef32_pk_bf16_fp8 v210, v136, 1.0
	v_cvt_scalef32_pk_bf16_fp8 v211, v136, 1.0 op_sel:[1,0,0]
	v_mfma_f32_4x4x4_16b_bf16 v[232:235], v[224:225], v[102:103], v[232:235]
	v_cvt_scalef32_pk_bf16_fp8 v212, v137, 1.0
	v_cvt_scalef32_pk_bf16_fp8 v213, v137, 1.0 op_sel:[1,0,0]
	v_cndmask_b32_e64 v188, v228, v229, s[22:23]
	v_cndmask_b32_e64 v188, v188, v230, s[24:25]
	v_cndmask_b32_e64 v188, v188, v231, s[26:27]
	v_mfma_f32_4x4x4_16b_bf16 v[228:231], v[210:211], v[108:109], 0
	v_cvt_scalef32_pk_bf16_fp8 v214, v138, 1.0
	v_cvt_scalef32_pk_bf16_fp8 v215, v138, 1.0 op_sel:[1,0,0]
	v_mfma_f32_4x4x4_16b_bf16 v[228:231], v[212:213], v[110:111], v[228:231]
	v_cvt_scalef32_pk_bf16_fp8 v216, v139, 1.0
	v_cvt_scalef32_pk_bf16_fp8 v217, v139, 1.0 op_sel:[1,0,0]
	v_lshl_or_b32 v74, v74, 7, v209
	global_load_dwordx4 v[136:139], v74, s[6:7] sc0
	v_mfma_f32_4x4x4_16b_bf16 v[228:231], v[214:215], v[100:101], v[228:231]
	v_cvt_scalef32_pk_bf16_fp8 v218, v140, 1.0
	v_cvt_scalef32_pk_bf16_fp8 v219, v140, 1.0 op_sel:[1,0,0]
	v_mfma_f32_4x4x4_16b_bf16 v[228:231], v[216:217], v[102:103], v[228:231]
	v_cvt_scalef32_pk_bf16_fp8 v220, v141, 1.0
	v_cvt_scalef32_pk_bf16_fp8 v221, v141, 1.0 op_sel:[1,0,0]
	v_cndmask_b32_e64 v189, v232, v233, s[22:23]
	v_cndmask_b32_e64 v189, v189, v234, s[24:25]
	v_cndmask_b32_e64 v189, v189, v235, s[26:27]
	v_mfma_f32_4x4x4_16b_bf16 v[232:235], v[218:219], v[108:109], 0
	v_cvt_scalef32_pk_bf16_fp8 v222, v142, 1.0
	v_cvt_scalef32_pk_bf16_fp8 v223, v142, 1.0 op_sel:[1,0,0]
	v_mfma_f32_4x4x4_16b_bf16 v[232:235], v[220:221], v[110:111], v[232:235]
	v_cvt_scalef32_pk_bf16_fp8 v224, v143, 1.0
	v_cvt_scalef32_pk_bf16_fp8 v225, v143, 1.0 op_sel:[1,0,0]
	v_lshl_or_b32 v75, v75, 7, v209
	global_load_dwordx4 v[140:143], v75, s[6:7] sc0
	v_mfma_f32_4x4x4_16b_bf16 v[232:235], v[222:223], v[100:101], v[232:235]
	v_cvt_scalef32_pk_bf16_fp8 v210, v144, 1.0
	v_cvt_scalef32_pk_bf16_fp8 v211, v144, 1.0 op_sel:[1,0,0]
	v_mfma_f32_4x4x4_16b_bf16 v[232:235], v[224:225], v[102:103], v[232:235]
	v_cvt_scalef32_pk_bf16_fp8 v212, v145, 1.0
	v_cvt_scalef32_pk_bf16_fp8 v213, v145, 1.0 op_sel:[1,0,0]
	v_cndmask_b32_e64 v190, v228, v229, s[22:23]
	v_cndmask_b32_e64 v190, v190, v230, s[24:25]
	v_cndmask_b32_e64 v190, v190, v231, s[26:27]
	v_mfma_f32_4x4x4_16b_bf16 v[228:231], v[210:211], v[108:109], 0
	v_cvt_scalef32_pk_bf16_fp8 v214, v146, 1.0
	v_cvt_scalef32_pk_bf16_fp8 v215, v146, 1.0 op_sel:[1,0,0]
	v_mfma_f32_4x4x4_16b_bf16 v[228:231], v[212:213], v[110:111], v[228:231]
	v_cvt_scalef32_pk_bf16_fp8 v216, v147, 1.0
	v_cvt_scalef32_pk_bf16_fp8 v217, v147, 1.0 op_sel:[1,0,0]
	v_lshl_or_b32 v68, v68, 7, v209
	global_load_dwordx4 v[144:147], v68, s[6:7] sc0
	v_mfma_f32_4x4x4_16b_bf16 v[228:231], v[214:215], v[100:101], v[228:231]
	v_cvt_scalef32_pk_bf16_fp8 v218, v148, 1.0
	v_cvt_scalef32_pk_bf16_fp8 v219, v148, 1.0 op_sel:[1,0,0]
	v_mfma_f32_4x4x4_16b_bf16 v[228:231], v[216:217], v[102:103], v[228:231]
	v_cvt_scalef32_pk_bf16_fp8 v220, v149, 1.0
	v_cvt_scalef32_pk_bf16_fp8 v221, v149, 1.0 op_sel:[1,0,0]
	v_cndmask_b32_e64 v191, v232, v233, s[22:23]
	v_cndmask_b32_e64 v191, v191, v234, s[24:25]
	v_cndmask_b32_e64 v191, v191, v235, s[26:27]
	v_mfma_f32_4x4x4_16b_bf16 v[232:235], v[218:219], v[108:109], 0
	v_cvt_scalef32_pk_bf16_fp8 v222, v150, 1.0
	v_cvt_scalef32_pk_bf16_fp8 v223, v150, 1.0 op_sel:[1,0,0]
	v_mfma_f32_4x4x4_16b_bf16 v[232:235], v[220:221], v[110:111], v[232:235]
	v_cvt_scalef32_pk_bf16_fp8 v224, v151, 1.0
	v_cvt_scalef32_pk_bf16_fp8 v225, v151, 1.0 op_sel:[1,0,0]
	v_lshl_or_b32 v69, v69, 7, v209
	global_load_dwordx4 v[148:151], v69, s[6:7] sc0
	v_mfma_f32_4x4x4_16b_bf16 v[232:235], v[222:223], v[100:101], v[232:235]
	v_cvt_scalef32_pk_bf16_fp8 v210, v152, 1.0
	v_cvt_scalef32_pk_bf16_fp8 v211, v152, 1.0 op_sel:[1,0,0]
	v_mfma_f32_4x4x4_16b_bf16 v[232:235], v[224:225], v[102:103], v[232:235]
	v_cvt_scalef32_pk_bf16_fp8 v212, v153, 1.0
	v_cvt_scalef32_pk_bf16_fp8 v213, v153, 1.0 op_sel:[1,0,0]
	v_cndmask_b32_e64 v192, v228, v229, s[22:23]
	v_cndmask_b32_e64 v192, v192, v230, s[24:25]
	v_cndmask_b32_e64 v192, v192, v231, s[26:27]
	v_mfma_f32_4x4x4_16b_bf16 v[228:231], v[210:211], v[108:109], 0
	v_cvt_scalef32_pk_bf16_fp8 v214, v154, 1.0
	v_cvt_scalef32_pk_bf16_fp8 v215, v154, 1.0 op_sel:[1,0,0]
	v_mfma_f32_4x4x4_16b_bf16 v[228:231], v[212:213], v[110:111], v[228:231]
	v_cvt_scalef32_pk_bf16_fp8 v216, v155, 1.0
	v_cvt_scalef32_pk_bf16_fp8 v217, v155, 1.0 op_sel:[1,0,0]
	v_lshl_or_b32 v70, v70, 7, v209
	global_load_dwordx4 v[152:155], v70, s[6:7] sc0
	v_mfma_f32_4x4x4_16b_bf16 v[228:231], v[214:215], v[100:101], v[228:231]
	v_cvt_scalef32_pk_bf16_fp8 v218, v156, 1.0
	v_cvt_scalef32_pk_bf16_fp8 v219, v156, 1.0 op_sel:[1,0,0]
	v_mfma_f32_4x4x4_16b_bf16 v[228:231], v[216:217], v[102:103], v[228:231]
	v_cvt_scalef32_pk_bf16_fp8 v220, v157, 1.0
	v_cvt_scalef32_pk_bf16_fp8 v221, v157, 1.0 op_sel:[1,0,0]
	v_cndmask_b32_e64 v193, v232, v233, s[22:23]
	v_cndmask_b32_e64 v193, v193, v234, s[24:25]
	v_cndmask_b32_e64 v193, v193, v235, s[26:27]
	v_mfma_f32_4x4x4_16b_bf16 v[232:235], v[218:219], v[108:109], 0
	v_cvt_scalef32_pk_bf16_fp8 v222, v158, 1.0
	v_cvt_scalef32_pk_bf16_fp8 v223, v158, 1.0 op_sel:[1,0,0]
	v_mfma_f32_4x4x4_16b_bf16 v[232:235], v[220:221], v[110:111], v[232:235]
	v_cvt_scalef32_pk_bf16_fp8 v224, v159, 1.0
	v_cvt_scalef32_pk_bf16_fp8 v225, v159, 1.0 op_sel:[1,0,0]
	v_lshl_or_b32 v71, v71, 7, v209
	global_load_dwordx4 v[156:159], v71, s[6:7] sc0
	v_mfma_f32_4x4x4_16b_bf16 v[232:235], v[222:223], v[100:101], v[232:235]
	v_cvt_scalef32_pk_bf16_fp8 v210, v160, 1.0
	v_cvt_scalef32_pk_bf16_fp8 v211, v160, 1.0 op_sel:[1,0,0]
	v_mfma_f32_4x4x4_16b_bf16 v[232:235], v[224:225], v[102:103], v[232:235]
	v_cvt_scalef32_pk_bf16_fp8 v212, v161, 1.0
	v_cvt_scalef32_pk_bf16_fp8 v213, v161, 1.0 op_sel:[1,0,0]
	v_cndmask_b32_e64 v194, v228, v229, s[22:23]
	v_cndmask_b32_e64 v194, v194, v230, s[24:25]
	v_cndmask_b32_e64 v194, v194, v231, s[26:27]
	v_mfma_f32_4x4x4_16b_bf16 v[228:231], v[210:211], v[108:109], 0
	v_cvt_scalef32_pk_bf16_fp8 v214, v162, 1.0
	v_cvt_scalef32_pk_bf16_fp8 v215, v162, 1.0 op_sel:[1,0,0]
	v_mfma_f32_4x4x4_16b_bf16 v[228:231], v[212:213], v[110:111], v[228:231]
	v_cvt_scalef32_pk_bf16_fp8 v216, v163, 1.0
	v_cvt_scalef32_pk_bf16_fp8 v217, v163, 1.0 op_sel:[1,0,0]
	v_lshl_or_b32 v64, v64, 7, v209
	global_load_dwordx4 v[160:163], v64, s[6:7] sc0
	v_mfma_f32_4x4x4_16b_bf16 v[228:231], v[214:215], v[100:101], v[228:231]
	v_cvt_scalef32_pk_bf16_fp8 v218, v164, 1.0
	v_cvt_scalef32_pk_bf16_fp8 v219, v164, 1.0 op_sel:[1,0,0]
	v_mfma_f32_4x4x4_16b_bf16 v[228:231], v[216:217], v[102:103], v[228:231]
	v_cvt_scalef32_pk_bf16_fp8 v220, v165, 1.0
	v_cvt_scalef32_pk_bf16_fp8 v221, v165, 1.0 op_sel:[1,0,0]
	v_cndmask_b32_e64 v195, v232, v233, s[22:23]
	v_cndmask_b32_e64 v195, v195, v234, s[24:25]
	v_cndmask_b32_e64 v195, v195, v235, s[26:27]
	v_mfma_f32_4x4x4_16b_bf16 v[232:235], v[218:219], v[108:109], 0
	v_cvt_scalef32_pk_bf16_fp8 v222, v166, 1.0
	v_cvt_scalef32_pk_bf16_fp8 v223, v166, 1.0 op_sel:[1,0,0]
	v_mfma_f32_4x4x4_16b_bf16 v[232:235], v[220:221], v[110:111], v[232:235]
	v_cvt_scalef32_pk_bf16_fp8 v224, v167, 1.0
	v_cvt_scalef32_pk_bf16_fp8 v225, v167, 1.0 op_sel:[1,0,0]
	v_lshl_or_b32 v65, v65, 7, v209
	global_load_dwordx4 v[164:167], v65, s[6:7] sc0
	v_mfma_f32_4x4x4_16b_bf16 v[232:235], v[222:223], v[100:101], v[232:235]
	v_cvt_scalef32_pk_bf16_fp8 v210, v168, 1.0
	v_cvt_scalef32_pk_bf16_fp8 v211, v168, 1.0 op_sel:[1,0,0]
	v_mfma_f32_4x4x4_16b_bf16 v[232:235], v[224:225], v[102:103], v[232:235]
	v_cvt_scalef32_pk_bf16_fp8 v212, v169, 1.0
	v_cvt_scalef32_pk_bf16_fp8 v213, v169, 1.0 op_sel:[1,0,0]
	v_cndmask_b32_e64 v196, v228, v229, s[22:23]
	v_cndmask_b32_e64 v196, v196, v230, s[24:25]
	v_cndmask_b32_e64 v196, v196, v231, s[26:27]
	v_mfma_f32_4x4x4_16b_bf16 v[228:231], v[210:211], v[108:109], 0
	v_cvt_scalef32_pk_bf16_fp8 v214, v170, 1.0
	v_cvt_scalef32_pk_bf16_fp8 v215, v170, 1.0 op_sel:[1,0,0]
	v_mfma_f32_4x4x4_16b_bf16 v[228:231], v[212:213], v[110:111], v[228:231]
	v_cvt_scalef32_pk_bf16_fp8 v216, v171, 1.0
	v_cvt_scalef32_pk_bf16_fp8 v217, v171, 1.0 op_sel:[1,0,0]
	v_lshl_or_b32 v66, v66, 7, v209
	global_load_dwordx4 v[168:171], v66, s[6:7] sc0
	v_mfma_f32_4x4x4_16b_bf16 v[228:231], v[214:215], v[100:101], v[228:231]
	v_cvt_scalef32_pk_bf16_fp8 v218, v172, 1.0
	v_cvt_scalef32_pk_bf16_fp8 v219, v172, 1.0 op_sel:[1,0,0]
	v_mfma_f32_4x4x4_16b_bf16 v[228:231], v[216:217], v[102:103], v[228:231]
	v_cvt_scalef32_pk_bf16_fp8 v220, v173, 1.0
	v_cvt_scalef32_pk_bf16_fp8 v221, v173, 1.0 op_sel:[1,0,0]
	v_cndmask_b32_e64 v197, v232, v233, s[22:23]
	v_cndmask_b32_e64 v197, v197, v234, s[24:25]
	v_cndmask_b32_e64 v197, v197, v235, s[26:27]
	v_mfma_f32_4x4x4_16b_bf16 v[232:235], v[218:219], v[108:109], 0
	v_cvt_scalef32_pk_bf16_fp8 v222, v174, 1.0
	v_cvt_scalef32_pk_bf16_fp8 v223, v174, 1.0 op_sel:[1,0,0]
	v_mfma_f32_4x4x4_16b_bf16 v[232:235], v[220:221], v[110:111], v[232:235]
	v_cvt_scalef32_pk_bf16_fp8 v224, v175, 1.0
	v_cvt_scalef32_pk_bf16_fp8 v225, v175, 1.0 op_sel:[1,0,0]
	v_lshl_or_b32 v67, v67, 7, v209
	global_load_dwordx4 v[172:175], v67, s[6:7] sc0
	v_mfma_f32_4x4x4_16b_bf16 v[232:235], v[222:223], v[100:101], v[232:235]
	s_nop 1
	v_mfma_f32_4x4x4_16b_bf16 v[232:235], v[224:225], v[102:103], v[232:235]
	v_cndmask_b32_e64 v198, v228, v229, s[22:23]
	v_cndmask_b32_e64 v198, v198, v230, s[24:25]
	v_cndmask_b32_e64 v198, v198, v231, s[26:27]
	s_nop 4
	v_cndmask_b32_e64 v199, v232, v233, s[22:23]
	v_cndmask_b32_e64 v199, v199, v234, s[24:25]
	v_cndmask_b32_e64 v199, v199, v235, s[26:27]
	v_cndmask_b32_e64 v200, v184, v192, s[4:5]
	v_cndmask_b32_e64 v201, v192, v184, s[4:5]
	v_cndmask_b32_e64 v202, v185, v193, s[4:5]
	v_cndmask_b32_e64 v203, v193, v185, s[4:5]
	v_cndmask_b32_e64 v204, v186, v194, s[4:5]
	v_cndmask_b32_e64 v205, v194, v186, s[4:5]
	v_cndmask_b32_e64 v236, v187, v195, s[4:5]
	v_cndmask_b32_e64 v237, v195, v187, s[4:5]
	v_cndmask_b32_e64 v238, v188, v196, s[4:5]
	v_cndmask_b32_e64 v239, v196, v188, s[4:5]
	v_cndmask_b32_e64 v240, v189, v197, s[4:5]
	v_cndmask_b32_e64 v241, v197, v189, s[4:5]
	v_cndmask_b32_e64 v242, v190, v198, s[4:5]
	v_cndmask_b32_e64 v243, v198, v190, s[4:5]
	v_cndmask_b32_e64 v244, v191, v199, s[4:5]
	v_cndmask_b32_e64 v245, v199, v191, s[4:5]
	v_add_f32_dpp v246, v200, v201 row_half_mirror row_mask:0xf bank_mask:0xf
	v_add_f32_dpp v247, v202, v203 row_half_mirror row_mask:0xf bank_mask:0xf
	v_add_f32_dpp v248, v204, v205 row_half_mirror row_mask:0xf bank_mask:0xf
	v_add_f32_dpp v249, v236, v237 row_half_mirror row_mask:0xf bank_mask:0xf
	v_add_f32_dpp v226, v238, v239 row_half_mirror row_mask:0xf bank_mask:0xf
	v_add_f32_dpp v227, v240, v241 row_half_mirror row_mask:0xf bank_mask:0xf
	v_add_f32_dpp v210, v242, v243 row_half_mirror row_mask:0xf bank_mask:0xf
	v_add_f32_dpp v211, v244, v245 row_half_mirror row_mask:0xf bank_mask:0xf
	v_cndmask_b32_e64 v200, v246, v226, s[2:3]
	v_cndmask_b32_e64 v201, v226, v246, s[2:3]
	v_cndmask_b32_e64 v202, v247, v227, s[2:3]
	v_cndmask_b32_e64 v203, v227, v247, s[2:3]
	v_cndmask_b32_e64 v204, v248, v210, s[2:3]
	v_cndmask_b32_e64 v205, v210, v248, s[2:3]
	v_cndmask_b32_e64 v236, v249, v211, s[2:3]
	v_cndmask_b32_e64 v237, v211, v249, s[2:3]
	v_add_f32_dpp v212, v200, v201 quad_perm:[2,3,0,1] row_mask:0xf bank_mask:0xf
	v_add_f32_dpp v213, v202, v203 quad_perm:[2,3,0,1] row_mask:0xf bank_mask:0xf
	v_add_f32_dpp v214, v204, v205 quad_perm:[2,3,0,1] row_mask:0xf bank_mask:0xf
	v_add_f32_dpp v215, v236, v237 quad_perm:[2,3,0,1] row_mask:0xf bank_mask:0xf
	v_cndmask_b32_e64 v200, v212, v214, s[0:1]
	v_cndmask_b32_e64 v201, v214, v212, s[0:1]
	v_cndmask_b32_e64 v202, v213, v215, s[0:1]
	v_cndmask_b32_e64 v203, v215, v213, s[0:1]
	s_nop 1
	v_add_f32_dpp v216, v200, v201 quad_perm:[1,0,3,2] row_mask:0xf bank_mask:0xf
	v_add_f32_dpp v217, v202, v203 quad_perm:[1,0,3,2] row_mask:0xf bank_mask:0xf
	s_ashr_i32 s11, s10, 31
	s_lshl_b64 s[10:11], s[10:11], 8
	v_cvt_pk_bf16_f32 v186, v216, v217
	v_lshl_add_u64 v[184:185], v[178:179], 0, s[10:11]
	global_store_dword v[184:185], v186, off
	s_add_u32 s20, s12, 0x300
	s_lshl_b32 s20, s20, 11
	v_lshl_add_u64 v[108:109], v[182:183], 0, s[20:21]
	global_load_dwordx4 v[100:103], v[108:109], off offset:16
	s_nop 0
	global_load_dwordx4 v[108:111], v[108:109], off
	s_add_u32 s20, s12, 0x500
	s_lshl_b32 s20, s20, 9
	v_lshl_add_u64 v[80:81], v[180:181], 0, s[20:21]
	global_load_dwordx4 v[64:67], v[80:81], off offset:48
	global_load_dwordx4 v[68:71], v[80:81], off offset:32
	global_load_dwordx4 v[72:75], v[80:81], off offset:16
	s_nop 0
	global_load_dwordx4 v[80:83], v[80:81], off
	s_add_u32 s12, s12, 0x200
	s_mov_b32 s13, 61
.Lpd2_loop:
	s_mov_b32 s14, s12
	s_waitcnt vmcnt(23)
	v_cvt_scalef32_pk_bf16_fp8 v210, v24, 1.0
	v_cvt_scalef32_pk_bf16_fp8 v211, v24, 1.0 op_sel:[1,0,0]
	v_cvt_scalef32_pk_bf16_fp8 v212, v25, 1.0
	v_cvt_scalef32_pk_bf16_fp8 v213, v25, 1.0 op_sel:[1,0,0]
	v_mfma_f32_4x4x4_16b_bf16 v[228:231], v[210:211], v[20:21], 0
	v_cvt_scalef32_pk_bf16_fp8 v214, v26, 1.0
	v_cvt_scalef32_pk_bf16_fp8 v215, v26, 1.0 op_sel:[1,0,0]
	v_mfma_f32_4x4x4_16b_bf16 v[228:231], v[212:213], v[22:23], v[228:231]
	v_cvt_scalef32_pk_bf16_fp8 v216, v27, 1.0
	v_cvt_scalef32_pk_bf16_fp8 v217, v27, 1.0 op_sel:[1,0,0]
	v_lshl_or_b32 v0, v0, 7, v209
	global_load_dwordx4 v[24:27], v0, s[6:7] sc0
	v_mfma_f32_4x4x4_16b_bf16 v[228:231], v[214:215], v[16:17], v[228:231]
	v_cvt_scalef32_pk_bf16_fp8 v218, v28, 1.0
	v_cvt_scalef32_pk_bf16_fp8 v219, v28, 1.0 op_sel:[1,0,0]
	v_mfma_f32_4x4x4_16b_bf16 v[228:231], v[216:217], v[18:19], v[228:231]
	v_cvt_scalef32_pk_bf16_fp8 v220, v29, 1.0
	v_cvt_scalef32_pk_bf16_fp8 v221, v29, 1.0 op_sel:[1,0,0]
	v_mfma_f32_4x4x4_16b_bf16 v[232:235], v[218:219], v[20:21], 0
	v_cvt_scalef32_pk_bf16_fp8 v222, v30, 1.0
	v_cvt_scalef32_pk_bf16_fp8 v223, v30, 1.0 op_sel:[1,0,0]
	v_mfma_f32_4x4x4_16b_bf16 v[232:235], v[220:221], v[22:23], v[232:235]
	v_cvt_scalef32_pk_bf16_fp8 v224, v31, 1.0
	v_cvt_scalef32_pk_bf16_fp8 v225, v31, 1.0 op_sel:[1,0,0]
	v_lshl_or_b32 v1, v1, 7, v209
	global_load_dwordx4 v[28:31], v1, s[6:7] sc0
	v_mfma_f32_4x4x4_16b_bf16 v[232:235], v[222:223], v[16:17], v[232:235]
	v_cvt_scalef32_pk_bf16_fp8 v210, v32, 1.0
	v_cvt_scalef32_pk_bf16_fp8 v211, v32, 1.0 op_sel:[1,0,0]
	v_mfma_f32_4x4x4_16b_bf16 v[232:235], v[224:225], v[18:19], v[232:235]
	v_cvt_scalef32_pk_bf16_fp8 v212, v33, 1.0
	v_cvt_scalef32_pk_bf16_fp8 v213, v33, 1.0 op_sel:[1,0,0]
	v_cndmask_b32_e64 v184, v228, v229, s[22:23]
	v_cndmask_b32_e64 v184, v184, v230, s[24:25]
	v_cndmask_b32_e64 v184, v184, v231, s[26:27]
	v_mfma_f32_4x4x4_16b_bf16 v[228:231], v[210:211], v[20:21], 0
	v_cvt_scalef32_pk_bf16_fp8 v214, v34, 1.0
	v_cvt_scalef32_pk_bf16_fp8 v215, v34, 1.0 op_sel:[1,0,0]
	v_mfma_f32_4x4x4_16b_bf16 v[228:231], v[212:213], v[22:23], v[228:231]
	v_cvt_scalef32_pk_bf16_fp8 v216, v35, 1.0
	v_cvt_scalef32_pk_bf16_fp8 v217, v35, 1.0 op_sel:[1,0,0]
	v_lshl_or_b32 v2, v2, 7, v209
	global_load_dwordx4 v[32:35], v2, s[6:7] sc0
	v_mfma_f32_4x4x4_16b_bf16 v[228:231], v[214:215], v[16:17], v[228:231]
	v_cvt_scalef32_pk_bf16_fp8 v218, v36, 1.0
	v_cvt_scalef32_pk_bf16_fp8 v219, v36, 1.0 op_sel:[1,0,0]
	v_mfma_f32_4x4x4_16b_bf16 v[228:231], v[216:217], v[18:19], v[228:231]
	v_cvt_scalef32_pk_bf16_fp8 v220, v37, 1.0
	v_cvt_scalef32_pk_bf16_fp8 v221, v37, 1.0 op_sel:[1,0,0]
	v_cndmask_b32_e64 v185, v232, v233, s[22:23]
	v_cndmask_b32_e64 v185, v185, v234, s[24:25]
	v_cndmask_b32_e64 v185, v185, v235, s[26:27]
	v_mfma_f32_4x4x4_16b_bf16 v[232:235], v[218:219], v[20:21], 0
	v_cvt_scalef32_pk_bf16_fp8 v222, v38, 1.0
	v_cvt_scalef32_pk_bf16_fp8 v223, v38, 1.0 op_sel:[1,0,0]
	v_mfma_f32_4x4x4_16b_bf16 v[232:235], v[220:221], v[22:23], v[232:235]
	v_cvt_scalef32_pk_bf16_fp8 v224, v39, 1.0
	v_cvt_scalef32_pk_bf16_fp8 v225, v39, 1.0 op_sel:[1,0,0]
	v_lshl_or_b32 v3, v3, 7, v209
	global_load_dwordx4 v[36:39], v3, s[6:7] sc0
	v_mfma_f32_4x4x4_16b_bf16 v[232:235], v[222:223], v[16:17], v[232:235]
	v_cvt_scalef32_pk_bf16_fp8 v210, v40, 1.0
	v_cvt_scalef32_pk_bf16_fp8 v211, v40, 1.0 op_sel:[1,0,0]
	v_mfma_f32_4x4x4_16b_bf16 v[232:235], v[224:225], v[18:19], v[232:235]
	v_cvt_scalef32_pk_bf16_fp8 v212, v41, 1.0
	v_cvt_scalef32_pk_bf16_fp8 v213, v41, 1.0 op_sel:[1,0,0]
	v_cndmask_b32_e64 v186, v228, v229, s[22:23]
	v_cndmask_b32_e64 v186, v186, v230, s[24:25]
	v_cndmask_b32_e64 v186, v186, v231, s[26:27]
	v_mfma_f32_4x4x4_16b_bf16 v[228:231], v[210:211], v[20:21], 0
	v_cvt_scalef32_pk_bf16_fp8 v214, v42, 1.0
	v_cvt_scalef32_pk_bf16_fp8 v215, v42, 1.0 op_sel:[1,0,0]
	v_mfma_f32_4x4x4_16b_bf16 v[228:231], v[212:213], v[22:23], v[228:231]
	v_cvt_scalef32_pk_bf16_fp8 v216, v43, 1.0
	v_cvt_scalef32_pk_bf16_fp8 v217, v43, 1.0 op_sel:[1,0,0]
	v_lshl_or_b32 v4, v4, 7, v209
	global_load_dwordx4 v[40:43], v4, s[6:7] sc0
	v_mfma_f32_4x4x4_16b_bf16 v[228:231], v[214:215], v[16:17], v[228:231]
	v_cvt_scalef32_pk_bf16_fp8 v218, v44, 1.0
	v_cvt_scalef32_pk_bf16_fp8 v219, v44, 1.0 op_sel:[1,0,0]
	v_mfma_f32_4x4x4_16b_bf16 v[228:231], v[216:217], v[18:19], v[228:231]
	v_cvt_scalef32_pk_bf16_fp8 v220, v45, 1.0
	v_cvt_scalef32_pk_bf16_fp8 v221, v45, 1.0 op_sel:[1,0,0]
	v_cndmask_b32_e64 v187, v232, v233, s[22:23]
	v_cndmask_b32_e64 v187, v187, v234, s[24:25]
	v_cndmask_b32_e64 v187, v187, v235, s[26:27]
	v_mfma_f32_4x4x4_16b_bf16 v[232:235], v[218:219], v[20:21], 0
	v_cvt_scalef32_pk_bf16_fp8 v222, v46, 1.0
	v_cvt_scalef32_pk_bf16_fp8 v223, v46, 1.0 op_sel:[1,0,0]
	v_mfma_f32_4x4x4_16b_bf16 v[232:235], v[220:221], v[22:23], v[232:235]
	v_cvt_scalef32_pk_bf16_fp8 v224, v47, 1.0
	v_cvt_scalef32_pk_bf16_fp8 v225, v47, 1.0 op_sel:[1,0,0]
	v_lshl_or_b32 v5, v5, 7, v209
	global_load_dwordx4 v[44:47], v5, s[6:7] sc0
	v_mfma_f32_4x4x4_16b_bf16 v[232:235], v[222:223], v[16:17], v[232:235]
	v_cvt_scalef32_pk_bf16_fp8 v210, v48, 1.0
	v_cvt_scalef32_pk_bf16_fp8 v211, v48, 1.0 op_sel:[1,0,0]
	v_mfma_f32_4x4x4_16b_bf16 v[232:235], v[224:225], v[18:19], v[232:235]
	v_cvt_scalef32_pk_bf16_fp8 v212, v49, 1.0
	v_cvt_scalef32_pk_bf16_fp8 v213, v49, 1.0 op_sel:[1,0,0]
	v_cndmask_b32_e64 v188, v228, v229, s[22:23]
	v_cndmask_b32_e64 v188, v188, v230, s[24:25]
	v_cndmask_b32_e64 v188, v188, v231, s[26:27]
	v_mfma_f32_4x4x4_16b_bf16 v[228:231], v[210:211], v[20:21], 0
	v_cvt_scalef32_pk_bf16_fp8 v214, v50, 1.0
	v_cvt_scalef32_pk_bf16_fp8 v215, v50, 1.0 op_sel:[1,0,0]
	v_mfma_f32_4x4x4_16b_bf16 v[228:231], v[212:213], v[22:23], v[228:231]
	v_cvt_scalef32_pk_bf16_fp8 v216, v51, 1.0
	v_cvt_scalef32_pk_bf16_fp8 v217, v51, 1.0 op_sel:[1,0,0]
	v_lshl_or_b32 v6, v6, 7, v209
	global_load_dwordx4 v[48:51], v6, s[6:7] sc0
	v_mfma_f32_4x4x4_16b_bf16 v[228:231], v[214:215], v[16:17], v[228:231]
	v_cvt_scalef32_pk_bf16_fp8 v218, v52, 1.0
	v_cvt_scalef32_pk_bf16_fp8 v219, v52, 1.0 op_sel:[1,0,0]
	v_mfma_f32_4x4x4_16b_bf16 v[228:231], v[216:217], v[18:19], v[228:231]
	v_cvt_scalef32_pk_bf16_fp8 v220, v53, 1.0
	v_cvt_scalef32_pk_bf16_fp8 v221, v53, 1.0 op_sel:[1,0,0]
	v_cndmask_b32_e64 v189, v232, v233, s[22:23]
	v_cndmask_b32_e64 v189, v189, v234, s[24:25]
	v_cndmask_b32_e64 v189, v189, v235, s[26:27]
	v_mfma_f32_4x4x4_16b_bf16 v[232:235], v[218:219], v[20:21], 0
	v_cvt_scalef32_pk_bf16_fp8 v222, v54, 1.0
	v_cvt_scalef32_pk_bf16_fp8 v223, v54, 1.0 op_sel:[1,0,0]
	v_mfma_f32_4x4x4_16b_bf16 v[232:235], v[220:221], v[22:23], v[232:235]
	v_cvt_scalef32_pk_bf16_fp8 v224, v55, 1.0
	v_cvt_scalef32_pk_bf16_fp8 v225, v55, 1.0 op_sel:[1,0,0]
	v_lshl_or_b32 v7, v7, 7, v209
	global_load_dwordx4 v[52:55], v7, s[6:7] sc0
	v_mfma_f32_4x4x4_16b_bf16 v[232:235], v[222:223], v[16:17], v[232:235]
	v_cvt_scalef32_pk_bf16_fp8 v210, v56, 1.0
	v_cvt_scalef32_pk_bf16_fp8 v211, v56, 1.0 op_sel:[1,0,0]
	v_mfma_f32_4x4x4_16b_bf16 v[232:235], v[224:225], v[18:19], v[232:235]
	v_cvt_scalef32_pk_bf16_fp8 v212, v57, 1.0
	v_cvt_scalef32_pk_bf16_fp8 v213, v57, 1.0 op_sel:[1,0,0]
	v_cndmask_b32_e64 v190, v228, v229, s[22:23]
	v_cndmask_b32_e64 v190, v190, v230, s[24:25]
	v_cndmask_b32_e64 v190, v190, v231, s[26:27]
	v_mfma_f32_4x4x4_16b_bf16 v[228:231], v[210:211], v[20:21], 0
	v_cvt_scalef32_pk_bf16_fp8 v214, v58, 1.0
	v_cvt_scalef32_pk_bf16_fp8 v215, v58, 1.0 op_sel:[1,0,0]
	v_mfma_f32_4x4x4_16b_bf16 v[228:231], v[212:213], v[22:23], v[228:231]
	v_cvt_scalef32_pk_bf16_fp8 v216, v59, 1.0
	v_cvt_scalef32_pk_bf16_fp8 v217, v59, 1.0 op_sel:[1,0,0]
	v_lshl_or_b32 v8, v8, 7, v209
	global_load_dwordx4 v[56:59], v8, s[6:7] sc0
	v_mfma_f32_4x4x4_16b_bf16 v[228:231], v[214:215], v[16:17], v[228:231]
	v_cvt_scalef32_pk_bf16_fp8 v218, v60, 1.0
	v_cvt_scalef32_pk_bf16_fp8 v219, v60, 1.0 op_sel:[1,0,0]
	v_mfma_f32_4x4x4_16b_bf16 v[228:231], v[216:217], v[18:19], v[228:231]
	v_cvt_scalef32_pk_bf16_fp8 v220, v61, 1.0
	v_cvt_scalef32_pk_bf16_fp8 v221, v61, 1.0 op_sel:[1,0,0]
	v_cndmask_b32_e64 v191, v232, v233, s[22:23]
	v_cndmask_b32_e64 v191, v191, v234, s[24:25]
	v_cndmask_b32_e64 v191, v191, v235, s[26:27]
	v_mfma_f32_4x4x4_16b_bf16 v[232:235], v[218:219], v[20:21], 0
	v_cvt_scalef32_pk_bf16_fp8 v222, v62, 1.0
	v_cvt_scalef32_pk_bf16_fp8 v223, v62, 1.0 op_sel:[1,0,0]
	v_mfma_f32_4x4x4_16b_bf16 v[232:235], v[220:221], v[22:23], v[232:235]
	v_cvt_scalef32_pk_bf16_fp8 v224, v63, 1.0
	v_cvt_scalef32_pk_bf16_fp8 v225, v63, 1.0 op_sel:[1,0,0]
	v_lshl_or_b32 v9, v9, 7, v209
	global_load_dwordx4 v[60:63], v9, s[6:7] sc0
	v_mfma_f32_4x4x4_16b_bf16 v[232:235], v[222:223], v[16:17], v[232:235]
	v_cvt_scalef32_pk_bf16_fp8 v210, v76, 1.0
	v_cvt_scalef32_pk_bf16_fp8 v211, v76, 1.0 op_sel:[1,0,0]
	v_mfma_f32_4x4x4_16b_bf16 v[232:235], v[224:225], v[18:19], v[232:235]
	v_cvt_scalef32_pk_bf16_fp8 v212, v77, 1.0
	v_cvt_scalef32_pk_bf16_fp8 v213, v77, 1.0 op_sel:[1,0,0]
	v_cndmask_b32_e64 v192, v228, v229, s[22:23]
	v_cndmask_b32_e64 v192, v192, v230, s[24:25]
	v_cndmask_b32_e64 v192, v192, v231, s[26:27]
	v_mfma_f32_4x4x4_16b_bf16 v[228:231], v[210:211], v[20:21], 0
	v_cvt_scalef32_pk_bf16_fp8 v214, v78, 1.0
	v_cvt_scalef32_pk_bf16_fp8 v215, v78, 1.0 op_sel:[1,0,0]
	v_mfma_f32_4x4x4_16b_bf16 v[228:231], v[212:213], v[22:23], v[228:231]
	v_cvt_scalef32_pk_bf16_fp8 v216, v79, 1.0
	v_cvt_scalef32_pk_bf16_fp8 v217, v79, 1.0 op_sel:[1,0,0]
	v_lshl_or_b32 v10, v10, 7, v209
	global_load_dwordx4 v[76:79], v10, s[6:7] sc0
	v_mfma_f32_4x4x4_16b_bf16 v[228:231], v[214:215], v[16:17], v[228:231]
	v_cvt_scalef32_pk_bf16_fp8 v218, v84, 1.0
	v_cvt_scalef32_pk_bf16_fp8 v219, v84, 1.0 op_sel:[1,0,0]
	v_mfma_f32_4x4x4_16b_bf16 v[228:231], v[216:217], v[18:19], v[228:231]
	v_cvt_scalef32_pk_bf16_fp8 v220, v85, 1.0
	v_cvt_scalef32_pk_bf16_fp8 v221, v85, 1.0 op_sel:[1,0,0]
	v_cndmask_b32_e64 v193, v232, v233, s[22:23]
	v_cndmask_b32_e64 v193, v193, v234, s[24:25]
	v_cndmask_b32_e64 v193, v193, v235, s[26:27]
	v_mfma_f32_4x4x4_16b_bf16 v[232:235], v[218:219], v[20:21], 0
	v_cvt_scalef32_pk_bf16_fp8 v222, v86, 1.0
	v_cvt_scalef32_pk_bf16_fp8 v223, v86, 1.0 op_sel:[1,0,0]
	v_mfma_f32_4x4x4_16b_bf16 v[232:235], v[220:221], v[22:23], v[232:235]
	v_cvt_scalef32_pk_bf16_fp8 v224, v87, 1.0
	v_cvt_scalef32_pk_bf16_fp8 v225, v87, 1.0 op_sel:[1,0,0]
	v_lshl_or_b32 v11, v11, 7, v209
	global_load_dwordx4 v[84:87], v11, s[6:7] sc0
	v_mfma_f32_4x4x4_16b_bf16 v[232:235], v[222:223], v[16:17], v[232:235]
	v_cvt_scalef32_pk_bf16_fp8 v210, v88, 1.0
	v_cvt_scalef32_pk_bf16_fp8 v211, v88, 1.0 op_sel:[1,0,0]
	v_mfma_f32_4x4x4_16b_bf16 v[232:235], v[224:225], v[18:19], v[232:235]
	v_cvt_scalef32_pk_bf16_fp8 v212, v89, 1.0
	v_cvt_scalef32_pk_bf16_fp8 v213, v89, 1.0 op_sel:[1,0,0]
	v_cndmask_b32_e64 v194, v228, v229, s[22:23]
	v_cndmask_b32_e64 v194, v194, v230, s[24:25]
	v_cndmask_b32_e64 v194, v194, v231, s[26:27]
	v_mfma_f32_4x4x4_16b_bf16 v[228:231], v[210:211], v[20:21], 0
	v_cvt_scalef32_pk_bf16_fp8 v214, v90, 1.0
	v_cvt_scalef32_pk_bf16_fp8 v215, v90, 1.0 op_sel:[1,0,0]
	v_mfma_f32_4x4x4_16b_bf16 v[228:231], v[212:213], v[22:23], v[228:231]
	v_cvt_scalef32_pk_bf16_fp8 v216, v91, 1.0
	v_cvt_scalef32_pk_bf16_fp8 v217, v91, 1.0 op_sel:[1,0,0]
	v_lshl_or_b32 v12, v12, 7, v209
	global_load_dwordx4 v[88:91], v12, s[6:7] sc0
	v_mfma_f32_4x4x4_16b_bf16 v[228:231], v[214:215], v[16:17], v[228:231]
	v_cvt_scalef32_pk_bf16_fp8 v218, v92, 1.0
	v_cvt_scalef32_pk_bf16_fp8 v219, v92, 1.0 op_sel:[1,0,0]
	v_mfma_f32_4x4x4_16b_bf16 v[228:231], v[216:217], v[18:19], v[228:231]
	v_cvt_scalef32_pk_bf16_fp8 v220, v93, 1.0
	v_cvt_scalef32_pk_bf16_fp8 v221, v93, 1.0 op_sel:[1,0,0]
	v_cndmask_b32_e64 v195, v232, v233, s[22:23]
	v_cndmask_b32_e64 v195, v195, v234, s[24:25]
	v_cndmask_b32_e64 v195, v195, v235, s[26:27]
	v_mfma_f32_4x4x4_16b_bf16 v[232:235], v[218:219], v[20:21], 0
	v_cvt_scalef32_pk_bf16_fp8 v222, v94, 1.0
	v_cvt_scalef32_pk_bf16_fp8 v223, v94, 1.0 op_sel:[1,0,0]
	v_mfma_f32_4x4x4_16b_bf16 v[232:235], v[220:221], v[22:23], v[232:235]
	v_cvt_scalef32_pk_bf16_fp8 v224, v95, 1.0
	v_cvt_scalef32_pk_bf16_fp8 v225, v95, 1.0 op_sel:[1,0,0]
	v_lshl_or_b32 v13, v13, 7, v209
	global_load_dwordx4 v[92:95], v13, s[6:7] sc0
	v_mfma_f32_4x4x4_16b_bf16 v[232:235], v[222:223], v[16:17], v[232:235]
	v_cvt_scalef32_pk_bf16_fp8 v210, v96, 1.0
	v_cvt_scalef32_pk_bf16_fp8 v211, v96, 1.0 op_sel:[1,0,0]
	v_mfma_f32_4x4x4_16b_bf16 v[232:235], v[224:225], v[18:19], v[232:235]
	v_cvt_scalef32_pk_bf16_fp8 v212, v97, 1.0
	v_cvt_scalef32_pk_bf16_fp8 v213, v97, 1.0 op_sel:[1,0,0]
	v_cndmask_b32_e64 v196, v228, v229, s[22:23]
	v_cndmask_b32_e64 v196, v196, v230, s[24:25]
	v_cndmask_b32_e64 v196, v196, v231, s[26:27]
	v_mfma_f32_4x4x4_16b_bf16 v[228:231], v[210:211], v[20:21], 0
	v_cvt_scalef32_pk_bf16_fp8 v214, v98, 1.0
	v_cvt_scalef32_pk_bf16_fp8 v215, v98, 1.0 op_sel:[1,0,0]
	v_mfma_f32_4x4x4_16b_bf16 v[228:231], v[212:213], v[22:23], v[228:231]
	v_cvt_scalef32_pk_bf16_fp8 v216, v99, 1.0
	v_cvt_scalef32_pk_bf16_fp8 v217, v99, 1.0 op_sel:[1,0,0]
	v_lshl_or_b32 v14, v14, 7, v209
	global_load_dwordx4 v[96:99], v14, s[6:7] sc0
	v_mfma_f32_4x4x4_16b_bf16 v[228:231], v[214:215], v[16:17], v[228:231]
	v_cvt_scalef32_pk_bf16_fp8 v218, v104, 1.0
	v_cvt_scalef32_pk_bf16_fp8 v219, v104, 1.0 op_sel:[1,0,0]
	v_mfma_f32_4x4x4_16b_bf16 v[228:231], v[216:217], v[18:19], v[228:231]
	v_cvt_scalef32_pk_bf16_fp8 v220, v105, 1.0
	v_cvt_scalef32_pk_bf16_fp8 v221, v105, 1.0 op_sel:[1,0,0]
	v_cndmask_b32_e64 v197, v232, v233, s[22:23]
	v_cndmask_b32_e64 v197, v197, v234, s[24:25]
	v_cndmask_b32_e64 v197, v197, v235, s[26:27]
	v_mfma_f32_4x4x4_16b_bf16 v[232:235], v[218:219], v[20:21], 0
	v_cvt_scalef32_pk_bf16_fp8 v222, v106, 1.0
	v_cvt_scalef32_pk_bf16_fp8 v223, v106, 1.0 op_sel:[1,0,0]
	v_mfma_f32_4x4x4_16b_bf16 v[232:235], v[220:221], v[22:23], v[232:235]
	v_cvt_scalef32_pk_bf16_fp8 v224, v107, 1.0
	v_cvt_scalef32_pk_bf16_fp8 v225, v107, 1.0 op_sel:[1,0,0]
	v_lshl_or_b32 v15, v15, 7, v209
	global_load_dwordx4 v[104:107], v15, s[6:7] sc0
	v_mfma_f32_4x4x4_16b_bf16 v[232:235], v[222:223], v[16:17], v[232:235]
	s_nop 1
	v_mfma_f32_4x4x4_16b_bf16 v[232:235], v[224:225], v[18:19], v[232:235]
	v_cndmask_b32_e64 v198, v228, v229, s[22:23]
	v_cndmask_b32_e64 v198, v198, v230, s[24:25]
	v_cndmask_b32_e64 v198, v198, v231, s[26:27]
	s_nop 4
	v_cndmask_b32_e64 v199, v232, v233, s[22:23]
	v_cndmask_b32_e64 v199, v199, v234, s[24:25]
	v_cndmask_b32_e64 v199, v199, v235, s[26:27]
	v_cndmask_b32_e64 v200, v184, v192, s[4:5]
	v_cndmask_b32_e64 v201, v192, v184, s[4:5]
	v_cndmask_b32_e64 v202, v185, v193, s[4:5]
	v_cndmask_b32_e64 v203, v193, v185, s[4:5]
	v_cndmask_b32_e64 v204, v186, v194, s[4:5]
	v_cndmask_b32_e64 v205, v194, v186, s[4:5]
	v_cndmask_b32_e64 v236, v187, v195, s[4:5]
	v_cndmask_b32_e64 v237, v195, v187, s[4:5]
	v_cndmask_b32_e64 v238, v188, v196, s[4:5]
	v_cndmask_b32_e64 v239, v196, v188, s[4:5]
	v_cndmask_b32_e64 v240, v189, v197, s[4:5]
	v_cndmask_b32_e64 v241, v197, v189, s[4:5]
	v_cndmask_b32_e64 v242, v190, v198, s[4:5]
	v_cndmask_b32_e64 v243, v198, v190, s[4:5]
	v_cndmask_b32_e64 v244, v191, v199, s[4:5]
	v_cndmask_b32_e64 v245, v199, v191, s[4:5]
	v_add_f32_dpp v246, v200, v201 row_half_mirror row_mask:0xf bank_mask:0xf
	v_add_f32_dpp v247, v202, v203 row_half_mirror row_mask:0xf bank_mask:0xf
	v_add_f32_dpp v248, v204, v205 row_half_mirror row_mask:0xf bank_mask:0xf
	v_add_f32_dpp v249, v236, v237 row_half_mirror row_mask:0xf bank_mask:0xf
	v_add_f32_dpp v226, v238, v239 row_half_mirror row_mask:0xf bank_mask:0xf
	v_add_f32_dpp v227, v240, v241 row_half_mirror row_mask:0xf bank_mask:0xf
	v_add_f32_dpp v210, v242, v243 row_half_mirror row_mask:0xf bank_mask:0xf
	v_add_f32_dpp v211, v244, v245 row_half_mirror row_mask:0xf bank_mask:0xf
	v_cndmask_b32_e64 v200, v246, v226, s[2:3]
	v_cndmask_b32_e64 v201, v226, v246, s[2:3]
	v_cndmask_b32_e64 v202, v247, v227, s[2:3]
	v_cndmask_b32_e64 v203, v227, v247, s[2:3]
	v_cndmask_b32_e64 v204, v248, v210, s[2:3]
	v_cndmask_b32_e64 v205, v210, v248, s[2:3]
	v_cndmask_b32_e64 v236, v249, v211, s[2:3]
	v_cndmask_b32_e64 v237, v211, v249, s[2:3]
	v_add_f32_dpp v212, v200, v201 quad_perm:[2,3,0,1] row_mask:0xf bank_mask:0xf
	v_add_f32_dpp v213, v202, v203 quad_perm:[2,3,0,1] row_mask:0xf bank_mask:0xf
	v_add_f32_dpp v214, v204, v205 quad_perm:[2,3,0,1] row_mask:0xf bank_mask:0xf
	v_add_f32_dpp v215, v236, v237 quad_perm:[2,3,0,1] row_mask:0xf bank_mask:0xf
	v_cndmask_b32_e64 v200, v212, v214, s[0:1]
	v_cndmask_b32_e64 v201, v214, v212, s[0:1]
	v_cndmask_b32_e64 v202, v213, v215, s[0:1]
	v_cndmask_b32_e64 v203, v215, v213, s[0:1]
	s_nop 1
	v_add_f32_dpp v216, v200, v201 quad_perm:[1,0,3,2] row_mask:0xf bank_mask:0xf
	v_add_f32_dpp v217, v202, v203 quad_perm:[1,0,3,2] row_mask:0xf bank_mask:0xf
	s_ashr_i32 s15, s14, 31
	s_lshl_b64 s[14:15], s[14:15], 8
	v_cvt_pk_bf16_f32 v186, v216, v217
	v_lshl_add_u64 v[184:185], v[178:179], 0, s[14:15]
	global_store_dword v[184:185], v186, off
	s_add_u32 s20, s12, 0x200
	s_lshl_b32 s20, s20, 11
	v_lshl_add_u64 v[20:21], v[182:183], 0, s[20:21]
	global_load_dwordx4 v[16:19], v[20:21], off offset:16
	s_nop 0
	global_load_dwordx4 v[20:23], v[20:21], off
	s_add_u32 s20, s12, 0x400
	s_lshl_b32 s20, s20, 9
	v_lshl_add_u64 v[0:1], v[180:181], 0, s[20:21]
	global_load_dwordx4 v[12:15], v[0:1], off offset:48
	global_load_dwordx4 v[8:11], v[0:1], off offset:32
	global_load_dwordx4 v[4:7], v[0:1], off offset:16
	s_nop 0
	global_load_dwordx4 v[0:3], v[0:1], off
	s_add_u32 s10, s12, 0x100
	s_waitcnt vmcnt(23)
	v_cvt_scalef32_pk_bf16_fp8 v210, v112, 1.0
	v_cvt_scalef32_pk_bf16_fp8 v211, v112, 1.0 op_sel:[1,0,0]
	v_cvt_scalef32_pk_bf16_fp8 v212, v113, 1.0
	v_cvt_scalef32_pk_bf16_fp8 v213, v113, 1.0 op_sel:[1,0,0]
	v_mfma_f32_4x4x4_16b_bf16 v[228:231], v[210:211], v[108:109], 0
	v_cvt_scalef32_pk_bf16_fp8 v214, v114, 1.0
	v_cvt_scalef32_pk_bf16_fp8 v215, v114, 1.0 op_sel:[1,0,0]
	v_mfma_f32_4x4x4_16b_bf16 v[228:231], v[212:213], v[110:111], v[228:231]
	v_cvt_scalef32_pk_bf16_fp8 v216, v115, 1.0
	v_cvt_scalef32_pk_bf16_fp8 v217, v115, 1.0 op_sel:[1,0,0]
	v_lshl_or_b32 v80, v80, 7, v209
	global_load_dwordx4 v[112:115], v80, s[6:7] sc0
	v_mfma_f32_4x4x4_16b_bf16 v[228:231], v[214:215], v[100:101], v[228:231]
	v_cvt_scalef32_pk_bf16_fp8 v218, v116, 1.0
	v_cvt_scalef32_pk_bf16_fp8 v219, v116, 1.0 op_sel:[1,0,0]
	v_mfma_f32_4x4x4_16b_bf16 v[228:231], v[216:217], v[102:103], v[228:231]
	v_cvt_scalef32_pk_bf16_fp8 v220, v117, 1.0
	v_cvt_scalef32_pk_bf16_fp8 v221, v117, 1.0 op_sel:[1,0,0]
	v_mfma_f32_4x4x4_16b_bf16 v[232:235], v[218:219], v[108:109], 0
	v_cvt_scalef32_pk_bf16_fp8 v222, v118, 1.0
	v_cvt_scalef32_pk_bf16_fp8 v223, v118, 1.0 op_sel:[1,0,0]
	v_mfma_f32_4x4x4_16b_bf16 v[232:235], v[220:221], v[110:111], v[232:235]
	v_cvt_scalef32_pk_bf16_fp8 v224, v119, 1.0
	v_cvt_scalef32_pk_bf16_fp8 v225, v119, 1.0 op_sel:[1,0,0]
	v_lshl_or_b32 v81, v81, 7, v209
	global_load_dwordx4 v[116:119], v81, s[6:7] sc0
	v_mfma_f32_4x4x4_16b_bf16 v[232:235], v[222:223], v[100:101], v[232:235]
	v_cvt_scalef32_pk_bf16_fp8 v210, v120, 1.0
	v_cvt_scalef32_pk_bf16_fp8 v211, v120, 1.0 op_sel:[1,0,0]
	v_mfma_f32_4x4x4_16b_bf16 v[232:235], v[224:225], v[102:103], v[232:235]
	v_cvt_scalef32_pk_bf16_fp8 v212, v121, 1.0
	v_cvt_scalef32_pk_bf16_fp8 v213, v121, 1.0 op_sel:[1,0,0]
	v_cndmask_b32_e64 v184, v228, v229, s[22:23]
	v_cndmask_b32_e64 v184, v184, v230, s[24:25]
	v_cndmask_b32_e64 v184, v184, v231, s[26:27]
	v_mfma_f32_4x4x4_16b_bf16 v[228:231], v[210:211], v[108:109], 0
	v_cvt_scalef32_pk_bf16_fp8 v214, v122, 1.0
	v_cvt_scalef32_pk_bf16_fp8 v215, v122, 1.0 op_sel:[1,0,0]
	v_mfma_f32_4x4x4_16b_bf16 v[228:231], v[212:213], v[110:111], v[228:231]
	v_cvt_scalef32_pk_bf16_fp8 v216, v123, 1.0
	v_cvt_scalef32_pk_bf16_fp8 v217, v123, 1.0 op_sel:[1,0,0]
	v_lshl_or_b32 v82, v82, 7, v209
	global_load_dwordx4 v[120:123], v82, s[6:7] sc0
	v_mfma_f32_4x4x4_16b_bf16 v[228:231], v[214:215], v[100:101], v[228:231]
	v_cvt_scalef32_pk_bf16_fp8 v218, v124, 1.0
	v_cvt_scalef32_pk_bf16_fp8 v219, v124, 1.0 op_sel:[1,0,0]
	v_mfma_f32_4x4x4_16b_bf16 v[228:231], v[216:217], v[102:103], v[228:231]
	v_cvt_scalef32_pk_bf16_fp8 v220, v125, 1.0
	v_cvt_scalef32_pk_bf16_fp8 v221, v125, 1.0 op_sel:[1,0,0]
	v_cndmask_b32_e64 v185, v232, v233, s[22:23]
	v_cndmask_b32_e64 v185, v185, v234, s[24:25]
	v_cndmask_b32_e64 v185, v185, v235, s[26:27]
	v_mfma_f32_4x4x4_16b_bf16 v[232:235], v[218:219], v[108:109], 0
	v_cvt_scalef32_pk_bf16_fp8 v222, v126, 1.0
	v_cvt_scalef32_pk_bf16_fp8 v223, v126, 1.0 op_sel:[1,0,0]
	v_mfma_f32_4x4x4_16b_bf16 v[232:235], v[220:221], v[110:111], v[232:235]
	v_cvt_scalef32_pk_bf16_fp8 v224, v127, 1.0
	v_cvt_scalef32_pk_bf16_fp8 v225, v127, 1.0 op_sel:[1,0,0]
	v_lshl_or_b32 v83, v83, 7, v209
	global_load_dwordx4 v[124:127], v83, s[6:7] sc0
	v_mfma_f32_4x4x4_16b_bf16 v[232:235], v[222:223], v[100:101], v[232:235]
	v_cvt_scalef32_pk_bf16_fp8 v210, v128, 1.0
	v_cvt_scalef32_pk_bf16_fp8 v211, v128, 1.0 op_sel:[1,0,0]
	v_mfma_f32_4x4x4_16b_bf16 v[232:235], v[224:225], v[102:103], v[232:235]
	v_cvt_scalef32_pk_bf16_fp8 v212, v129, 1.0
	v_cvt_scalef32_pk_bf16_fp8 v213, v129, 1.0 op_sel:[1,0,0]
	v_cndmask_b32_e64 v186, v228, v229, s[22:23]
	v_cndmask_b32_e64 v186, v186, v230, s[24:25]
	v_cndmask_b32_e64 v186, v186, v231, s[26:27]
	v_mfma_f32_4x4x4_16b_bf16 v[228:231], v[210:211], v[108:109], 0
	v_cvt_scalef32_pk_bf16_fp8 v214, v130, 1.0
	v_cvt_scalef32_pk_bf16_fp8 v215, v130, 1.0 op_sel:[1,0,0]
	v_mfma_f32_4x4x4_16b_bf16 v[228:231], v[212:213], v[110:111], v[228:231]
	v_cvt_scalef32_pk_bf16_fp8 v216, v131, 1.0
	v_cvt_scalef32_pk_bf16_fp8 v217, v131, 1.0 op_sel:[1,0,0]
	v_lshl_or_b32 v72, v72, 7, v209
	global_load_dwordx4 v[128:131], v72, s[6:7] sc0
	v_mfma_f32_4x4x4_16b_bf16 v[228:231], v[214:215], v[100:101], v[228:231]
	v_cvt_scalef32_pk_bf16_fp8 v218, v132, 1.0
	v_cvt_scalef32_pk_bf16_fp8 v219, v132, 1.0 op_sel:[1,0,0]
	v_mfma_f32_4x4x4_16b_bf16 v[228:231], v[216:217], v[102:103], v[228:231]
	v_cvt_scalef32_pk_bf16_fp8 v220, v133, 1.0
	v_cvt_scalef32_pk_bf16_fp8 v221, v133, 1.0 op_sel:[1,0,0]
	v_cndmask_b32_e64 v187, v232, v233, s[22:23]
	v_cndmask_b32_e64 v187, v187, v234, s[24:25]
	v_cndmask_b32_e64 v187, v187, v235, s[26:27]
	v_mfma_f32_4x4x4_16b_bf16 v[232:235], v[218:219], v[108:109], 0
	v_cvt_scalef32_pk_bf16_fp8 v222, v134, 1.0
	v_cvt_scalef32_pk_bf16_fp8 v223, v134, 1.0 op_sel:[1,0,0]
	v_mfma_f32_4x4x4_16b_bf16 v[232:235], v[220:221], v[110:111], v[232:235]
	v_cvt_scalef32_pk_bf16_fp8 v224, v135, 1.0
	v_cvt_scalef32_pk_bf16_fp8 v225, v135, 1.0 op_sel:[1,0,0]
	v_lshl_or_b32 v73, v73, 7, v209
	global_load_dwordx4 v[132:135], v73, s[6:7] sc0
	v_mfma_f32_4x4x4_16b_bf16 v[232:235], v[222:223], v[100:101], v[232:235]
	v_cvt_scalef32_pk_bf16_fp8 v210, v136, 1.0
	v_cvt_scalef32_pk_bf16_fp8 v211, v136, 1.0 op_sel:[1,0,0]
	v_mfma_f32_4x4x4_16b_bf16 v[232:235], v[224:225], v[102:103], v[232:235]
	v_cvt_scalef32_pk_bf16_fp8 v212, v137, 1.0
	v_cvt_scalef32_pk_bf16_fp8 v213, v137, 1.0 op_sel:[1,0,0]
	v_cndmask_b32_e64 v188, v228, v229, s[22:23]
	v_cndmask_b32_e64 v188, v188, v230, s[24:25]
	v_cndmask_b32_e64 v188, v188, v231, s[26:27]
	v_mfma_f32_4x4x4_16b_bf16 v[228:231], v[210:211], v[108:109], 0
	v_cvt_scalef32_pk_bf16_fp8 v214, v138, 1.0
	v_cvt_scalef32_pk_bf16_fp8 v215, v138, 1.0 op_sel:[1,0,0]
	v_mfma_f32_4x4x4_16b_bf16 v[228:231], v[212:213], v[110:111], v[228:231]
	v_cvt_scalef32_pk_bf16_fp8 v216, v139, 1.0
	v_cvt_scalef32_pk_bf16_fp8 v217, v139, 1.0 op_sel:[1,0,0]
	v_lshl_or_b32 v74, v74, 7, v209
	global_load_dwordx4 v[136:139], v74, s[6:7] sc0
	v_mfma_f32_4x4x4_16b_bf16 v[228:231], v[214:215], v[100:101], v[228:231]
	v_cvt_scalef32_pk_bf16_fp8 v218, v140, 1.0
	v_cvt_scalef32_pk_bf16_fp8 v219, v140, 1.0 op_sel:[1,0,0]
	v_mfma_f32_4x4x4_16b_bf16 v[228:231], v[216:217], v[102:103], v[228:231]
	v_cvt_scalef32_pk_bf16_fp8 v220, v141, 1.0
	v_cvt_scalef32_pk_bf16_fp8 v221, v141, 1.0 op_sel:[1,0,0]
	v_cndmask_b32_e64 v189, v232, v233, s[22:23]
	v_cndmask_b32_e64 v189, v189, v234, s[24:25]
	v_cndmask_b32_e64 v189, v189, v235, s[26:27]
	v_mfma_f32_4x4x4_16b_bf16 v[232:235], v[218:219], v[108:109], 0
	v_cvt_scalef32_pk_bf16_fp8 v222, v142, 1.0
	v_cvt_scalef32_pk_bf16_fp8 v223, v142, 1.0 op_sel:[1,0,0]
	v_mfma_f32_4x4x4_16b_bf16 v[232:235], v[220:221], v[110:111], v[232:235]
	v_cvt_scalef32_pk_bf16_fp8 v224, v143, 1.0
	v_cvt_scalef32_pk_bf16_fp8 v225, v143, 1.0 op_sel:[1,0,0]
	v_lshl_or_b32 v75, v75, 7, v209
	global_load_dwordx4 v[140:143], v75, s[6:7] sc0
	v_mfma_f32_4x4x4_16b_bf16 v[232:235], v[222:223], v[100:101], v[232:235]
	v_cvt_scalef32_pk_bf16_fp8 v210, v144, 1.0
	v_cvt_scalef32_pk_bf16_fp8 v211, v144, 1.0 op_sel:[1,0,0]
	v_mfma_f32_4x4x4_16b_bf16 v[232:235], v[224:225], v[102:103], v[232:235]
	v_cvt_scalef32_pk_bf16_fp8 v212, v145, 1.0
	v_cvt_scalef32_pk_bf16_fp8 v213, v145, 1.0 op_sel:[1,0,0]
	v_cndmask_b32_e64 v190, v228, v229, s[22:23]
	v_cndmask_b32_e64 v190, v190, v230, s[24:25]
	v_cndmask_b32_e64 v190, v190, v231, s[26:27]
	v_mfma_f32_4x4x4_16b_bf16 v[228:231], v[210:211], v[108:109], 0
	v_cvt_scalef32_pk_bf16_fp8 v214, v146, 1.0
	v_cvt_scalef32_pk_bf16_fp8 v215, v146, 1.0 op_sel:[1,0,0]
	v_mfma_f32_4x4x4_16b_bf16 v[228:231], v[212:213], v[110:111], v[228:231]
	v_cvt_scalef32_pk_bf16_fp8 v216, v147, 1.0
	v_cvt_scalef32_pk_bf16_fp8 v217, v147, 1.0 op_sel:[1,0,0]
	v_lshl_or_b32 v68, v68, 7, v209
	global_load_dwordx4 v[144:147], v68, s[6:7] sc0
	v_mfma_f32_4x4x4_16b_bf16 v[228:231], v[214:215], v[100:101], v[228:231]
	v_cvt_scalef32_pk_bf16_fp8 v218, v148, 1.0
	v_cvt_scalef32_pk_bf16_fp8 v219, v148, 1.0 op_sel:[1,0,0]
	v_mfma_f32_4x4x4_16b_bf16 v[228:231], v[216:217], v[102:103], v[228:231]
	v_cvt_scalef32_pk_bf16_fp8 v220, v149, 1.0
	v_cvt_scalef32_pk_bf16_fp8 v221, v149, 1.0 op_sel:[1,0,0]
	v_cndmask_b32_e64 v191, v232, v233, s[22:23]
	v_cndmask_b32_e64 v191, v191, v234, s[24:25]
	v_cndmask_b32_e64 v191, v191, v235, s[26:27]
	v_mfma_f32_4x4x4_16b_bf16 v[232:235], v[218:219], v[108:109], 0
	v_cvt_scalef32_pk_bf16_fp8 v222, v150, 1.0
	v_cvt_scalef32_pk_bf16_fp8 v223, v150, 1.0 op_sel:[1,0,0]
	v_mfma_f32_4x4x4_16b_bf16 v[232:235], v[220:221], v[110:111], v[232:235]
	v_cvt_scalef32_pk_bf16_fp8 v224, v151, 1.0
	v_cvt_scalef32_pk_bf16_fp8 v225, v151, 1.0 op_sel:[1,0,0]
	v_lshl_or_b32 v69, v69, 7, v209
	global_load_dwordx4 v[148:151], v69, s[6:7] sc0
	v_mfma_f32_4x4x4_16b_bf16 v[232:235], v[222:223], v[100:101], v[232:235]
	v_cvt_scalef32_pk_bf16_fp8 v210, v152, 1.0
	v_cvt_scalef32_pk_bf16_fp8 v211, v152, 1.0 op_sel:[1,0,0]
	v_mfma_f32_4x4x4_16b_bf16 v[232:235], v[224:225], v[102:103], v[232:235]
	v_cvt_scalef32_pk_bf16_fp8 v212, v153, 1.0
	v_cvt_scalef32_pk_bf16_fp8 v213, v153, 1.0 op_sel:[1,0,0]
	v_cndmask_b32_e64 v192, v228, v229, s[22:23]
	v_cndmask_b32_e64 v192, v192, v230, s[24:25]
	v_cndmask_b32_e64 v192, v192, v231, s[26:27]
	v_mfma_f32_4x4x4_16b_bf16 v[228:231], v[210:211], v[108:109], 0
	v_cvt_scalef32_pk_bf16_fp8 v214, v154, 1.0
	v_cvt_scalef32_pk_bf16_fp8 v215, v154, 1.0 op_sel:[1,0,0]
	v_mfma_f32_4x4x4_16b_bf16 v[228:231], v[212:213], v[110:111], v[228:231]
	v_cvt_scalef32_pk_bf16_fp8 v216, v155, 1.0
	v_cvt_scalef32_pk_bf16_fp8 v217, v155, 1.0 op_sel:[1,0,0]
	v_lshl_or_b32 v70, v70, 7, v209
	global_load_dwordx4 v[152:155], v70, s[6:7] sc0
	v_mfma_f32_4x4x4_16b_bf16 v[228:231], v[214:215], v[100:101], v[228:231]
	v_cvt_scalef32_pk_bf16_fp8 v218, v156, 1.0
	v_cvt_scalef32_pk_bf16_fp8 v219, v156, 1.0 op_sel:[1,0,0]
	v_mfma_f32_4x4x4_16b_bf16 v[228:231], v[216:217], v[102:103], v[228:231]
	v_cvt_scalef32_pk_bf16_fp8 v220, v157, 1.0
	v_cvt_scalef32_pk_bf16_fp8 v221, v157, 1.0 op_sel:[1,0,0]
	v_cndmask_b32_e64 v193, v232, v233, s[22:23]
	v_cndmask_b32_e64 v193, v193, v234, s[24:25]
	v_cndmask_b32_e64 v193, v193, v235, s[26:27]
	v_mfma_f32_4x4x4_16b_bf16 v[232:235], v[218:219], v[108:109], 0
	v_cvt_scalef32_pk_bf16_fp8 v222, v158, 1.0
	v_cvt_scalef32_pk_bf16_fp8 v223, v158, 1.0 op_sel:[1,0,0]
	v_mfma_f32_4x4x4_16b_bf16 v[232:235], v[220:221], v[110:111], v[232:235]
	v_cvt_scalef32_pk_bf16_fp8 v224, v159, 1.0
	v_cvt_scalef32_pk_bf16_fp8 v225, v159, 1.0 op_sel:[1,0,0]
	v_lshl_or_b32 v71, v71, 7, v209
	global_load_dwordx4 v[156:159], v71, s[6:7] sc0
	v_mfma_f32_4x4x4_16b_bf16 v[232:235], v[222:223], v[100:101], v[232:235]
	v_cvt_scalef32_pk_bf16_fp8 v210, v160, 1.0
	v_cvt_scalef32_pk_bf16_fp8 v211, v160, 1.0 op_sel:[1,0,0]
	v_mfma_f32_4x4x4_16b_bf16 v[232:235], v[224:225], v[102:103], v[232:235]
	v_cvt_scalef32_pk_bf16_fp8 v212, v161, 1.0
	v_cvt_scalef32_pk_bf16_fp8 v213, v161, 1.0 op_sel:[1,0,0]
	v_cndmask_b32_e64 v194, v228, v229, s[22:23]
	v_cndmask_b32_e64 v194, v194, v230, s[24:25]
	v_cndmask_b32_e64 v194, v194, v231, s[26:27]
	v_mfma_f32_4x4x4_16b_bf16 v[228:231], v[210:211], v[108:109], 0
	v_cvt_scalef32_pk_bf16_fp8 v214, v162, 1.0
	v_cvt_scalef32_pk_bf16_fp8 v215, v162, 1.0 op_sel:[1,0,0]
	v_mfma_f32_4x4x4_16b_bf16 v[228:231], v[212:213], v[110:111], v[228:231]
	v_cvt_scalef32_pk_bf16_fp8 v216, v163, 1.0
	v_cvt_scalef32_pk_bf16_fp8 v217, v163, 1.0 op_sel:[1,0,0]
	v_lshl_or_b32 v64, v64, 7, v209
	global_load_dwordx4 v[160:163], v64, s[6:7] sc0
	v_mfma_f32_4x4x4_16b_bf16 v[228:231], v[214:215], v[100:101], v[228:231]
	v_cvt_scalef32_pk_bf16_fp8 v218, v164, 1.0
	v_cvt_scalef32_pk_bf16_fp8 v219, v164, 1.0 op_sel:[1,0,0]
	v_mfma_f32_4x4x4_16b_bf16 v[228:231], v[216:217], v[102:103], v[228:231]
	v_cvt_scalef32_pk_bf16_fp8 v220, v165, 1.0
	v_cvt_scalef32_pk_bf16_fp8 v221, v165, 1.0 op_sel:[1,0,0]
	v_cndmask_b32_e64 v195, v232, v233, s[22:23]
	v_cndmask_b32_e64 v195, v195, v234, s[24:25]
	v_cndmask_b32_e64 v195, v195, v235, s[26:27]
	v_mfma_f32_4x4x4_16b_bf16 v[232:235], v[218:219], v[108:109], 0
	v_cvt_scalef32_pk_bf16_fp8 v222, v166, 1.0
	v_cvt_scalef32_pk_bf16_fp8 v223, v166, 1.0 op_sel:[1,0,0]
	v_mfma_f32_4x4x4_16b_bf16 v[232:235], v[220:221], v[110:111], v[232:235]
	v_cvt_scalef32_pk_bf16_fp8 v224, v167, 1.0
	v_cvt_scalef32_pk_bf16_fp8 v225, v167, 1.0 op_sel:[1,0,0]
	v_lshl_or_b32 v65, v65, 7, v209
	global_load_dwordx4 v[164:167], v65, s[6:7] sc0
	v_mfma_f32_4x4x4_16b_bf16 v[232:235], v[222:223], v[100:101], v[232:235]
	v_cvt_scalef32_pk_bf16_fp8 v210, v168, 1.0
	v_cvt_scalef32_pk_bf16_fp8 v211, v168, 1.0 op_sel:[1,0,0]
	v_mfma_f32_4x4x4_16b_bf16 v[232:235], v[224:225], v[102:103], v[232:235]
	v_cvt_scalef32_pk_bf16_fp8 v212, v169, 1.0
	v_cvt_scalef32_pk_bf16_fp8 v213, v169, 1.0 op_sel:[1,0,0]
	v_cndmask_b32_e64 v196, v228, v229, s[22:23]
	v_cndmask_b32_e64 v196, v196, v230, s[24:25]
	v_cndmask_b32_e64 v196, v196, v231, s[26:27]
	v_mfma_f32_4x4x4_16b_bf16 v[228:231], v[210:211], v[108:109], 0
	v_cvt_scalef32_pk_bf16_fp8 v214, v170, 1.0
	v_cvt_scalef32_pk_bf16_fp8 v215, v170, 1.0 op_sel:[1,0,0]
	v_mfma_f32_4x4x4_16b_bf16 v[228:231], v[212:213], v[110:111], v[228:231]
	v_cvt_scalef32_pk_bf16_fp8 v216, v171, 1.0
	v_cvt_scalef32_pk_bf16_fp8 v217, v171, 1.0 op_sel:[1,0,0]
	v_lshl_or_b32 v66, v66, 7, v209
	global_load_dwordx4 v[168:171], v66, s[6:7] sc0
	v_mfma_f32_4x4x4_16b_bf16 v[228:231], v[214:215], v[100:101], v[228:231]
	v_cvt_scalef32_pk_bf16_fp8 v218, v172, 1.0
	v_cvt_scalef32_pk_bf16_fp8 v219, v172, 1.0 op_sel:[1,0,0]
	v_mfma_f32_4x4x4_16b_bf16 v[228:231], v[216:217], v[102:103], v[228:231]
	v_cvt_scalef32_pk_bf16_fp8 v220, v173, 1.0
	v_cvt_scalef32_pk_bf16_fp8 v221, v173, 1.0 op_sel:[1,0,0]
	v_cndmask_b32_e64 v197, v232, v233, s[22:23]
	v_cndmask_b32_e64 v197, v197, v234, s[24:25]
	v_cndmask_b32_e64 v197, v197, v235, s[26:27]
	v_mfma_f32_4x4x4_16b_bf16 v[232:235], v[218:219], v[108:109], 0
	v_cvt_scalef32_pk_bf16_fp8 v222, v174, 1.0
	v_cvt_scalef32_pk_bf16_fp8 v223, v174, 1.0 op_sel:[1,0,0]
	v_mfma_f32_4x4x4_16b_bf16 v[232:235], v[220:221], v[110:111], v[232:235]
	v_cvt_scalef32_pk_bf16_fp8 v224, v175, 1.0
	v_cvt_scalef32_pk_bf16_fp8 v225, v175, 1.0 op_sel:[1,0,0]
	v_lshl_or_b32 v67, v67, 7, v209
	global_load_dwordx4 v[172:175], v67, s[6:7] sc0
	v_mfma_f32_4x4x4_16b_bf16 v[232:235], v[222:223], v[100:101], v[232:235]
	s_nop 1
	v_mfma_f32_4x4x4_16b_bf16 v[232:235], v[224:225], v[102:103], v[232:235]
	v_cndmask_b32_e64 v198, v228, v229, s[22:23]
	v_cndmask_b32_e64 v198, v198, v230, s[24:25]
	v_cndmask_b32_e64 v198, v198, v231, s[26:27]
	s_nop 4
	v_cndmask_b32_e64 v199, v232, v233, s[22:23]
	v_cndmask_b32_e64 v199, v199, v234, s[24:25]
	v_cndmask_b32_e64 v199, v199, v235, s[26:27]
	v_cndmask_b32_e64 v200, v184, v192, s[4:5]
	v_cndmask_b32_e64 v201, v192, v184, s[4:5]
	v_cndmask_b32_e64 v202, v185, v193, s[4:5]
	v_cndmask_b32_e64 v203, v193, v185, s[4:5]
	v_cndmask_b32_e64 v204, v186, v194, s[4:5]
	v_cndmask_b32_e64 v205, v194, v186, s[4:5]
	v_cndmask_b32_e64 v236, v187, v195, s[4:5]
	v_cndmask_b32_e64 v237, v195, v187, s[4:5]
	v_cndmask_b32_e64 v238, v188, v196, s[4:5]
	v_cndmask_b32_e64 v239, v196, v188, s[4:5]
	v_cndmask_b32_e64 v240, v189, v197, s[4:5]
	v_cndmask_b32_e64 v241, v197, v189, s[4:5]
	v_cndmask_b32_e64 v242, v190, v198, s[4:5]
	v_cndmask_b32_e64 v243, v198, v190, s[4:5]
	v_cndmask_b32_e64 v244, v191, v199, s[4:5]
	v_cndmask_b32_e64 v245, v199, v191, s[4:5]
	v_add_f32_dpp v246, v200, v201 row_half_mirror row_mask:0xf bank_mask:0xf
	v_add_f32_dpp v247, v202, v203 row_half_mirror row_mask:0xf bank_mask:0xf
	v_add_f32_dpp v248, v204, v205 row_half_mirror row_mask:0xf bank_mask:0xf
	v_add_f32_dpp v249, v236, v237 row_half_mirror row_mask:0xf bank_mask:0xf
	v_add_f32_dpp v226, v238, v239 row_half_mirror row_mask:0xf bank_mask:0xf
	v_add_f32_dpp v227, v240, v241 row_half_mirror row_mask:0xf bank_mask:0xf
	v_add_f32_dpp v210, v242, v243 row_half_mirror row_mask:0xf bank_mask:0xf
	v_add_f32_dpp v211, v244, v245 row_half_mirror row_mask:0xf bank_mask:0xf
	v_cndmask_b32_e64 v200, v246, v226, s[2:3]
	v_cndmask_b32_e64 v201, v226, v246, s[2:3]
	v_cndmask_b32_e64 v202, v247, v227, s[2:3]
	v_cndmask_b32_e64 v203, v227, v247, s[2:3]
	v_cndmask_b32_e64 v204, v248, v210, s[2:3]
	v_cndmask_b32_e64 v205, v210, v248, s[2:3]
	v_cndmask_b32_e64 v236, v249, v211, s[2:3]
	v_cndmask_b32_e64 v237, v211, v249, s[2:3]
	v_add_f32_dpp v212, v200, v201 quad_perm:[2,3,0,1] row_mask:0xf bank_mask:0xf
	v_add_f32_dpp v213, v202, v203 quad_perm:[2,3,0,1] row_mask:0xf bank_mask:0xf
	v_add_f32_dpp v214, v204, v205 quad_perm:[2,3,0,1] row_mask:0xf bank_mask:0xf
	v_add_f32_dpp v215, v236, v237 quad_perm:[2,3,0,1] row_mask:0xf bank_mask:0xf
	v_cndmask_b32_e64 v200, v212, v214, s[0:1]
	v_cndmask_b32_e64 v201, v214, v212, s[0:1]
	v_cndmask_b32_e64 v202, v213, v215, s[0:1]
	v_cndmask_b32_e64 v203, v215, v213, s[0:1]
	s_nop 1
	v_add_f32_dpp v216, v200, v201 quad_perm:[1,0,3,2] row_mask:0xf bank_mask:0xf
	v_add_f32_dpp v217, v202, v203 quad_perm:[1,0,3,2] row_mask:0xf bank_mask:0xf
	s_ashr_i32 s11, s10, 31
	s_lshl_b64 s[10:11], s[10:11], 8
	v_cvt_pk_bf16_f32 v186, v216, v217
	v_lshl_add_u64 v[184:185], v[178:179], 0, s[10:11]
	global_store_dword v[184:185], v186, off
	s_add_u32 s20, s12, 0x300
	s_lshl_b32 s20, s20, 11
	v_lshl_add_u64 v[108:109], v[182:183], 0, s[20:21]
	global_load_dwordx4 v[100:103], v[108:109], off offset:16
	s_nop 0
	global_load_dwordx4 v[108:111], v[108:109], off
	s_add_u32 s20, s12, 0x500
	s_lshl_b32 s20, s20, 9
	v_lshl_add_u64 v[80:81], v[180:181], 0, s[20:21]
	global_load_dwordx4 v[64:67], v[80:81], off offset:48
	global_load_dwordx4 v[68:71], v[80:81], off offset:32
	global_load_dwordx4 v[72:75], v[80:81], off offset:16
	s_nop 0
	global_load_dwordx4 v[80:83], v[80:81], off
	s_add_u32 s12, s12, 0x200
	s_sub_u32 s13, s13, 1
	s_cmp_lg_u32 s13, 0
	s_cbranch_scc1 .Lpd2_loop
	s_mov_b32 s14, s12
	s_waitcnt vmcnt(23)
	v_cvt_scalef32_pk_bf16_fp8 v210, v24, 1.0
	v_cvt_scalef32_pk_bf16_fp8 v211, v24, 1.0 op_sel:[1,0,0]
	v_cvt_scalef32_pk_bf16_fp8 v212, v25, 1.0
	v_cvt_scalef32_pk_bf16_fp8 v213, v25, 1.0 op_sel:[1,0,0]
	v_mfma_f32_4x4x4_16b_bf16 v[228:231], v[210:211], v[20:21], 0
	v_cvt_scalef32_pk_bf16_fp8 v214, v26, 1.0
	v_cvt_scalef32_pk_bf16_fp8 v215, v26, 1.0 op_sel:[1,0,0]
	v_mfma_f32_4x4x4_16b_bf16 v[228:231], v[212:213], v[22:23], v[228:231]
	v_cvt_scalef32_pk_bf16_fp8 v216, v27, 1.0
	v_cvt_scalef32_pk_bf16_fp8 v217, v27, 1.0 op_sel:[1,0,0]
	v_lshl_or_b32 v0, v0, 7, v209
	global_load_dwordx4 v[24:27], v0, s[6:7] sc0
	v_mfma_f32_4x4x4_16b_bf16 v[228:231], v[214:215], v[16:17], v[228:231]
	v_cvt_scalef32_pk_bf16_fp8 v218, v28, 1.0
	v_cvt_scalef32_pk_bf16_fp8 v219, v28, 1.0 op_sel:[1,0,0]
	v_mfma_f32_4x4x4_16b_bf16 v[228:231], v[216:217], v[18:19], v[228:231]
	v_cvt_scalef32_pk_bf16_fp8 v220, v29, 1.0
	v_cvt_scalef32_pk_bf16_fp8 v221, v29, 1.0 op_sel:[1,0,0]
	v_mfma_f32_4x4x4_16b_bf16 v[232:235], v[218:219], v[20:21], 0
	v_cvt_scalef32_pk_bf16_fp8 v222, v30, 1.0
	v_cvt_scalef32_pk_bf16_fp8 v223, v30, 1.0 op_sel:[1,0,0]
	v_mfma_f32_4x4x4_16b_bf16 v[232:235], v[220:221], v[22:23], v[232:235]
	v_cvt_scalef32_pk_bf16_fp8 v224, v31, 1.0
	v_cvt_scalef32_pk_bf16_fp8 v225, v31, 1.0 op_sel:[1,0,0]
	v_lshl_or_b32 v1, v1, 7, v209
	global_load_dwordx4 v[28:31], v1, s[6:7] sc0
	v_mfma_f32_4x4x4_16b_bf16 v[232:235], v[222:223], v[16:17], v[232:235]
	v_cvt_scalef32_pk_bf16_fp8 v210, v32, 1.0
	v_cvt_scalef32_pk_bf16_fp8 v211, v32, 1.0 op_sel:[1,0,0]
	v_mfma_f32_4x4x4_16b_bf16 v[232:235], v[224:225], v[18:19], v[232:235]
	v_cvt_scalef32_pk_bf16_fp8 v212, v33, 1.0
	v_cvt_scalef32_pk_bf16_fp8 v213, v33, 1.0 op_sel:[1,0,0]
	v_cndmask_b32_e64 v184, v228, v229, s[22:23]
	v_cndmask_b32_e64 v184, v184, v230, s[24:25]
	v_cndmask_b32_e64 v184, v184, v231, s[26:27]
	v_mfma_f32_4x4x4_16b_bf16 v[228:231], v[210:211], v[20:21], 0
	v_cvt_scalef32_pk_bf16_fp8 v214, v34, 1.0
	v_cvt_scalef32_pk_bf16_fp8 v215, v34, 1.0 op_sel:[1,0,0]
	v_mfma_f32_4x4x4_16b_bf16 v[228:231], v[212:213], v[22:23], v[228:231]
	v_cvt_scalef32_pk_bf16_fp8 v216, v35, 1.0
	v_cvt_scalef32_pk_bf16_fp8 v217, v35, 1.0 op_sel:[1,0,0]
	v_lshl_or_b32 v2, v2, 7, v209
	global_load_dwordx4 v[32:35], v2, s[6:7] sc0
	v_mfma_f32_4x4x4_16b_bf16 v[228:231], v[214:215], v[16:17], v[228:231]
	v_cvt_scalef32_pk_bf16_fp8 v218, v36, 1.0
	v_cvt_scalef32_pk_bf16_fp8 v219, v36, 1.0 op_sel:[1,0,0]
	v_mfma_f32_4x4x4_16b_bf16 v[228:231], v[216:217], v[18:19], v[228:231]
	v_cvt_scalef32_pk_bf16_fp8 v220, v37, 1.0
	v_cvt_scalef32_pk_bf16_fp8 v221, v37, 1.0 op_sel:[1,0,0]
	v_cndmask_b32_e64 v185, v232, v233, s[22:23]
	v_cndmask_b32_e64 v185, v185, v234, s[24:25]
	v_cndmask_b32_e64 v185, v185, v235, s[26:27]
	v_mfma_f32_4x4x4_16b_bf16 v[232:235], v[218:219], v[20:21], 0
	v_cvt_scalef32_pk_bf16_fp8 v222, v38, 1.0
	v_cvt_scalef32_pk_bf16_fp8 v223, v38, 1.0 op_sel:[1,0,0]
	v_mfma_f32_4x4x4_16b_bf16 v[232:235], v[220:221], v[22:23], v[232:235]
	v_cvt_scalef32_pk_bf16_fp8 v224, v39, 1.0
	v_cvt_scalef32_pk_bf16_fp8 v225, v39, 1.0 op_sel:[1,0,0]
	v_lshl_or_b32 v3, v3, 7, v209
	global_load_dwordx4 v[36:39], v3, s[6:7] sc0
	v_mfma_f32_4x4x4_16b_bf16 v[232:235], v[222:223], v[16:17], v[232:235]
	v_cvt_scalef32_pk_bf16_fp8 v210, v40, 1.0
	v_cvt_scalef32_pk_bf16_fp8 v211, v40, 1.0 op_sel:[1,0,0]
	v_mfma_f32_4x4x4_16b_bf16 v[232:235], v[224:225], v[18:19], v[232:235]
	v_cvt_scalef32_pk_bf16_fp8 v212, v41, 1.0
	v_cvt_scalef32_pk_bf16_fp8 v213, v41, 1.0 op_sel:[1,0,0]
	v_cndmask_b32_e64 v186, v228, v229, s[22:23]
	v_cndmask_b32_e64 v186, v186, v230, s[24:25]
	v_cndmask_b32_e64 v186, v186, v231, s[26:27]
	v_mfma_f32_4x4x4_16b_bf16 v[228:231], v[210:211], v[20:21], 0
	v_cvt_scalef32_pk_bf16_fp8 v214, v42, 1.0
	v_cvt_scalef32_pk_bf16_fp8 v215, v42, 1.0 op_sel:[1,0,0]
	v_mfma_f32_4x4x4_16b_bf16 v[228:231], v[212:213], v[22:23], v[228:231]
	v_cvt_scalef32_pk_bf16_fp8 v216, v43, 1.0
	v_cvt_scalef32_pk_bf16_fp8 v217, v43, 1.0 op_sel:[1,0,0]
	v_lshl_or_b32 v4, v4, 7, v209
	global_load_dwordx4 v[40:43], v4, s[6:7] sc0
	v_mfma_f32_4x4x4_16b_bf16 v[228:231], v[214:215], v[16:17], v[228:231]
	v_cvt_scalef32_pk_bf16_fp8 v218, v44, 1.0
	v_cvt_scalef32_pk_bf16_fp8 v219, v44, 1.0 op_sel:[1,0,0]
	v_mfma_f32_4x4x4_16b_bf16 v[228:231], v[216:217], v[18:19], v[228:231]
	v_cvt_scalef32_pk_bf16_fp8 v220, v45, 1.0
	v_cvt_scalef32_pk_bf16_fp8 v221, v45, 1.0 op_sel:[1,0,0]
	v_cndmask_b32_e64 v187, v232, v233, s[22:23]
	v_cndmask_b32_e64 v187, v187, v234, s[24:25]
	v_cndmask_b32_e64 v187, v187, v235, s[26:27]
	v_mfma_f32_4x4x4_16b_bf16 v[232:235], v[218:219], v[20:21], 0
	v_cvt_scalef32_pk_bf16_fp8 v222, v46, 1.0
	v_cvt_scalef32_pk_bf16_fp8 v223, v46, 1.0 op_sel:[1,0,0]
	v_mfma_f32_4x4x4_16b_bf16 v[232:235], v[220:221], v[22:23], v[232:235]
	v_cvt_scalef32_pk_bf16_fp8 v224, v47, 1.0
	v_cvt_scalef32_pk_bf16_fp8 v225, v47, 1.0 op_sel:[1,0,0]
	v_lshl_or_b32 v5, v5, 7, v209
	global_load_dwordx4 v[44:47], v5, s[6:7] sc0
	v_mfma_f32_4x4x4_16b_bf16 v[232:235], v[222:223], v[16:17], v[232:235]
	v_cvt_scalef32_pk_bf16_fp8 v210, v48, 1.0
	v_cvt_scalef32_pk_bf16_fp8 v211, v48, 1.0 op_sel:[1,0,0]
	v_mfma_f32_4x4x4_16b_bf16 v[232:235], v[224:225], v[18:19], v[232:235]
	v_cvt_scalef32_pk_bf16_fp8 v212, v49, 1.0
	v_cvt_scalef32_pk_bf16_fp8 v213, v49, 1.0 op_sel:[1,0,0]
	v_cndmask_b32_e64 v188, v228, v229, s[22:23]
	v_cndmask_b32_e64 v188, v188, v230, s[24:25]
	v_cndmask_b32_e64 v188, v188, v231, s[26:27]
	v_mfma_f32_4x4x4_16b_bf16 v[228:231], v[210:211], v[20:21], 0
	v_cvt_scalef32_pk_bf16_fp8 v214, v50, 1.0
	v_cvt_scalef32_pk_bf16_fp8 v215, v50, 1.0 op_sel:[1,0,0]
	v_mfma_f32_4x4x4_16b_bf16 v[228:231], v[212:213], v[22:23], v[228:231]
	v_cvt_scalef32_pk_bf16_fp8 v216, v51, 1.0
	v_cvt_scalef32_pk_bf16_fp8 v217, v51, 1.0 op_sel:[1,0,0]
	v_lshl_or_b32 v6, v6, 7, v209
	global_load_dwordx4 v[48:51], v6, s[6:7] sc0
	v_mfma_f32_4x4x4_16b_bf16 v[228:231], v[214:215], v[16:17], v[228:231]
	v_cvt_scalef32_pk_bf16_fp8 v218, v52, 1.0
	v_cvt_scalef32_pk_bf16_fp8 v219, v52, 1.0 op_sel:[1,0,0]
	v_mfma_f32_4x4x4_16b_bf16 v[228:231], v[216:217], v[18:19], v[228:231]
	v_cvt_scalef32_pk_bf16_fp8 v220, v53, 1.0
	v_cvt_scalef32_pk_bf16_fp8 v221, v53, 1.0 op_sel:[1,0,0]
	v_cndmask_b32_e64 v189, v232, v233, s[22:23]
	v_cndmask_b32_e64 v189, v189, v234, s[24:25]
	v_cndmask_b32_e64 v189, v189, v235, s[26:27]
	v_mfma_f32_4x4x4_16b_bf16 v[232:235], v[218:219], v[20:21], 0
	v_cvt_scalef32_pk_bf16_fp8 v222, v54, 1.0
	v_cvt_scalef32_pk_bf16_fp8 v223, v54, 1.0 op_sel:[1,0,0]
	v_mfma_f32_4x4x4_16b_bf16 v[232:235], v[220:221], v[22:23], v[232:235]
	v_cvt_scalef32_pk_bf16_fp8 v224, v55, 1.0
	v_cvt_scalef32_pk_bf16_fp8 v225, v55, 1.0 op_sel:[1,0,0]
	v_lshl_or_b32 v7, v7, 7, v209
	global_load_dwordx4 v[52:55], v7, s[6:7] sc0
	v_mfma_f32_4x4x4_16b_bf16 v[232:235], v[222:223], v[16:17], v[232:235]
	v_cvt_scalef32_pk_bf16_fp8 v210, v56, 1.0
	v_cvt_scalef32_pk_bf16_fp8 v211, v56, 1.0 op_sel:[1,0,0]
	v_mfma_f32_4x4x4_16b_bf16 v[232:235], v[224:225], v[18:19], v[232:235]
	v_cvt_scalef32_pk_bf16_fp8 v212, v57, 1.0
	v_cvt_scalef32_pk_bf16_fp8 v213, v57, 1.0 op_sel:[1,0,0]
	v_cndmask_b32_e64 v190, v228, v229, s[22:23]
	v_cndmask_b32_e64 v190, v190, v230, s[24:25]
	v_cndmask_b32_e64 v190, v190, v231, s[26:27]
	v_mfma_f32_4x4x4_16b_bf16 v[228:231], v[210:211], v[20:21], 0
	v_cvt_scalef32_pk_bf16_fp8 v214, v58, 1.0
	v_cvt_scalef32_pk_bf16_fp8 v215, v58, 1.0 op_sel:[1,0,0]
	v_mfma_f32_4x4x4_16b_bf16 v[228:231], v[212:213], v[22:23], v[228:231]
	v_cvt_scalef32_pk_bf16_fp8 v216, v59, 1.0
	v_cvt_scalef32_pk_bf16_fp8 v217, v59, 1.0 op_sel:[1,0,0]
	v_lshl_or_b32 v8, v8, 7, v209
	global_load_dwordx4 v[56:59], v8, s[6:7] sc0
	v_mfma_f32_4x4x4_16b_bf16 v[228:231], v[214:215], v[16:17], v[228:231]
	v_cvt_scalef32_pk_bf16_fp8 v218, v60, 1.0
	v_cvt_scalef32_pk_bf16_fp8 v219, v60, 1.0 op_sel:[1,0,0]
	v_mfma_f32_4x4x4_16b_bf16 v[228:231], v[216:217], v[18:19], v[228:231]
	v_cvt_scalef32_pk_bf16_fp8 v220, v61, 1.0
	v_cvt_scalef32_pk_bf16_fp8 v221, v61, 1.0 op_sel:[1,0,0]
	v_cndmask_b32_e64 v191, v232, v233, s[22:23]
	v_cndmask_b32_e64 v191, v191, v234, s[24:25]
	v_cndmask_b32_e64 v191, v191, v235, s[26:27]
	v_mfma_f32_4x4x4_16b_bf16 v[232:235], v[218:219], v[20:21], 0
	v_cvt_scalef32_pk_bf16_fp8 v222, v62, 1.0
	v_cvt_scalef32_pk_bf16_fp8 v223, v62, 1.0 op_sel:[1,0,0]
	v_mfma_f32_4x4x4_16b_bf16 v[232:235], v[220:221], v[22:23], v[232:235]
	v_cvt_scalef32_pk_bf16_fp8 v224, v63, 1.0
	v_cvt_scalef32_pk_bf16_fp8 v225, v63, 1.0 op_sel:[1,0,0]
	v_lshl_or_b32 v9, v9, 7, v209
	global_load_dwordx4 v[60:63], v9, s[6:7] sc0
	v_mfma_f32_4x4x4_16b_bf16 v[232:235], v[222:223], v[16:17], v[232:235]
	v_cvt_scalef32_pk_bf16_fp8 v210, v76, 1.0
	v_cvt_scalef32_pk_bf16_fp8 v211, v76, 1.0 op_sel:[1,0,0]
	v_mfma_f32_4x4x4_16b_bf16 v[232:235], v[224:225], v[18:19], v[232:235]
	v_cvt_scalef32_pk_bf16_fp8 v212, v77, 1.0
	v_cvt_scalef32_pk_bf16_fp8 v213, v77, 1.0 op_sel:[1,0,0]
	v_cndmask_b32_e64 v192, v228, v229, s[22:23]
	v_cndmask_b32_e64 v192, v192, v230, s[24:25]
	v_cndmask_b32_e64 v192, v192, v231, s[26:27]
	v_mfma_f32_4x4x4_16b_bf16 v[228:231], v[210:211], v[20:21], 0
	v_cvt_scalef32_pk_bf16_fp8 v214, v78, 1.0
	v_cvt_scalef32_pk_bf16_fp8 v215, v78, 1.0 op_sel:[1,0,0]
	v_mfma_f32_4x4x4_16b_bf16 v[228:231], v[212:213], v[22:23], v[228:231]
	v_cvt_scalef32_pk_bf16_fp8 v216, v79, 1.0
	v_cvt_scalef32_pk_bf16_fp8 v217, v79, 1.0 op_sel:[1,0,0]
	v_lshl_or_b32 v10, v10, 7, v209
	global_load_dwordx4 v[76:79], v10, s[6:7] sc0
	v_mfma_f32_4x4x4_16b_bf16 v[228:231], v[214:215], v[16:17], v[228:231]
	v_cvt_scalef32_pk_bf16_fp8 v218, v84, 1.0
	v_cvt_scalef32_pk_bf16_fp8 v219, v84, 1.0 op_sel:[1,0,0]
	v_mfma_f32_4x4x4_16b_bf16 v[228:231], v[216:217], v[18:19], v[228:231]
	v_cvt_scalef32_pk_bf16_fp8 v220, v85, 1.0
	v_cvt_scalef32_pk_bf16_fp8 v221, v85, 1.0 op_sel:[1,0,0]
	v_cndmask_b32_e64 v193, v232, v233, s[22:23]
	v_cndmask_b32_e64 v193, v193, v234, s[24:25]
	v_cndmask_b32_e64 v193, v193, v235, s[26:27]
	v_mfma_f32_4x4x4_16b_bf16 v[232:235], v[218:219], v[20:21], 0
	v_cvt_scalef32_pk_bf16_fp8 v222, v86, 1.0
	v_cvt_scalef32_pk_bf16_fp8 v223, v86, 1.0 op_sel:[1,0,0]
	v_mfma_f32_4x4x4_16b_bf16 v[232:235], v[220:221], v[22:23], v[232:235]
	v_cvt_scalef32_pk_bf16_fp8 v224, v87, 1.0
	v_cvt_scalef32_pk_bf16_fp8 v225, v87, 1.0 op_sel:[1,0,0]
	v_lshl_or_b32 v11, v11, 7, v209
	global_load_dwordx4 v[84:87], v11, s[6:7] sc0
	v_mfma_f32_4x4x4_16b_bf16 v[232:235], v[222:223], v[16:17], v[232:235]
	v_cvt_scalef32_pk_bf16_fp8 v210, v88, 1.0
	v_cvt_scalef32_pk_bf16_fp8 v211, v88, 1.0 op_sel:[1,0,0]
	v_mfma_f32_4x4x4_16b_bf16 v[232:235], v[224:225], v[18:19], v[232:235]
	v_cvt_scalef32_pk_bf16_fp8 v212, v89, 1.0
	v_cvt_scalef32_pk_bf16_fp8 v213, v89, 1.0 op_sel:[1,0,0]
	v_cndmask_b32_e64 v194, v228, v229, s[22:23]
	v_cndmask_b32_e64 v194, v194, v230, s[24:25]
	v_cndmask_b32_e64 v194, v194, v231, s[26:27]
	v_mfma_f32_4x4x4_16b_bf16 v[228:231], v[210:211], v[20:21], 0
	v_cvt_scalef32_pk_bf16_fp8 v214, v90, 1.0
	v_cvt_scalef32_pk_bf16_fp8 v215, v90, 1.0 op_sel:[1,0,0]
	v_mfma_f32_4x4x4_16b_bf16 v[228:231], v[212:213], v[22:23], v[228:231]
	v_cvt_scalef32_pk_bf16_fp8 v216, v91, 1.0
	v_cvt_scalef32_pk_bf16_fp8 v217, v91, 1.0 op_sel:[1,0,0]
	v_lshl_or_b32 v12, v12, 7, v209
	global_load_dwordx4 v[88:91], v12, s[6:7] sc0
	v_mfma_f32_4x4x4_16b_bf16 v[228:231], v[214:215], v[16:17], v[228:231]
	v_cvt_scalef32_pk_bf16_fp8 v218, v92, 1.0
	v_cvt_scalef32_pk_bf16_fp8 v219, v92, 1.0 op_sel:[1,0,0]
	v_mfma_f32_4x4x4_16b_bf16 v[228:231], v[216:217], v[18:19], v[228:231]
	v_cvt_scalef32_pk_bf16_fp8 v220, v93, 1.0
	v_cvt_scalef32_pk_bf16_fp8 v221, v93, 1.0 op_sel:[1,0,0]
	v_cndmask_b32_e64 v195, v232, v233, s[22:23]
	v_cndmask_b32_e64 v195, v195, v234, s[24:25]
	v_cndmask_b32_e64 v195, v195, v235, s[26:27]
	v_mfma_f32_4x4x4_16b_bf16 v[232:235], v[218:219], v[20:21], 0
	v_cvt_scalef32_pk_bf16_fp8 v222, v94, 1.0
	v_cvt_scalef32_pk_bf16_fp8 v223, v94, 1.0 op_sel:[1,0,0]
	v_mfma_f32_4x4x4_16b_bf16 v[232:235], v[220:221], v[22:23], v[232:235]
	v_cvt_scalef32_pk_bf16_fp8 v224, v95, 1.0
	v_cvt_scalef32_pk_bf16_fp8 v225, v95, 1.0 op_sel:[1,0,0]
	v_lshl_or_b32 v13, v13, 7, v209
	global_load_dwordx4 v[92:95], v13, s[6:7] sc0
	v_mfma_f32_4x4x4_16b_bf16 v[232:235], v[222:223], v[16:17], v[232:235]
	v_cvt_scalef32_pk_bf16_fp8 v210, v96, 1.0
	v_cvt_scalef32_pk_bf16_fp8 v211, v96, 1.0 op_sel:[1,0,0]
	v_mfma_f32_4x4x4_16b_bf16 v[232:235], v[224:225], v[18:19], v[232:235]
	v_cvt_scalef32_pk_bf16_fp8 v212, v97, 1.0
	v_cvt_scalef32_pk_bf16_fp8 v213, v97, 1.0 op_sel:[1,0,0]
	v_cndmask_b32_e64 v196, v228, v229, s[22:23]
	v_cndmask_b32_e64 v196, v196, v230, s[24:25]
	v_cndmask_b32_e64 v196, v196, v231, s[26:27]
	v_mfma_f32_4x4x4_16b_bf16 v[228:231], v[210:211], v[20:21], 0
	v_cvt_scalef32_pk_bf16_fp8 v214, v98, 1.0
	v_cvt_scalef32_pk_bf16_fp8 v215, v98, 1.0 op_sel:[1,0,0]
	v_mfma_f32_4x4x4_16b_bf16 v[228:231], v[212:213], v[22:23], v[228:231]
	v_cvt_scalef32_pk_bf16_fp8 v216, v99, 1.0
	v_cvt_scalef32_pk_bf16_fp8 v217, v99, 1.0 op_sel:[1,0,0]
	v_lshl_or_b32 v14, v14, 7, v209
	global_load_dwordx4 v[96:99], v14, s[6:7] sc0
	v_mfma_f32_4x4x4_16b_bf16 v[228:231], v[214:215], v[16:17], v[228:231]
	v_cvt_scalef32_pk_bf16_fp8 v218, v104, 1.0
	v_cvt_scalef32_pk_bf16_fp8 v219, v104, 1.0 op_sel:[1,0,0]
	v_mfma_f32_4x4x4_16b_bf16 v[228:231], v[216:217], v[18:19], v[228:231]
	v_cvt_scalef32_pk_bf16_fp8 v220, v105, 1.0
	v_cvt_scalef32_pk_bf16_fp8 v221, v105, 1.0 op_sel:[1,0,0]
	v_cndmask_b32_e64 v197, v232, v233, s[22:23]
	v_cndmask_b32_e64 v197, v197, v234, s[24:25]
	v_cndmask_b32_e64 v197, v197, v235, s[26:27]
	v_mfma_f32_4x4x4_16b_bf16 v[232:235], v[218:219], v[20:21], 0
	v_cvt_scalef32_pk_bf16_fp8 v222, v106, 1.0
	v_cvt_scalef32_pk_bf16_fp8 v223, v106, 1.0 op_sel:[1,0,0]
	v_mfma_f32_4x4x4_16b_bf16 v[232:235], v[220:221], v[22:23], v[232:235]
	v_cvt_scalef32_pk_bf16_fp8 v224, v107, 1.0
	v_cvt_scalef32_pk_bf16_fp8 v225, v107, 1.0 op_sel:[1,0,0]
	v_lshl_or_b32 v15, v15, 7, v209
	global_load_dwordx4 v[104:107], v15, s[6:7] sc0
	v_mfma_f32_4x4x4_16b_bf16 v[232:235], v[222:223], v[16:17], v[232:235]
	s_nop 1
	v_mfma_f32_4x4x4_16b_bf16 v[232:235], v[224:225], v[18:19], v[232:235]
	v_cndmask_b32_e64 v198, v228, v229, s[22:23]
	v_cndmask_b32_e64 v198, v198, v230, s[24:25]
	v_cndmask_b32_e64 v198, v198, v231, s[26:27]
	s_nop 4
	v_cndmask_b32_e64 v199, v232, v233, s[22:23]
	v_cndmask_b32_e64 v199, v199, v234, s[24:25]
	v_cndmask_b32_e64 v199, v199, v235, s[26:27]
	v_cndmask_b32_e64 v200, v184, v192, s[4:5]
	v_cndmask_b32_e64 v201, v192, v184, s[4:5]
	v_cndmask_b32_e64 v202, v185, v193, s[4:5]
	v_cndmask_b32_e64 v203, v193, v185, s[4:5]
	v_cndmask_b32_e64 v204, v186, v194, s[4:5]
	v_cndmask_b32_e64 v205, v194, v186, s[4:5]
	v_cndmask_b32_e64 v236, v187, v195, s[4:5]
	v_cndmask_b32_e64 v237, v195, v187, s[4:5]
	v_cndmask_b32_e64 v238, v188, v196, s[4:5]
	v_cndmask_b32_e64 v239, v196, v188, s[4:5]
	v_cndmask_b32_e64 v240, v189, v197, s[4:5]
	v_cndmask_b32_e64 v241, v197, v189, s[4:5]
	v_cndmask_b32_e64 v242, v190, v198, s[4:5]
	v_cndmask_b32_e64 v243, v198, v190, s[4:5]
	v_cndmask_b32_e64 v244, v191, v199, s[4:5]
	v_cndmask_b32_e64 v245, v199, v191, s[4:5]
	v_add_f32_dpp v246, v200, v201 row_half_mirror row_mask:0xf bank_mask:0xf
	v_add_f32_dpp v247, v202, v203 row_half_mirror row_mask:0xf bank_mask:0xf
	v_add_f32_dpp v248, v204, v205 row_half_mirror row_mask:0xf bank_mask:0xf
	v_add_f32_dpp v249, v236, v237 row_half_mirror row_mask:0xf bank_mask:0xf
	v_add_f32_dpp v226, v238, v239 row_half_mirror row_mask:0xf bank_mask:0xf
	v_add_f32_dpp v227, v240, v241 row_half_mirror row_mask:0xf bank_mask:0xf
	v_add_f32_dpp v210, v242, v243 row_half_mirror row_mask:0xf bank_mask:0xf
	v_add_f32_dpp v211, v244, v245 row_half_mirror row_mask:0xf bank_mask:0xf
	v_cndmask_b32_e64 v200, v246, v226, s[2:3]
	v_cndmask_b32_e64 v201, v226, v246, s[2:3]
	v_cndmask_b32_e64 v202, v247, v227, s[2:3]
	v_cndmask_b32_e64 v203, v227, v247, s[2:3]
	v_cndmask_b32_e64 v204, v248, v210, s[2:3]
	v_cndmask_b32_e64 v205, v210, v248, s[2:3]
	v_cndmask_b32_e64 v236, v249, v211, s[2:3]
	v_cndmask_b32_e64 v237, v211, v249, s[2:3]
	v_add_f32_dpp v212, v200, v201 quad_perm:[2,3,0,1] row_mask:0xf bank_mask:0xf
	v_add_f32_dpp v213, v202, v203 quad_perm:[2,3,0,1] row_mask:0xf bank_mask:0xf
	v_add_f32_dpp v214, v204, v205 quad_perm:[2,3,0,1] row_mask:0xf bank_mask:0xf
	v_add_f32_dpp v215, v236, v237 quad_perm:[2,3,0,1] row_mask:0xf bank_mask:0xf
	v_cndmask_b32_e64 v200, v212, v214, s[0:1]
	v_cndmask_b32_e64 v201, v214, v212, s[0:1]
	v_cndmask_b32_e64 v202, v213, v215, s[0:1]
	v_cndmask_b32_e64 v203, v215, v213, s[0:1]
	s_nop 1
	v_add_f32_dpp v216, v200, v201 quad_perm:[1,0,3,2] row_mask:0xf bank_mask:0xf
	v_add_f32_dpp v217, v202, v203 quad_perm:[1,0,3,2] row_mask:0xf bank_mask:0xf
	s_ashr_i32 s15, s14, 31
	s_lshl_b64 s[14:15], s[14:15], 8
	v_cvt_pk_bf16_f32 v186, v216, v217
	v_lshl_add_u64 v[184:185], v[178:179], 0, s[14:15]
	global_store_dword v[184:185], v186, off
	s_add_u32 s20, s12, 0x200
	s_lshl_b32 s20, s20, 11
	v_lshl_add_u64 v[20:21], v[182:183], 0, s[20:21]
	global_load_dwordx4 v[16:19], v[20:21], off offset:16
	s_nop 0
	global_load_dwordx4 v[20:23], v[20:21], off
	s_add_u32 s10, s12, 0x100
	s_waitcnt vmcnt(19)
	v_cvt_scalef32_pk_bf16_fp8 v210, v112, 1.0
	v_cvt_scalef32_pk_bf16_fp8 v211, v112, 1.0 op_sel:[1,0,0]
	v_cvt_scalef32_pk_bf16_fp8 v212, v113, 1.0
	v_cvt_scalef32_pk_bf16_fp8 v213, v113, 1.0 op_sel:[1,0,0]
	v_mfma_f32_4x4x4_16b_bf16 v[228:231], v[210:211], v[108:109], 0
	v_cvt_scalef32_pk_bf16_fp8 v214, v114, 1.0
	v_cvt_scalef32_pk_bf16_fp8 v215, v114, 1.0 op_sel:[1,0,0]
	v_mfma_f32_4x4x4_16b_bf16 v[228:231], v[212:213], v[110:111], v[228:231]
	v_cvt_scalef32_pk_bf16_fp8 v216, v115, 1.0
	v_cvt_scalef32_pk_bf16_fp8 v217, v115, 1.0 op_sel:[1,0,0]
	v_lshl_or_b32 v80, v80, 7, v209
	global_load_dwordx4 v[112:115], v80, s[6:7] sc0
	v_mfma_f32_4x4x4_16b_bf16 v[228:231], v[214:215], v[100:101], v[228:231]
	v_cvt_scalef32_pk_bf16_fp8 v218, v116, 1.0
	v_cvt_scalef32_pk_bf16_fp8 v219, v116, 1.0 op_sel:[1,0,0]
	v_mfma_f32_4x4x4_16b_bf16 v[228:231], v[216:217], v[102:103], v[228:231]
	v_cvt_scalef32_pk_bf16_fp8 v220, v117, 1.0
	v_cvt_scalef32_pk_bf16_fp8 v221, v117, 1.0 op_sel:[1,0,0]
	v_mfma_f32_4x4x4_16b_bf16 v[232:235], v[218:219], v[108:109], 0
	v_cvt_scalef32_pk_bf16_fp8 v222, v118, 1.0
	v_cvt_scalef32_pk_bf16_fp8 v223, v118, 1.0 op_sel:[1,0,0]
	v_mfma_f32_4x4x4_16b_bf16 v[232:235], v[220:221], v[110:111], v[232:235]
	v_cvt_scalef32_pk_bf16_fp8 v224, v119, 1.0
	v_cvt_scalef32_pk_bf16_fp8 v225, v119, 1.0 op_sel:[1,0,0]
	v_lshl_or_b32 v81, v81, 7, v209
	global_load_dwordx4 v[116:119], v81, s[6:7] sc0
	v_mfma_f32_4x4x4_16b_bf16 v[232:235], v[222:223], v[100:101], v[232:235]
	v_cvt_scalef32_pk_bf16_fp8 v210, v120, 1.0
	v_cvt_scalef32_pk_bf16_fp8 v211, v120, 1.0 op_sel:[1,0,0]
	v_mfma_f32_4x4x4_16b_bf16 v[232:235], v[224:225], v[102:103], v[232:235]
	v_cvt_scalef32_pk_bf16_fp8 v212, v121, 1.0
	v_cvt_scalef32_pk_bf16_fp8 v213, v121, 1.0 op_sel:[1,0,0]
	v_cndmask_b32_e64 v184, v228, v229, s[22:23]
	v_cndmask_b32_e64 v184, v184, v230, s[24:25]
	v_cndmask_b32_e64 v184, v184, v231, s[26:27]
	v_mfma_f32_4x4x4_16b_bf16 v[228:231], v[210:211], v[108:109], 0
	v_cvt_scalef32_pk_bf16_fp8 v214, v122, 1.0
	v_cvt_scalef32_pk_bf16_fp8 v215, v122, 1.0 op_sel:[1,0,0]
	v_mfma_f32_4x4x4_16b_bf16 v[228:231], v[212:213], v[110:111], v[228:231]
	v_cvt_scalef32_pk_bf16_fp8 v216, v123, 1.0
	v_cvt_scalef32_pk_bf16_fp8 v217, v123, 1.0 op_sel:[1,0,0]
	v_lshl_or_b32 v82, v82, 7, v209
	global_load_dwordx4 v[120:123], v82, s[6:7] sc0
	v_mfma_f32_4x4x4_16b_bf16 v[228:231], v[214:215], v[100:101], v[228:231]
	v_cvt_scalef32_pk_bf16_fp8 v218, v124, 1.0
	v_cvt_scalef32_pk_bf16_fp8 v219, v124, 1.0 op_sel:[1,0,0]
	v_mfma_f32_4x4x4_16b_bf16 v[228:231], v[216:217], v[102:103], v[228:231]
	v_cvt_scalef32_pk_bf16_fp8 v220, v125, 1.0
	v_cvt_scalef32_pk_bf16_fp8 v221, v125, 1.0 op_sel:[1,0,0]
	v_cndmask_b32_e64 v185, v232, v233, s[22:23]
	v_cndmask_b32_e64 v185, v185, v234, s[24:25]
	v_cndmask_b32_e64 v185, v185, v235, s[26:27]
	v_mfma_f32_4x4x4_16b_bf16 v[232:235], v[218:219], v[108:109], 0
	v_cvt_scalef32_pk_bf16_fp8 v222, v126, 1.0
	v_cvt_scalef32_pk_bf16_fp8 v223, v126, 1.0 op_sel:[1,0,0]
	v_mfma_f32_4x4x4_16b_bf16 v[232:235], v[220:221], v[110:111], v[232:235]
	v_cvt_scalef32_pk_bf16_fp8 v224, v127, 1.0
	v_cvt_scalef32_pk_bf16_fp8 v225, v127, 1.0 op_sel:[1,0,0]
	v_lshl_or_b32 v83, v83, 7, v209
	global_load_dwordx4 v[124:127], v83, s[6:7] sc0
	v_mfma_f32_4x4x4_16b_bf16 v[232:235], v[222:223], v[100:101], v[232:235]
	v_cvt_scalef32_pk_bf16_fp8 v210, v128, 1.0
	v_cvt_scalef32_pk_bf16_fp8 v211, v128, 1.0 op_sel:[1,0,0]
	v_mfma_f32_4x4x4_16b_bf16 v[232:235], v[224:225], v[102:103], v[232:235]
	v_cvt_scalef32_pk_bf16_fp8 v212, v129, 1.0
	v_cvt_scalef32_pk_bf16_fp8 v213, v129, 1.0 op_sel:[1,0,0]
	v_cndmask_b32_e64 v186, v228, v229, s[22:23]
	v_cndmask_b32_e64 v186, v186, v230, s[24:25]
	v_cndmask_b32_e64 v186, v186, v231, s[26:27]
	v_mfma_f32_4x4x4_16b_bf16 v[228:231], v[210:211], v[108:109], 0
	v_cvt_scalef32_pk_bf16_fp8 v214, v130, 1.0
	v_cvt_scalef32_pk_bf16_fp8 v215, v130, 1.0 op_sel:[1,0,0]
	v_mfma_f32_4x4x4_16b_bf16 v[228:231], v[212:213], v[110:111], v[228:231]
	v_cvt_scalef32_pk_bf16_fp8 v216, v131, 1.0
	v_cvt_scalef32_pk_bf16_fp8 v217, v131, 1.0 op_sel:[1,0,0]
	v_lshl_or_b32 v72, v72, 7, v209
	global_load_dwordx4 v[128:131], v72, s[6:7] sc0
	v_mfma_f32_4x4x4_16b_bf16 v[228:231], v[214:215], v[100:101], v[228:231]
	v_cvt_scalef32_pk_bf16_fp8 v218, v132, 1.0
	v_cvt_scalef32_pk_bf16_fp8 v219, v132, 1.0 op_sel:[1,0,0]
	v_mfma_f32_4x4x4_16b_bf16 v[228:231], v[216:217], v[102:103], v[228:231]
	v_cvt_scalef32_pk_bf16_fp8 v220, v133, 1.0
	v_cvt_scalef32_pk_bf16_fp8 v221, v133, 1.0 op_sel:[1,0,0]
	v_cndmask_b32_e64 v187, v232, v233, s[22:23]
	v_cndmask_b32_e64 v187, v187, v234, s[24:25]
	v_cndmask_b32_e64 v187, v187, v235, s[26:27]
	v_mfma_f32_4x4x4_16b_bf16 v[232:235], v[218:219], v[108:109], 0
	v_cvt_scalef32_pk_bf16_fp8 v222, v134, 1.0
	v_cvt_scalef32_pk_bf16_fp8 v223, v134, 1.0 op_sel:[1,0,0]
	v_mfma_f32_4x4x4_16b_bf16 v[232:235], v[220:221], v[110:111], v[232:235]
	v_cvt_scalef32_pk_bf16_fp8 v224, v135, 1.0
	v_cvt_scalef32_pk_bf16_fp8 v225, v135, 1.0 op_sel:[1,0,0]
	v_lshl_or_b32 v73, v73, 7, v209
	global_load_dwordx4 v[132:135], v73, s[6:7] sc0
	v_mfma_f32_4x4x4_16b_bf16 v[232:235], v[222:223], v[100:101], v[232:235]
	v_cvt_scalef32_pk_bf16_fp8 v210, v136, 1.0
	v_cvt_scalef32_pk_bf16_fp8 v211, v136, 1.0 op_sel:[1,0,0]
	v_mfma_f32_4x4x4_16b_bf16 v[232:235], v[224:225], v[102:103], v[232:235]
	v_cvt_scalef32_pk_bf16_fp8 v212, v137, 1.0
	v_cvt_scalef32_pk_bf16_fp8 v213, v137, 1.0 op_sel:[1,0,0]
	v_cndmask_b32_e64 v188, v228, v229, s[22:23]
	v_cndmask_b32_e64 v188, v188, v230, s[24:25]
	v_cndmask_b32_e64 v188, v188, v231, s[26:27]
	v_mfma_f32_4x4x4_16b_bf16 v[228:231], v[210:211], v[108:109], 0
	v_cvt_scalef32_pk_bf16_fp8 v214, v138, 1.0
	v_cvt_scalef32_pk_bf16_fp8 v215, v138, 1.0 op_sel:[1,0,0]
	v_mfma_f32_4x4x4_16b_bf16 v[228:231], v[212:213], v[110:111], v[228:231]
	v_cvt_scalef32_pk_bf16_fp8 v216, v139, 1.0
	v_cvt_scalef32_pk_bf16_fp8 v217, v139, 1.0 op_sel:[1,0,0]
	v_lshl_or_b32 v74, v74, 7, v209
	global_load_dwordx4 v[136:139], v74, s[6:7] sc0
	v_mfma_f32_4x4x4_16b_bf16 v[228:231], v[214:215], v[100:101], v[228:231]
	v_cvt_scalef32_pk_bf16_fp8 v218, v140, 1.0
	v_cvt_scalef32_pk_bf16_fp8 v219, v140, 1.0 op_sel:[1,0,0]
	v_mfma_f32_4x4x4_16b_bf16 v[228:231], v[216:217], v[102:103], v[228:231]
	v_cvt_scalef32_pk_bf16_fp8 v220, v141, 1.0
	v_cvt_scalef32_pk_bf16_fp8 v221, v141, 1.0 op_sel:[1,0,0]
	v_cndmask_b32_e64 v189, v232, v233, s[22:23]
	v_cndmask_b32_e64 v189, v189, v234, s[24:25]
	v_cndmask_b32_e64 v189, v189, v235, s[26:27]
	v_mfma_f32_4x4x4_16b_bf16 v[232:235], v[218:219], v[108:109], 0
	v_cvt_scalef32_pk_bf16_fp8 v222, v142, 1.0
	v_cvt_scalef32_pk_bf16_fp8 v223, v142, 1.0 op_sel:[1,0,0]
	v_mfma_f32_4x4x4_16b_bf16 v[232:235], v[220:221], v[110:111], v[232:235]
	v_cvt_scalef32_pk_bf16_fp8 v224, v143, 1.0
	v_cvt_scalef32_pk_bf16_fp8 v225, v143, 1.0 op_sel:[1,0,0]
	v_lshl_or_b32 v75, v75, 7, v209
	global_load_dwordx4 v[140:143], v75, s[6:7] sc0
	v_mfma_f32_4x4x4_16b_bf16 v[232:235], v[222:223], v[100:101], v[232:235]
	v_cvt_scalef32_pk_bf16_fp8 v210, v144, 1.0
	v_cvt_scalef32_pk_bf16_fp8 v211, v144, 1.0 op_sel:[1,0,0]
	v_mfma_f32_4x4x4_16b_bf16 v[232:235], v[224:225], v[102:103], v[232:235]
	v_cvt_scalef32_pk_bf16_fp8 v212, v145, 1.0
	v_cvt_scalef32_pk_bf16_fp8 v213, v145, 1.0 op_sel:[1,0,0]
	v_cndmask_b32_e64 v190, v228, v229, s[22:23]
	v_cndmask_b32_e64 v190, v190, v230, s[24:25]
	v_cndmask_b32_e64 v190, v190, v231, s[26:27]
	v_mfma_f32_4x4x4_16b_bf16 v[228:231], v[210:211], v[108:109], 0
	v_cvt_scalef32_pk_bf16_fp8 v214, v146, 1.0
	v_cvt_scalef32_pk_bf16_fp8 v215, v146, 1.0 op_sel:[1,0,0]
	v_mfma_f32_4x4x4_16b_bf16 v[228:231], v[212:213], v[110:111], v[228:231]
	v_cvt_scalef32_pk_bf16_fp8 v216, v147, 1.0
	v_cvt_scalef32_pk_bf16_fp8 v217, v147, 1.0 op_sel:[1,0,0]
	v_lshl_or_b32 v68, v68, 7, v209
	global_load_dwordx4 v[144:147], v68, s[6:7] sc0
	v_mfma_f32_4x4x4_16b_bf16 v[228:231], v[214:215], v[100:101], v[228:231]
	v_cvt_scalef32_pk_bf16_fp8 v218, v148, 1.0
	v_cvt_scalef32_pk_bf16_fp8 v219, v148, 1.0 op_sel:[1,0,0]
	v_mfma_f32_4x4x4_16b_bf16 v[228:231], v[216:217], v[102:103], v[228:231]
	v_cvt_scalef32_pk_bf16_fp8 v220, v149, 1.0
	v_cvt_scalef32_pk_bf16_fp8 v221, v149, 1.0 op_sel:[1,0,0]
	v_cndmask_b32_e64 v191, v232, v233, s[22:23]
	v_cndmask_b32_e64 v191, v191, v234, s[24:25]
	v_cndmask_b32_e64 v191, v191, v235, s[26:27]
	v_mfma_f32_4x4x4_16b_bf16 v[232:235], v[218:219], v[108:109], 0
	v_cvt_scalef32_pk_bf16_fp8 v222, v150, 1.0
	v_cvt_scalef32_pk_bf16_fp8 v223, v150, 1.0 op_sel:[1,0,0]
	v_mfma_f32_4x4x4_16b_bf16 v[232:235], v[220:221], v[110:111], v[232:235]
	v_cvt_scalef32_pk_bf16_fp8 v224, v151, 1.0
	v_cvt_scalef32_pk_bf16_fp8 v225, v151, 1.0 op_sel:[1,0,0]
	v_lshl_or_b32 v69, v69, 7, v209
	global_load_dwordx4 v[148:151], v69, s[6:7] sc0
	v_mfma_f32_4x4x4_16b_bf16 v[232:235], v[222:223], v[100:101], v[232:235]
	v_cvt_scalef32_pk_bf16_fp8 v210, v152, 1.0
	v_cvt_scalef32_pk_bf16_fp8 v211, v152, 1.0 op_sel:[1,0,0]
	v_mfma_f32_4x4x4_16b_bf16 v[232:235], v[224:225], v[102:103], v[232:235]
	v_cvt_scalef32_pk_bf16_fp8 v212, v153, 1.0
	v_cvt_scalef32_pk_bf16_fp8 v213, v153, 1.0 op_sel:[1,0,0]
	v_cndmask_b32_e64 v192, v228, v229, s[22:23]
	v_cndmask_b32_e64 v192, v192, v230, s[24:25]
	v_cndmask_b32_e64 v192, v192, v231, s[26:27]
	v_mfma_f32_4x4x4_16b_bf16 v[228:231], v[210:211], v[108:109], 0
	v_cvt_scalef32_pk_bf16_fp8 v214, v154, 1.0
	v_cvt_scalef32_pk_bf16_fp8 v215, v154, 1.0 op_sel:[1,0,0]
	v_mfma_f32_4x4x4_16b_bf16 v[228:231], v[212:213], v[110:111], v[228:231]
	v_cvt_scalef32_pk_bf16_fp8 v216, v155, 1.0
	v_cvt_scalef32_pk_bf16_fp8 v217, v155, 1.0 op_sel:[1,0,0]
	v_lshl_or_b32 v70, v70, 7, v209
	global_load_dwordx4 v[152:155], v70, s[6:7] sc0
	v_mfma_f32_4x4x4_16b_bf16 v[228:231], v[214:215], v[100:101], v[228:231]
	v_cvt_scalef32_pk_bf16_fp8 v218, v156, 1.0
	v_cvt_scalef32_pk_bf16_fp8 v219, v156, 1.0 op_sel:[1,0,0]
	v_mfma_f32_4x4x4_16b_bf16 v[228:231], v[216:217], v[102:103], v[228:231]
	v_cvt_scalef32_pk_bf16_fp8 v220, v157, 1.0
	v_cvt_scalef32_pk_bf16_fp8 v221, v157, 1.0 op_sel:[1,0,0]
	v_cndmask_b32_e64 v193, v232, v233, s[22:23]
	v_cndmask_b32_e64 v193, v193, v234, s[24:25]
	v_cndmask_b32_e64 v193, v193, v235, s[26:27]
	v_mfma_f32_4x4x4_16b_bf16 v[232:235], v[218:219], v[108:109], 0
	v_cvt_scalef32_pk_bf16_fp8 v222, v158, 1.0
	v_cvt_scalef32_pk_bf16_fp8 v223, v158, 1.0 op_sel:[1,0,0]
	v_mfma_f32_4x4x4_16b_bf16 v[232:235], v[220:221], v[110:111], v[232:235]
	v_cvt_scalef32_pk_bf16_fp8 v224, v159, 1.0
	v_cvt_scalef32_pk_bf16_fp8 v225, v159, 1.0 op_sel:[1,0,0]
	v_lshl_or_b32 v71, v71, 7, v209
	global_load_dwordx4 v[156:159], v71, s[6:7] sc0
	v_mfma_f32_4x4x4_16b_bf16 v[232:235], v[222:223], v[100:101], v[232:235]
	v_cvt_scalef32_pk_bf16_fp8 v210, v160, 1.0
	v_cvt_scalef32_pk_bf16_fp8 v211, v160, 1.0 op_sel:[1,0,0]
	v_mfma_f32_4x4x4_16b_bf16 v[232:235], v[224:225], v[102:103], v[232:235]
	v_cvt_scalef32_pk_bf16_fp8 v212, v161, 1.0
	v_cvt_scalef32_pk_bf16_fp8 v213, v161, 1.0 op_sel:[1,0,0]
	v_cndmask_b32_e64 v194, v228, v229, s[22:23]
	v_cndmask_b32_e64 v194, v194, v230, s[24:25]
	v_cndmask_b32_e64 v194, v194, v231, s[26:27]
	v_mfma_f32_4x4x4_16b_bf16 v[228:231], v[210:211], v[108:109], 0
	v_cvt_scalef32_pk_bf16_fp8 v214, v162, 1.0
	v_cvt_scalef32_pk_bf16_fp8 v215, v162, 1.0 op_sel:[1,0,0]
	v_mfma_f32_4x4x4_16b_bf16 v[228:231], v[212:213], v[110:111], v[228:231]
	v_cvt_scalef32_pk_bf16_fp8 v216, v163, 1.0
	v_cvt_scalef32_pk_bf16_fp8 v217, v163, 1.0 op_sel:[1,0,0]
	v_lshl_or_b32 v64, v64, 7, v209
	global_load_dwordx4 v[160:163], v64, s[6:7] sc0
	v_mfma_f32_4x4x4_16b_bf16 v[228:231], v[214:215], v[100:101], v[228:231]
	v_cvt_scalef32_pk_bf16_fp8 v218, v164, 1.0
	v_cvt_scalef32_pk_bf16_fp8 v219, v164, 1.0 op_sel:[1,0,0]
	v_mfma_f32_4x4x4_16b_bf16 v[228:231], v[216:217], v[102:103], v[228:231]
	v_cvt_scalef32_pk_bf16_fp8 v220, v165, 1.0
	v_cvt_scalef32_pk_bf16_fp8 v221, v165, 1.0 op_sel:[1,0,0]
	v_cndmask_b32_e64 v195, v232, v233, s[22:23]
	v_cndmask_b32_e64 v195, v195, v234, s[24:25]
	v_cndmask_b32_e64 v195, v195, v235, s[26:27]
	v_mfma_f32_4x4x4_16b_bf16 v[232:235], v[218:219], v[108:109], 0
	v_cvt_scalef32_pk_bf16_fp8 v222, v166, 1.0
	v_cvt_scalef32_pk_bf16_fp8 v223, v166, 1.0 op_sel:[1,0,0]
	v_mfma_f32_4x4x4_16b_bf16 v[232:235], v[220:221], v[110:111], v[232:235]
	v_cvt_scalef32_pk_bf16_fp8 v224, v167, 1.0
	v_cvt_scalef32_pk_bf16_fp8 v225, v167, 1.0 op_sel:[1,0,0]
	v_lshl_or_b32 v65, v65, 7, v209
	global_load_dwordx4 v[164:167], v65, s[6:7] sc0
	v_mfma_f32_4x4x4_16b_bf16 v[232:235], v[222:223], v[100:101], v[232:235]
	v_cvt_scalef32_pk_bf16_fp8 v210, v168, 1.0
	v_cvt_scalef32_pk_bf16_fp8 v211, v168, 1.0 op_sel:[1,0,0]
	v_mfma_f32_4x4x4_16b_bf16 v[232:235], v[224:225], v[102:103], v[232:235]
	v_cvt_scalef32_pk_bf16_fp8 v212, v169, 1.0
	v_cvt_scalef32_pk_bf16_fp8 v213, v169, 1.0 op_sel:[1,0,0]
	v_cndmask_b32_e64 v196, v228, v229, s[22:23]
	v_cndmask_b32_e64 v196, v196, v230, s[24:25]
	v_cndmask_b32_e64 v196, v196, v231, s[26:27]
	v_mfma_f32_4x4x4_16b_bf16 v[228:231], v[210:211], v[108:109], 0
	v_cvt_scalef32_pk_bf16_fp8 v214, v170, 1.0
	v_cvt_scalef32_pk_bf16_fp8 v215, v170, 1.0 op_sel:[1,0,0]
	v_mfma_f32_4x4x4_16b_bf16 v[228:231], v[212:213], v[110:111], v[228:231]
	v_cvt_scalef32_pk_bf16_fp8 v216, v171, 1.0
	v_cvt_scalef32_pk_bf16_fp8 v217, v171, 1.0 op_sel:[1,0,0]
	v_lshl_or_b32 v66, v66, 7, v209
	global_load_dwordx4 v[168:171], v66, s[6:7] sc0
	v_mfma_f32_4x4x4_16b_bf16 v[228:231], v[214:215], v[100:101], v[228:231]
	v_cvt_scalef32_pk_bf16_fp8 v218, v172, 1.0
	v_cvt_scalef32_pk_bf16_fp8 v219, v172, 1.0 op_sel:[1,0,0]
	v_mfma_f32_4x4x4_16b_bf16 v[228:231], v[216:217], v[102:103], v[228:231]
	v_cvt_scalef32_pk_bf16_fp8 v220, v173, 1.0
	v_cvt_scalef32_pk_bf16_fp8 v221, v173, 1.0 op_sel:[1,0,0]
	v_cndmask_b32_e64 v197, v232, v233, s[22:23]
	v_cndmask_b32_e64 v197, v197, v234, s[24:25]
	v_cndmask_b32_e64 v197, v197, v235, s[26:27]
	v_mfma_f32_4x4x4_16b_bf16 v[232:235], v[218:219], v[108:109], 0
	v_cvt_scalef32_pk_bf16_fp8 v222, v174, 1.0
	v_cvt_scalef32_pk_bf16_fp8 v223, v174, 1.0 op_sel:[1,0,0]
	v_mfma_f32_4x4x4_16b_bf16 v[232:235], v[220:221], v[110:111], v[232:235]
	v_cvt_scalef32_pk_bf16_fp8 v224, v175, 1.0
	v_cvt_scalef32_pk_bf16_fp8 v225, v175, 1.0 op_sel:[1,0,0]
	v_lshl_or_b32 v67, v67, 7, v209
	global_load_dwordx4 v[172:175], v67, s[6:7] sc0
	v_mfma_f32_4x4x4_16b_bf16 v[232:235], v[222:223], v[100:101], v[232:235]
	s_nop 1
	v_mfma_f32_4x4x4_16b_bf16 v[232:235], v[224:225], v[102:103], v[232:235]
	v_cndmask_b32_e64 v198, v228, v229, s[22:23]
	v_cndmask_b32_e64 v198, v198, v230, s[24:25]
	v_cndmask_b32_e64 v198, v198, v231, s[26:27]
	s_nop 4
	v_cndmask_b32_e64 v199, v232, v233, s[22:23]
	v_cndmask_b32_e64 v199, v199, v234, s[24:25]
	v_cndmask_b32_e64 v199, v199, v235, s[26:27]
	v_cndmask_b32_e64 v200, v184, v192, s[4:5]
	v_cndmask_b32_e64 v201, v192, v184, s[4:5]
	v_cndmask_b32_e64 v202, v185, v193, s[4:5]
	v_cndmask_b32_e64 v203, v193, v185, s[4:5]
	v_cndmask_b32_e64 v204, v186, v194, s[4:5]
	v_cndmask_b32_e64 v205, v194, v186, s[4:5]
	v_cndmask_b32_e64 v236, v187, v195, s[4:5]
	v_cndmask_b32_e64 v237, v195, v187, s[4:5]
	v_cndmask_b32_e64 v238, v188, v196, s[4:5]
	v_cndmask_b32_e64 v239, v196, v188, s[4:5]
	v_cndmask_b32_e64 v240, v189, v197, s[4:5]
	v_cndmask_b32_e64 v241, v197, v189, s[4:5]
	v_cndmask_b32_e64 v242, v190, v198, s[4:5]
	v_cndmask_b32_e64 v243, v198, v190, s[4:5]
	v_cndmask_b32_e64 v244, v191, v199, s[4:5]
	v_cndmask_b32_e64 v245, v199, v191, s[4:5]
	v_add_f32_dpp v246, v200, v201 row_half_mirror row_mask:0xf bank_mask:0xf
	v_add_f32_dpp v247, v202, v203 row_half_mirror row_mask:0xf bank_mask:0xf
	v_add_f32_dpp v248, v204, v205 row_half_mirror row_mask:0xf bank_mask:0xf
	v_add_f32_dpp v249, v236, v237 row_half_mirror row_mask:0xf bank_mask:0xf
	v_add_f32_dpp v226, v238, v239 row_half_mirror row_mask:0xf bank_mask:0xf
	v_add_f32_dpp v227, v240, v241 row_half_mirror row_mask:0xf bank_mask:0xf
	v_add_f32_dpp v210, v242, v243 row_half_mirror row_mask:0xf bank_mask:0xf
	v_add_f32_dpp v211, v244, v245 row_half_mirror row_mask:0xf bank_mask:0xf
	v_cndmask_b32_e64 v200, v246, v226, s[2:3]
	v_cndmask_b32_e64 v201, v226, v246, s[2:3]
	v_cndmask_b32_e64 v202, v247, v227, s[2:3]
	v_cndmask_b32_e64 v203, v227, v247, s[2:3]
	v_cndmask_b32_e64 v204, v248, v210, s[2:3]
	v_cndmask_b32_e64 v205, v210, v248, s[2:3]
	v_cndmask_b32_e64 v236, v249, v211, s[2:3]
	v_cndmask_b32_e64 v237, v211, v249, s[2:3]
	v_add_f32_dpp v212, v200, v201 quad_perm:[2,3,0,1] row_mask:0xf bank_mask:0xf
	v_add_f32_dpp v213, v202, v203 quad_perm:[2,3,0,1] row_mask:0xf bank_mask:0xf
	v_add_f32_dpp v214, v204, v205 quad_perm:[2,3,0,1] row_mask:0xf bank_mask:0xf
	v_add_f32_dpp v215, v236, v237 quad_perm:[2,3,0,1] row_mask:0xf bank_mask:0xf
	v_cndmask_b32_e64 v200, v212, v214, s[0:1]
	v_cndmask_b32_e64 v201, v214, v212, s[0:1]
	v_cndmask_b32_e64 v202, v213, v215, s[0:1]
	v_cndmask_b32_e64 v203, v215, v213, s[0:1]
	s_nop 1
	v_add_f32_dpp v216, v200, v201 quad_perm:[1,0,3,2] row_mask:0xf bank_mask:0xf
	v_add_f32_dpp v217, v202, v203 quad_perm:[1,0,3,2] row_mask:0xf bank_mask:0xf
	s_ashr_i32 s11, s10, 31
	s_lshl_b64 s[10:11], s[10:11], 8
	v_cvt_pk_bf16_f32 v186, v216, v217
	v_lshl_add_u64 v[184:185], v[178:179], 0, s[10:11]
	global_store_dword v[184:185], v186, off
	s_add_u32 s20, s12, 0x300
	s_lshl_b32 s20, s20, 11
	v_lshl_add_u64 v[108:109], v[182:183], 0, s[20:21]
	global_load_dwordx4 v[100:103], v[108:109], off offset:16
	s_nop 0
	global_load_dwordx4 v[108:111], v[108:109], off
	s_add_u32 s12, s12, 0x200
	s_mov_b32 s14, s12
	s_waitcnt vmcnt(19)
	v_cvt_scalef32_pk_bf16_fp8 v210, v24, 1.0
	v_cvt_scalef32_pk_bf16_fp8 v211, v24, 1.0 op_sel:[1,0,0]
	v_cvt_scalef32_pk_bf16_fp8 v212, v25, 1.0
	v_cvt_scalef32_pk_bf16_fp8 v213, v25, 1.0 op_sel:[1,0,0]
	v_mfma_f32_4x4x4_16b_bf16 v[228:231], v[210:211], v[20:21], 0
	v_cvt_scalef32_pk_bf16_fp8 v214, v26, 1.0
	v_cvt_scalef32_pk_bf16_fp8 v215, v26, 1.0 op_sel:[1,0,0]
	v_mfma_f32_4x4x4_16b_bf16 v[228:231], v[212:213], v[22:23], v[228:231]
	v_cvt_scalef32_pk_bf16_fp8 v216, v27, 1.0
	v_cvt_scalef32_pk_bf16_fp8 v217, v27, 1.0 op_sel:[1,0,0]
	v_mfma_f32_4x4x4_16b_bf16 v[228:231], v[214:215], v[16:17], v[228:231]
	v_cvt_scalef32_pk_bf16_fp8 v218, v28, 1.0
	v_cvt_scalef32_pk_bf16_fp8 v219, v28, 1.0 op_sel:[1,0,0]
	v_mfma_f32_4x4x4_16b_bf16 v[228:231], v[216:217], v[18:19], v[228:231]
	v_cvt_scalef32_pk_bf16_fp8 v220, v29, 1.0
	v_cvt_scalef32_pk_bf16_fp8 v221, v29, 1.0 op_sel:[1,0,0]
	v_mfma_f32_4x4x4_16b_bf16 v[232:235], v[218:219], v[20:21], 0
	v_cvt_scalef32_pk_bf16_fp8 v222, v30, 1.0
	v_cvt_scalef32_pk_bf16_fp8 v223, v30, 1.0 op_sel:[1,0,0]
	v_mfma_f32_4x4x4_16b_bf16 v[232:235], v[220:221], v[22:23], v[232:235]
	v_cvt_scalef32_pk_bf16_fp8 v224, v31, 1.0
	v_cvt_scalef32_pk_bf16_fp8 v225, v31, 1.0 op_sel:[1,0,0]
	v_mfma_f32_4x4x4_16b_bf16 v[232:235], v[222:223], v[16:17], v[232:235]
	v_cvt_scalef32_pk_bf16_fp8 v210, v32, 1.0
	v_cvt_scalef32_pk_bf16_fp8 v211, v32, 1.0 op_sel:[1,0,0]
	v_mfma_f32_4x4x4_16b_bf16 v[232:235], v[224:225], v[18:19], v[232:235]
	v_cvt_scalef32_pk_bf16_fp8 v212, v33, 1.0
	v_cvt_scalef32_pk_bf16_fp8 v213, v33, 1.0 op_sel:[1,0,0]
	v_cndmask_b32_e64 v184, v228, v229, s[22:23]
	v_cndmask_b32_e64 v184, v184, v230, s[24:25]
	v_cndmask_b32_e64 v184, v184, v231, s[26:27]
	v_mfma_f32_4x4x4_16b_bf16 v[228:231], v[210:211], v[20:21], 0
	v_cvt_scalef32_pk_bf16_fp8 v214, v34, 1.0
	v_cvt_scalef32_pk_bf16_fp8 v215, v34, 1.0 op_sel:[1,0,0]
	v_mfma_f32_4x4x4_16b_bf16 v[228:231], v[212:213], v[22:23], v[228:231]
	v_cvt_scalef32_pk_bf16_fp8 v216, v35, 1.0
	v_cvt_scalef32_pk_bf16_fp8 v217, v35, 1.0 op_sel:[1,0,0]
	v_mfma_f32_4x4x4_16b_bf16 v[228:231], v[214:215], v[16:17], v[228:231]
	v_cvt_scalef32_pk_bf16_fp8 v218, v36, 1.0
	v_cvt_scalef32_pk_bf16_fp8 v219, v36, 1.0 op_sel:[1,0,0]
	v_mfma_f32_4x4x4_16b_bf16 v[228:231], v[216:217], v[18:19], v[228:231]
	v_cvt_scalef32_pk_bf16_fp8 v220, v37, 1.0
	v_cvt_scalef32_pk_bf16_fp8 v221, v37, 1.0 op_sel:[1,0,0]
	v_cndmask_b32_e64 v185, v232, v233, s[22:23]
	v_cndmask_b32_e64 v185, v185, v234, s[24:25]
	v_cndmask_b32_e64 v185, v185, v235, s[26:27]
	v_mfma_f32_4x4x4_16b_bf16 v[232:235], v[218:219], v[20:21], 0
	v_cvt_scalef32_pk_bf16_fp8 v222, v38, 1.0
	v_cvt_scalef32_pk_bf16_fp8 v223, v38, 1.0 op_sel:[1,0,0]
	v_mfma_f32_4x4x4_16b_bf16 v[232:235], v[220:221], v[22:23], v[232:235]
	v_cvt_scalef32_pk_bf16_fp8 v224, v39, 1.0
	v_cvt_scalef32_pk_bf16_fp8 v225, v39, 1.0 op_sel:[1,0,0]
	v_mfma_f32_4x4x4_16b_bf16 v[232:235], v[222:223], v[16:17], v[232:235]
	v_cvt_scalef32_pk_bf16_fp8 v210, v40, 1.0
	v_cvt_scalef32_pk_bf16_fp8 v211, v40, 1.0 op_sel:[1,0,0]
	v_mfma_f32_4x4x4_16b_bf16 v[232:235], v[224:225], v[18:19], v[232:235]
	v_cvt_scalef32_pk_bf16_fp8 v212, v41, 1.0
	v_cvt_scalef32_pk_bf16_fp8 v213, v41, 1.0 op_sel:[1,0,0]
	v_cndmask_b32_e64 v186, v228, v229, s[22:23]
	v_cndmask_b32_e64 v186, v186, v230, s[24:25]
	v_cndmask_b32_e64 v186, v186, v231, s[26:27]
	v_mfma_f32_4x4x4_16b_bf16 v[228:231], v[210:211], v[20:21], 0
	v_cvt_scalef32_pk_bf16_fp8 v214, v42, 1.0
	v_cvt_scalef32_pk_bf16_fp8 v215, v42, 1.0 op_sel:[1,0,0]
	v_mfma_f32_4x4x4_16b_bf16 v[228:231], v[212:213], v[22:23], v[228:231]
	v_cvt_scalef32_pk_bf16_fp8 v216, v43, 1.0
	v_cvt_scalef32_pk_bf16_fp8 v217, v43, 1.0 op_sel:[1,0,0]
	v_mfma_f32_4x4x4_16b_bf16 v[228:231], v[214:215], v[16:17], v[228:231]
	v_cvt_scalef32_pk_bf16_fp8 v218, v44, 1.0
	v_cvt_scalef32_pk_bf16_fp8 v219, v44, 1.0 op_sel:[1,0,0]
	v_mfma_f32_4x4x4_16b_bf16 v[228:231], v[216:217], v[18:19], v[228:231]
	v_cvt_scalef32_pk_bf16_fp8 v220, v45, 1.0
	v_cvt_scalef32_pk_bf16_fp8 v221, v45, 1.0 op_sel:[1,0,0]
	v_cndmask_b32_e64 v187, v232, v233, s[22:23]
	v_cndmask_b32_e64 v187, v187, v234, s[24:25]
	v_cndmask_b32_e64 v187, v187, v235, s[26:27]
	v_mfma_f32_4x4x4_16b_bf16 v[232:235], v[218:219], v[20:21], 0
	v_cvt_scalef32_pk_bf16_fp8 v222, v46, 1.0
	v_cvt_scalef32_pk_bf16_fp8 v223, v46, 1.0 op_sel:[1,0,0]
	v_mfma_f32_4x4x4_16b_bf16 v[232:235], v[220:221], v[22:23], v[232:235]
	v_cvt_scalef32_pk_bf16_fp8 v224, v47, 1.0
	v_cvt_scalef32_pk_bf16_fp8 v225, v47, 1.0 op_sel:[1,0,0]
	v_mfma_f32_4x4x4_16b_bf16 v[232:235], v[222:223], v[16:17], v[232:235]
	v_cvt_scalef32_pk_bf16_fp8 v210, v48, 1.0
	v_cvt_scalef32_pk_bf16_fp8 v211, v48, 1.0 op_sel:[1,0,0]
	v_mfma_f32_4x4x4_16b_bf16 v[232:235], v[224:225], v[18:19], v[232:235]
	v_cvt_scalef32_pk_bf16_fp8 v212, v49, 1.0
	v_cvt_scalef32_pk_bf16_fp8 v213, v49, 1.0 op_sel:[1,0,0]
	v_cndmask_b32_e64 v188, v228, v229, s[22:23]
	v_cndmask_b32_e64 v188, v188, v230, s[24:25]
	v_cndmask_b32_e64 v188, v188, v231, s[26:27]
	v_mfma_f32_4x4x4_16b_bf16 v[228:231], v[210:211], v[20:21], 0
	v_cvt_scalef32_pk_bf16_fp8 v214, v50, 1.0
	v_cvt_scalef32_pk_bf16_fp8 v215, v50, 1.0 op_sel:[1,0,0]
	v_mfma_f32_4x4x4_16b_bf16 v[228:231], v[212:213], v[22:23], v[228:231]
	v_cvt_scalef32_pk_bf16_fp8 v216, v51, 1.0
	v_cvt_scalef32_pk_bf16_fp8 v217, v51, 1.0 op_sel:[1,0,0]
	v_mfma_f32_4x4x4_16b_bf16 v[228:231], v[214:215], v[16:17], v[228:231]
	v_cvt_scalef32_pk_bf16_fp8 v218, v52, 1.0
	v_cvt_scalef32_pk_bf16_fp8 v219, v52, 1.0 op_sel:[1,0,0]
	v_mfma_f32_4x4x4_16b_bf16 v[228:231], v[216:217], v[18:19], v[228:231]
	v_cvt_scalef32_pk_bf16_fp8 v220, v53, 1.0
	v_cvt_scalef32_pk_bf16_fp8 v221, v53, 1.0 op_sel:[1,0,0]
	v_cndmask_b32_e64 v189, v232, v233, s[22:23]
	v_cndmask_b32_e64 v189, v189, v234, s[24:25]
	v_cndmask_b32_e64 v189, v189, v235, s[26:27]
	v_mfma_f32_4x4x4_16b_bf16 v[232:235], v[218:219], v[20:21], 0
	v_cvt_scalef32_pk_bf16_fp8 v222, v54, 1.0
	v_cvt_scalef32_pk_bf16_fp8 v223, v54, 1.0 op_sel:[1,0,0]
	v_mfma_f32_4x4x4_16b_bf16 v[232:235], v[220:221], v[22:23], v[232:235]
	v_cvt_scalef32_pk_bf16_fp8 v224, v55, 1.0
	v_cvt_scalef32_pk_bf16_fp8 v225, v55, 1.0 op_sel:[1,0,0]
	v_mfma_f32_4x4x4_16b_bf16 v[232:235], v[222:223], v[16:17], v[232:235]
	v_cvt_scalef32_pk_bf16_fp8 v210, v56, 1.0
	v_cvt_scalef32_pk_bf16_fp8 v211, v56, 1.0 op_sel:[1,0,0]
	v_mfma_f32_4x4x4_16b_bf16 v[232:235], v[224:225], v[18:19], v[232:235]
	v_cvt_scalef32_pk_bf16_fp8 v212, v57, 1.0
	v_cvt_scalef32_pk_bf16_fp8 v213, v57, 1.0 op_sel:[1,0,0]
	v_cndmask_b32_e64 v190, v228, v229, s[22:23]
	v_cndmask_b32_e64 v190, v190, v230, s[24:25]
	v_cndmask_b32_e64 v190, v190, v231, s[26:27]
	v_mfma_f32_4x4x4_16b_bf16 v[228:231], v[210:211], v[20:21], 0
	v_cvt_scalef32_pk_bf16_fp8 v214, v58, 1.0
	v_cvt_scalef32_pk_bf16_fp8 v215, v58, 1.0 op_sel:[1,0,0]
	v_mfma_f32_4x4x4_16b_bf16 v[228:231], v[212:213], v[22:23], v[228:231]
	v_cvt_scalef32_pk_bf16_fp8 v216, v59, 1.0
	v_cvt_scalef32_pk_bf16_fp8 v217, v59, 1.0 op_sel:[1,0,0]
	v_mfma_f32_4x4x4_16b_bf16 v[228:231], v[214:215], v[16:17], v[228:231]
	v_cvt_scalef32_pk_bf16_fp8 v218, v60, 1.0
	v_cvt_scalef32_pk_bf16_fp8 v219, v60, 1.0 op_sel:[1,0,0]
	v_mfma_f32_4x4x4_16b_bf16 v[228:231], v[216:217], v[18:19], v[228:231]
	v_cvt_scalef32_pk_bf16_fp8 v220, v61, 1.0
	v_cvt_scalef32_pk_bf16_fp8 v221, v61, 1.0 op_sel:[1,0,0]
	v_cndmask_b32_e64 v191, v232, v233, s[22:23]
	v_cndmask_b32_e64 v191, v191, v234, s[24:25]
	v_cndmask_b32_e64 v191, v191, v235, s[26:27]
	v_mfma_f32_4x4x4_16b_bf16 v[232:235], v[218:219], v[20:21], 0
	v_cvt_scalef32_pk_bf16_fp8 v222, v62, 1.0
	v_cvt_scalef32_pk_bf16_fp8 v223, v62, 1.0 op_sel:[1,0,0]
	v_mfma_f32_4x4x4_16b_bf16 v[232:235], v[220:221], v[22:23], v[232:235]
	v_cvt_scalef32_pk_bf16_fp8 v224, v63, 1.0
	v_cvt_scalef32_pk_bf16_fp8 v225, v63, 1.0 op_sel:[1,0,0]
	v_mfma_f32_4x4x4_16b_bf16 v[232:235], v[222:223], v[16:17], v[232:235]
	v_cvt_scalef32_pk_bf16_fp8 v210, v76, 1.0
	v_cvt_scalef32_pk_bf16_fp8 v211, v76, 1.0 op_sel:[1,0,0]
	v_mfma_f32_4x4x4_16b_bf16 v[232:235], v[224:225], v[18:19], v[232:235]
	v_cvt_scalef32_pk_bf16_fp8 v212, v77, 1.0
	v_cvt_scalef32_pk_bf16_fp8 v213, v77, 1.0 op_sel:[1,0,0]
	v_cndmask_b32_e64 v192, v228, v229, s[22:23]
	v_cndmask_b32_e64 v192, v192, v230, s[24:25]
	v_cndmask_b32_e64 v192, v192, v231, s[26:27]
	v_mfma_f32_4x4x4_16b_bf16 v[228:231], v[210:211], v[20:21], 0
	v_cvt_scalef32_pk_bf16_fp8 v214, v78, 1.0
	v_cvt_scalef32_pk_bf16_fp8 v215, v78, 1.0 op_sel:[1,0,0]
	v_mfma_f32_4x4x4_16b_bf16 v[228:231], v[212:213], v[22:23], v[228:231]
	v_cvt_scalef32_pk_bf16_fp8 v216, v79, 1.0
	v_cvt_scalef32_pk_bf16_fp8 v217, v79, 1.0 op_sel:[1,0,0]
	v_mfma_f32_4x4x4_16b_bf16 v[228:231], v[214:215], v[16:17], v[228:231]
	v_cvt_scalef32_pk_bf16_fp8 v218, v84, 1.0
	v_cvt_scalef32_pk_bf16_fp8 v219, v84, 1.0 op_sel:[1,0,0]
	v_mfma_f32_4x4x4_16b_bf16 v[228:231], v[216:217], v[18:19], v[228:231]
	v_cvt_scalef32_pk_bf16_fp8 v220, v85, 1.0
	v_cvt_scalef32_pk_bf16_fp8 v221, v85, 1.0 op_sel:[1,0,0]
	v_cndmask_b32_e64 v193, v232, v233, s[22:23]
	v_cndmask_b32_e64 v193, v193, v234, s[24:25]
	v_cndmask_b32_e64 v193, v193, v235, s[26:27]
	v_mfma_f32_4x4x4_16b_bf16 v[232:235], v[218:219], v[20:21], 0
	v_cvt_scalef32_pk_bf16_fp8 v222, v86, 1.0
	v_cvt_scalef32_pk_bf16_fp8 v223, v86, 1.0 op_sel:[1,0,0]
	v_mfma_f32_4x4x4_16b_bf16 v[232:235], v[220:221], v[22:23], v[232:235]
	v_cvt_scalef32_pk_bf16_fp8 v224, v87, 1.0
	v_cvt_scalef32_pk_bf16_fp8 v225, v87, 1.0 op_sel:[1,0,0]
	v_mfma_f32_4x4x4_16b_bf16 v[232:235], v[222:223], v[16:17], v[232:235]
	v_cvt_scalef32_pk_bf16_fp8 v210, v88, 1.0
	v_cvt_scalef32_pk_bf16_fp8 v211, v88, 1.0 op_sel:[1,0,0]
	v_mfma_f32_4x4x4_16b_bf16 v[232:235], v[224:225], v[18:19], v[232:235]
	v_cvt_scalef32_pk_bf16_fp8 v212, v89, 1.0
	v_cvt_scalef32_pk_bf16_fp8 v213, v89, 1.0 op_sel:[1,0,0]
	v_cndmask_b32_e64 v194, v228, v229, s[22:23]
	v_cndmask_b32_e64 v194, v194, v230, s[24:25]
	v_cndmask_b32_e64 v194, v194, v231, s[26:27]
	v_mfma_f32_4x4x4_16b_bf16 v[228:231], v[210:211], v[20:21], 0
	v_cvt_scalef32_pk_bf16_fp8 v214, v90, 1.0
	v_cvt_scalef32_pk_bf16_fp8 v215, v90, 1.0 op_sel:[1,0,0]
	v_mfma_f32_4x4x4_16b_bf16 v[228:231], v[212:213], v[22:23], v[228:231]
	v_cvt_scalef32_pk_bf16_fp8 v216, v91, 1.0
	v_cvt_scalef32_pk_bf16_fp8 v217, v91, 1.0 op_sel:[1,0,0]
	v_mfma_f32_4x4x4_16b_bf16 v[228:231], v[214:215], v[16:17], v[228:231]
	v_cvt_scalef32_pk_bf16_fp8 v218, v92, 1.0
	v_cvt_scalef32_pk_bf16_fp8 v219, v92, 1.0 op_sel:[1,0,0]
	v_mfma_f32_4x4x4_16b_bf16 v[228:231], v[216:217], v[18:19], v[228:231]
	v_cvt_scalef32_pk_bf16_fp8 v220, v93, 1.0
	v_cvt_scalef32_pk_bf16_fp8 v221, v93, 1.0 op_sel:[1,0,0]
	v_cndmask_b32_e64 v195, v232, v233, s[22:23]
	v_cndmask_b32_e64 v195, v195, v234, s[24:25]
	v_cndmask_b32_e64 v195, v195, v235, s[26:27]
	v_mfma_f32_4x4x4_16b_bf16 v[232:235], v[218:219], v[20:21], 0
	v_cvt_scalef32_pk_bf16_fp8 v222, v94, 1.0
	v_cvt_scalef32_pk_bf16_fp8 v223, v94, 1.0 op_sel:[1,0,0]
	v_mfma_f32_4x4x4_16b_bf16 v[232:235], v[220:221], v[22:23], v[232:235]
	v_cvt_scalef32_pk_bf16_fp8 v224, v95, 1.0
	v_cvt_scalef32_pk_bf16_fp8 v225, v95, 1.0 op_sel:[1,0,0]
	v_mfma_f32_4x4x4_16b_bf16 v[232:235], v[222:223], v[16:17], v[232:235]
	v_cvt_scalef32_pk_bf16_fp8 v210, v96, 1.0
	v_cvt_scalef32_pk_bf16_fp8 v211, v96, 1.0 op_sel:[1,0,0]
	v_mfma_f32_4x4x4_16b_bf16 v[232:235], v[224:225], v[18:19], v[232:235]
	v_cvt_scalef32_pk_bf16_fp8 v212, v97, 1.0
	v_cvt_scalef32_pk_bf16_fp8 v213, v97, 1.0 op_sel:[1,0,0]
	v_cndmask_b32_e64 v196, v228, v229, s[22:23]
	v_cndmask_b32_e64 v196, v196, v230, s[24:25]
	v_cndmask_b32_e64 v196, v196, v231, s[26:27]
	v_mfma_f32_4x4x4_16b_bf16 v[228:231], v[210:211], v[20:21], 0
	v_cvt_scalef32_pk_bf16_fp8 v214, v98, 1.0
	v_cvt_scalef32_pk_bf16_fp8 v215, v98, 1.0 op_sel:[1,0,0]
	v_mfma_f32_4x4x4_16b_bf16 v[228:231], v[212:213], v[22:23], v[228:231]
	v_cvt_scalef32_pk_bf16_fp8 v216, v99, 1.0
	v_cvt_scalef32_pk_bf16_fp8 v217, v99, 1.0 op_sel:[1,0,0]
	v_mfma_f32_4x4x4_16b_bf16 v[228:231], v[214:215], v[16:17], v[228:231]
	v_cvt_scalef32_pk_bf16_fp8 v218, v104, 1.0
	v_cvt_scalef32_pk_bf16_fp8 v219, v104, 1.0 op_sel:[1,0,0]
	v_mfma_f32_4x4x4_16b_bf16 v[228:231], v[216:217], v[18:19], v[228:231]
	v_cvt_scalef32_pk_bf16_fp8 v220, v105, 1.0
	v_cvt_scalef32_pk_bf16_fp8 v221, v105, 1.0 op_sel:[1,0,0]
	v_cndmask_b32_e64 v197, v232, v233, s[22:23]
	v_cndmask_b32_e64 v197, v197, v234, s[24:25]
	v_cndmask_b32_e64 v197, v197, v235, s[26:27]
	v_mfma_f32_4x4x4_16b_bf16 v[232:235], v[218:219], v[20:21], 0
	v_cvt_scalef32_pk_bf16_fp8 v222, v106, 1.0
	v_cvt_scalef32_pk_bf16_fp8 v223, v106, 1.0 op_sel:[1,0,0]
	v_mfma_f32_4x4x4_16b_bf16 v[232:235], v[220:221], v[22:23], v[232:235]
	v_cvt_scalef32_pk_bf16_fp8 v224, v107, 1.0
	v_cvt_scalef32_pk_bf16_fp8 v225, v107, 1.0 op_sel:[1,0,0]
	v_mfma_f32_4x4x4_16b_bf16 v[232:235], v[222:223], v[16:17], v[232:235]
	s_nop 1
	v_mfma_f32_4x4x4_16b_bf16 v[232:235], v[224:225], v[18:19], v[232:235]
	v_cndmask_b32_e64 v198, v228, v229, s[22:23]
	v_cndmask_b32_e64 v198, v198, v230, s[24:25]
	v_cndmask_b32_e64 v198, v198, v231, s[26:27]
	s_nop 4
	v_cndmask_b32_e64 v199, v232, v233, s[22:23]
	v_cndmask_b32_e64 v199, v199, v234, s[24:25]
	v_cndmask_b32_e64 v199, v199, v235, s[26:27]
	v_cndmask_b32_e64 v200, v184, v192, s[4:5]
	v_cndmask_b32_e64 v201, v192, v184, s[4:5]
	v_cndmask_b32_e64 v202, v185, v193, s[4:5]
	v_cndmask_b32_e64 v203, v193, v185, s[4:5]
	v_cndmask_b32_e64 v204, v186, v194, s[4:5]
	v_cndmask_b32_e64 v205, v194, v186, s[4:5]
	v_cndmask_b32_e64 v236, v187, v195, s[4:5]
	v_cndmask_b32_e64 v237, v195, v187, s[4:5]
	v_cndmask_b32_e64 v238, v188, v196, s[4:5]
	v_cndmask_b32_e64 v239, v196, v188, s[4:5]
	v_cndmask_b32_e64 v240, v189, v197, s[4:5]
	v_cndmask_b32_e64 v241, v197, v189, s[4:5]
	v_cndmask_b32_e64 v242, v190, v198, s[4:5]
	v_cndmask_b32_e64 v243, v198, v190, s[4:5]
	v_cndmask_b32_e64 v244, v191, v199, s[4:5]
	v_cndmask_b32_e64 v245, v199, v191, s[4:5]
	v_add_f32_dpp v246, v200, v201 row_half_mirror row_mask:0xf bank_mask:0xf
	v_add_f32_dpp v247, v202, v203 row_half_mirror row_mask:0xf bank_mask:0xf
	v_add_f32_dpp v248, v204, v205 row_half_mirror row_mask:0xf bank_mask:0xf
	v_add_f32_dpp v249, v236, v237 row_half_mirror row_mask:0xf bank_mask:0xf
	v_add_f32_dpp v226, v238, v239 row_half_mirror row_mask:0xf bank_mask:0xf
	v_add_f32_dpp v227, v240, v241 row_half_mirror row_mask:0xf bank_mask:0xf
	v_add_f32_dpp v210, v242, v243 row_half_mirror row_mask:0xf bank_mask:0xf
	v_add_f32_dpp v211, v244, v245 row_half_mirror row_mask:0xf bank_mask:0xf
	v_cndmask_b32_e64 v200, v246, v226, s[2:3]
	v_cndmask_b32_e64 v201, v226, v246, s[2:3]
	v_cndmask_b32_e64 v202, v247, v227, s[2:3]
	v_cndmask_b32_e64 v203, v227, v247, s[2:3]
	v_cndmask_b32_e64 v204, v248, v210, s[2:3]
	v_cndmask_b32_e64 v205, v210, v248, s[2:3]
	v_cndmask_b32_e64 v236, v249, v211, s[2:3]
	v_cndmask_b32_e64 v237, v211, v249, s[2:3]
	v_add_f32_dpp v212, v200, v201 quad_perm:[2,3,0,1] row_mask:0xf bank_mask:0xf
	v_add_f32_dpp v213, v202, v203 quad_perm:[2,3,0,1] row_mask:0xf bank_mask:0xf
	v_add_f32_dpp v214, v204, v205 quad_perm:[2,3,0,1] row_mask:0xf bank_mask:0xf
	v_add_f32_dpp v215, v236, v237 quad_perm:[2,3,0,1] row_mask:0xf bank_mask:0xf
	v_cndmask_b32_e64 v200, v212, v214, s[0:1]
	v_cndmask_b32_e64 v201, v214, v212, s[0:1]
	v_cndmask_b32_e64 v202, v213, v215, s[0:1]
	v_cndmask_b32_e64 v203, v215, v213, s[0:1]
	s_nop 1
	v_add_f32_dpp v216, v200, v201 quad_perm:[1,0,3,2] row_mask:0xf bank_mask:0xf
	v_add_f32_dpp v217, v202, v203 quad_perm:[1,0,3,2] row_mask:0xf bank_mask:0xf
	s_ashr_i32 s15, s14, 31
	s_lshl_b64 s[14:15], s[14:15], 8
	v_cvt_pk_bf16_f32 v186, v216, v217
	v_lshl_add_u64 v[184:185], v[178:179], 0, s[14:15]
	global_store_dword v[184:185], v186, off
	s_add_u32 s10, s12, 0x100
	s_waitcnt vmcnt(1)
	v_cvt_scalef32_pk_bf16_fp8 v210, v112, 1.0
	v_cvt_scalef32_pk_bf16_fp8 v211, v112, 1.0 op_sel:[1,0,0]
	v_cvt_scalef32_pk_bf16_fp8 v212, v113, 1.0
	v_cvt_scalef32_pk_bf16_fp8 v213, v113, 1.0 op_sel:[1,0,0]
	v_mfma_f32_4x4x4_16b_bf16 v[228:231], v[210:211], v[108:109], 0
	v_cvt_scalef32_pk_bf16_fp8 v214, v114, 1.0
	v_cvt_scalef32_pk_bf16_fp8 v215, v114, 1.0 op_sel:[1,0,0]
	v_mfma_f32_4x4x4_16b_bf16 v[228:231], v[212:213], v[110:111], v[228:231]
	v_cvt_scalef32_pk_bf16_fp8 v216, v115, 1.0
	v_cvt_scalef32_pk_bf16_fp8 v217, v115, 1.0 op_sel:[1,0,0]
	v_mfma_f32_4x4x4_16b_bf16 v[228:231], v[214:215], v[100:101], v[228:231]
	v_cvt_scalef32_pk_bf16_fp8 v218, v116, 1.0
	v_cvt_scalef32_pk_bf16_fp8 v219, v116, 1.0 op_sel:[1,0,0]
	v_mfma_f32_4x4x4_16b_bf16 v[228:231], v[216:217], v[102:103], v[228:231]
	v_cvt_scalef32_pk_bf16_fp8 v220, v117, 1.0
	v_cvt_scalef32_pk_bf16_fp8 v221, v117, 1.0 op_sel:[1,0,0]
	v_mfma_f32_4x4x4_16b_bf16 v[232:235], v[218:219], v[108:109], 0
	v_cvt_scalef32_pk_bf16_fp8 v222, v118, 1.0
	v_cvt_scalef32_pk_bf16_fp8 v223, v118, 1.0 op_sel:[1,0,0]
	v_mfma_f32_4x4x4_16b_bf16 v[232:235], v[220:221], v[110:111], v[232:235]
	v_cvt_scalef32_pk_bf16_fp8 v224, v119, 1.0
	v_cvt_scalef32_pk_bf16_fp8 v225, v119, 1.0 op_sel:[1,0,0]
	v_mfma_f32_4x4x4_16b_bf16 v[232:235], v[222:223], v[100:101], v[232:235]
	v_cvt_scalef32_pk_bf16_fp8 v210, v120, 1.0
	v_cvt_scalef32_pk_bf16_fp8 v211, v120, 1.0 op_sel:[1,0,0]
	v_mfma_f32_4x4x4_16b_bf16 v[232:235], v[224:225], v[102:103], v[232:235]
	v_cvt_scalef32_pk_bf16_fp8 v212, v121, 1.0
	v_cvt_scalef32_pk_bf16_fp8 v213, v121, 1.0 op_sel:[1,0,0]
	v_cndmask_b32_e64 v184, v228, v229, s[22:23]
	v_cndmask_b32_e64 v184, v184, v230, s[24:25]
	v_cndmask_b32_e64 v184, v184, v231, s[26:27]
	v_mfma_f32_4x4x4_16b_bf16 v[228:231], v[210:211], v[108:109], 0
	v_cvt_scalef32_pk_bf16_fp8 v214, v122, 1.0
	v_cvt_scalef32_pk_bf16_fp8 v215, v122, 1.0 op_sel:[1,0,0]
	v_mfma_f32_4x4x4_16b_bf16 v[228:231], v[212:213], v[110:111], v[228:231]
	v_cvt_scalef32_pk_bf16_fp8 v216, v123, 1.0
	v_cvt_scalef32_pk_bf16_fp8 v217, v123, 1.0 op_sel:[1,0,0]
	v_mfma_f32_4x4x4_16b_bf16 v[228:231], v[214:215], v[100:101], v[228:231]
	v_cvt_scalef32_pk_bf16_fp8 v218, v124, 1.0
	v_cvt_scalef32_pk_bf16_fp8 v219, v124, 1.0 op_sel:[1,0,0]
	v_mfma_f32_4x4x4_16b_bf16 v[228:231], v[216:217], v[102:103], v[228:231]
	v_cvt_scalef32_pk_bf16_fp8 v220, v125, 1.0
	v_cvt_scalef32_pk_bf16_fp8 v221, v125, 1.0 op_sel:[1,0,0]
	v_cndmask_b32_e64 v185, v232, v233, s[22:23]
	v_cndmask_b32_e64 v185, v185, v234, s[24:25]
	v_cndmask_b32_e64 v185, v185, v235, s[26:27]
	v_mfma_f32_4x4x4_16b_bf16 v[232:235], v[218:219], v[108:109], 0
	v_cvt_scalef32_pk_bf16_fp8 v222, v126, 1.0
	v_cvt_scalef32_pk_bf16_fp8 v223, v126, 1.0 op_sel:[1,0,0]
	v_mfma_f32_4x4x4_16b_bf16 v[232:235], v[220:221], v[110:111], v[232:235]
	v_cvt_scalef32_pk_bf16_fp8 v224, v127, 1.0
	v_cvt_scalef32_pk_bf16_fp8 v225, v127, 1.0 op_sel:[1,0,0]
	v_mfma_f32_4x4x4_16b_bf16 v[232:235], v[222:223], v[100:101], v[232:235]
	v_cvt_scalef32_pk_bf16_fp8 v210, v128, 1.0
	v_cvt_scalef32_pk_bf16_fp8 v211, v128, 1.0 op_sel:[1,0,0]
	v_mfma_f32_4x4x4_16b_bf16 v[232:235], v[224:225], v[102:103], v[232:235]
	v_cvt_scalef32_pk_bf16_fp8 v212, v129, 1.0
	v_cvt_scalef32_pk_bf16_fp8 v213, v129, 1.0 op_sel:[1,0,0]
	v_cndmask_b32_e64 v186, v228, v229, s[22:23]
	v_cndmask_b32_e64 v186, v186, v230, s[24:25]
	v_cndmask_b32_e64 v186, v186, v231, s[26:27]
	v_mfma_f32_4x4x4_16b_bf16 v[228:231], v[210:211], v[108:109], 0
	v_cvt_scalef32_pk_bf16_fp8 v214, v130, 1.0
	v_cvt_scalef32_pk_bf16_fp8 v215, v130, 1.0 op_sel:[1,0,0]
	v_mfma_f32_4x4x4_16b_bf16 v[228:231], v[212:213], v[110:111], v[228:231]
	v_cvt_scalef32_pk_bf16_fp8 v216, v131, 1.0
	v_cvt_scalef32_pk_bf16_fp8 v217, v131, 1.0 op_sel:[1,0,0]
	v_mfma_f32_4x4x4_16b_bf16 v[228:231], v[214:215], v[100:101], v[228:231]
	v_cvt_scalef32_pk_bf16_fp8 v218, v132, 1.0
	v_cvt_scalef32_pk_bf16_fp8 v219, v132, 1.0 op_sel:[1,0,0]
	v_mfma_f32_4x4x4_16b_bf16 v[228:231], v[216:217], v[102:103], v[228:231]
	v_cvt_scalef32_pk_bf16_fp8 v220, v133, 1.0
	v_cvt_scalef32_pk_bf16_fp8 v221, v133, 1.0 op_sel:[1,0,0]
	v_cndmask_b32_e64 v187, v232, v233, s[22:23]
	v_cndmask_b32_e64 v187, v187, v234, s[24:25]
	v_cndmask_b32_e64 v187, v187, v235, s[26:27]
	v_mfma_f32_4x4x4_16b_bf16 v[232:235], v[218:219], v[108:109], 0
	v_cvt_scalef32_pk_bf16_fp8 v222, v134, 1.0
	v_cvt_scalef32_pk_bf16_fp8 v223, v134, 1.0 op_sel:[1,0,0]
	v_mfma_f32_4x4x4_16b_bf16 v[232:235], v[220:221], v[110:111], v[232:235]
	v_cvt_scalef32_pk_bf16_fp8 v224, v135, 1.0
	v_cvt_scalef32_pk_bf16_fp8 v225, v135, 1.0 op_sel:[1,0,0]
	v_mfma_f32_4x4x4_16b_bf16 v[232:235], v[222:223], v[100:101], v[232:235]
	v_cvt_scalef32_pk_bf16_fp8 v210, v136, 1.0
	v_cvt_scalef32_pk_bf16_fp8 v211, v136, 1.0 op_sel:[1,0,0]
	v_mfma_f32_4x4x4_16b_bf16 v[232:235], v[224:225], v[102:103], v[232:235]
	v_cvt_scalef32_pk_bf16_fp8 v212, v137, 1.0
	v_cvt_scalef32_pk_bf16_fp8 v213, v137, 1.0 op_sel:[1,0,0]
	v_cndmask_b32_e64 v188, v228, v229, s[22:23]
	v_cndmask_b32_e64 v188, v188, v230, s[24:25]
	v_cndmask_b32_e64 v188, v188, v231, s[26:27]
	v_mfma_f32_4x4x4_16b_bf16 v[228:231], v[210:211], v[108:109], 0
	v_cvt_scalef32_pk_bf16_fp8 v214, v138, 1.0
	v_cvt_scalef32_pk_bf16_fp8 v215, v138, 1.0 op_sel:[1,0,0]
	v_mfma_f32_4x4x4_16b_bf16 v[228:231], v[212:213], v[110:111], v[228:231]
	v_cvt_scalef32_pk_bf16_fp8 v216, v139, 1.0
	v_cvt_scalef32_pk_bf16_fp8 v217, v139, 1.0 op_sel:[1,0,0]
	v_mfma_f32_4x4x4_16b_bf16 v[228:231], v[214:215], v[100:101], v[228:231]
	v_cvt_scalef32_pk_bf16_fp8 v218, v140, 1.0
	v_cvt_scalef32_pk_bf16_fp8 v219, v140, 1.0 op_sel:[1,0,0]
	v_mfma_f32_4x4x4_16b_bf16 v[228:231], v[216:217], v[102:103], v[228:231]
	v_cvt_scalef32_pk_bf16_fp8 v220, v141, 1.0
	v_cvt_scalef32_pk_bf16_fp8 v221, v141, 1.0 op_sel:[1,0,0]
	v_cndmask_b32_e64 v189, v232, v233, s[22:23]
	v_cndmask_b32_e64 v189, v189, v234, s[24:25]
	v_cndmask_b32_e64 v189, v189, v235, s[26:27]
	v_mfma_f32_4x4x4_16b_bf16 v[232:235], v[218:219], v[108:109], 0
	v_cvt_scalef32_pk_bf16_fp8 v222, v142, 1.0
	v_cvt_scalef32_pk_bf16_fp8 v223, v142, 1.0 op_sel:[1,0,0]
	v_mfma_f32_4x4x4_16b_bf16 v[232:235], v[220:221], v[110:111], v[232:235]
	v_cvt_scalef32_pk_bf16_fp8 v224, v143, 1.0
	v_cvt_scalef32_pk_bf16_fp8 v225, v143, 1.0 op_sel:[1,0,0]
	v_mfma_f32_4x4x4_16b_bf16 v[232:235], v[222:223], v[100:101], v[232:235]
	v_cvt_scalef32_pk_bf16_fp8 v210, v144, 1.0
	v_cvt_scalef32_pk_bf16_fp8 v211, v144, 1.0 op_sel:[1,0,0]
	v_mfma_f32_4x4x4_16b_bf16 v[232:235], v[224:225], v[102:103], v[232:235]
	v_cvt_scalef32_pk_bf16_fp8 v212, v145, 1.0
	v_cvt_scalef32_pk_bf16_fp8 v213, v145, 1.0 op_sel:[1,0,0]
	v_cndmask_b32_e64 v190, v228, v229, s[22:23]
	v_cndmask_b32_e64 v190, v190, v230, s[24:25]
	v_cndmask_b32_e64 v190, v190, v231, s[26:27]
	v_mfma_f32_4x4x4_16b_bf16 v[228:231], v[210:211], v[108:109], 0
	v_cvt_scalef32_pk_bf16_fp8 v214, v146, 1.0
	v_cvt_scalef32_pk_bf16_fp8 v215, v146, 1.0 op_sel:[1,0,0]
	v_mfma_f32_4x4x4_16b_bf16 v[228:231], v[212:213], v[110:111], v[228:231]
	v_cvt_scalef32_pk_bf16_fp8 v216, v147, 1.0
	v_cvt_scalef32_pk_bf16_fp8 v217, v147, 1.0 op_sel:[1,0,0]
	v_mfma_f32_4x4x4_16b_bf16 v[228:231], v[214:215], v[100:101], v[228:231]
	v_cvt_scalef32_pk_bf16_fp8 v218, v148, 1.0
	v_cvt_scalef32_pk_bf16_fp8 v219, v148, 1.0 op_sel:[1,0,0]
	v_mfma_f32_4x4x4_16b_bf16 v[228:231], v[216:217], v[102:103], v[228:231]
	v_cvt_scalef32_pk_bf16_fp8 v220, v149, 1.0
	v_cvt_scalef32_pk_bf16_fp8 v221, v149, 1.0 op_sel:[1,0,0]
	v_cndmask_b32_e64 v191, v232, v233, s[22:23]
	v_cndmask_b32_e64 v191, v191, v234, s[24:25]
	v_cndmask_b32_e64 v191, v191, v235, s[26:27]
	v_mfma_f32_4x4x4_16b_bf16 v[232:235], v[218:219], v[108:109], 0
	v_cvt_scalef32_pk_bf16_fp8 v222, v150, 1.0
	v_cvt_scalef32_pk_bf16_fp8 v223, v150, 1.0 op_sel:[1,0,0]
	v_mfma_f32_4x4x4_16b_bf16 v[232:235], v[220:221], v[110:111], v[232:235]
	v_cvt_scalef32_pk_bf16_fp8 v224, v151, 1.0
	v_cvt_scalef32_pk_bf16_fp8 v225, v151, 1.0 op_sel:[1,0,0]
	v_mfma_f32_4x4x4_16b_bf16 v[232:235], v[222:223], v[100:101], v[232:235]
	v_cvt_scalef32_pk_bf16_fp8 v210, v152, 1.0
	v_cvt_scalef32_pk_bf16_fp8 v211, v152, 1.0 op_sel:[1,0,0]
	v_mfma_f32_4x4x4_16b_bf16 v[232:235], v[224:225], v[102:103], v[232:235]
	v_cvt_scalef32_pk_bf16_fp8 v212, v153, 1.0
	v_cvt_scalef32_pk_bf16_fp8 v213, v153, 1.0 op_sel:[1,0,0]
	v_cndmask_b32_e64 v192, v228, v229, s[22:23]
	v_cndmask_b32_e64 v192, v192, v230, s[24:25]
	v_cndmask_b32_e64 v192, v192, v231, s[26:27]
	v_mfma_f32_4x4x4_16b_bf16 v[228:231], v[210:211], v[108:109], 0
	v_cvt_scalef32_pk_bf16_fp8 v214, v154, 1.0
	v_cvt_scalef32_pk_bf16_fp8 v215, v154, 1.0 op_sel:[1,0,0]
	v_mfma_f32_4x4x4_16b_bf16 v[228:231], v[212:213], v[110:111], v[228:231]
	v_cvt_scalef32_pk_bf16_fp8 v216, v155, 1.0
	v_cvt_scalef32_pk_bf16_fp8 v217, v155, 1.0 op_sel:[1,0,0]
	v_mfma_f32_4x4x4_16b_bf16 v[228:231], v[214:215], v[100:101], v[228:231]
	v_cvt_scalef32_pk_bf16_fp8 v218, v156, 1.0
	v_cvt_scalef32_pk_bf16_fp8 v219, v156, 1.0 op_sel:[1,0,0]
	v_mfma_f32_4x4x4_16b_bf16 v[228:231], v[216:217], v[102:103], v[228:231]
	v_cvt_scalef32_pk_bf16_fp8 v220, v157, 1.0
	v_cvt_scalef32_pk_bf16_fp8 v221, v157, 1.0 op_sel:[1,0,0]
	v_cndmask_b32_e64 v193, v232, v233, s[22:23]
	v_cndmask_b32_e64 v193, v193, v234, s[24:25]
	v_cndmask_b32_e64 v193, v193, v235, s[26:27]
	v_mfma_f32_4x4x4_16b_bf16 v[232:235], v[218:219], v[108:109], 0
	v_cvt_scalef32_pk_bf16_fp8 v222, v158, 1.0
	v_cvt_scalef32_pk_bf16_fp8 v223, v158, 1.0 op_sel:[1,0,0]
	v_mfma_f32_4x4x4_16b_bf16 v[232:235], v[220:221], v[110:111], v[232:235]
	v_cvt_scalef32_pk_bf16_fp8 v224, v159, 1.0
	v_cvt_scalef32_pk_bf16_fp8 v225, v159, 1.0 op_sel:[1,0,0]
	v_mfma_f32_4x4x4_16b_bf16 v[232:235], v[222:223], v[100:101], v[232:235]
	v_cvt_scalef32_pk_bf16_fp8 v210, v160, 1.0
	v_cvt_scalef32_pk_bf16_fp8 v211, v160, 1.0 op_sel:[1,0,0]
	v_mfma_f32_4x4x4_16b_bf16 v[232:235], v[224:225], v[102:103], v[232:235]
	v_cvt_scalef32_pk_bf16_fp8 v212, v161, 1.0
	v_cvt_scalef32_pk_bf16_fp8 v213, v161, 1.0 op_sel:[1,0,0]
	v_cndmask_b32_e64 v194, v228, v229, s[22:23]
	v_cndmask_b32_e64 v194, v194, v230, s[24:25]
	v_cndmask_b32_e64 v194, v194, v231, s[26:27]
	v_mfma_f32_4x4x4_16b_bf16 v[228:231], v[210:211], v[108:109], 0
	v_cvt_scalef32_pk_bf16_fp8 v214, v162, 1.0
	v_cvt_scalef32_pk_bf16_fp8 v215, v162, 1.0 op_sel:[1,0,0]
	v_mfma_f32_4x4x4_16b_bf16 v[228:231], v[212:213], v[110:111], v[228:231]
	v_cvt_scalef32_pk_bf16_fp8 v216, v163, 1.0
	v_cvt_scalef32_pk_bf16_fp8 v217, v163, 1.0 op_sel:[1,0,0]
	v_mfma_f32_4x4x4_16b_bf16 v[228:231], v[214:215], v[100:101], v[228:231]
	v_cvt_scalef32_pk_bf16_fp8 v218, v164, 1.0
	v_cvt_scalef32_pk_bf16_fp8 v219, v164, 1.0 op_sel:[1,0,0]
	v_mfma_f32_4x4x4_16b_bf16 v[228:231], v[216:217], v[102:103], v[228:231]
	v_cvt_scalef32_pk_bf16_fp8 v220, v165, 1.0
	v_cvt_scalef32_pk_bf16_fp8 v221, v165, 1.0 op_sel:[1,0,0]
	v_cndmask_b32_e64 v195, v232, v233, s[22:23]
	v_cndmask_b32_e64 v195, v195, v234, s[24:25]
	v_cndmask_b32_e64 v195, v195, v235, s[26:27]
	v_mfma_f32_4x4x4_16b_bf16 v[232:235], v[218:219], v[108:109], 0
	v_cvt_scalef32_pk_bf16_fp8 v222, v166, 1.0
	v_cvt_scalef32_pk_bf16_fp8 v223, v166, 1.0 op_sel:[1,0,0]
	v_mfma_f32_4x4x4_16b_bf16 v[232:235], v[220:221], v[110:111], v[232:235]
	v_cvt_scalef32_pk_bf16_fp8 v224, v167, 1.0
	v_cvt_scalef32_pk_bf16_fp8 v225, v167, 1.0 op_sel:[1,0,0]
	v_mfma_f32_4x4x4_16b_bf16 v[232:235], v[222:223], v[100:101], v[232:235]
	v_cvt_scalef32_pk_bf16_fp8 v210, v168, 1.0
	v_cvt_scalef32_pk_bf16_fp8 v211, v168, 1.0 op_sel:[1,0,0]
	v_mfma_f32_4x4x4_16b_bf16 v[232:235], v[224:225], v[102:103], v[232:235]
	v_cvt_scalef32_pk_bf16_fp8 v212, v169, 1.0
	v_cvt_scalef32_pk_bf16_fp8 v213, v169, 1.0 op_sel:[1,0,0]
	v_cndmask_b32_e64 v196, v228, v229, s[22:23]
	v_cndmask_b32_e64 v196, v196, v230, s[24:25]
	v_cndmask_b32_e64 v196, v196, v231, s[26:27]
	v_mfma_f32_4x4x4_16b_bf16 v[228:231], v[210:211], v[108:109], 0
	v_cvt_scalef32_pk_bf16_fp8 v214, v170, 1.0
	v_cvt_scalef32_pk_bf16_fp8 v215, v170, 1.0 op_sel:[1,0,0]
	v_mfma_f32_4x4x4_16b_bf16 v[228:231], v[212:213], v[110:111], v[228:231]
	v_cvt_scalef32_pk_bf16_fp8 v216, v171, 1.0
	v_cvt_scalef32_pk_bf16_fp8 v217, v171, 1.0 op_sel:[1,0,0]
	v_mfma_f32_4x4x4_16b_bf16 v[228:231], v[214:215], v[100:101], v[228:231]
	v_cvt_scalef32_pk_bf16_fp8 v218, v172, 1.0
	v_cvt_scalef32_pk_bf16_fp8 v219, v172, 1.0 op_sel:[1,0,0]
	v_mfma_f32_4x4x4_16b_bf16 v[228:231], v[216:217], v[102:103], v[228:231]
	v_cvt_scalef32_pk_bf16_fp8 v220, v173, 1.0
	v_cvt_scalef32_pk_bf16_fp8 v221, v173, 1.0 op_sel:[1,0,0]
	v_cndmask_b32_e64 v197, v232, v233, s[22:23]
	v_cndmask_b32_e64 v197, v197, v234, s[24:25]
	v_cndmask_b32_e64 v197, v197, v235, s[26:27]
	v_mfma_f32_4x4x4_16b_bf16 v[232:235], v[218:219], v[108:109], 0
	v_cvt_scalef32_pk_bf16_fp8 v222, v174, 1.0
	v_cvt_scalef32_pk_bf16_fp8 v223, v174, 1.0 op_sel:[1,0,0]
	v_mfma_f32_4x4x4_16b_bf16 v[232:235], v[220:221], v[110:111], v[232:235]
	v_cvt_scalef32_pk_bf16_fp8 v224, v175, 1.0
	v_cvt_scalef32_pk_bf16_fp8 v225, v175, 1.0 op_sel:[1,0,0]
	v_mfma_f32_4x4x4_16b_bf16 v[232:235], v[222:223], v[100:101], v[232:235]
	s_nop 1
	v_mfma_f32_4x4x4_16b_bf16 v[232:235], v[224:225], v[102:103], v[232:235]
	v_cndmask_b32_e64 v198, v228, v229, s[22:23]
	v_cndmask_b32_e64 v198, v198, v230, s[24:25]
	v_cndmask_b32_e64 v198, v198, v231, s[26:27]
	s_nop 4
	v_cndmask_b32_e64 v199, v232, v233, s[22:23]
	v_cndmask_b32_e64 v199, v199, v234, s[24:25]
	v_cndmask_b32_e64 v199, v199, v235, s[26:27]
	v_cndmask_b32_e64 v200, v184, v192, s[4:5]
	v_cndmask_b32_e64 v201, v192, v184, s[4:5]
	v_cndmask_b32_e64 v202, v185, v193, s[4:5]
	v_cndmask_b32_e64 v203, v193, v185, s[4:5]
	v_cndmask_b32_e64 v204, v186, v194, s[4:5]
	v_cndmask_b32_e64 v205, v194, v186, s[4:5]
	v_cndmask_b32_e64 v236, v187, v195, s[4:5]
	v_cndmask_b32_e64 v237, v195, v187, s[4:5]
	v_cndmask_b32_e64 v238, v188, v196, s[4:5]
	v_cndmask_b32_e64 v239, v196, v188, s[4:5]
	v_cndmask_b32_e64 v240, v189, v197, s[4:5]
	v_cndmask_b32_e64 v241, v197, v189, s[4:5]
	v_cndmask_b32_e64 v242, v190, v198, s[4:5]
	v_cndmask_b32_e64 v243, v198, v190, s[4:5]
	v_cndmask_b32_e64 v244, v191, v199, s[4:5]
	v_cndmask_b32_e64 v245, v199, v191, s[4:5]
	v_add_f32_dpp v246, v200, v201 row_half_mirror row_mask:0xf bank_mask:0xf
	v_add_f32_dpp v247, v202, v203 row_half_mirror row_mask:0xf bank_mask:0xf
	v_add_f32_dpp v248, v204, v205 row_half_mirror row_mask:0xf bank_mask:0xf
	v_add_f32_dpp v249, v236, v237 row_half_mirror row_mask:0xf bank_mask:0xf
	v_add_f32_dpp v226, v238, v239 row_half_mirror row_mask:0xf bank_mask:0xf
	v_add_f32_dpp v227, v240, v241 row_half_mirror row_mask:0xf bank_mask:0xf
	v_add_f32_dpp v210, v242, v243 row_half_mirror row_mask:0xf bank_mask:0xf
	v_add_f32_dpp v211, v244, v245 row_half_mirror row_mask:0xf bank_mask:0xf
	v_cndmask_b32_e64 v200, v246, v226, s[2:3]
	v_cndmask_b32_e64 v201, v226, v246, s[2:3]
	v_cndmask_b32_e64 v202, v247, v227, s[2:3]
	v_cndmask_b32_e64 v203, v227, v247, s[2:3]
	v_cndmask_b32_e64 v204, v248, v210, s[2:3]
	v_cndmask_b32_e64 v205, v210, v248, s[2:3]
	v_cndmask_b32_e64 v236, v249, v211, s[2:3]
	v_cndmask_b32_e64 v237, v211, v249, s[2:3]
	v_add_f32_dpp v212, v200, v201 quad_perm:[2,3,0,1] row_mask:0xf bank_mask:0xf
	v_add_f32_dpp v213, v202, v203 quad_perm:[2,3,0,1] row_mask:0xf bank_mask:0xf
	v_add_f32_dpp v214, v204, v205 quad_perm:[2,3,0,1] row_mask:0xf bank_mask:0xf
	v_add_f32_dpp v215, v236, v237 quad_perm:[2,3,0,1] row_mask:0xf bank_mask:0xf
	v_cndmask_b32_e64 v200, v212, v214, s[0:1]
	v_cndmask_b32_e64 v201, v214, v212, s[0:1]
	v_cndmask_b32_e64 v202, v213, v215, s[0:1]
	v_cndmask_b32_e64 v203, v215, v213, s[0:1]
	s_nop 1
	v_add_f32_dpp v216, v200, v201 quad_perm:[1,0,3,2] row_mask:0xf bank_mask:0xf
	v_add_f32_dpp v217, v202, v203 quad_perm:[1,0,3,2] row_mask:0xf bank_mask:0xf
	s_ashr_i32 s11, s10, 31
	s_lshl_b64 s[10:11], s[10:11], 8
	v_cvt_pk_bf16_f32 v186, v216, v217
	v_lshl_add_u64 v[184:185], v[178:179], 0, s[10:11]
	global_store_dword v[184:185], v186, off

; DI int tidx() { int t = threadIdx.x & 255; asm volatile("" : "+v"(t)); return t; }
; DI int ftid() { int t = threadIdx.x; asm volatile("" : "+v"(t)); return t; }
; #define PU_IDX(t, E, C) do { const char* eb_ = eiu + (size_t)(t) * 512; const char* cb_ = cfu + (size_t)(t) * 512; \
;     _Pragma("unroll") for (int q = 0; q < 4; ++q) { E[q] = *(const i32x4_t*)(eb_ + (eio + 16u * q)); C[q] = *(const f32x4*)(cb_ + (eio + 16u * q)); } } while (0)
; #define PU_TAB(E, W) do { _Pragma("unroll") for (int q = 0; q < 16; ++q) W[q] = *(const u32x4*)(tabu + ((unsigned)E[q >> 2][q & 3] * 128u + tabo)); } while (0)
; DI void phase_peerup(const Params& p, int bid, int nb) {
;   const int lane = tidx() & 63, wid = __builtin_amdgcn_readfirstlane(ftid() >> 6), e8 = lane >> 3, c = lane & 7;
;   const int x = bid & 7, gw = (bid >> 3) * 8 + wid, nw = (nb >> 3) * 8;
;   const char* tabu = p.ws + WS_PV + (size_t)x * 16384 * 128; const unsigned tabo = 16u * c;
;   const char* eiu = p.ws + WS_EIDX; const char* cfu = p.ws + WS_COEF; const unsigned eio = 64u * e8;
;   bf16_t* y2 = (bf16_t*)(p.ws + WS_Y2) + 128 * x + 16 * c; float* ssq = (float*)(p.ws + WS_SSQ) + (size_t)x * T_;
;   const bool b3 = (lane & 8) != 0;
;     ...
;   i32x4_t eA[4], eB[4]; f32x4 cA[4], cB[4]; u32x4 w[16];
;   int t = gw; if (t >= T_) return;
;   PU_IDX(t, eA, cA);
;   for (;;) {
;     PU_TAB(eA, w);
;     const int t1 = t + nw; if (t1 < T_) PU_IDX(t1, eB, cB);
.LBB0_1876:
	s_or_b64 exec, exec, s[0:1]
	s_waitcnt vmcnt(14)
	v_mov_b32_e32 v32, v206
	s_waitcnt lgkmcnt(0)
	s_barrier
	s_nop 0
	v_readfirstlane_b32 s0, v207
	s_ashr_i32 s0, s0, 6
	s_add_i32 s8, s0, s49
	s_cmpk_gt_i32 s8, 0x7fff
	s_cbranch_scc1 .LBB0_1889
	s_add_u32 s0, s84, s48
	s_addc_u32 s1, s85, 0
	s_add_u32 s4, s0, 0xf000000
	s_addc_u32 s5, s1, 0
	s_lshl_b32 s0, s19, 17
	s_add_u32 s0, s84, s0
	s_addc_u32 s1, s85, 0
	s_add_u32 s12, s0, 0x3000000
	v_lshlrev_b32_e32 v0, 4, v32
	s_addc_u32 s13, s1, 0
	s_lshl_b32 s0, s19, 8
	v_and_b32_e32 v136, 0x70, v0
	s_add_u32 s0, s58, s0
	s_addc_u32 s1, s59, 0
	v_lshlrev_b32_e32 v128, 1, v136
	v_mov_b32_e32 v129, 0
	s_ashr_i32 s9, s8, 31
	v_lshl_add_u64 v[34:35], s[0:1], 0, v[128:129]
	s_lshl_b64 s[0:1], s[8:9], 9
	s_add_u32 s2, s16, s0
	v_bfe_u32 v33, v32, 3, 3
	s_addc_u32 s3, s17, s1
	v_lshlrev_b32_e32 v128, 6, v33
	s_add_u32 s0, s56, s0
	s_addc_u32 s1, s57, s1
	v_and_b32_e32 v36, 8, v32
	v_cmp_eq_u32_e64 s[0:1], 0, v36
	v_and_b32_e32 v36, 63, v32
	v_lshlrev_b32_e32 v32, 2, v33
	v_mov_b32_e32 v33, v129
	v_lshl_add_u64 v[130:131], v[34:35], 0, v[32:33]
	v_cmp_eq_u32_e64 s[2:3], 0, v36
	v_lshl_add_u64 v[132:133], s[16:17], 0, v[128:129]
	v_lshl_add_u64 v[134:135], s[56:57], 0, v[128:129]
	s_and_b32 s14, s90, -16
	s_mov_b32 s20, s8
	s_mov_b32 s23, 0
	s_add_u32 s22, s20, 0x0
	s_lshl_b32 s22, s22, 9
	v_lshl_add_u64 v[12:13], v[132:133], 0, s[22:23]
	global_load_dwordx4 v[0:3], v[12:13], off offset:48
	global_load_dwordx4 v[4:7], v[12:13], off offset:32
	global_load_dwordx4 v[8:11], v[12:13], off offset:16
	s_nop 0
	global_load_dwordx4 v[12:15], v[12:13], off
	s_add_u32 s22, s20, 0x0
	s_lshl_b32 s22, s22, 9
	v_lshl_add_u64 v[28:29], v[134:135], 0, s[22:23]
	global_load_dwordx4 v[16:19], v[28:29], off offset:48
	global_load_dwordx4 v[20:23], v[28:29], off offset:32
	global_load_dwordx4 v[24:27], v[28:29], off offset:16
	s_nop 0
	global_load_dwordx4 v[28:31], v[28:29], off
	s_add_u32 s22, s20, 0x100
	s_lshl_b32 s22, s22, 9
	v_lshl_add_u64 v[32:33], v[132:133], 0, s[22:23]
	global_load_dwordx4 v[44:47], v[32:33], off offset:48
	global_load_dwordx4 v[40:43], v[32:33], off offset:32
	global_load_dwordx4 v[36:39], v[32:33], off offset:16
	s_nop 0
	global_load_dwordx4 v[32:35], v[32:33], off
	s_add_u32 s22, s20, 0x100
	s_lshl_b32 s22, s22, 9
	v_lshl_add_u64 v[48:49], v[134:135], 0, s[22:23]
	global_load_dwordx4 v[60:63], v[48:49], off offset:48
	global_load_dwordx4 v[56:59], v[48:49], off offset:32
	global_load_dwordx4 v[52:55], v[48:49], off offset:16
	s_nop 0
	global_load_dwordx4 v[48:51], v[48:49], off
	s_waitcnt vmcnt(12)
	v_lshl_or_b32 v12, v12, 7, v136
	global_load_dwordx4 v[124:127], v12, s[4:5] sc0
	v_lshl_or_b32 v13, v13, 7, v136
	global_load_dwordx4 v[120:123], v13, s[4:5] sc0
	v_lshl_or_b32 v14, v14, 7, v136
	global_load_dwordx4 v[116:119], v14, s[4:5] sc0
	v_lshl_or_b32 v15, v15, 7, v136
	global_load_dwordx4 v[112:115], v15, s[4:5] sc0
	v_lshl_or_b32 v8, v8, 7, v136
	global_load_dwordx4 v[108:111], v8, s[4:5] sc0
	v_lshl_or_b32 v9, v9, 7, v136
	global_load_dwordx4 v[104:107], v9, s[4:5] sc0
	v_lshl_or_b32 v10, v10, 7, v136
	global_load_dwordx4 v[100:103], v10, s[4:5] sc0
	v_lshl_or_b32 v11, v11, 7, v136
	global_load_dwordx4 v[96:99], v11, s[4:5] sc0
	v_lshl_or_b32 v4, v4, 7, v136
	global_load_dwordx4 v[92:95], v4, s[4:5] sc0
	v_lshl_or_b32 v5, v5, 7, v136
	global_load_dwordx4 v[88:91], v5, s[4:5] sc0
	v_lshl_or_b32 v6, v6, 7, v136
	global_load_dwordx4 v[84:87], v6, s[4:5] sc0
	v_lshl_or_b32 v7, v7, 7, v136
	global_load_dwordx4 v[80:83], v7, s[4:5] sc0
	v_lshl_or_b32 v0, v0, 7, v136
	global_load_dwordx4 v[76:79], v0, s[4:5] sc0
	v_lshl_or_b32 v1, v1, 7, v136
	global_load_dwordx4 v[72:75], v1, s[4:5] sc0
	v_lshl_or_b32 v2, v2, 7, v136
	global_load_dwordx4 v[68:71], v2, s[4:5] sc0
	v_lshl_or_b32 v3, v3, 7, v136
	global_load_dwordx4 v[64:67], v3, s[4:5] sc0
	s_add_u32 s22, s20, 0x200
	s_lshl_b32 s22, s22, 9
	v_lshl_add_u64 v[12:13], v[132:133], 0, s[22:23]
	global_load_dwordx4 v[0:3], v[12:13], off offset:48
	global_load_dwordx4 v[4:7], v[12:13], off offset:32
	global_load_dwordx4 v[8:11], v[12:13], off offset:16
	s_nop 0
	global_load_dwordx4 v[12:15], v[12:13], off
	s_waitcnt vmcnt(24)
	v_lshl_or_b32 v32, v32, 7, v136
	global_load_dwordx4 v[240:243], v32, s[4:5] sc0
	v_lshl_or_b32 v33, v33, 7, v136
	global_load_dwordx4 v[236:239], v33, s[4:5] sc0
	v_lshl_or_b32 v34, v34, 7, v136
	global_load_dwordx4 v[232:235], v34, s[4:5] sc0
	v_lshl_or_b32 v35, v35, 7, v136
	global_load_dwordx4 v[228:231], v35, s[4:5] sc0
	v_lshl_or_b32 v36, v36, 7, v136
	global_load_dwordx4 v[224:227], v36, s[4:5] sc0
	v_lshl_or_b32 v37, v37, 7, v136
	global_load_dwordx4 v[220:223], v37, s[4:5] sc0
	v_lshl_or_b32 v38, v38, 7, v136
	global_load_dwordx4 v[216:219], v38, s[4:5] sc0
	v_lshl_or_b32 v39, v39, 7, v136
	global_load_dwordx4 v[212:215], v39, s[4:5] sc0
	v_lshl_or_b32 v40, v40, 7, v136
	global_load_dwordx4 v[200:203], v40, s[4:5] sc0
	v_lshl_or_b32 v41, v41, 7, v136
	global_load_dwordx4 v[196:199], v41, s[4:5] sc0
	v_lshl_or_b32 v42, v42, 7, v136
	global_load_dwordx4 v[192:195], v42, s[4:5] sc0
	v_lshl_or_b32 v43, v43, 7, v136
	global_load_dwordx4 v[184:187], v43, s[4:5] sc0
	v_lshl_or_b32 v44, v44, 7, v136
	global_load_dwordx4 v[180:183], v44, s[4:5] sc0
	v_lshl_or_b32 v45, v45, 7, v136
	global_load_dwordx4 v[172:175], v45, s[4:5] sc0
	v_lshl_or_b32 v46, v46, 7, v136
	global_load_dwordx4 v[168:171], v46, s[4:5] sc0
	v_lshl_or_b32 v47, v47, 7, v136
	global_load_dwordx4 v[164:167], v47, s[4:5] sc0
	s_add_u32 s22, s20, 0x300
	s_lshl_b32 s22, s22, 9
	v_lshl_add_u64 v[32:33], v[132:133], 0, s[22:23]
	global_load_dwordx4 v[44:47], v[32:33], off offset:48
	global_load_dwordx4 v[40:43], v[32:33], off offset:32
	global_load_dwordx4 v[36:39], v[32:33], off offset:16
	s_nop 0
	global_load_dwordx4 v[32:35], v[32:33], off
	s_mov_b32 s8, s20
	s_waitcnt vmcnt(20)
; DI void unpack8x2_fp8(const u32x4 w, f32x2 (&f)[8]) {
; #pragma unroll
;   for (int i = 0; i < 4; ++i) { f[2 * i] = __builtin_amdgcn_cvt_pk_f32_fp8((int)w[i], false); f[2 * i + 1] = __builtin_amdgcn_cvt_pk_f32_fp8((int)w[i], true); }
; }
	v_cvt_pk_f32_fp8_e32 v[138:139], v124
	v_cvt_pk_f32_fp8_sdwa v[140:141], v124 src0_sel:WORD_1
	v_cvt_pk_f32_fp8_e32 v[142:143], v125
	v_cvt_pk_f32_fp8_sdwa v[124:125], v125 src0_sel:WORD_1
	v_cvt_pk_f32_fp8_e32 v[144:145], v126
	v_cvt_pk_f32_fp8_sdwa v[146:147], v126 src0_sel:WORD_1
	v_cvt_pk_f32_fp8_e32 v[148:149], v127
	v_cvt_pk_f32_fp8_sdwa v[126:127], v127 src0_sel:WORD_1
	v_cvt_pk_f32_fp8_e32 v[150:151], v120
	v_cvt_pk_f32_fp8_sdwa v[152:153], v120 src0_sel:WORD_1
	v_cvt_pk_f32_fp8_e32 v[154:155], v121
	v_cvt_pk_f32_fp8_sdwa v[120:121], v121 src0_sel:WORD_1
	v_cvt_pk_f32_fp8_e32 v[156:157], v122
	v_cvt_pk_f32_fp8_sdwa v[158:159], v122 src0_sel:WORD_1
	v_cvt_pk_f32_fp8_e32 v[160:161], v123
	v_cvt_pk_f32_fp8_sdwa v[122:123], v123 src0_sel:WORD_1
	v_pk_fma_f32 v[138:139], v[138:139], v[28:29], 0 op_sel_hi:[1,0,0]
	v_pk_fma_f32 v[140:141], v[140:141], v[28:29], 0 op_sel_hi:[1,0,0]
	v_pk_fma_f32 v[142:143], v[142:143], v[28:29], 0 op_sel_hi:[1,0,0]
	v_pk_fma_f32 v[124:125], v[124:125], v[28:29], 0 op_sel_hi:[1,0,0]
	v_pk_fma_f32 v[144:145], v[144:145], v[28:29], 0 op_sel_hi:[1,0,0]
	v_pk_fma_f32 v[146:147], v[146:147], v[28:29], 0 op_sel_hi:[1,0,0]
	v_pk_fma_f32 v[148:149], v[148:149], v[28:29], 0 op_sel_hi:[1,0,0]
	v_pk_fma_f32 v[126:127], v[126:127], v[28:29], 0 op_sel_hi:[1,0,0]
	v_pk_fma_f32 v[138:139], v[150:151], v[28:29], v[138:139] op_sel:[0,1,0]
	v_pk_fma_f32 v[140:141], v[152:153], v[28:29], v[140:141] op_sel:[0,1,0]
	v_pk_fma_f32 v[142:143], v[154:155], v[28:29], v[142:143] op_sel:[0,1,0]
	v_pk_fma_f32 v[120:121], v[120:121], v[28:29], v[124:125] op_sel:[0,1,0]
	v_pk_fma_f32 v[124:125], v[156:157], v[28:29], v[144:145] op_sel:[0,1,0]
	v_pk_fma_f32 v[144:145], v[158:159], v[28:29], v[146:147] op_sel:[0,1,0]
	v_pk_fma_f32 v[146:147], v[160:161], v[28:29], v[148:149] op_sel:[0,1,0]
	v_pk_fma_f32 v[122:123], v[122:123], v[28:29], v[126:127] op_sel:[0,1,0]
	v_cvt_pk_f32_fp8_e32 v[126:127], v116
	v_cvt_pk_f32_fp8_sdwa v[148:149], v116 src0_sel:WORD_1
	v_cvt_pk_f32_fp8_e32 v[150:151], v117
	v_cvt_pk_f32_fp8_sdwa v[116:117], v117 src0_sel:WORD_1
	v_cvt_pk_f32_fp8_e32 v[152:153], v118
	v_cvt_pk_f32_fp8_sdwa v[154:155], v118 src0_sel:WORD_1
	v_cvt_pk_f32_fp8_e32 v[156:157], v119
	v_cvt_pk_f32_fp8_sdwa v[118:119], v119 src0_sel:WORD_1
	v_pk_fma_f32 v[126:127], v[126:127], v[30:31], v[138:139] op_sel_hi:[1,0,1]
	v_pk_fma_f32 v[138:139], v[148:149], v[30:31], v[140:141] op_sel_hi:[1,0,1]
	v_pk_fma_f32 v[140:141], v[150:151], v[30:31], v[142:143] op_sel_hi:[1,0,1]
	v_pk_fma_f32 v[116:117], v[116:117], v[30:31], v[120:121] op_sel_hi:[1,0,1]
	v_pk_fma_f32 v[120:121], v[152:153], v[30:31], v[124:125] op_sel_hi:[1,0,1]
	v_pk_fma_f32 v[124:125], v[154:155], v[30:31], v[144:145] op_sel_hi:[1,0,1]
	v_pk_fma_f32 v[142:143], v[156:157], v[30:31], v[146:147] op_sel_hi:[1,0,1]
	v_pk_fma_f32 v[118:119], v[118:119], v[30:31], v[122:123] op_sel_hi:[1,0,1]
	v_cvt_pk_f32_fp8_e32 v[122:123], v112
	v_cvt_pk_f32_fp8_sdwa v[144:145], v112 src0_sel:WORD_1
	v_cvt_pk_f32_fp8_e32 v[146:147], v113
	v_cvt_pk_f32_fp8_sdwa v[112:113], v113 src0_sel:WORD_1
	v_cvt_pk_f32_fp8_e32 v[148:149], v114
	v_cvt_pk_f32_fp8_sdwa v[150:151], v114 src0_sel:WORD_1
	v_cvt_pk_f32_fp8_e32 v[152:153], v115
	v_cvt_pk_f32_fp8_sdwa v[114:115], v115 src0_sel:WORD_1
	v_mov_b32_e32 v128, v31
	v_pk_fma_f32 v[122:123], v[122:123], v[128:129], v[126:127] op_sel_hi:[1,0,1]
	v_pk_fma_f32 v[126:127], v[144:145], v[128:129], v[138:139] op_sel_hi:[1,0,1]
	v_pk_fma_f32 v[138:139], v[146:147], v[128:129], v[140:141] op_sel_hi:[1,0,1]
	v_pk_fma_f32 v[112:113], v[112:113], v[128:129], v[116:117] op_sel_hi:[1,0,1]
	v_pk_fma_f32 v[116:117], v[148:149], v[128:129], v[120:121] op_sel_hi:[1,0,1]
	v_pk_fma_f32 v[120:121], v[150:151], v[128:129], v[124:125] op_sel_hi:[1,0,1]
	v_pk_fma_f32 v[124:125], v[152:153], v[128:129], v[142:143] op_sel_hi:[1,0,1]
	v_pk_fma_f32 v[114:115], v[114:115], v[128:129], v[118:119] op_sel_hi:[1,0,1]
	v_cvt_pk_f32_fp8_e32 v[118:119], v108
	v_cvt_pk_f32_fp8_sdwa v[140:141], v108 src0_sel:WORD_1
	v_cvt_pk_f32_fp8_e32 v[142:143], v109
	v_cvt_pk_f32_fp8_sdwa v[108:109], v109 src0_sel:WORD_1
	v_cvt_pk_f32_fp8_e32 v[144:145], v110
	v_cvt_pk_f32_fp8_sdwa v[146:147], v110 src0_sel:WORD_1
	v_cvt_pk_f32_fp8_e32 v[148:149], v111
	v_cvt_pk_f32_fp8_sdwa v[110:111], v111 src0_sel:WORD_1
	v_pk_fma_f32 v[118:119], v[118:119], v[24:25], v[122:123] op_sel_hi:[1,0,1]
	v_pk_fma_f32 v[122:123], v[140:141], v[24:25], v[126:127] op_sel_hi:[1,0,1]
	v_pk_fma_f32 v[126:127], v[142:143], v[24:25], v[138:139] op_sel_hi:[1,0,1]
	v_pk_fma_f32 v[108:109], v[108:109], v[24:25], v[112:113] op_sel_hi:[1,0,1]
	v_pk_fma_f32 v[112:113], v[144:145], v[24:25], v[116:117] op_sel_hi:[1,0,1]
	v_pk_fma_f32 v[116:117], v[146:147], v[24:25], v[120:121] op_sel_hi:[1,0,1]
	v_pk_fma_f32 v[120:121], v[148:149], v[24:25], v[124:125] op_sel_hi:[1,0,1]
	v_pk_fma_f32 v[110:111], v[110:111], v[24:25], v[114:115] op_sel_hi:[1,0,1]
	v_cvt_pk_f32_fp8_e32 v[114:115], v104
	v_cvt_pk_f32_fp8_sdwa v[124:125], v104 src0_sel:WORD_1
	v_cvt_pk_f32_fp8_e32 v[138:139], v105
	v_cvt_pk_f32_fp8_sdwa v[104:105], v105 src0_sel:WORD_1
	v_cvt_pk_f32_fp8_e32 v[140:141], v106
	v_cvt_pk_f32_fp8_sdwa v[142:143], v106 src0_sel:WORD_1
	v_cvt_pk_f32_fp8_e32 v[144:145], v107
	v_cvt_pk_f32_fp8_sdwa v[106:107], v107 src0_sel:WORD_1
	v_pk_fma_f32 v[114:115], v[114:115], v[24:25], v[118:119] op_sel:[0,1,0]
	v_pk_fma_f32 v[118:119], v[124:125], v[24:25], v[122:123] op_sel:[0,1,0]
	v_pk_fma_f32 v[122:123], v[138:139], v[24:25], v[126:127] op_sel:[0,1,0]
	v_pk_fma_f32 v[104:105], v[104:105], v[24:25], v[108:109] op_sel:[0,1,0]
	v_pk_fma_f32 v[108:109], v[140:141], v[24:25], v[112:113] op_sel:[0,1,0]
	v_pk_fma_f32 v[112:113], v[142:143], v[24:25], v[116:117] op_sel:[0,1,0]
	v_pk_fma_f32 v[116:117], v[144:145], v[24:25], v[120:121] op_sel:[0,1,0]
	v_pk_fma_f32 v[106:107], v[106:107], v[24:25], v[110:111] op_sel:[0,1,0]
	v_cvt_pk_f32_fp8_e32 v[110:111], v100
	v_cvt_pk_f32_fp8_sdwa v[120:121], v100 src0_sel:WORD_1
	v_cvt_pk_f32_fp8_e32 v[124:125], v101
	v_cvt_pk_f32_fp8_sdwa v[100:101], v101 src0_sel:WORD_1
	v_cvt_pk_f32_fp8_e32 v[126:127], v102
	v_cvt_pk_f32_fp8_sdwa v[138:139], v102 src0_sel:WORD_1
	v_cvt_pk_f32_fp8_e32 v[140:141], v103
	v_cvt_pk_f32_fp8_sdwa v[102:103], v103 src0_sel:WORD_1
	v_pk_fma_f32 v[110:111], v[110:111], v[26:27], v[114:115] op_sel_hi:[1,0,1]
	v_pk_fma_f32 v[114:115], v[120:121], v[26:27], v[118:119] op_sel_hi:[1,0,1]
	v_pk_fma_f32 v[118:119], v[124:125], v[26:27], v[122:123] op_sel_hi:[1,0,1]
	v_pk_fma_f32 v[100:101], v[100:101], v[26:27], v[104:105] op_sel_hi:[1,0,1]
	v_pk_fma_f32 v[104:105], v[126:127], v[26:27], v[108:109] op_sel_hi:[1,0,1]
	v_pk_fma_f32 v[108:109], v[138:139], v[26:27], v[112:113] op_sel_hi:[1,0,1]
	v_pk_fma_f32 v[112:113], v[140:141], v[26:27], v[116:117] op_sel_hi:[1,0,1]
	v_pk_fma_f32 v[102:103], v[102:103], v[26:27], v[106:107] op_sel_hi:[1,0,1]
	v_cvt_pk_f32_fp8_e32 v[106:107], v96
	v_cvt_pk_f32_fp8_sdwa v[116:117], v96 src0_sel:WORD_1
	v_cvt_pk_f32_fp8_e32 v[120:121], v97
	v_cvt_pk_f32_fp8_sdwa v[96:97], v97 src0_sel:WORD_1
	v_cvt_pk_f32_fp8_e32 v[122:123], v98
	v_cvt_pk_f32_fp8_sdwa v[124:125], v98 src0_sel:WORD_1
	v_cvt_pk_f32_fp8_e32 v[126:127], v99
	v_cvt_pk_f32_fp8_sdwa v[98:99], v99 src0_sel:WORD_1
	v_mov_b32_e32 v128, v27
	v_pk_fma_f32 v[106:107], v[106:107], v[128:129], v[110:111] op_sel_hi:[1,0,1]
	v_pk_fma_f32 v[110:111], v[116:117], v[128:129], v[114:115] op_sel_hi:[1,0,1]
	v_pk_fma_f32 v[114:115], v[120:121], v[128:129], v[118:119] op_sel_hi:[1,0,1]
	v_pk_fma_f32 v[96:97], v[96:97], v[128:129], v[100:101] op_sel_hi:[1,0,1]
	v_pk_fma_f32 v[100:101], v[122:123], v[128:129], v[104:105] op_sel_hi:[1,0,1]
	v_pk_fma_f32 v[104:105], v[124:125], v[128:129], v[108:109] op_sel_hi:[1,0,1]
	v_pk_fma_f32 v[108:109], v[126:127], v[128:129], v[112:113] op_sel_hi:[1,0,1]
	v_lshl_or_b32 v12, v12, 7, v136
	global_load_dwordx4 v[124:127], v12, s[4:5] sc0
	v_pk_fma_f32 v[98:99], v[98:99], v[128:129], v[102:103] op_sel_hi:[1,0,1]
	v_cvt_pk_f32_fp8_e32 v[102:103], v92
	v_cvt_pk_f32_fp8_sdwa v[112:113], v92 src0_sel:WORD_1
	v_cvt_pk_f32_fp8_e32 v[116:117], v93
	v_cvt_pk_f32_fp8_sdwa v[92:93], v93 src0_sel:WORD_1
	v_cvt_pk_f32_fp8_e32 v[118:119], v94
	v_cvt_pk_f32_fp8_sdwa v[120:121], v94 src0_sel:WORD_1
	v_cvt_pk_f32_fp8_e32 v[122:123], v95
	v_cvt_pk_f32_fp8_sdwa v[94:95], v95 src0_sel:WORD_1
	v_pk_fma_f32 v[102:103], v[102:103], v[20:21], v[106:107] op_sel_hi:[1,0,1]
	v_pk_fma_f32 v[106:107], v[112:113], v[20:21], v[110:111] op_sel_hi:[1,0,1]
	v_pk_fma_f32 v[110:111], v[116:117], v[20:21], v[114:115] op_sel_hi:[1,0,1]
	v_pk_fma_f32 v[92:93], v[92:93], v[20:21], v[96:97] op_sel_hi:[1,0,1]
	v_pk_fma_f32 v[96:97], v[118:119], v[20:21], v[100:101] op_sel_hi:[1,0,1]
	v_pk_fma_f32 v[100:101], v[120:121], v[20:21], v[104:105] op_sel_hi:[1,0,1]
	v_pk_fma_f32 v[104:105], v[122:123], v[20:21], v[108:109] op_sel_hi:[1,0,1]
	v_lshl_or_b32 v13, v13, 7, v136
	global_load_dwordx4 v[120:123], v13, s[4:5] sc0
	v_pk_fma_f32 v[94:95], v[94:95], v[20:21], v[98:99] op_sel_hi:[1,0,1]
	v_cvt_pk_f32_fp8_e32 v[98:99], v88
	v_cvt_pk_f32_fp8_sdwa v[108:109], v88 src0_sel:WORD_1
	v_cvt_pk_f32_fp8_e32 v[112:113], v89
	v_cvt_pk_f32_fp8_sdwa v[88:89], v89 src0_sel:WORD_1
	v_cvt_pk_f32_fp8_e32 v[114:115], v90
	v_cvt_pk_f32_fp8_sdwa v[116:117], v90 src0_sel:WORD_1
	v_cvt_pk_f32_fp8_e32 v[118:119], v91
	v_cvt_pk_f32_fp8_sdwa v[90:91], v91 src0_sel:WORD_1
	v_pk_fma_f32 v[98:99], v[98:99], v[20:21], v[102:103] op_sel:[0,1,0]
	v_pk_fma_f32 v[102:103], v[108:109], v[20:21], v[106:107] op_sel:[0,1,0]
	v_pk_fma_f32 v[106:107], v[112:113], v[20:21], v[110:111] op_sel:[0,1,0]
	v_pk_fma_f32 v[88:89], v[88:89], v[20:21], v[92:93] op_sel:[0,1,0]
	v_pk_fma_f32 v[92:93], v[114:115], v[20:21], v[96:97] op_sel:[0,1,0]
	v_pk_fma_f32 v[96:97], v[116:117], v[20:21], v[100:101] op_sel:[0,1,0]
	v_pk_fma_f32 v[100:101], v[118:119], v[20:21], v[104:105] op_sel:[0,1,0]
	v_lshl_or_b32 v14, v14, 7, v136
	global_load_dwordx4 v[116:119], v14, s[4:5] sc0
	v_pk_fma_f32 v[90:91], v[90:91], v[20:21], v[94:95] op_sel:[0,1,0]
	v_cvt_pk_f32_fp8_e32 v[94:95], v84
	v_cvt_pk_f32_fp8_sdwa v[104:105], v84 src0_sel:WORD_1
	v_cvt_pk_f32_fp8_e32 v[108:109], v85
	v_cvt_pk_f32_fp8_sdwa v[84:85], v85 src0_sel:WORD_1
	v_cvt_pk_f32_fp8_e32 v[110:111], v86
	v_cvt_pk_f32_fp8_sdwa v[112:113], v86 src0_sel:WORD_1
	v_cvt_pk_f32_fp8_e32 v[114:115], v87
	v_cvt_pk_f32_fp8_sdwa v[86:87], v87 src0_sel:WORD_1
	v_pk_fma_f32 v[94:95], v[94:95], v[22:23], v[98:99] op_sel_hi:[1,0,1]
	v_pk_fma_f32 v[98:99], v[104:105], v[22:23], v[102:103] op_sel_hi:[1,0,1]
	v_pk_fma_f32 v[102:103], v[108:109], v[22:23], v[106:107] op_sel_hi:[1,0,1]
	v_pk_fma_f32 v[84:85], v[84:85], v[22:23], v[88:89] op_sel_hi:[1,0,1]
	v_pk_fma_f32 v[88:89], v[110:111], v[22:23], v[92:93] op_sel_hi:[1,0,1]
	v_pk_fma_f32 v[92:93], v[112:113], v[22:23], v[96:97] op_sel_hi:[1,0,1]
	v_pk_fma_f32 v[96:97], v[114:115], v[22:23], v[100:101] op_sel_hi:[1,0,1]
	v_pk_fma_f32 v[86:87], v[86:87], v[22:23], v[90:91] op_sel_hi:[1,0,1]
	v_cvt_pk_f32_fp8_e32 v[90:91], v80
	v_cvt_pk_f32_fp8_sdwa v[100:101], v80 src0_sel:WORD_1
	v_cvt_pk_f32_fp8_e32 v[104:105], v81
	v_cvt_pk_f32_fp8_sdwa v[80:81], v81 src0_sel:WORD_1
	v_cvt_pk_f32_fp8_e32 v[106:107], v82
	v_cvt_pk_f32_fp8_sdwa v[108:109], v82 src0_sel:WORD_1
	v_cvt_pk_f32_fp8_e32 v[110:111], v83
	v_cvt_pk_f32_fp8_sdwa v[82:83], v83 src0_sel:WORD_1
	v_mov_b32_e32 v112, v23
	v_pk_fma_f32 v[90:91], v[90:91], v[112:113], v[94:95] op_sel_hi:[1,0,1]
	v_pk_fma_f32 v[94:95], v[100:101], v[112:113], v[98:99] op_sel_hi:[1,0,1]
	v_pk_fma_f32 v[98:99], v[104:105], v[112:113], v[102:103] op_sel_hi:[1,0,1]
	v_pk_fma_f32 v[80:81], v[80:81], v[112:113], v[84:85] op_sel_hi:[1,0,1]
	v_pk_fma_f32 v[84:85], v[106:107], v[112:113], v[88:89] op_sel_hi:[1,0,1]
	v_pk_fma_f32 v[88:89], v[108:109], v[112:113], v[92:93] op_sel_hi:[1,0,1]
	v_pk_fma_f32 v[92:93], v[110:111], v[112:113], v[96:97] op_sel_hi:[1,0,1]
	v_lshl_or_b32 v8, v8, 7, v136
	global_load_dwordx4 v[108:111], v8, s[4:5] sc0
	v_pk_fma_f32 v[82:83], v[82:83], v[112:113], v[86:87] op_sel_hi:[1,0,1]
	v_lshl_or_b32 v15, v15, 7, v136
	global_load_dwordx4 v[112:115], v15, s[4:5] sc0
	v_cvt_pk_f32_fp8_e32 v[86:87], v76
	v_cvt_pk_f32_fp8_sdwa v[96:97], v76 src0_sel:WORD_1
	v_cvt_pk_f32_fp8_e32 v[100:101], v77
	v_cvt_pk_f32_fp8_sdwa v[76:77], v77 src0_sel:WORD_1
	v_cvt_pk_f32_fp8_e32 v[102:103], v78
	v_cvt_pk_f32_fp8_sdwa v[104:105], v78 src0_sel:WORD_1
	v_cvt_pk_f32_fp8_e32 v[106:107], v79
	v_cvt_pk_f32_fp8_sdwa v[78:79], v79 src0_sel:WORD_1
	v_pk_fma_f32 v[86:87], v[86:87], v[16:17], v[90:91] op_sel_hi:[1,0,1]
	v_pk_fma_f32 v[90:91], v[96:97], v[16:17], v[94:95] op_sel_hi:[1,0,1]
	v_pk_fma_f32 v[94:95], v[100:101], v[16:17], v[98:99] op_sel_hi:[1,0,1]
	v_pk_fma_f32 v[76:77], v[76:77], v[16:17], v[80:81] op_sel_hi:[1,0,1]
	v_pk_fma_f32 v[80:81], v[102:103], v[16:17], v[84:85] op_sel_hi:[1,0,1]
	v_pk_fma_f32 v[84:85], v[104:105], v[16:17], v[88:89] op_sel_hi:[1,0,1]
	v_pk_fma_f32 v[88:89], v[106:107], v[16:17], v[92:93] op_sel_hi:[1,0,1]
	v_lshl_or_b32 v9, v9, 7, v136
	global_load_dwordx4 v[104:107], v9, s[4:5] sc0
	v_pk_fma_f32 v[78:79], v[78:79], v[16:17], v[82:83] op_sel_hi:[1,0,1]
	v_cvt_pk_f32_fp8_e32 v[82:83], v72
	v_cvt_pk_f32_fp8_sdwa v[92:93], v72 src0_sel:WORD_1
	v_cvt_pk_f32_fp8_e32 v[96:97], v73
	v_cvt_pk_f32_fp8_sdwa v[72:73], v73 src0_sel:WORD_1
	v_cvt_pk_f32_fp8_e32 v[98:99], v74
	v_cvt_pk_f32_fp8_sdwa v[100:101], v74 src0_sel:WORD_1
	v_cvt_pk_f32_fp8_e32 v[102:103], v75
	v_cvt_pk_f32_fp8_sdwa v[74:75], v75 src0_sel:WORD_1
	v_pk_fma_f32 v[82:83], v[82:83], v[16:17], v[86:87] op_sel:[0,1,0]
	v_pk_fma_f32 v[86:87], v[92:93], v[16:17], v[90:91] op_sel:[0,1,0]
	v_pk_fma_f32 v[90:91], v[96:97], v[16:17], v[94:95] op_sel:[0,1,0]
	v_pk_fma_f32 v[72:73], v[72:73], v[16:17], v[76:77] op_sel:[0,1,0]
	v_pk_fma_f32 v[76:77], v[98:99], v[16:17], v[80:81] op_sel:[0,1,0]
	v_pk_fma_f32 v[80:81], v[100:101], v[16:17], v[84:85] op_sel:[0,1,0]
	v_pk_fma_f32 v[84:85], v[102:103], v[16:17], v[88:89] op_sel:[0,1,0]
	v_lshl_or_b32 v10, v10, 7, v136
	global_load_dwordx4 v[100:103], v10, s[4:5] sc0
	v_pk_fma_f32 v[74:75], v[74:75], v[16:17], v[78:79] op_sel:[0,1,0]
	v_cvt_pk_f32_fp8_e32 v[78:79], v68
	v_cvt_pk_f32_fp8_sdwa v[88:89], v68 src0_sel:WORD_1
	v_cvt_pk_f32_fp8_e32 v[92:93], v69
	v_cvt_pk_f32_fp8_sdwa v[68:69], v69 src0_sel:WORD_1
	v_cvt_pk_f32_fp8_e32 v[94:95], v70
	v_cvt_pk_f32_fp8_sdwa v[96:97], v70 src0_sel:WORD_1
	v_cvt_pk_f32_fp8_e32 v[98:99], v71
	v_cvt_pk_f32_fp8_sdwa v[70:71], v71 src0_sel:WORD_1
	v_pk_fma_f32 v[78:79], v[78:79], v[18:19], v[82:83] op_sel_hi:[1,0,1]
	v_pk_fma_f32 v[82:83], v[88:89], v[18:19], v[86:87] op_sel_hi:[1,0,1]
	v_pk_fma_f32 v[86:87], v[92:93], v[18:19], v[90:91] op_sel_hi:[1,0,1]
	v_pk_fma_f32 v[68:69], v[68:69], v[18:19], v[72:73] op_sel_hi:[1,0,1]
	v_pk_fma_f32 v[72:73], v[94:95], v[18:19], v[76:77] op_sel_hi:[1,0,1]
	v_pk_fma_f32 v[76:77], v[96:97], v[18:19], v[80:81] op_sel_hi:[1,0,1]
	v_pk_fma_f32 v[80:81], v[98:99], v[18:19], v[84:85] op_sel_hi:[1,0,1]
	v_pk_fma_f32 v[70:71], v[70:71], v[18:19], v[74:75] op_sel_hi:[1,0,1]
	v_cvt_pk_f32_fp8_e32 v[74:75], v64
	v_cvt_pk_f32_fp8_sdwa v[84:85], v64 src0_sel:WORD_1
	v_cvt_pk_f32_fp8_e32 v[88:89], v65
	v_cvt_pk_f32_fp8_sdwa v[64:65], v65 src0_sel:WORD_1
	v_cvt_pk_f32_fp8_e32 v[90:91], v66
	v_cvt_pk_f32_fp8_sdwa v[92:93], v66 src0_sel:WORD_1
	v_cvt_pk_f32_fp8_e32 v[94:95], v67
	v_cvt_pk_f32_fp8_sdwa v[66:67], v67 src0_sel:WORD_1
	v_mov_b32_e32 v96, v19
	v_pk_fma_f32 v[74:75], v[74:75], v[96:97], v[78:79] op_sel_hi:[1,0,1]
	v_pk_fma_f32 v[78:79], v[84:85], v[96:97], v[82:83] op_sel_hi:[1,0,1]
	v_pk_fma_f32 v[82:83], v[88:89], v[96:97], v[86:87] op_sel_hi:[1,0,1]
	v_lshl_or_b32 v6, v6, 7, v136
	global_load_dwordx4 v[84:87], v6, s[4:5] sc0
	v_pk_fma_f32 v[64:65], v[64:65], v[96:97], v[68:69] op_sel_hi:[1,0,1]
	v_pk_fma_f32 v[68:69], v[90:91], v[96:97], v[72:73] op_sel_hi:[1,0,1]
	v_lshl_or_b32 v5, v5, 7, v136
	global_load_dwordx4 v[88:91], v5, s[4:5] sc0
	v_pk_fma_f32 v[72:73], v[92:93], v[96:97], v[76:77] op_sel_hi:[1,0,1]
	v_pk_fma_f32 v[76:77], v[94:95], v[96:97], v[80:81] op_sel_hi:[1,0,1]
	v_lshl_or_b32 v4, v4, 7, v136
	global_load_dwordx4 v[92:95], v4, s[4:5] sc0
	v_pk_fma_f32 v[66:67], v[66:67], v[96:97], v[70:71] op_sel_hi:[1,0,1]
	v_lshl_or_b32 v11, v11, 7, v136
	global_load_dwordx4 v[96:99], v11, s[4:5] sc0
	v_permlane32_swap_b32_e32 v74, v68
	v_permlane32_swap_b32_e32 v75, v69
	v_permlane32_swap_b32_e32 v78, v72
	v_permlane32_swap_b32_e32 v79, v73
	v_permlane32_swap_b32_e32 v82, v76
	v_permlane32_swap_b32_e32 v83, v77
	v_permlane32_swap_b32_e32 v64, v66
	v_permlane32_swap_b32_e32 v65, v67
	v_add_f32_e32 v68, v74, v68
	v_add_f32_e32 v69, v75, v69
	v_add_f32_e32 v70, v78, v72
	v_add_f32_e32 v71, v79, v73
	v_add_f32_e32 v72, v82, v76
	v_add_f32_e32 v73, v83, v77
	v_lshl_or_b32 v7, v7, 7, v136
	global_load_dwordx4 v[80:83], v7, s[4:5] sc0
	v_lshl_or_b32 v0, v0, 7, v136
	global_load_dwordx4 v[76:79], v0, s[4:5] sc0
	v_add_f32_e32 v64, v64, v66
	v_add_f32_e32 v65, v65, v67
	v_permlane16_swap_b32_e32 v68, v72
	v_permlane16_swap_b32_e32 v69, v73
	v_permlane16_swap_b32_e32 v70, v64
	v_permlane16_swap_b32_e32 v71, v65
	v_pk_add_f32 v[66:67], v[68:69], v[72:73]
	v_lshl_or_b32 v1, v1, 7, v136
	global_load_dwordx4 v[72:75], v1, s[4:5] sc0
	v_pk_add_f32 v[64:65], v[70:71], v[64:65]
	s_ashr_i32 s9, s8, 31
	v_cndmask_b32_e64 v68, v66, v64, s[0:1]
	v_cndmask_b32_e64 v70, v64, v66, s[0:1]
	v_cndmask_b32_e64 v64, v67, v65, s[0:1]
	v_mov_b32_dpp v68, v68 row_ror:8 row_mask:0xf bank_mask:0xf bound_ctrl:1
	v_cndmask_b32_e64 v71, v65, v67, s[0:1]
	v_mov_b32_dpp v69, v64 row_ror:8 row_mask:0xf bank_mask:0xf bound_ctrl:1
	v_pk_add_f32 v[66:67], v[70:71], v[68:69]
	s_lshl_b64 s[10:11], s[8:9], 11
	v_pk_mul_f32 v[64:65], v[66:67], v[66:67]
	v_cvt_pk_bf16_f32 v68, v66, v67
	v_add_f32_e32 v64, v64, v65
	v_lshl_add_u64 v[66:67], v[130:131], 0, s[10:11]
	global_store_dword v[66:67], v68, off
	v_add_f32_dpp v64, v64, v64 quad_perm:[1,0,3,2] row_mask:0xf bank_mask:0xf bound_ctrl:1
	s_nop 1
	v_add_f32_dpp v64, v64, v64 quad_perm:[2,3,0,1] row_mask:0xf bank_mask:0xf bound_ctrl:1
	s_nop 1
	v_add_f32_dpp v64, v64, v64 row_half_mirror row_mask:0xf bank_mask:0xf bound_ctrl:1
	s_nop 1
	v_add_f32_dpp v64, v64, v64 row_ror:8 row_mask:0xf bank_mask:0xf bound_ctrl:1
	v_mov_b32_e32 v65, v64
	s_nop 1
	v_permlane16_swap_b32_e32 v64, v65
	v_add_f32_e32 v64, v64, v65
	v_mov_b32_e32 v65, v64
	s_nop 1
	v_permlane32_swap_b32_e32 v64, v65
	s_and_saveexec_b64 s[10:11], s[2:3]
	s_lshl_b64 s[16:17], s[8:9], 2
	s_add_u32 s16, s12, s16
	v_add_f32_e32 v64, v64, v65
	s_addc_u32 s17, s13, s17
	global_store_dword v129, v64, s[16:17]
	s_or_b64 exec, exec, s[10:11]
	v_lshl_or_b32 v2, v2, 7, v136
	global_load_dwordx4 v[68:71], v2, s[4:5] sc0
	v_lshl_or_b32 v3, v3, 7, v136
	global_load_dwordx4 v[64:67], v3, s[4:5] sc0
	s_add_u32 s22, s20, 0x200
	s_lshl_b32 s22, s22, 9
	v_lshl_add_u64 v[28:29], v[134:135], 0, s[22:23]
	global_load_dwordx4 v[16:19], v[28:29], off offset:48
	global_load_dwordx4 v[20:23], v[28:29], off offset:32
	global_load_dwordx4 v[24:27], v[28:29], off offset:16
	s_nop 0
	global_load_dwordx4 v[28:31], v[28:29], off
	s_add_u32 s22, s20, 0x400
	s_lshl_b32 s22, s22, 9
	v_lshl_add_u64 v[12:13], v[132:133], 0, s[22:23]
	global_load_dwordx4 v[0:3], v[12:13], off offset:48
	global_load_dwordx4 v[4:7], v[12:13], off offset:32
	global_load_dwordx4 v[8:11], v[12:13], off offset:16
	s_nop 0
	global_load_dwordx4 v[12:15], v[12:13], off
	s_add_u32 s6, s20, 0x100
	s_waitcnt vmcnt(26)
	v_cvt_pk_f32_fp8_e32 v[138:139], v240
	v_cvt_pk_f32_fp8_sdwa v[140:141], v240 src0_sel:WORD_1
	v_cvt_pk_f32_fp8_e32 v[142:143], v241
	v_cvt_pk_f32_fp8_sdwa v[240:241], v241 src0_sel:WORD_1
	v_cvt_pk_f32_fp8_e32 v[144:145], v242
	v_cvt_pk_f32_fp8_sdwa v[146:147], v242 src0_sel:WORD_1
	v_cvt_pk_f32_fp8_e32 v[148:149], v243
	v_cvt_pk_f32_fp8_sdwa v[242:243], v243 src0_sel:WORD_1
	v_cvt_pk_f32_fp8_e32 v[150:151], v236
	v_cvt_pk_f32_fp8_sdwa v[152:153], v236 src0_sel:WORD_1
	v_cvt_pk_f32_fp8_e32 v[154:155], v237
	v_cvt_pk_f32_fp8_sdwa v[236:237], v237 src0_sel:WORD_1
	v_cvt_pk_f32_fp8_e32 v[156:157], v238
	v_cvt_pk_f32_fp8_sdwa v[158:159], v238 src0_sel:WORD_1
	v_cvt_pk_f32_fp8_e32 v[160:161], v239
	v_cvt_pk_f32_fp8_sdwa v[238:239], v239 src0_sel:WORD_1
	v_pk_fma_f32 v[138:139], v[138:139], v[48:49], 0 op_sel_hi:[1,0,0]
	v_pk_fma_f32 v[140:141], v[140:141], v[48:49], 0 op_sel_hi:[1,0,0]
	v_pk_fma_f32 v[142:143], v[142:143], v[48:49], 0 op_sel_hi:[1,0,0]
	v_pk_fma_f32 v[240:241], v[240:241], v[48:49], 0 op_sel_hi:[1,0,0]
	v_pk_fma_f32 v[144:145], v[144:145], v[48:49], 0 op_sel_hi:[1,0,0]
	v_pk_fma_f32 v[146:147], v[146:147], v[48:49], 0 op_sel_hi:[1,0,0]
	v_pk_fma_f32 v[148:149], v[148:149], v[48:49], 0 op_sel_hi:[1,0,0]
	v_pk_fma_f32 v[242:243], v[242:243], v[48:49], 0 op_sel_hi:[1,0,0]
	v_pk_fma_f32 v[138:139], v[150:151], v[48:49], v[138:139] op_sel:[0,1,0]
	v_pk_fma_f32 v[140:141], v[152:153], v[48:49], v[140:141] op_sel:[0,1,0]
	v_pk_fma_f32 v[142:143], v[154:155], v[48:49], v[142:143] op_sel:[0,1,0]
	v_pk_fma_f32 v[236:237], v[236:237], v[48:49], v[240:241] op_sel:[0,1,0]
	v_pk_fma_f32 v[240:241], v[156:157], v[48:49], v[144:145] op_sel:[0,1,0]
	v_pk_fma_f32 v[144:145], v[158:159], v[48:49], v[146:147] op_sel:[0,1,0]
	v_pk_fma_f32 v[146:147], v[160:161], v[48:49], v[148:149] op_sel:[0,1,0]
	v_pk_fma_f32 v[238:239], v[238:239], v[48:49], v[242:243] op_sel:[0,1,0]
	v_cvt_pk_f32_fp8_e32 v[242:243], v232
	v_cvt_pk_f32_fp8_sdwa v[148:149], v232 src0_sel:WORD_1
	v_cvt_pk_f32_fp8_e32 v[150:151], v233
	v_cvt_pk_f32_fp8_sdwa v[232:233], v233 src0_sel:WORD_1
	v_cvt_pk_f32_fp8_e32 v[152:153], v234
	v_cvt_pk_f32_fp8_sdwa v[154:155], v234 src0_sel:WORD_1
	v_cvt_pk_f32_fp8_e32 v[156:157], v235
	v_cvt_pk_f32_fp8_sdwa v[234:235], v235 src0_sel:WORD_1
	v_pk_fma_f32 v[242:243], v[242:243], v[50:51], v[138:139] op_sel_hi:[1,0,1]
	v_pk_fma_f32 v[138:139], v[148:149], v[50:51], v[140:141] op_sel_hi:[1,0,1]
	v_pk_fma_f32 v[140:141], v[150:151], v[50:51], v[142:143] op_sel_hi:[1,0,1]
	v_pk_fma_f32 v[232:233], v[232:233], v[50:51], v[236:237] op_sel_hi:[1,0,1]
	v_pk_fma_f32 v[236:237], v[152:153], v[50:51], v[240:241] op_sel_hi:[1,0,1]
	v_pk_fma_f32 v[240:241], v[154:155], v[50:51], v[144:145] op_sel_hi:[1,0,1]
	v_pk_fma_f32 v[142:143], v[156:157], v[50:51], v[146:147] op_sel_hi:[1,0,1]
	v_pk_fma_f32 v[234:235], v[234:235], v[50:51], v[238:239] op_sel_hi:[1,0,1]
	v_cvt_pk_f32_fp8_e32 v[238:239], v228
	v_cvt_pk_f32_fp8_sdwa v[144:145], v228 src0_sel:WORD_1
	v_cvt_pk_f32_fp8_e32 v[146:147], v229
	v_cvt_pk_f32_fp8_sdwa v[228:229], v229 src0_sel:WORD_1
	v_cvt_pk_f32_fp8_e32 v[148:149], v230
	v_cvt_pk_f32_fp8_sdwa v[150:151], v230 src0_sel:WORD_1
	v_cvt_pk_f32_fp8_e32 v[152:153], v231
	v_cvt_pk_f32_fp8_sdwa v[230:231], v231 src0_sel:WORD_1
	v_mov_b32_e32 v128, v51
	v_pk_fma_f32 v[238:239], v[238:239], v[128:129], v[242:243] op_sel_hi:[1,0,1]
	v_pk_fma_f32 v[242:243], v[144:145], v[128:129], v[138:139] op_sel_hi:[1,0,1]
	v_pk_fma_f32 v[138:139], v[146:147], v[128:129], v[140:141] op_sel_hi:[1,0,1]
	v_pk_fma_f32 v[228:229], v[228:229], v[128:129], v[232:233] op_sel_hi:[1,0,1]
	v_pk_fma_f32 v[232:233], v[148:149], v[128:129], v[236:237] op_sel_hi:[1,0,1]
	v_pk_fma_f32 v[236:237], v[150:151], v[128:129], v[240:241] op_sel_hi:[1,0,1]
	v_pk_fma_f32 v[240:241], v[152:153], v[128:129], v[142:143] op_sel_hi:[1,0,1]
	v_pk_fma_f32 v[230:231], v[230:231], v[128:129], v[234:235] op_sel_hi:[1,0,1]
	v_cvt_pk_f32_fp8_e32 v[234:235], v224
	v_cvt_pk_f32_fp8_sdwa v[140:141], v224 src0_sel:WORD_1
	v_cvt_pk_f32_fp8_e32 v[142:143], v225
	v_cvt_pk_f32_fp8_sdwa v[224:225], v225 src0_sel:WORD_1
	v_cvt_pk_f32_fp8_e32 v[144:145], v226
	v_cvt_pk_f32_fp8_sdwa v[146:147], v226 src0_sel:WORD_1
	v_cvt_pk_f32_fp8_e32 v[148:149], v227
	v_cvt_pk_f32_fp8_sdwa v[226:227], v227 src0_sel:WORD_1
	v_pk_fma_f32 v[234:235], v[234:235], v[52:53], v[238:239] op_sel_hi:[1,0,1]
	v_pk_fma_f32 v[238:239], v[140:141], v[52:53], v[242:243] op_sel_hi:[1,0,1]
	v_pk_fma_f32 v[242:243], v[142:143], v[52:53], v[138:139] op_sel_hi:[1,0,1]
	v_pk_fma_f32 v[224:225], v[224:225], v[52:53], v[228:229] op_sel_hi:[1,0,1]
	v_pk_fma_f32 v[228:229], v[144:145], v[52:53], v[232:233] op_sel_hi:[1,0,1]
	v_pk_fma_f32 v[232:233], v[146:147], v[52:53], v[236:237] op_sel_hi:[1,0,1]
	v_pk_fma_f32 v[236:237], v[148:149], v[52:53], v[240:241] op_sel_hi:[1,0,1]
	v_pk_fma_f32 v[226:227], v[226:227], v[52:53], v[230:231] op_sel_hi:[1,0,1]
	v_cvt_pk_f32_fp8_e32 v[230:231], v220
	v_cvt_pk_f32_fp8_sdwa v[240:241], v220 src0_sel:WORD_1
	v_cvt_pk_f32_fp8_e32 v[138:139], v221
	v_cvt_pk_f32_fp8_sdwa v[220:221], v221 src0_sel:WORD_1
	v_cvt_pk_f32_fp8_e32 v[140:141], v222
	v_cvt_pk_f32_fp8_sdwa v[142:143], v222 src0_sel:WORD_1
	v_cvt_pk_f32_fp8_e32 v[144:145], v223
	v_cvt_pk_f32_fp8_sdwa v[222:223], v223 src0_sel:WORD_1
	v_pk_fma_f32 v[230:231], v[230:231], v[52:53], v[234:235] op_sel:[0,1,0]
	v_pk_fma_f32 v[234:235], v[240:241], v[52:53], v[238:239] op_sel:[0,1,0]
	v_pk_fma_f32 v[238:239], v[138:139], v[52:53], v[242:243] op_sel:[0,1,0]
	v_pk_fma_f32 v[220:221], v[220:221], v[52:53], v[224:225] op_sel:[0,1,0]
	v_pk_fma_f32 v[224:225], v[140:141], v[52:53], v[228:229] op_sel:[0,1,0]
	v_pk_fma_f32 v[228:229], v[142:143], v[52:53], v[232:233] op_sel:[0,1,0]
	v_pk_fma_f32 v[232:233], v[144:145], v[52:53], v[236:237] op_sel:[0,1,0]
	v_pk_fma_f32 v[222:223], v[222:223], v[52:53], v[226:227] op_sel:[0,1,0]
	v_cvt_pk_f32_fp8_e32 v[226:227], v216
	v_cvt_pk_f32_fp8_sdwa v[236:237], v216 src0_sel:WORD_1
	v_cvt_pk_f32_fp8_e32 v[240:241], v217
	v_cvt_pk_f32_fp8_sdwa v[216:217], v217 src0_sel:WORD_1
	v_cvt_pk_f32_fp8_e32 v[242:243], v218
	v_cvt_pk_f32_fp8_sdwa v[138:139], v218 src0_sel:WORD_1
	v_cvt_pk_f32_fp8_e32 v[140:141], v219
	v_cvt_pk_f32_fp8_sdwa v[218:219], v219 src0_sel:WORD_1
	v_pk_fma_f32 v[226:227], v[226:227], v[54:55], v[230:231] op_sel_hi:[1,0,1]
	v_pk_fma_f32 v[230:231], v[236:237], v[54:55], v[234:235] op_sel_hi:[1,0,1]
	v_pk_fma_f32 v[234:235], v[240:241], v[54:55], v[238:239] op_sel_hi:[1,0,1]
	v_pk_fma_f32 v[216:217], v[216:217], v[54:55], v[220:221] op_sel_hi:[1,0,1]
	v_pk_fma_f32 v[220:221], v[242:243], v[54:55], v[224:225] op_sel_hi:[1,0,1]
	v_pk_fma_f32 v[224:225], v[138:139], v[54:55], v[228:229] op_sel_hi:[1,0,1]
	v_pk_fma_f32 v[228:229], v[140:141], v[54:55], v[232:233] op_sel_hi:[1,0,1]
	v_pk_fma_f32 v[218:219], v[218:219], v[54:55], v[222:223] op_sel_hi:[1,0,1]
	v_cvt_pk_f32_fp8_e32 v[222:223], v212
	v_cvt_pk_f32_fp8_sdwa v[232:233], v212 src0_sel:WORD_1
	v_cvt_pk_f32_fp8_e32 v[236:237], v213
	v_cvt_pk_f32_fp8_sdwa v[212:213], v213 src0_sel:WORD_1
	v_cvt_pk_f32_fp8_e32 v[238:239], v214
	v_cvt_pk_f32_fp8_sdwa v[240:241], v214 src0_sel:WORD_1
	v_cvt_pk_f32_fp8_e32 v[242:243], v215
	v_cvt_pk_f32_fp8_sdwa v[214:215], v215 src0_sel:WORD_1
	v_mov_b32_e32 v128, v55
	v_pk_fma_f32 v[222:223], v[222:223], v[128:129], v[226:227] op_sel_hi:[1,0,1]
	v_pk_fma_f32 v[226:227], v[232:233], v[128:129], v[230:231] op_sel_hi:[1,0,1]
	v_pk_fma_f32 v[230:231], v[236:237], v[128:129], v[234:235] op_sel_hi:[1,0,1]
	v_pk_fma_f32 v[212:213], v[212:213], v[128:129], v[216:217] op_sel_hi:[1,0,1]
	v_pk_fma_f32 v[216:217], v[238:239], v[128:129], v[220:221] op_sel_hi:[1,0,1]
	v_pk_fma_f32 v[220:221], v[240:241], v[128:129], v[224:225] op_sel_hi:[1,0,1]
	v_pk_fma_f32 v[224:225], v[242:243], v[128:129], v[228:229] op_sel_hi:[1,0,1]
	v_lshl_or_b32 v32, v32, 7, v136
	global_load_dwordx4 v[240:243], v32, s[4:5] sc0
	v_pk_fma_f32 v[214:215], v[214:215], v[128:129], v[218:219] op_sel_hi:[1,0,1]
	v_cvt_pk_f32_fp8_e32 v[218:219], v200
	v_cvt_pk_f32_fp8_sdwa v[228:229], v200 src0_sel:WORD_1
	v_cvt_pk_f32_fp8_e32 v[232:233], v201
	v_cvt_pk_f32_fp8_sdwa v[200:201], v201 src0_sel:WORD_1
	v_cvt_pk_f32_fp8_e32 v[234:235], v202
	v_cvt_pk_f32_fp8_sdwa v[236:237], v202 src0_sel:WORD_1
	v_cvt_pk_f32_fp8_e32 v[238:239], v203
	v_cvt_pk_f32_fp8_sdwa v[202:203], v203 src0_sel:WORD_1
	v_pk_fma_f32 v[218:219], v[218:219], v[56:57], v[222:223] op_sel_hi:[1,0,1]
	v_pk_fma_f32 v[222:223], v[228:229], v[56:57], v[226:227] op_sel_hi:[1,0,1]
	v_pk_fma_f32 v[226:227], v[232:233], v[56:57], v[230:231] op_sel_hi:[1,0,1]
	v_pk_fma_f32 v[200:201], v[200:201], v[56:57], v[212:213] op_sel_hi:[1,0,1]
	v_pk_fma_f32 v[212:213], v[234:235], v[56:57], v[216:217] op_sel_hi:[1,0,1]
	v_pk_fma_f32 v[216:217], v[236:237], v[56:57], v[220:221] op_sel_hi:[1,0,1]
	v_pk_fma_f32 v[220:221], v[238:239], v[56:57], v[224:225] op_sel_hi:[1,0,1]
	v_lshl_or_b32 v33, v33, 7, v136
	global_load_dwordx4 v[236:239], v33, s[4:5] sc0
	v_pk_fma_f32 v[202:203], v[202:203], v[56:57], v[214:215] op_sel_hi:[1,0,1]
	v_cvt_pk_f32_fp8_e32 v[214:215], v196
	v_cvt_pk_f32_fp8_sdwa v[224:225], v196 src0_sel:WORD_1
	v_cvt_pk_f32_fp8_e32 v[228:229], v197
	v_cvt_pk_f32_fp8_sdwa v[196:197], v197 src0_sel:WORD_1
	v_cvt_pk_f32_fp8_e32 v[230:231], v198
	v_cvt_pk_f32_fp8_sdwa v[232:233], v198 src0_sel:WORD_1
	v_cvt_pk_f32_fp8_e32 v[234:235], v199
	v_cvt_pk_f32_fp8_sdwa v[198:199], v199 src0_sel:WORD_1
	v_pk_fma_f32 v[214:215], v[214:215], v[56:57], v[218:219] op_sel:[0,1,0]
	v_pk_fma_f32 v[218:219], v[224:225], v[56:57], v[222:223] op_sel:[0,1,0]
	v_pk_fma_f32 v[222:223], v[228:229], v[56:57], v[226:227] op_sel:[0,1,0]
	v_pk_fma_f32 v[196:197], v[196:197], v[56:57], v[200:201] op_sel:[0,1,0]
	v_pk_fma_f32 v[200:201], v[230:231], v[56:57], v[212:213] op_sel:[0,1,0]
	v_pk_fma_f32 v[212:213], v[232:233], v[56:57], v[216:217] op_sel:[0,1,0]
	v_pk_fma_f32 v[216:217], v[234:235], v[56:57], v[220:221] op_sel:[0,1,0]
	v_lshl_or_b32 v34, v34, 7, v136
	global_load_dwordx4 v[232:235], v34, s[4:5] sc0
	v_pk_fma_f32 v[198:199], v[198:199], v[56:57], v[202:203] op_sel:[0,1,0]
	v_cvt_pk_f32_fp8_e32 v[202:203], v192
	v_cvt_pk_f32_fp8_sdwa v[220:221], v192 src0_sel:WORD_1
	v_cvt_pk_f32_fp8_e32 v[224:225], v193
	v_cvt_pk_f32_fp8_sdwa v[192:193], v193 src0_sel:WORD_1
	v_cvt_pk_f32_fp8_e32 v[226:227], v194
	v_cvt_pk_f32_fp8_sdwa v[228:229], v194 src0_sel:WORD_1
	v_cvt_pk_f32_fp8_e32 v[230:231], v195
	v_cvt_pk_f32_fp8_sdwa v[194:195], v195 src0_sel:WORD_1
	v_pk_fma_f32 v[202:203], v[202:203], v[58:59], v[214:215] op_sel_hi:[1,0,1]
	v_pk_fma_f32 v[214:215], v[220:221], v[58:59], v[218:219] op_sel_hi:[1,0,1]
	v_pk_fma_f32 v[218:219], v[224:225], v[58:59], v[222:223] op_sel_hi:[1,0,1]
	v_pk_fma_f32 v[192:193], v[192:193], v[58:59], v[196:197] op_sel_hi:[1,0,1]
	v_pk_fma_f32 v[196:197], v[226:227], v[58:59], v[200:201] op_sel_hi:[1,0,1]
	v_pk_fma_f32 v[200:201], v[228:229], v[58:59], v[212:213] op_sel_hi:[1,0,1]
	v_pk_fma_f32 v[212:213], v[230:231], v[58:59], v[216:217] op_sel_hi:[1,0,1]
	v_pk_fma_f32 v[194:195], v[194:195], v[58:59], v[198:199] op_sel_hi:[1,0,1]
	v_cvt_pk_f32_fp8_e32 v[198:199], v184
	v_cvt_pk_f32_fp8_sdwa v[216:217], v184 src0_sel:WORD_1
	v_cvt_pk_f32_fp8_e32 v[220:221], v185
	v_cvt_pk_f32_fp8_sdwa v[184:185], v185 src0_sel:WORD_1
	v_cvt_pk_f32_fp8_e32 v[222:223], v186
	v_cvt_pk_f32_fp8_sdwa v[224:225], v186 src0_sel:WORD_1
	v_cvt_pk_f32_fp8_e32 v[226:227], v187
	v_cvt_pk_f32_fp8_sdwa v[186:187], v187 src0_sel:WORD_1
	v_mov_b32_e32 v228, v59
	v_pk_fma_f32 v[198:199], v[198:199], v[228:229], v[202:203] op_sel_hi:[1,0,1]
	v_pk_fma_f32 v[202:203], v[216:217], v[228:229], v[214:215] op_sel_hi:[1,0,1]
	v_pk_fma_f32 v[214:215], v[220:221], v[228:229], v[218:219] op_sel_hi:[1,0,1]
	v_pk_fma_f32 v[184:185], v[184:185], v[228:229], v[192:193] op_sel_hi:[1,0,1]
	v_pk_fma_f32 v[192:193], v[222:223], v[228:229], v[196:197] op_sel_hi:[1,0,1]
	v_pk_fma_f32 v[196:197], v[224:225], v[228:229], v[200:201] op_sel_hi:[1,0,1]
	v_pk_fma_f32 v[200:201], v[226:227], v[228:229], v[212:213] op_sel_hi:[1,0,1]
	v_lshl_or_b32 v36, v36, 7, v136
	global_load_dwordx4 v[224:227], v36, s[4:5] sc0
	v_pk_fma_f32 v[186:187], v[186:187], v[228:229], v[194:195] op_sel_hi:[1,0,1]
	v_lshl_or_b32 v35, v35, 7, v136
	global_load_dwordx4 v[228:231], v35, s[4:5] sc0
	v_cvt_pk_f32_fp8_e32 v[194:195], v180
	v_cvt_pk_f32_fp8_sdwa v[212:213], v180 src0_sel:WORD_1
	v_cvt_pk_f32_fp8_e32 v[216:217], v181
	v_cvt_pk_f32_fp8_sdwa v[180:181], v181 src0_sel:WORD_1
	v_cvt_pk_f32_fp8_e32 v[218:219], v182
	v_cvt_pk_f32_fp8_sdwa v[220:221], v182 src0_sel:WORD_1
	v_cvt_pk_f32_fp8_e32 v[222:223], v183
	v_cvt_pk_f32_fp8_sdwa v[182:183], v183 src0_sel:WORD_1
	v_pk_fma_f32 v[194:195], v[194:195], v[60:61], v[198:199] op_sel_hi:[1,0,1]
	v_pk_fma_f32 v[198:199], v[212:213], v[60:61], v[202:203] op_sel_hi:[1,0,1]
	v_pk_fma_f32 v[202:203], v[216:217], v[60:61], v[214:215] op_sel_hi:[1,0,1]
	v_pk_fma_f32 v[180:181], v[180:181], v[60:61], v[184:185] op_sel_hi:[1,0,1]
	v_pk_fma_f32 v[184:185], v[218:219], v[60:61], v[192:193] op_sel_hi:[1,0,1]
	v_pk_fma_f32 v[192:193], v[220:221], v[60:61], v[196:197] op_sel_hi:[1,0,1]
	v_pk_fma_f32 v[196:197], v[222:223], v[60:61], v[200:201] op_sel_hi:[1,0,1]
	v_lshl_or_b32 v37, v37, 7, v136
	global_load_dwordx4 v[220:223], v37, s[4:5] sc0
	v_pk_fma_f32 v[182:183], v[182:183], v[60:61], v[186:187] op_sel_hi:[1,0,1]
	v_cvt_pk_f32_fp8_e32 v[186:187], v172
	v_cvt_pk_f32_fp8_sdwa v[200:201], v172 src0_sel:WORD_1
	v_cvt_pk_f32_fp8_e32 v[212:213], v173
	v_cvt_pk_f32_fp8_sdwa v[172:173], v173 src0_sel:WORD_1
	v_cvt_pk_f32_fp8_e32 v[214:215], v174
	v_cvt_pk_f32_fp8_sdwa v[216:217], v174 src0_sel:WORD_1
	v_cvt_pk_f32_fp8_e32 v[218:219], v175
	v_cvt_pk_f32_fp8_sdwa v[174:175], v175 src0_sel:WORD_1
	v_pk_fma_f32 v[186:187], v[186:187], v[60:61], v[194:195] op_sel:[0,1,0]
	v_pk_fma_f32 v[194:195], v[200:201], v[60:61], v[198:199] op_sel:[0,1,0]
	v_pk_fma_f32 v[198:199], v[212:213], v[60:61], v[202:203] op_sel:[0,1,0]
	v_pk_fma_f32 v[172:173], v[172:173], v[60:61], v[180:181] op_sel:[0,1,0]
	v_pk_fma_f32 v[180:181], v[214:215], v[60:61], v[184:185] op_sel:[0,1,0]
	v_pk_fma_f32 v[184:185], v[216:217], v[60:61], v[192:193] op_sel:[0,1,0]
	v_pk_fma_f32 v[192:193], v[218:219], v[60:61], v[196:197] op_sel:[0,1,0]
	v_lshl_or_b32 v38, v38, 7, v136
	global_load_dwordx4 v[216:219], v38, s[4:5] sc0
	v_pk_fma_f32 v[174:175], v[174:175], v[60:61], v[182:183] op_sel:[0,1,0]
	v_cvt_pk_f32_fp8_e32 v[182:183], v168
	v_cvt_pk_f32_fp8_sdwa v[196:197], v168 src0_sel:WORD_1
	v_cvt_pk_f32_fp8_e32 v[200:201], v169
	v_cvt_pk_f32_fp8_sdwa v[168:169], v169 src0_sel:WORD_1
	v_cvt_pk_f32_fp8_e32 v[202:203], v170
	v_cvt_pk_f32_fp8_sdwa v[212:213], v170 src0_sel:WORD_1
	v_cvt_pk_f32_fp8_e32 v[214:215], v171
	v_cvt_pk_f32_fp8_sdwa v[170:171], v171 src0_sel:WORD_1
	v_pk_fma_f32 v[182:183], v[182:183], v[62:63], v[186:187] op_sel_hi:[1,0,1]
	v_pk_fma_f32 v[186:187], v[196:197], v[62:63], v[194:195] op_sel_hi:[1,0,1]
	v_pk_fma_f32 v[194:195], v[200:201], v[62:63], v[198:199] op_sel_hi:[1,0,1]
	v_pk_fma_f32 v[168:169], v[168:169], v[62:63], v[172:173] op_sel_hi:[1,0,1]
	v_pk_fma_f32 v[172:173], v[202:203], v[62:63], v[180:181] op_sel_hi:[1,0,1]
	v_pk_fma_f32 v[180:181], v[212:213], v[62:63], v[184:185] op_sel_hi:[1,0,1]
	v_pk_fma_f32 v[184:185], v[214:215], v[62:63], v[192:193] op_sel_hi:[1,0,1]
	v_pk_fma_f32 v[170:171], v[170:171], v[62:63], v[174:175] op_sel_hi:[1,0,1]
	v_cvt_pk_f32_fp8_e32 v[174:175], v164
	v_cvt_pk_f32_fp8_sdwa v[192:193], v164 src0_sel:WORD_1
	v_cvt_pk_f32_fp8_e32 v[196:197], v165
	v_cvt_pk_f32_fp8_sdwa v[164:165], v165 src0_sel:WORD_1
	v_cvt_pk_f32_fp8_e32 v[198:199], v166
	v_cvt_pk_f32_fp8_sdwa v[200:201], v166 src0_sel:WORD_1
	v_cvt_pk_f32_fp8_e32 v[202:203], v167
	v_cvt_pk_f32_fp8_sdwa v[166:167], v167 src0_sel:WORD_1
	v_mov_b32_e32 v212, v63
	v_pk_fma_f32 v[174:175], v[174:175], v[212:213], v[182:183] op_sel_hi:[1,0,1]
	v_pk_fma_f32 v[182:183], v[192:193], v[212:213], v[186:187] op_sel_hi:[1,0,1]
	v_pk_fma_f32 v[186:187], v[196:197], v[212:213], v[194:195] op_sel_hi:[1,0,1]
	v_lshl_or_b32 v42, v42, 7, v136
	global_load_dwordx4 v[192:195], v42, s[4:5] sc0
	v_pk_fma_f32 v[164:165], v[164:165], v[212:213], v[168:169] op_sel_hi:[1,0,1]
	v_pk_fma_f32 v[168:169], v[198:199], v[212:213], v[172:173] op_sel_hi:[1,0,1]
	v_lshl_or_b32 v41, v41, 7, v136
	global_load_dwordx4 v[196:199], v41, s[4:5] sc0
	v_pk_fma_f32 v[172:173], v[200:201], v[212:213], v[180:181] op_sel_hi:[1,0,1]
	v_pk_fma_f32 v[180:181], v[202:203], v[212:213], v[184:185] op_sel_hi:[1,0,1]
	v_lshl_or_b32 v40, v40, 7, v136
	global_load_dwordx4 v[200:203], v40, s[4:5] sc0
	v_pk_fma_f32 v[166:167], v[166:167], v[212:213], v[170:171] op_sel_hi:[1,0,1]
	v_lshl_or_b32 v39, v39, 7, v136
	global_load_dwordx4 v[212:215], v39, s[4:5] sc0
	v_permlane32_swap_b32_e32 v174, v168
	v_permlane32_swap_b32_e32 v175, v169
	v_permlane32_swap_b32_e32 v182, v172
	v_permlane32_swap_b32_e32 v183, v173
	v_permlane32_swap_b32_e32 v186, v180
	v_permlane32_swap_b32_e32 v187, v181
	v_permlane32_swap_b32_e32 v164, v166
	v_permlane32_swap_b32_e32 v165, v167
	v_add_f32_e32 v168, v174, v168
	v_add_f32_e32 v169, v175, v169
	v_add_f32_e32 v170, v182, v172
	v_add_f32_e32 v171, v183, v173
	v_add_f32_e32 v172, v186, v180
	v_add_f32_e32 v173, v187, v181
	v_lshl_or_b32 v43, v43, 7, v136
	global_load_dwordx4 v[184:187], v43, s[4:5] sc0
	v_lshl_or_b32 v44, v44, 7, v136
	global_load_dwordx4 v[180:183], v44, s[4:5] sc0
	v_add_f32_e32 v164, v164, v166
	v_add_f32_e32 v165, v165, v167
	v_permlane16_swap_b32_e32 v168, v172
	v_permlane16_swap_b32_e32 v169, v173
	v_permlane16_swap_b32_e32 v170, v164
	v_permlane16_swap_b32_e32 v171, v165
	v_pk_add_f32 v[166:167], v[168:169], v[172:173]
	v_lshl_or_b32 v45, v45, 7, v136
	global_load_dwordx4 v[172:175], v45, s[4:5] sc0
	v_pk_add_f32 v[164:165], v[170:171], v[164:165]
	s_ashr_i32 s7, s6, 31
	v_cndmask_b32_e64 v168, v166, v164, s[0:1]
	v_cndmask_b32_e64 v170, v164, v166, s[0:1]
	v_cndmask_b32_e64 v164, v167, v165, s[0:1]
	v_mov_b32_dpp v168, v168 row_ror:8 row_mask:0xf bank_mask:0xf bound_ctrl:1
	v_cndmask_b32_e64 v171, v165, v167, s[0:1]
	v_mov_b32_dpp v169, v164 row_ror:8 row_mask:0xf bank_mask:0xf bound_ctrl:1
	v_pk_add_f32 v[166:167], v[170:171], v[168:169]
	s_lshl_b64 s[8:9], s[6:7], 11
	v_pk_mul_f32 v[164:165], v[166:167], v[166:167]
	v_cvt_pk_bf16_f32 v168, v166, v167
	v_add_f32_e32 v164, v164, v165
	v_lshl_add_u64 v[166:167], v[130:131], 0, s[8:9]
	global_store_dword v[166:167], v168, off
	v_add_f32_dpp v164, v164, v164 quad_perm:[1,0,3,2] row_mask:0xf bank_mask:0xf bound_ctrl:1
	s_nop 1
	v_add_f32_dpp v164, v164, v164 quad_perm:[2,3,0,1] row_mask:0xf bank_mask:0xf bound_ctrl:1
	s_nop 1
	v_add_f32_dpp v164, v164, v164 row_half_mirror row_mask:0xf bank_mask:0xf bound_ctrl:1
	s_nop 1
	v_add_f32_dpp v164, v164, v164 row_ror:8 row_mask:0xf bank_mask:0xf bound_ctrl:1
	v_mov_b32_e32 v165, v164
	s_nop 1
	v_permlane16_swap_b32_e32 v164, v165
	v_add_f32_e32 v164, v164, v165
	v_mov_b32_e32 v165, v164
	s_nop 1
	v_permlane32_swap_b32_e32 v164, v165
	s_and_saveexec_b64 s[8:9], s[2:3]
	s_lshl_b64 s[10:11], s[6:7], 2
	s_add_u32 s10, s12, s10
	v_add_f32_e32 v164, v164, v165
	s_addc_u32 s11, s13, s11
	global_store_dword v129, v164, s[10:11]
	s_or_b64 exec, exec, s[8:9]
	v_lshl_or_b32 v46, v46, 7, v136
	global_load_dwordx4 v[168:171], v46, s[4:5] sc0
	v_lshl_or_b32 v47, v47, 7, v136
	global_load_dwordx4 v[164:167], v47, s[4:5] sc0
	s_add_u32 s22, s20, 0x300
	s_lshl_b32 s22, s22, 9
	v_lshl_add_u64 v[48:49], v[134:135], 0, s[22:23]
	global_load_dwordx4 v[60:63], v[48:49], off offset:48
	global_load_dwordx4 v[56:59], v[48:49], off offset:32
	global_load_dwordx4 v[52:55], v[48:49], off offset:16
	s_nop 0
	global_load_dwordx4 v[48:51], v[48:49], off
	s_add_u32 s22, s20, 0x500
	s_lshl_b32 s22, s22, 9
	v_lshl_add_u64 v[32:33], v[132:133], 0, s[22:23]
	global_load_dwordx4 v[44:47], v[32:33], off offset:48
	global_load_dwordx4 v[40:43], v[32:33], off offset:32
	global_load_dwordx4 v[36:39], v[32:33], off offset:16
	s_nop 0
	global_load_dwordx4 v[32:35], v[32:33], off
	s_add_u32 s20, s20, 0x200
	s_mov_b32 s24, 61
; #define PU_IDX(t, E, C) do { const char* eb_ = eiu + (size_t)(t) * 512; const char* cb_ = cfu + (size_t)(t) * 512; \
;     _Pragma("unroll") for (int q = 0; q < 4; ++q) { E[q] = *(const i32x4_t*)(eb_ + (eio + 16u * q)); C[q] = *(const f32x4*)(cb_ + (eio + 16u * q)); } } while (0)
; #define PU_TAB(E, W) do { _Pragma("unroll") for (int q = 0; q < 16; ++q) W[q] = *(const u32x4*)(tabu + ((unsigned)E[q >> 2][q & 3] * 128u + tabo)); } while (0)
; DI void phase_peerup(const Params& p, int bid, int nb) {
;     ...
;   for (;;) {
;     PU_TAB(eA, w);
;     const int t1 = t + nw; if (t1 < T_) PU_IDX(t1, eB, cB);
;     PU_MATH(t, w, cA);
.Lpu2_loop:
	s_mov_b32 s8, s20
	s_waitcnt vmcnt(26)
	v_cvt_pk_f32_fp8_e32 v[138:139], v124
	v_cvt_pk_f32_fp8_sdwa v[140:141], v124 src0_sel:WORD_1
	v_cvt_pk_f32_fp8_e32 v[142:143], v125
	v_cvt_pk_f32_fp8_sdwa v[124:125], v125 src0_sel:WORD_1
	v_cvt_pk_f32_fp8_e32 v[144:145], v126
	v_cvt_pk_f32_fp8_sdwa v[146:147], v126 src0_sel:WORD_1
	v_cvt_pk_f32_fp8_e32 v[148:149], v127
	v_cvt_pk_f32_fp8_sdwa v[126:127], v127 src0_sel:WORD_1
	v_cvt_pk_f32_fp8_e32 v[150:151], v120
	v_cvt_pk_f32_fp8_sdwa v[152:153], v120 src0_sel:WORD_1
	v_cvt_pk_f32_fp8_e32 v[154:155], v121
	v_cvt_pk_f32_fp8_sdwa v[120:121], v121 src0_sel:WORD_1
	v_cvt_pk_f32_fp8_e32 v[156:157], v122
	v_cvt_pk_f32_fp8_sdwa v[158:159], v122 src0_sel:WORD_1
	v_cvt_pk_f32_fp8_e32 v[160:161], v123
	v_cvt_pk_f32_fp8_sdwa v[122:123], v123 src0_sel:WORD_1
	v_pk_fma_f32 v[138:139], v[138:139], v[28:29], 0 op_sel_hi:[1,0,0]
	v_pk_fma_f32 v[140:141], v[140:141], v[28:29], 0 op_sel_hi:[1,0,0]
	v_pk_fma_f32 v[142:143], v[142:143], v[28:29], 0 op_sel_hi:[1,0,0]
	v_pk_fma_f32 v[124:125], v[124:125], v[28:29], 0 op_sel_hi:[1,0,0]
	v_pk_fma_f32 v[144:145], v[144:145], v[28:29], 0 op_sel_hi:[1,0,0]
	v_pk_fma_f32 v[146:147], v[146:147], v[28:29], 0 op_sel_hi:[1,0,0]
	v_pk_fma_f32 v[148:149], v[148:149], v[28:29], 0 op_sel_hi:[1,0,0]
	v_pk_fma_f32 v[126:127], v[126:127], v[28:29], 0 op_sel_hi:[1,0,0]
	v_pk_fma_f32 v[138:139], v[150:151], v[28:29], v[138:139] op_sel:[0,1,0]
	v_pk_fma_f32 v[140:141], v[152:153], v[28:29], v[140:141] op_sel:[0,1,0]
	v_pk_fma_f32 v[142:143], v[154:155], v[28:29], v[142:143] op_sel:[0,1,0]
	v_pk_fma_f32 v[120:121], v[120:121], v[28:29], v[124:125] op_sel:[0,1,0]
	v_pk_fma_f32 v[124:125], v[156:157], v[28:29], v[144:145] op_sel:[0,1,0]
	v_pk_fma_f32 v[144:145], v[158:159], v[28:29], v[146:147] op_sel:[0,1,0]
	v_pk_fma_f32 v[146:147], v[160:161], v[28:29], v[148:149] op_sel:[0,1,0]
	v_pk_fma_f32 v[122:123], v[122:123], v[28:29], v[126:127] op_sel:[0,1,0]
	v_cvt_pk_f32_fp8_e32 v[126:127], v116
	v_cvt_pk_f32_fp8_sdwa v[148:149], v116 src0_sel:WORD_1
	v_cvt_pk_f32_fp8_e32 v[150:151], v117
	v_cvt_pk_f32_fp8_sdwa v[116:117], v117 src0_sel:WORD_1
	v_cvt_pk_f32_fp8_e32 v[152:153], v118
	v_cvt_pk_f32_fp8_sdwa v[154:155], v118 src0_sel:WORD_1
	v_cvt_pk_f32_fp8_e32 v[156:157], v119
	v_cvt_pk_f32_fp8_sdwa v[118:119], v119 src0_sel:WORD_1
	v_pk_fma_f32 v[126:127], v[126:127], v[30:31], v[138:139] op_sel_hi:[1,0,1]
	v_pk_fma_f32 v[138:139], v[148:149], v[30:31], v[140:141] op_sel_hi:[1,0,1]
	v_pk_fma_f32 v[140:141], v[150:151], v[30:31], v[142:143] op_sel_hi:[1,0,1]
	v_pk_fma_f32 v[116:117], v[116:117], v[30:31], v[120:121] op_sel_hi:[1,0,1]
	v_pk_fma_f32 v[120:121], v[152:153], v[30:31], v[124:125] op_sel_hi:[1,0,1]
	v_pk_fma_f32 v[124:125], v[154:155], v[30:31], v[144:145] op_sel_hi:[1,0,1]
	v_pk_fma_f32 v[142:143], v[156:157], v[30:31], v[146:147] op_sel_hi:[1,0,1]
	v_pk_fma_f32 v[118:119], v[118:119], v[30:31], v[122:123] op_sel_hi:[1,0,1]
	v_cvt_pk_f32_fp8_e32 v[122:123], v112
	v_cvt_pk_f32_fp8_sdwa v[144:145], v112 src0_sel:WORD_1
	v_cvt_pk_f32_fp8_e32 v[146:147], v113
	v_cvt_pk_f32_fp8_sdwa v[112:113], v113 src0_sel:WORD_1
	v_cvt_pk_f32_fp8_e32 v[148:149], v114
	v_cvt_pk_f32_fp8_sdwa v[150:151], v114 src0_sel:WORD_1
	v_cvt_pk_f32_fp8_e32 v[152:153], v115
	v_cvt_pk_f32_fp8_sdwa v[114:115], v115 src0_sel:WORD_1
	v_mov_b32_e32 v128, v31
	v_pk_fma_f32 v[122:123], v[122:123], v[128:129], v[126:127] op_sel_hi:[1,0,1]
	v_pk_fma_f32 v[126:127], v[144:145], v[128:129], v[138:139] op_sel_hi:[1,0,1]
	v_pk_fma_f32 v[138:139], v[146:147], v[128:129], v[140:141] op_sel_hi:[1,0,1]
	v_pk_fma_f32 v[112:113], v[112:113], v[128:129], v[116:117] op_sel_hi:[1,0,1]
	v_pk_fma_f32 v[116:117], v[148:149], v[128:129], v[120:121] op_sel_hi:[1,0,1]
	v_pk_fma_f32 v[120:121], v[150:151], v[128:129], v[124:125] op_sel_hi:[1,0,1]
	v_pk_fma_f32 v[124:125], v[152:153], v[128:129], v[142:143] op_sel_hi:[1,0,1]
	v_pk_fma_f32 v[114:115], v[114:115], v[128:129], v[118:119] op_sel_hi:[1,0,1]
	v_cvt_pk_f32_fp8_e32 v[118:119], v108
	v_cvt_pk_f32_fp8_sdwa v[140:141], v108 src0_sel:WORD_1
	v_cvt_pk_f32_fp8_e32 v[142:143], v109
	v_cvt_pk_f32_fp8_sdwa v[108:109], v109 src0_sel:WORD_1
	v_cvt_pk_f32_fp8_e32 v[144:145], v110
	v_cvt_pk_f32_fp8_sdwa v[146:147], v110 src0_sel:WORD_1
	v_cvt_pk_f32_fp8_e32 v[148:149], v111
	v_cvt_pk_f32_fp8_sdwa v[110:111], v111 src0_sel:WORD_1
	v_pk_fma_f32 v[118:119], v[118:119], v[24:25], v[122:123] op_sel_hi:[1,0,1]
	v_pk_fma_f32 v[122:123], v[140:141], v[24:25], v[126:127] op_sel_hi:[1,0,1]
	v_pk_fma_f32 v[126:127], v[142:143], v[24:25], v[138:139] op_sel_hi:[1,0,1]
	v_pk_fma_f32 v[108:109], v[108:109], v[24:25], v[112:113] op_sel_hi:[1,0,1]
	v_pk_fma_f32 v[112:113], v[144:145], v[24:25], v[116:117] op_sel_hi:[1,0,1]
	v_pk_fma_f32 v[116:117], v[146:147], v[24:25], v[120:121] op_sel_hi:[1,0,1]
	v_pk_fma_f32 v[120:121], v[148:149], v[24:25], v[124:125] op_sel_hi:[1,0,1]
	v_pk_fma_f32 v[110:111], v[110:111], v[24:25], v[114:115] op_sel_hi:[1,0,1]
	v_cvt_pk_f32_fp8_e32 v[114:115], v104
	v_cvt_pk_f32_fp8_sdwa v[124:125], v104 src0_sel:WORD_1
	v_cvt_pk_f32_fp8_e32 v[138:139], v105
	v_cvt_pk_f32_fp8_sdwa v[104:105], v105 src0_sel:WORD_1
	v_cvt_pk_f32_fp8_e32 v[140:141], v106
	v_cvt_pk_f32_fp8_sdwa v[142:143], v106 src0_sel:WORD_1
	v_cvt_pk_f32_fp8_e32 v[144:145], v107
	v_cvt_pk_f32_fp8_sdwa v[106:107], v107 src0_sel:WORD_1
	v_pk_fma_f32 v[114:115], v[114:115], v[24:25], v[118:119] op_sel:[0,1,0]
	v_pk_fma_f32 v[118:119], v[124:125], v[24:25], v[122:123] op_sel:[0,1,0]
	v_pk_fma_f32 v[122:123], v[138:139], v[24:25], v[126:127] op_sel:[0,1,0]
	v_pk_fma_f32 v[104:105], v[104:105], v[24:25], v[108:109] op_sel:[0,1,0]
	v_pk_fma_f32 v[108:109], v[140:141], v[24:25], v[112:113] op_sel:[0,1,0]
	v_pk_fma_f32 v[112:113], v[142:143], v[24:25], v[116:117] op_sel:[0,1,0]
	v_pk_fma_f32 v[116:117], v[144:145], v[24:25], v[120:121] op_sel:[0,1,0]
	v_pk_fma_f32 v[106:107], v[106:107], v[24:25], v[110:111] op_sel:[0,1,0]
	v_cvt_pk_f32_fp8_e32 v[110:111], v100
	v_cvt_pk_f32_fp8_sdwa v[120:121], v100 src0_sel:WORD_1
	v_cvt_pk_f32_fp8_e32 v[124:125], v101
	v_cvt_pk_f32_fp8_sdwa v[100:101], v101 src0_sel:WORD_1
	v_cvt_pk_f32_fp8_e32 v[126:127], v102
	v_cvt_pk_f32_fp8_sdwa v[138:139], v102 src0_sel:WORD_1
	v_cvt_pk_f32_fp8_e32 v[140:141], v103
	v_cvt_pk_f32_fp8_sdwa v[102:103], v103 src0_sel:WORD_1
	v_pk_fma_f32 v[110:111], v[110:111], v[26:27], v[114:115] op_sel_hi:[1,0,1]
	v_pk_fma_f32 v[114:115], v[120:121], v[26:27], v[118:119] op_sel_hi:[1,0,1]
	v_pk_fma_f32 v[118:119], v[124:125], v[26:27], v[122:123] op_sel_hi:[1,0,1]
	v_pk_fma_f32 v[100:101], v[100:101], v[26:27], v[104:105] op_sel_hi:[1,0,1]
	v_pk_fma_f32 v[104:105], v[126:127], v[26:27], v[108:109] op_sel_hi:[1,0,1]
	v_pk_fma_f32 v[108:109], v[138:139], v[26:27], v[112:113] op_sel_hi:[1,0,1]
	v_pk_fma_f32 v[112:113], v[140:141], v[26:27], v[116:117] op_sel_hi:[1,0,1]
	v_pk_fma_f32 v[102:103], v[102:103], v[26:27], v[106:107] op_sel_hi:[1,0,1]
	v_cvt_pk_f32_fp8_e32 v[106:107], v96
	v_cvt_pk_f32_fp8_sdwa v[116:117], v96 src0_sel:WORD_1
	v_cvt_pk_f32_fp8_e32 v[120:121], v97
	v_cvt_pk_f32_fp8_sdwa v[96:97], v97 src0_sel:WORD_1
	v_cvt_pk_f32_fp8_e32 v[122:123], v98
	v_cvt_pk_f32_fp8_sdwa v[124:125], v98 src0_sel:WORD_1
	v_cvt_pk_f32_fp8_e32 v[126:127], v99
	v_cvt_pk_f32_fp8_sdwa v[98:99], v99 src0_sel:WORD_1
	v_mov_b32_e32 v128, v27
	v_pk_fma_f32 v[106:107], v[106:107], v[128:129], v[110:111] op_sel_hi:[1,0,1]
	v_pk_fma_f32 v[110:111], v[116:117], v[128:129], v[114:115] op_sel_hi:[1,0,1]
	v_pk_fma_f32 v[114:115], v[120:121], v[128:129], v[118:119] op_sel_hi:[1,0,1]
	v_pk_fma_f32 v[96:97], v[96:97], v[128:129], v[100:101] op_sel_hi:[1,0,1]
	v_pk_fma_f32 v[100:101], v[122:123], v[128:129], v[104:105] op_sel_hi:[1,0,1]
	v_pk_fma_f32 v[104:105], v[124:125], v[128:129], v[108:109] op_sel_hi:[1,0,1]
	v_pk_fma_f32 v[108:109], v[126:127], v[128:129], v[112:113] op_sel_hi:[1,0,1]
	v_lshl_or_b32 v12, v12, 7, v136
	global_load_dwordx4 v[124:127], v12, s[4:5] sc0
	v_pk_fma_f32 v[98:99], v[98:99], v[128:129], v[102:103] op_sel_hi:[1,0,1]
	v_cvt_pk_f32_fp8_e32 v[102:103], v92
	v_cvt_pk_f32_fp8_sdwa v[112:113], v92 src0_sel:WORD_1
	v_cvt_pk_f32_fp8_e32 v[116:117], v93
	v_cvt_pk_f32_fp8_sdwa v[92:93], v93 src0_sel:WORD_1
	v_cvt_pk_f32_fp8_e32 v[118:119], v94
	v_cvt_pk_f32_fp8_sdwa v[120:121], v94 src0_sel:WORD_1
	v_cvt_pk_f32_fp8_e32 v[122:123], v95
	v_cvt_pk_f32_fp8_sdwa v[94:95], v95 src0_sel:WORD_1
	v_pk_fma_f32 v[102:103], v[102:103], v[20:21], v[106:107] op_sel_hi:[1,0,1]
	v_pk_fma_f32 v[106:107], v[112:113], v[20:21], v[110:111] op_sel_hi:[1,0,1]
	v_pk_fma_f32 v[110:111], v[116:117], v[20:21], v[114:115] op_sel_hi:[1,0,1]
	v_pk_fma_f32 v[92:93], v[92:93], v[20:21], v[96:97] op_sel_hi:[1,0,1]
	v_pk_fma_f32 v[96:97], v[118:119], v[20:21], v[100:101] op_sel_hi:[1,0,1]
	v_pk_fma_f32 v[100:101], v[120:121], v[20:21], v[104:105] op_sel_hi:[1,0,1]
	v_pk_fma_f32 v[104:105], v[122:123], v[20:21], v[108:109] op_sel_hi:[1,0,1]
	v_lshl_or_b32 v13, v13, 7, v136
	global_load_dwordx4 v[120:123], v13, s[4:5] sc0
	v_pk_fma_f32 v[94:95], v[94:95], v[20:21], v[98:99] op_sel_hi:[1,0,1]
	v_cvt_pk_f32_fp8_e32 v[98:99], v88
	v_cvt_pk_f32_fp8_sdwa v[108:109], v88 src0_sel:WORD_1
	v_cvt_pk_f32_fp8_e32 v[112:113], v89
	v_cvt_pk_f32_fp8_sdwa v[88:89], v89 src0_sel:WORD_1
	v_cvt_pk_f32_fp8_e32 v[114:115], v90
	v_cvt_pk_f32_fp8_sdwa v[116:117], v90 src0_sel:WORD_1
	v_cvt_pk_f32_fp8_e32 v[118:119], v91
	v_cvt_pk_f32_fp8_sdwa v[90:91], v91 src0_sel:WORD_1
	v_pk_fma_f32 v[98:99], v[98:99], v[20:21], v[102:103] op_sel:[0,1,0]
	v_pk_fma_f32 v[102:103], v[108:109], v[20:21], v[106:107] op_sel:[0,1,0]
	v_pk_fma_f32 v[106:107], v[112:113], v[20:21], v[110:111] op_sel:[0,1,0]
	v_pk_fma_f32 v[88:89], v[88:89], v[20:21], v[92:93] op_sel:[0,1,0]
	v_pk_fma_f32 v[92:93], v[114:115], v[20:21], v[96:97] op_sel:[0,1,0]
	v_pk_fma_f32 v[96:97], v[116:117], v[20:21], v[100:101] op_sel:[0,1,0]
	v_pk_fma_f32 v[100:101], v[118:119], v[20:21], v[104:105] op_sel:[0,1,0]
	v_lshl_or_b32 v14, v14, 7, v136
	global_load_dwordx4 v[116:119], v14, s[4:5] sc0
	v_pk_fma_f32 v[90:91], v[90:91], v[20:21], v[94:95] op_sel:[0,1,0]
	v_cvt_pk_f32_fp8_e32 v[94:95], v84
	v_cvt_pk_f32_fp8_sdwa v[104:105], v84 src0_sel:WORD_1
	v_cvt_pk_f32_fp8_e32 v[108:109], v85
	v_cvt_pk_f32_fp8_sdwa v[84:85], v85 src0_sel:WORD_1
	v_cvt_pk_f32_fp8_e32 v[110:111], v86
	v_cvt_pk_f32_fp8_sdwa v[112:113], v86 src0_sel:WORD_1
	v_cvt_pk_f32_fp8_e32 v[114:115], v87
	v_cvt_pk_f32_fp8_sdwa v[86:87], v87 src0_sel:WORD_1
	v_pk_fma_f32 v[94:95], v[94:95], v[22:23], v[98:99] op_sel_hi:[1,0,1]
	v_pk_fma_f32 v[98:99], v[104:105], v[22:23], v[102:103] op_sel_hi:[1,0,1]
	v_pk_fma_f32 v[102:103], v[108:109], v[22:23], v[106:107] op_sel_hi:[1,0,1]
	v_pk_fma_f32 v[84:85], v[84:85], v[22:23], v[88:89] op_sel_hi:[1,0,1]
	v_pk_fma_f32 v[88:89], v[110:111], v[22:23], v[92:93] op_sel_hi:[1,0,1]
	v_pk_fma_f32 v[92:93], v[112:113], v[22:23], v[96:97] op_sel_hi:[1,0,1]
	v_pk_fma_f32 v[96:97], v[114:115], v[22:23], v[100:101] op_sel_hi:[1,0,1]
	v_pk_fma_f32 v[86:87], v[86:87], v[22:23], v[90:91] op_sel_hi:[1,0,1]
	v_cvt_pk_f32_fp8_e32 v[90:91], v80
	v_cvt_pk_f32_fp8_sdwa v[100:101], v80 src0_sel:WORD_1
	v_cvt_pk_f32_fp8_e32 v[104:105], v81
	v_cvt_pk_f32_fp8_sdwa v[80:81], v81 src0_sel:WORD_1
	v_cvt_pk_f32_fp8_e32 v[106:107], v82
	v_cvt_pk_f32_fp8_sdwa v[108:109], v82 src0_sel:WORD_1
	v_cvt_pk_f32_fp8_e32 v[110:111], v83
	v_cvt_pk_f32_fp8_sdwa v[82:83], v83 src0_sel:WORD_1
	v_mov_b32_e32 v112, v23
	v_pk_fma_f32 v[90:91], v[90:91], v[112:113], v[94:95] op_sel_hi:[1,0,1]
	v_pk_fma_f32 v[94:95], v[100:101], v[112:113], v[98:99] op_sel_hi:[1,0,1]
	v_pk_fma_f32 v[98:99], v[104:105], v[112:113], v[102:103] op_sel_hi:[1,0,1]
	v_pk_fma_f32 v[80:81], v[80:81], v[112:113], v[84:85] op_sel_hi:[1,0,1]
	v_pk_fma_f32 v[84:85], v[106:107], v[112:113], v[88:89] op_sel_hi:[1,0,1]
	v_pk_fma_f32 v[88:89], v[108:109], v[112:113], v[92:93] op_sel_hi:[1,0,1]
	v_pk_fma_f32 v[92:93], v[110:111], v[112:113], v[96:97] op_sel_hi:[1,0,1]
	v_lshl_or_b32 v8, v8, 7, v136
	global_load_dwordx4 v[108:111], v8, s[4:5] sc0
	v_pk_fma_f32 v[82:83], v[82:83], v[112:113], v[86:87] op_sel_hi:[1,0,1]
	v_lshl_or_b32 v15, v15, 7, v136
	global_load_dwordx4 v[112:115], v15, s[4:5] sc0
	v_cvt_pk_f32_fp8_e32 v[86:87], v76
	v_cvt_pk_f32_fp8_sdwa v[96:97], v76 src0_sel:WORD_1
	v_cvt_pk_f32_fp8_e32 v[100:101], v77
	v_cvt_pk_f32_fp8_sdwa v[76:77], v77 src0_sel:WORD_1
	v_cvt_pk_f32_fp8_e32 v[102:103], v78
	v_cvt_pk_f32_fp8_sdwa v[104:105], v78 src0_sel:WORD_1
	v_cvt_pk_f32_fp8_e32 v[106:107], v79
	v_cvt_pk_f32_fp8_sdwa v[78:79], v79 src0_sel:WORD_1
	v_pk_fma_f32 v[86:87], v[86:87], v[16:17], v[90:91] op_sel_hi:[1,0,1]
	v_pk_fma_f32 v[90:91], v[96:97], v[16:17], v[94:95] op_sel_hi:[1,0,1]
	v_pk_fma_f32 v[94:95], v[100:101], v[16:17], v[98:99] op_sel_hi:[1,0,1]
	v_pk_fma_f32 v[76:77], v[76:77], v[16:17], v[80:81] op_sel_hi:[1,0,1]
	v_pk_fma_f32 v[80:81], v[102:103], v[16:17], v[84:85] op_sel_hi:[1,0,1]
	v_pk_fma_f32 v[84:85], v[104:105], v[16:17], v[88:89] op_sel_hi:[1,0,1]
	v_pk_fma_f32 v[88:89], v[106:107], v[16:17], v[92:93] op_sel_hi:[1,0,1]
	v_lshl_or_b32 v9, v9, 7, v136
	global_load_dwordx4 v[104:107], v9, s[4:5] sc0
	v_pk_fma_f32 v[78:79], v[78:79], v[16:17], v[82:83] op_sel_hi:[1,0,1]
	v_cvt_pk_f32_fp8_e32 v[82:83], v72
	v_cvt_pk_f32_fp8_sdwa v[92:93], v72 src0_sel:WORD_1
	v_cvt_pk_f32_fp8_e32 v[96:97], v73
	v_cvt_pk_f32_fp8_sdwa v[72:73], v73 src0_sel:WORD_1
	v_cvt_pk_f32_fp8_e32 v[98:99], v74
	v_cvt_pk_f32_fp8_sdwa v[100:101], v74 src0_sel:WORD_1
	v_cvt_pk_f32_fp8_e32 v[102:103], v75
	v_cvt_pk_f32_fp8_sdwa v[74:75], v75 src0_sel:WORD_1
	v_pk_fma_f32 v[82:83], v[82:83], v[16:17], v[86:87] op_sel:[0,1,0]
	v_pk_fma_f32 v[86:87], v[92:93], v[16:17], v[90:91] op_sel:[0,1,0]
	v_pk_fma_f32 v[90:91], v[96:97], v[16:17], v[94:95] op_sel:[0,1,0]
	v_pk_fma_f32 v[72:73], v[72:73], v[16:17], v[76:77] op_sel:[0,1,0]
	v_pk_fma_f32 v[76:77], v[98:99], v[16:17], v[80:81] op_sel:[0,1,0]
	v_pk_fma_f32 v[80:81], v[100:101], v[16:17], v[84:85] op_sel:[0,1,0]
	v_pk_fma_f32 v[84:85], v[102:103], v[16:17], v[88:89] op_sel:[0,1,0]
	v_lshl_or_b32 v10, v10, 7, v136
	global_load_dwordx4 v[100:103], v10, s[4:5] sc0
	v_pk_fma_f32 v[74:75], v[74:75], v[16:17], v[78:79] op_sel:[0,1,0]
	v_cvt_pk_f32_fp8_e32 v[78:79], v68
	v_cvt_pk_f32_fp8_sdwa v[88:89], v68 src0_sel:WORD_1
	v_cvt_pk_f32_fp8_e32 v[92:93], v69
	v_cvt_pk_f32_fp8_sdwa v[68:69], v69 src0_sel:WORD_1
	v_cvt_pk_f32_fp8_e32 v[94:95], v70
	v_cvt_pk_f32_fp8_sdwa v[96:97], v70 src0_sel:WORD_1
	v_cvt_pk_f32_fp8_e32 v[98:99], v71
	v_cvt_pk_f32_fp8_sdwa v[70:71], v71 src0_sel:WORD_1
	v_pk_fma_f32 v[78:79], v[78:79], v[18:19], v[82:83] op_sel_hi:[1,0,1]
	v_pk_fma_f32 v[82:83], v[88:89], v[18:19], v[86:87] op_sel_hi:[1,0,1]
	v_pk_fma_f32 v[86:87], v[92:93], v[18:19], v[90:91] op_sel_hi:[1,0,1]
	v_pk_fma_f32 v[68:69], v[68:69], v[18:19], v[72:73] op_sel_hi:[1,0,1]
	v_pk_fma_f32 v[72:73], v[94:95], v[18:19], v[76:77] op_sel_hi:[1,0,1]
	v_pk_fma_f32 v[76:77], v[96:97], v[18:19], v[80:81] op_sel_hi:[1,0,1]
	v_pk_fma_f32 v[80:81], v[98:99], v[18:19], v[84:85] op_sel_hi:[1,0,1]
	v_pk_fma_f32 v[70:71], v[70:71], v[18:19], v[74:75] op_sel_hi:[1,0,1]
	v_cvt_pk_f32_fp8_e32 v[74:75], v64
	v_cvt_pk_f32_fp8_sdwa v[84:85], v64 src0_sel:WORD_1
	v_cvt_pk_f32_fp8_e32 v[88:89], v65
	v_cvt_pk_f32_fp8_sdwa v[64:65], v65 src0_sel:WORD_1
	v_cvt_pk_f32_fp8_e32 v[90:91], v66
	v_cvt_pk_f32_fp8_sdwa v[92:93], v66 src0_sel:WORD_1
	v_cvt_pk_f32_fp8_e32 v[94:95], v67
	v_cvt_pk_f32_fp8_sdwa v[66:67], v67 src0_sel:WORD_1
	v_mov_b32_e32 v96, v19
	v_pk_fma_f32 v[74:75], v[74:75], v[96:97], v[78:79] op_sel_hi:[1,0,1]
	v_pk_fma_f32 v[78:79], v[84:85], v[96:97], v[82:83] op_sel_hi:[1,0,1]
	v_pk_fma_f32 v[82:83], v[88:89], v[96:97], v[86:87] op_sel_hi:[1,0,1]
	v_lshl_or_b32 v6, v6, 7, v136
	global_load_dwordx4 v[84:87], v6, s[4:5] sc0
	v_pk_fma_f32 v[64:65], v[64:65], v[96:97], v[68:69] op_sel_hi:[1,0,1]
	v_pk_fma_f32 v[68:69], v[90:91], v[96:97], v[72:73] op_sel_hi:[1,0,1]
	v_lshl_or_b32 v5, v5, 7, v136
	global_load_dwordx4 v[88:91], v5, s[4:5] sc0
	v_pk_fma_f32 v[72:73], v[92:93], v[96:97], v[76:77] op_sel_hi:[1,0,1]
	v_pk_fma_f32 v[76:77], v[94:95], v[96:97], v[80:81] op_sel_hi:[1,0,1]
	v_lshl_or_b32 v4, v4, 7, v136
	global_load_dwordx4 v[92:95], v4, s[4:5] sc0
	v_pk_fma_f32 v[66:67], v[66:67], v[96:97], v[70:71] op_sel_hi:[1,0,1]
	v_lshl_or_b32 v11, v11, 7, v136
	global_load_dwordx4 v[96:99], v11, s[4:5] sc0
	v_permlane32_swap_b32_e32 v74, v68
	v_permlane32_swap_b32_e32 v75, v69
	v_permlane32_swap_b32_e32 v78, v72
	v_permlane32_swap_b32_e32 v79, v73
	v_permlane32_swap_b32_e32 v82, v76
	v_permlane32_swap_b32_e32 v83, v77
	v_permlane32_swap_b32_e32 v64, v66
	v_permlane32_swap_b32_e32 v65, v67
	v_add_f32_e32 v68, v74, v68
	v_add_f32_e32 v69, v75, v69
	v_add_f32_e32 v70, v78, v72
	v_add_f32_e32 v71, v79, v73
	v_add_f32_e32 v72, v82, v76
	v_add_f32_e32 v73, v83, v77
	v_lshl_or_b32 v7, v7, 7, v136
	global_load_dwordx4 v[80:83], v7, s[4:5] sc0
	v_lshl_or_b32 v0, v0, 7, v136
	global_load_dwordx4 v[76:79], v0, s[4:5] sc0
	v_add_f32_e32 v64, v64, v66
	v_add_f32_e32 v65, v65, v67
	v_permlane16_swap_b32_e32 v68, v72
	v_permlane16_swap_b32_e32 v69, v73
	v_permlane16_swap_b32_e32 v70, v64
	v_permlane16_swap_b32_e32 v71, v65
	v_pk_add_f32 v[66:67], v[68:69], v[72:73]
	v_lshl_or_b32 v1, v1, 7, v136
	global_load_dwordx4 v[72:75], v1, s[4:5] sc0
	v_pk_add_f32 v[64:65], v[70:71], v[64:65]
	s_ashr_i32 s9, s8, 31
	v_cndmask_b32_e64 v68, v66, v64, s[0:1]
	v_cndmask_b32_e64 v70, v64, v66, s[0:1]
	v_cndmask_b32_e64 v64, v67, v65, s[0:1]
	v_mov_b32_dpp v68, v68 row_ror:8 row_mask:0xf bank_mask:0xf bound_ctrl:1
	v_cndmask_b32_e64 v71, v65, v67, s[0:1]
	v_mov_b32_dpp v69, v64 row_ror:8 row_mask:0xf bank_mask:0xf bound_ctrl:1
	v_pk_add_f32 v[66:67], v[70:71], v[68:69]
	s_lshl_b64 s[10:11], s[8:9], 11
	v_pk_mul_f32 v[64:65], v[66:67], v[66:67]
	v_cvt_pk_bf16_f32 v68, v66, v67
	v_add_f32_e32 v64, v64, v65
	v_lshl_add_u64 v[66:67], v[130:131], 0, s[10:11]
	global_store_dword v[66:67], v68, off
	v_add_f32_dpp v64, v64, v64 quad_perm:[1,0,3,2] row_mask:0xf bank_mask:0xf bound_ctrl:1
	s_nop 1
	v_add_f32_dpp v64, v64, v64 quad_perm:[2,3,0,1] row_mask:0xf bank_mask:0xf bound_ctrl:1
	s_nop 1
	v_add_f32_dpp v64, v64, v64 row_half_mirror row_mask:0xf bank_mask:0xf bound_ctrl:1
	s_nop 1
	v_add_f32_dpp v64, v64, v64 row_ror:8 row_mask:0xf bank_mask:0xf bound_ctrl:1
	v_mov_b32_e32 v65, v64
	s_nop 1
	v_permlane16_swap_b32_e32 v64, v65
	v_add_f32_e32 v64, v64, v65
	v_mov_b32_e32 v65, v64
	s_nop 1
	v_permlane32_swap_b32_e32 v64, v65
	s_and_saveexec_b64 s[10:11], s[2:3]
	s_lshl_b64 s[16:17], s[8:9], 2
	s_add_u32 s16, s12, s16
	v_add_f32_e32 v64, v64, v65
	s_addc_u32 s17, s13, s17
	global_store_dword v129, v64, s[16:17]
	s_or_b64 exec, exec, s[10:11]
	v_lshl_or_b32 v2, v2, 7, v136
	global_load_dwordx4 v[68:71], v2, s[4:5] sc0
	v_lshl_or_b32 v3, v3, 7, v136
	global_load_dwordx4 v[64:67], v3, s[4:5] sc0
	s_add_u32 s22, s20, 0x200
	s_lshl_b32 s22, s22, 9
	v_lshl_add_u64 v[28:29], v[134:135], 0, s[22:23]
	global_load_dwordx4 v[16:19], v[28:29], off offset:48
	global_load_dwordx4 v[20:23], v[28:29], off offset:32
	global_load_dwordx4 v[24:27], v[28:29], off offset:16
	s_nop 0
	global_load_dwordx4 v[28:31], v[28:29], off
	s_add_u32 s22, s20, 0x400
	s_lshl_b32 s22, s22, 9
	v_lshl_add_u64 v[12:13], v[132:133], 0, s[22:23]
	global_load_dwordx4 v[0:3], v[12:13], off offset:48
	global_load_dwordx4 v[4:7], v[12:13], off offset:32
	global_load_dwordx4 v[8:11], v[12:13], off offset:16
	s_nop 0
	global_load_dwordx4 v[12:15], v[12:13], off
	s_add_u32 s6, s20, 0x100
	s_waitcnt vmcnt(26)
	v_cvt_pk_f32_fp8_e32 v[138:139], v240
	v_cvt_pk_f32_fp8_sdwa v[140:141], v240 src0_sel:WORD_1
	v_cvt_pk_f32_fp8_e32 v[142:143], v241
	v_cvt_pk_f32_fp8_sdwa v[240:241], v241 src0_sel:WORD_1
	v_cvt_pk_f32_fp8_e32 v[144:145], v242
	v_cvt_pk_f32_fp8_sdwa v[146:147], v242 src0_sel:WORD_1
	v_cvt_pk_f32_fp8_e32 v[148:149], v243
	v_cvt_pk_f32_fp8_sdwa v[242:243], v243 src0_sel:WORD_1
	v_cvt_pk_f32_fp8_e32 v[150:151], v236
	v_cvt_pk_f32_fp8_sdwa v[152:153], v236 src0_sel:WORD_1
	v_cvt_pk_f32_fp8_e32 v[154:155], v237
	v_cvt_pk_f32_fp8_sdwa v[236:237], v237 src0_sel:WORD_1
	v_cvt_pk_f32_fp8_e32 v[156:157], v238
	v_cvt_pk_f32_fp8_sdwa v[158:159], v238 src0_sel:WORD_1
	v_cvt_pk_f32_fp8_e32 v[160:161], v239
	v_cvt_pk_f32_fp8_sdwa v[238:239], v239 src0_sel:WORD_1
	v_pk_fma_f32 v[138:139], v[138:139], v[48:49], 0 op_sel_hi:[1,0,0]
	v_pk_fma_f32 v[140:141], v[140:141], v[48:49], 0 op_sel_hi:[1,0,0]
	v_pk_fma_f32 v[142:143], v[142:143], v[48:49], 0 op_sel_hi:[1,0,0]
	v_pk_fma_f32 v[240:241], v[240:241], v[48:49], 0 op_sel_hi:[1,0,0]
	v_pk_fma_f32 v[144:145], v[144:145], v[48:49], 0 op_sel_hi:[1,0,0]
	v_pk_fma_f32 v[146:147], v[146:147], v[48:49], 0 op_sel_hi:[1,0,0]
	v_pk_fma_f32 v[148:149], v[148:149], v[48:49], 0 op_sel_hi:[1,0,0]
	v_pk_fma_f32 v[242:243], v[242:243], v[48:49], 0 op_sel_hi:[1,0,0]
	v_pk_fma_f32 v[138:139], v[150:151], v[48:49], v[138:139] op_sel:[0,1,0]
	v_pk_fma_f32 v[140:141], v[152:153], v[48:49], v[140:141] op_sel:[0,1,0]
	v_pk_fma_f32 v[142:143], v[154:155], v[48:49], v[142:143] op_sel:[0,1,0]
	v_pk_fma_f32 v[236:237], v[236:237], v[48:49], v[240:241] op_sel:[0,1,0]
	v_pk_fma_f32 v[240:241], v[156:157], v[48:49], v[144:145] op_sel:[0,1,0]
	v_pk_fma_f32 v[144:145], v[158:159], v[48:49], v[146:147] op_sel:[0,1,0]
	v_pk_fma_f32 v[146:147], v[160:161], v[48:49], v[148:149] op_sel:[0,1,0]
	v_pk_fma_f32 v[238:239], v[238:239], v[48:49], v[242:243] op_sel:[0,1,0]
	v_cvt_pk_f32_fp8_e32 v[242:243], v232
	v_cvt_pk_f32_fp8_sdwa v[148:149], v232 src0_sel:WORD_1
	v_cvt_pk_f32_fp8_e32 v[150:151], v233
	v_cvt_pk_f32_fp8_sdwa v[232:233], v233 src0_sel:WORD_1
	v_cvt_pk_f32_fp8_e32 v[152:153], v234
	v_cvt_pk_f32_fp8_sdwa v[154:155], v234 src0_sel:WORD_1
	v_cvt_pk_f32_fp8_e32 v[156:157], v235
	v_cvt_pk_f32_fp8_sdwa v[234:235], v235 src0_sel:WORD_1
	v_pk_fma_f32 v[242:243], v[242:243], v[50:51], v[138:139] op_sel_hi:[1,0,1]
	v_pk_fma_f32 v[138:139], v[148:149], v[50:51], v[140:141] op_sel_hi:[1,0,1]
	v_pk_fma_f32 v[140:141], v[150:151], v[50:51], v[142:143] op_sel_hi:[1,0,1]
	v_pk_fma_f32 v[232:233], v[232:233], v[50:51], v[236:237] op_sel_hi:[1,0,1]
	v_pk_fma_f32 v[236:237], v[152:153], v[50:51], v[240:241] op_sel_hi:[1,0,1]
	v_pk_fma_f32 v[240:241], v[154:155], v[50:51], v[144:145] op_sel_hi:[1,0,1]
	v_pk_fma_f32 v[142:143], v[156:157], v[50:51], v[146:147] op_sel_hi:[1,0,1]
	v_pk_fma_f32 v[234:235], v[234:235], v[50:51], v[238:239] op_sel_hi:[1,0,1]
	v_cvt_pk_f32_fp8_e32 v[238:239], v228
	v_cvt_pk_f32_fp8_sdwa v[144:145], v228 src0_sel:WORD_1
	v_cvt_pk_f32_fp8_e32 v[146:147], v229
	v_cvt_pk_f32_fp8_sdwa v[228:229], v229 src0_sel:WORD_1
	v_cvt_pk_f32_fp8_e32 v[148:149], v230
	v_cvt_pk_f32_fp8_sdwa v[150:151], v230 src0_sel:WORD_1
	v_cvt_pk_f32_fp8_e32 v[152:153], v231
	v_cvt_pk_f32_fp8_sdwa v[230:231], v231 src0_sel:WORD_1
	v_mov_b32_e32 v128, v51
	v_pk_fma_f32 v[238:239], v[238:239], v[128:129], v[242:243] op_sel_hi:[1,0,1]
	v_pk_fma_f32 v[242:243], v[144:145], v[128:129], v[138:139] op_sel_hi:[1,0,1]
	v_pk_fma_f32 v[138:139], v[146:147], v[128:129], v[140:141] op_sel_hi:[1,0,1]
	v_pk_fma_f32 v[228:229], v[228:229], v[128:129], v[232:233] op_sel_hi:[1,0,1]
	v_pk_fma_f32 v[232:233], v[148:149], v[128:129], v[236:237] op_sel_hi:[1,0,1]
	v_pk_fma_f32 v[236:237], v[150:151], v[128:129], v[240:241] op_sel_hi:[1,0,1]
	v_pk_fma_f32 v[240:241], v[152:153], v[128:129], v[142:143] op_sel_hi:[1,0,1]
	v_pk_fma_f32 v[230:231], v[230:231], v[128:129], v[234:235] op_sel_hi:[1,0,1]
	v_cvt_pk_f32_fp8_e32 v[234:235], v224
	v_cvt_pk_f32_fp8_sdwa v[140:141], v224 src0_sel:WORD_1
	v_cvt_pk_f32_fp8_e32 v[142:143], v225
	v_cvt_pk_f32_fp8_sdwa v[224:225], v225 src0_sel:WORD_1
	v_cvt_pk_f32_fp8_e32 v[144:145], v226
	v_cvt_pk_f32_fp8_sdwa v[146:147], v226 src0_sel:WORD_1
	v_cvt_pk_f32_fp8_e32 v[148:149], v227
	v_cvt_pk_f32_fp8_sdwa v[226:227], v227 src0_sel:WORD_1
	v_pk_fma_f32 v[234:235], v[234:235], v[52:53], v[238:239] op_sel_hi:[1,0,1]
	v_pk_fma_f32 v[238:239], v[140:141], v[52:53], v[242:243] op_sel_hi:[1,0,1]
	v_pk_fma_f32 v[242:243], v[142:143], v[52:53], v[138:139] op_sel_hi:[1,0,1]
	v_pk_fma_f32 v[224:225], v[224:225], v[52:53], v[228:229] op_sel_hi:[1,0,1]
	v_pk_fma_f32 v[228:229], v[144:145], v[52:53], v[232:233] op_sel_hi:[1,0,1]
	v_pk_fma_f32 v[232:233], v[146:147], v[52:53], v[236:237] op_sel_hi:[1,0,1]
	v_pk_fma_f32 v[236:237], v[148:149], v[52:53], v[240:241] op_sel_hi:[1,0,1]
	v_pk_fma_f32 v[226:227], v[226:227], v[52:53], v[230:231] op_sel_hi:[1,0,1]
	v_cvt_pk_f32_fp8_e32 v[230:231], v220
	v_cvt_pk_f32_fp8_sdwa v[240:241], v220 src0_sel:WORD_1
	v_cvt_pk_f32_fp8_e32 v[138:139], v221
	v_cvt_pk_f32_fp8_sdwa v[220:221], v221 src0_sel:WORD_1
	v_cvt_pk_f32_fp8_e32 v[140:141], v222
	v_cvt_pk_f32_fp8_sdwa v[142:143], v222 src0_sel:WORD_1
	v_cvt_pk_f32_fp8_e32 v[144:145], v223
	v_cvt_pk_f32_fp8_sdwa v[222:223], v223 src0_sel:WORD_1
	v_pk_fma_f32 v[230:231], v[230:231], v[52:53], v[234:235] op_sel:[0,1,0]
	v_pk_fma_f32 v[234:235], v[240:241], v[52:53], v[238:239] op_sel:[0,1,0]
	v_pk_fma_f32 v[238:239], v[138:139], v[52:53], v[242:243] op_sel:[0,1,0]
	v_pk_fma_f32 v[220:221], v[220:221], v[52:53], v[224:225] op_sel:[0,1,0]
	v_pk_fma_f32 v[224:225], v[140:141], v[52:53], v[228:229] op_sel:[0,1,0]
	v_pk_fma_f32 v[228:229], v[142:143], v[52:53], v[232:233] op_sel:[0,1,0]
	v_pk_fma_f32 v[232:233], v[144:145], v[52:53], v[236:237] op_sel:[0,1,0]
	v_pk_fma_f32 v[222:223], v[222:223], v[52:53], v[226:227] op_sel:[0,1,0]
	v_cvt_pk_f32_fp8_e32 v[226:227], v216
	v_cvt_pk_f32_fp8_sdwa v[236:237], v216 src0_sel:WORD_1
	v_cvt_pk_f32_fp8_e32 v[240:241], v217
	v_cvt_pk_f32_fp8_sdwa v[216:217], v217 src0_sel:WORD_1
	v_cvt_pk_f32_fp8_e32 v[242:243], v218
	v_cvt_pk_f32_fp8_sdwa v[138:139], v218 src0_sel:WORD_1
	v_cvt_pk_f32_fp8_e32 v[140:141], v219
	v_cvt_pk_f32_fp8_sdwa v[218:219], v219 src0_sel:WORD_1
	v_pk_fma_f32 v[226:227], v[226:227], v[54:55], v[230:231] op_sel_hi:[1,0,1]
	v_pk_fma_f32 v[230:231], v[236:237], v[54:55], v[234:235] op_sel_hi:[1,0,1]
	v_pk_fma_f32 v[234:235], v[240:241], v[54:55], v[238:239] op_sel_hi:[1,0,1]
	v_pk_fma_f32 v[216:217], v[216:217], v[54:55], v[220:221] op_sel_hi:[1,0,1]
	v_pk_fma_f32 v[220:221], v[242:243], v[54:55], v[224:225] op_sel_hi:[1,0,1]
	v_pk_fma_f32 v[224:225], v[138:139], v[54:55], v[228:229] op_sel_hi:[1,0,1]
	v_pk_fma_f32 v[228:229], v[140:141], v[54:55], v[232:233] op_sel_hi:[1,0,1]
	v_pk_fma_f32 v[218:219], v[218:219], v[54:55], v[222:223] op_sel_hi:[1,0,1]
	v_cvt_pk_f32_fp8_e32 v[222:223], v212
	v_cvt_pk_f32_fp8_sdwa v[232:233], v212 src0_sel:WORD_1
	v_cvt_pk_f32_fp8_e32 v[236:237], v213
	v_cvt_pk_f32_fp8_sdwa v[212:213], v213 src0_sel:WORD_1
	v_cvt_pk_f32_fp8_e32 v[238:239], v214
	v_cvt_pk_f32_fp8_sdwa v[240:241], v214 src0_sel:WORD_1
	v_cvt_pk_f32_fp8_e32 v[242:243], v215
	v_cvt_pk_f32_fp8_sdwa v[214:215], v215 src0_sel:WORD_1
	v_mov_b32_e32 v128, v55
	v_pk_fma_f32 v[222:223], v[222:223], v[128:129], v[226:227] op_sel_hi:[1,0,1]
	v_pk_fma_f32 v[226:227], v[232:233], v[128:129], v[230:231] op_sel_hi:[1,0,1]
	v_pk_fma_f32 v[230:231], v[236:237], v[128:129], v[234:235] op_sel_hi:[1,0,1]
	v_pk_fma_f32 v[212:213], v[212:213], v[128:129], v[216:217] op_sel_hi:[1,0,1]
	v_pk_fma_f32 v[216:217], v[238:239], v[128:129], v[220:221] op_sel_hi:[1,0,1]
	v_pk_fma_f32 v[220:221], v[240:241], v[128:129], v[224:225] op_sel_hi:[1,0,1]
	v_pk_fma_f32 v[224:225], v[242:243], v[128:129], v[228:229] op_sel_hi:[1,0,1]
	v_lshl_or_b32 v32, v32, 7, v136
	global_load_dwordx4 v[240:243], v32, s[4:5] sc0
	v_pk_fma_f32 v[214:215], v[214:215], v[128:129], v[218:219] op_sel_hi:[1,0,1]
	v_cvt_pk_f32_fp8_e32 v[218:219], v200
	v_cvt_pk_f32_fp8_sdwa v[228:229], v200 src0_sel:WORD_1
	v_cvt_pk_f32_fp8_e32 v[232:233], v201
	v_cvt_pk_f32_fp8_sdwa v[200:201], v201 src0_sel:WORD_1
	v_cvt_pk_f32_fp8_e32 v[234:235], v202
	v_cvt_pk_f32_fp8_sdwa v[236:237], v202 src0_sel:WORD_1
	v_cvt_pk_f32_fp8_e32 v[238:239], v203
	v_cvt_pk_f32_fp8_sdwa v[202:203], v203 src0_sel:WORD_1
	v_pk_fma_f32 v[218:219], v[218:219], v[56:57], v[222:223] op_sel_hi:[1,0,1]
	v_pk_fma_f32 v[222:223], v[228:229], v[56:57], v[226:227] op_sel_hi:[1,0,1]
	v_pk_fma_f32 v[226:227], v[232:233], v[56:57], v[230:231] op_sel_hi:[1,0,1]
	v_pk_fma_f32 v[200:201], v[200:201], v[56:57], v[212:213] op_sel_hi:[1,0,1]
	v_pk_fma_f32 v[212:213], v[234:235], v[56:57], v[216:217] op_sel_hi:[1,0,1]
	v_pk_fma_f32 v[216:217], v[236:237], v[56:57], v[220:221] op_sel_hi:[1,0,1]
	v_pk_fma_f32 v[220:221], v[238:239], v[56:57], v[224:225] op_sel_hi:[1,0,1]
	v_lshl_or_b32 v33, v33, 7, v136
	global_load_dwordx4 v[236:239], v33, s[4:5] sc0
	v_pk_fma_f32 v[202:203], v[202:203], v[56:57], v[214:215] op_sel_hi:[1,0,1]
	v_cvt_pk_f32_fp8_e32 v[214:215], v196
	v_cvt_pk_f32_fp8_sdwa v[224:225], v196 src0_sel:WORD_1
	v_cvt_pk_f32_fp8_e32 v[228:229], v197
	v_cvt_pk_f32_fp8_sdwa v[196:197], v197 src0_sel:WORD_1
	v_cvt_pk_f32_fp8_e32 v[230:231], v198
	v_cvt_pk_f32_fp8_sdwa v[232:233], v198 src0_sel:WORD_1
	v_cvt_pk_f32_fp8_e32 v[234:235], v199
	v_cvt_pk_f32_fp8_sdwa v[198:199], v199 src0_sel:WORD_1
	v_pk_fma_f32 v[214:215], v[214:215], v[56:57], v[218:219] op_sel:[0,1,0]
	v_pk_fma_f32 v[218:219], v[224:225], v[56:57], v[222:223] op_sel:[0,1,0]
	v_pk_fma_f32 v[222:223], v[228:229], v[56:57], v[226:227] op_sel:[0,1,0]
	v_pk_fma_f32 v[196:197], v[196:197], v[56:57], v[200:201] op_sel:[0,1,0]
	v_pk_fma_f32 v[200:201], v[230:231], v[56:57], v[212:213] op_sel:[0,1,0]
	v_pk_fma_f32 v[212:213], v[232:233], v[56:57], v[216:217] op_sel:[0,1,0]
	v_pk_fma_f32 v[216:217], v[234:235], v[56:57], v[220:221] op_sel:[0,1,0]
	v_lshl_or_b32 v34, v34, 7, v136
	global_load_dwordx4 v[232:235], v34, s[4:5] sc0
	v_pk_fma_f32 v[198:199], v[198:199], v[56:57], v[202:203] op_sel:[0,1,0]
	v_cvt_pk_f32_fp8_e32 v[202:203], v192
	v_cvt_pk_f32_fp8_sdwa v[220:221], v192 src0_sel:WORD_1
	v_cvt_pk_f32_fp8_e32 v[224:225], v193
	v_cvt_pk_f32_fp8_sdwa v[192:193], v193 src0_sel:WORD_1
	v_cvt_pk_f32_fp8_e32 v[226:227], v194
	v_cvt_pk_f32_fp8_sdwa v[228:229], v194 src0_sel:WORD_1
	v_cvt_pk_f32_fp8_e32 v[230:231], v195
	v_cvt_pk_f32_fp8_sdwa v[194:195], v195 src0_sel:WORD_1
	v_pk_fma_f32 v[202:203], v[202:203], v[58:59], v[214:215] op_sel_hi:[1,0,1]
	v_pk_fma_f32 v[214:215], v[220:221], v[58:59], v[218:219] op_sel_hi:[1,0,1]
	v_pk_fma_f32 v[218:219], v[224:225], v[58:59], v[222:223] op_sel_hi:[1,0,1]
	v_pk_fma_f32 v[192:193], v[192:193], v[58:59], v[196:197] op_sel_hi:[1,0,1]
	v_pk_fma_f32 v[196:197], v[226:227], v[58:59], v[200:201] op_sel_hi:[1,0,1]
	v_pk_fma_f32 v[200:201], v[228:229], v[58:59], v[212:213] op_sel_hi:[1,0,1]
	v_pk_fma_f32 v[212:213], v[230:231], v[58:59], v[216:217] op_sel_hi:[1,0,1]
	v_pk_fma_f32 v[194:195], v[194:195], v[58:59], v[198:199] op_sel_hi:[1,0,1]
	v_cvt_pk_f32_fp8_e32 v[198:199], v184
	v_cvt_pk_f32_fp8_sdwa v[216:217], v184 src0_sel:WORD_1
	v_cvt_pk_f32_fp8_e32 v[220:221], v185
	v_cvt_pk_f32_fp8_sdwa v[184:185], v185 src0_sel:WORD_1
	v_cvt_pk_f32_fp8_e32 v[222:223], v186
	v_cvt_pk_f32_fp8_sdwa v[224:225], v186 src0_sel:WORD_1
	v_cvt_pk_f32_fp8_e32 v[226:227], v187
	v_cvt_pk_f32_fp8_sdwa v[186:187], v187 src0_sel:WORD_1
	v_mov_b32_e32 v228, v59
	v_pk_fma_f32 v[198:199], v[198:199], v[228:229], v[202:203] op_sel_hi:[1,0,1]
	v_pk_fma_f32 v[202:203], v[216:217], v[228:229], v[214:215] op_sel_hi:[1,0,1]
	v_pk_fma_f32 v[214:215], v[220:221], v[228:229], v[218:219] op_sel_hi:[1,0,1]
	v_pk_fma_f32 v[184:185], v[184:185], v[228:229], v[192:193] op_sel_hi:[1,0,1]
	v_pk_fma_f32 v[192:193], v[222:223], v[228:229], v[196:197] op_sel_hi:[1,0,1]
	v_pk_fma_f32 v[196:197], v[224:225], v[228:229], v[200:201] op_sel_hi:[1,0,1]
	v_pk_fma_f32 v[200:201], v[226:227], v[228:229], v[212:213] op_sel_hi:[1,0,1]
	v_lshl_or_b32 v36, v36, 7, v136
	global_load_dwordx4 v[224:227], v36, s[4:5] sc0
	v_pk_fma_f32 v[186:187], v[186:187], v[228:229], v[194:195] op_sel_hi:[1,0,1]
	v_lshl_or_b32 v35, v35, 7, v136
	global_load_dwordx4 v[228:231], v35, s[4:5] sc0
	v_cvt_pk_f32_fp8_e32 v[194:195], v180
	v_cvt_pk_f32_fp8_sdwa v[212:213], v180 src0_sel:WORD_1
	v_cvt_pk_f32_fp8_e32 v[216:217], v181
	v_cvt_pk_f32_fp8_sdwa v[180:181], v181 src0_sel:WORD_1
	v_cvt_pk_f32_fp8_e32 v[218:219], v182
	v_cvt_pk_f32_fp8_sdwa v[220:221], v182 src0_sel:WORD_1
	v_cvt_pk_f32_fp8_e32 v[222:223], v183
	v_cvt_pk_f32_fp8_sdwa v[182:183], v183 src0_sel:WORD_1
	v_pk_fma_f32 v[194:195], v[194:195], v[60:61], v[198:199] op_sel_hi:[1,0,1]
	v_pk_fma_f32 v[198:199], v[212:213], v[60:61], v[202:203] op_sel_hi:[1,0,1]
	v_pk_fma_f32 v[202:203], v[216:217], v[60:61], v[214:215] op_sel_hi:[1,0,1]
	v_pk_fma_f32 v[180:181], v[180:181], v[60:61], v[184:185] op_sel_hi:[1,0,1]
	v_pk_fma_f32 v[184:185], v[218:219], v[60:61], v[192:193] op_sel_hi:[1,0,1]
	v_pk_fma_f32 v[192:193], v[220:221], v[60:61], v[196:197] op_sel_hi:[1,0,1]
	v_pk_fma_f32 v[196:197], v[222:223], v[60:61], v[200:201] op_sel_hi:[1,0,1]
	v_lshl_or_b32 v37, v37, 7, v136
	global_load_dwordx4 v[220:223], v37, s[4:5] sc0
	v_pk_fma_f32 v[182:183], v[182:183], v[60:61], v[186:187] op_sel_hi:[1,0,1]
	v_cvt_pk_f32_fp8_e32 v[186:187], v172
	v_cvt_pk_f32_fp8_sdwa v[200:201], v172 src0_sel:WORD_1
	v_cvt_pk_f32_fp8_e32 v[212:213], v173
	v_cvt_pk_f32_fp8_sdwa v[172:173], v173 src0_sel:WORD_1
	v_cvt_pk_f32_fp8_e32 v[214:215], v174
	v_cvt_pk_f32_fp8_sdwa v[216:217], v174 src0_sel:WORD_1
	v_cvt_pk_f32_fp8_e32 v[218:219], v175
	v_cvt_pk_f32_fp8_sdwa v[174:175], v175 src0_sel:WORD_1
	v_pk_fma_f32 v[186:187], v[186:187], v[60:61], v[194:195] op_sel:[0,1,0]
	v_pk_fma_f32 v[194:195], v[200:201], v[60:61], v[198:199] op_sel:[0,1,0]
	v_pk_fma_f32 v[198:199], v[212:213], v[60:61], v[202:203] op_sel:[0,1,0]
	v_pk_fma_f32 v[172:173], v[172:173], v[60:61], v[180:181] op_sel:[0,1,0]
	v_pk_fma_f32 v[180:181], v[214:215], v[60:61], v[184:185] op_sel:[0,1,0]
	v_pk_fma_f32 v[184:185], v[216:217], v[60:61], v[192:193] op_sel:[0,1,0]
; #define PU_IDX(t, E, C) do { const char* eb_ = eiu + (size_t)(t) * 512; const char* cb_ = cfu + (size_t)(t) * 512; \
;     _Pragma("unroll") for (int q = 0; q < 4; ++q) { E[q] = *(const i32x4_t*)(eb_ + (eio + 16u * q)); C[q] = *(const f32x4*)(cb_ + (eio + 16u * q)); } } while (0)
; #define PU_TAB(E, W) do { _Pragma("unroll") for (int q = 0; q < 16; ++q) W[q] = *(const u32x4*)(tabu + ((unsigned)E[q >> 2][q & 3] * 128u + tabo)); } while (0)
; DI void phase_peerup(const Params& p, int bid, int nb) {
;     ...
;   i32x4_t eA[4], eB[4]; f32x4 cA[4], cB[4]; u32x4 w[16];
;   int t = gw; if (t >= T_) return;
;   PU_IDX(t, eA, cA);
;   for (;;) {
;     PU_TAB(eA, w);
;     const int t1 = t + nw; if (t1 < T_) PU_IDX(t1, eB, cB);
;     PU_MATH(t, w, cA);
;     if (t1 >= T_) break;
;     PU_TAB(eB, w);
;     const int t2 = t1 + nw; if (t2 < T_) PU_IDX(t2, eA, cA);
;     PU_MATH(t1, w, cB);
;     if (t2 >= T_) break;
;     t = t2;
;   }
	v_pk_fma_f32 v[192:193], v[218:219], v[60:61], v[196:197] op_sel:[0,1,0]
	v_lshl_or_b32 v38, v38, 7, v136
	global_load_dwordx4 v[216:219], v38, s[4:5] sc0
	v_pk_fma_f32 v[174:175], v[174:175], v[60:61], v[182:183] op_sel:[0,1,0]
	v_cvt_pk_f32_fp8_e32 v[182:183], v168
	v_cvt_pk_f32_fp8_sdwa v[196:197], v168 src0_sel:WORD_1
	v_cvt_pk_f32_fp8_e32 v[200:201], v169
	v_cvt_pk_f32_fp8_sdwa v[168:169], v169 src0_sel:WORD_1
	v_cvt_pk_f32_fp8_e32 v[202:203], v170
	v_cvt_pk_f32_fp8_sdwa v[212:213], v170 src0_sel:WORD_1
	v_cvt_pk_f32_fp8_e32 v[214:215], v171
	v_cvt_pk_f32_fp8_sdwa v[170:171], v171 src0_sel:WORD_1
	v_pk_fma_f32 v[182:183], v[182:183], v[62:63], v[186:187] op_sel_hi:[1,0,1]
	v_pk_fma_f32 v[186:187], v[196:197], v[62:63], v[194:195] op_sel_hi:[1,0,1]
	v_pk_fma_f32 v[194:195], v[200:201], v[62:63], v[198:199] op_sel_hi:[1,0,1]
	v_pk_fma_f32 v[168:169], v[168:169], v[62:63], v[172:173] op_sel_hi:[1,0,1]
	v_pk_fma_f32 v[172:173], v[202:203], v[62:63], v[180:181] op_sel_hi:[1,0,1]
	v_pk_fma_f32 v[180:181], v[212:213], v[62:63], v[184:185] op_sel_hi:[1,0,1]
	v_pk_fma_f32 v[184:185], v[214:215], v[62:63], v[192:193] op_sel_hi:[1,0,1]
	v_pk_fma_f32 v[170:171], v[170:171], v[62:63], v[174:175] op_sel_hi:[1,0,1]
	v_cvt_pk_f32_fp8_e32 v[174:175], v164
	v_cvt_pk_f32_fp8_sdwa v[192:193], v164 src0_sel:WORD_1
	v_cvt_pk_f32_fp8_e32 v[196:197], v165
	v_cvt_pk_f32_fp8_sdwa v[164:165], v165 src0_sel:WORD_1
	v_cvt_pk_f32_fp8_e32 v[198:199], v166
	v_cvt_pk_f32_fp8_sdwa v[200:201], v166 src0_sel:WORD_1
	v_cvt_pk_f32_fp8_e32 v[202:203], v167
	v_cvt_pk_f32_fp8_sdwa v[166:167], v167 src0_sel:WORD_1
	v_mov_b32_e32 v212, v63
	v_pk_fma_f32 v[174:175], v[174:175], v[212:213], v[182:183] op_sel_hi:[1,0,1]
	v_pk_fma_f32 v[182:183], v[192:193], v[212:213], v[186:187] op_sel_hi:[1,0,1]
	v_pk_fma_f32 v[186:187], v[196:197], v[212:213], v[194:195] op_sel_hi:[1,0,1]
	v_lshl_or_b32 v42, v42, 7, v136
	global_load_dwordx4 v[192:195], v42, s[4:5] sc0
	v_pk_fma_f32 v[164:165], v[164:165], v[212:213], v[168:169] op_sel_hi:[1,0,1]
	v_pk_fma_f32 v[168:169], v[198:199], v[212:213], v[172:173] op_sel_hi:[1,0,1]
	v_lshl_or_b32 v41, v41, 7, v136
	global_load_dwordx4 v[196:199], v41, s[4:5] sc0
	v_pk_fma_f32 v[172:173], v[200:201], v[212:213], v[180:181] op_sel_hi:[1,0,1]
	v_pk_fma_f32 v[180:181], v[202:203], v[212:213], v[184:185] op_sel_hi:[1,0,1]
	v_lshl_or_b32 v40, v40, 7, v136
	global_load_dwordx4 v[200:203], v40, s[4:5] sc0
	v_pk_fma_f32 v[166:167], v[166:167], v[212:213], v[170:171] op_sel_hi:[1,0,1]
	v_lshl_or_b32 v39, v39, 7, v136
	global_load_dwordx4 v[212:215], v39, s[4:5] sc0
	v_permlane32_swap_b32_e32 v174, v168
	v_permlane32_swap_b32_e32 v175, v169
	v_permlane32_swap_b32_e32 v182, v172
	v_permlane32_swap_b32_e32 v183, v173
	v_permlane32_swap_b32_e32 v186, v180
	v_permlane32_swap_b32_e32 v187, v181
	v_permlane32_swap_b32_e32 v164, v166
	v_permlane32_swap_b32_e32 v165, v167
	v_add_f32_e32 v168, v174, v168
	v_add_f32_e32 v169, v175, v169
	v_add_f32_e32 v170, v182, v172
	v_add_f32_e32 v171, v183, v173
	v_add_f32_e32 v172, v186, v180
	v_add_f32_e32 v173, v187, v181
	v_lshl_or_b32 v43, v43, 7, v136
	global_load_dwordx4 v[184:187], v43, s[4:5] sc0
	v_lshl_or_b32 v44, v44, 7, v136
	global_load_dwordx4 v[180:183], v44, s[4:5] sc0
	v_add_f32_e32 v164, v164, v166
	v_add_f32_e32 v165, v165, v167
	v_permlane16_swap_b32_e32 v168, v172
	v_permlane16_swap_b32_e32 v169, v173
	v_permlane16_swap_b32_e32 v170, v164
	v_permlane16_swap_b32_e32 v171, v165
	v_pk_add_f32 v[166:167], v[168:169], v[172:173]
	v_lshl_or_b32 v45, v45, 7, v136
	global_load_dwordx4 v[172:175], v45, s[4:5] sc0
	v_pk_add_f32 v[164:165], v[170:171], v[164:165]
	s_ashr_i32 s7, s6, 31
	v_cndmask_b32_e64 v168, v166, v164, s[0:1]
	v_cndmask_b32_e64 v170, v164, v166, s[0:1]
	v_cndmask_b32_e64 v164, v167, v165, s[0:1]
	v_mov_b32_dpp v168, v168 row_ror:8 row_mask:0xf bank_mask:0xf bound_ctrl:1
	v_cndmask_b32_e64 v171, v165, v167, s[0:1]
	v_mov_b32_dpp v169, v164 row_ror:8 row_mask:0xf bank_mask:0xf bound_ctrl:1
	v_pk_add_f32 v[166:167], v[170:171], v[168:169]
	s_lshl_b64 s[8:9], s[6:7], 11
	v_pk_mul_f32 v[164:165], v[166:167], v[166:167]
	v_cvt_pk_bf16_f32 v168, v166, v167
	v_add_f32_e32 v164, v164, v165
	v_lshl_add_u64 v[166:167], v[130:131], 0, s[8:9]
	global_store_dword v[166:167], v168, off
	v_add_f32_dpp v164, v164, v164 quad_perm:[1,0,3,2] row_mask:0xf bank_mask:0xf bound_ctrl:1
	s_nop 1
	v_add_f32_dpp v164, v164, v164 quad_perm:[2,3,0,1] row_mask:0xf bank_mask:0xf bound_ctrl:1
	s_nop 1
	v_add_f32_dpp v164, v164, v164 row_half_mirror row_mask:0xf bank_mask:0xf bound_ctrl:1
	s_nop 1
	v_add_f32_dpp v164, v164, v164 row_ror:8 row_mask:0xf bank_mask:0xf bound_ctrl:1
	v_mov_b32_e32 v165, v164
	s_nop 1
	v_permlane16_swap_b32_e32 v164, v165
	v_add_f32_e32 v164, v164, v165
	v_mov_b32_e32 v165, v164
	s_nop 1
	v_permlane32_swap_b32_e32 v164, v165
	s_and_saveexec_b64 s[8:9], s[2:3]
	s_lshl_b64 s[10:11], s[6:7], 2
	s_add_u32 s10, s12, s10
	v_add_f32_e32 v164, v164, v165
	s_addc_u32 s11, s13, s11
	global_store_dword v129, v164, s[10:11]
	s_or_b64 exec, exec, s[8:9]
	v_lshl_or_b32 v46, v46, 7, v136
	global_load_dwordx4 v[168:171], v46, s[4:5] sc0
	v_lshl_or_b32 v47, v47, 7, v136
	global_load_dwordx4 v[164:167], v47, s[4:5] sc0
	s_add_u32 s22, s20, 0x300
	s_lshl_b32 s22, s22, 9
	v_lshl_add_u64 v[48:49], v[134:135], 0, s[22:23]
	global_load_dwordx4 v[60:63], v[48:49], off offset:48
	global_load_dwordx4 v[56:59], v[48:49], off offset:32
	global_load_dwordx4 v[52:55], v[48:49], off offset:16
	s_nop 0
	global_load_dwordx4 v[48:51], v[48:49], off
	s_add_u32 s22, s20, 0x500
	s_lshl_b32 s22, s22, 9
	v_lshl_add_u64 v[32:33], v[132:133], 0, s[22:23]
	global_load_dwordx4 v[44:47], v[32:33], off offset:48
	global_load_dwordx4 v[40:43], v[32:33], off offset:32
	global_load_dwordx4 v[36:39], v[32:33], off offset:16
	s_nop 0
	global_load_dwordx4 v[32:35], v[32:33], off
	s_add_u32 s20, s20, 0x200
	s_sub_u32 s24, s24, 1
	s_cmp_lg_u32 s24, 0
	s_cbranch_scc1 .Lpu2_loop
; DI void unpack8x2_fp8(const u32x4 w, f32x2 (&f)[8]) {
; #pragma unroll
;   for (int i = 0; i < 4; ++i) { f[2 * i] = __builtin_amdgcn_cvt_pk_f32_fp8((int)w[i], false); f[2 * i + 1] = __builtin_amdgcn_cvt_pk_f32_fp8((int)w[i], true); }
; }
	s_mov_b32 s8, s20
	s_waitcnt vmcnt(26)
	v_cvt_pk_f32_fp8_e32 v[138:139], v124
	v_cvt_pk_f32_fp8_sdwa v[140:141], v124 src0_sel:WORD_1
	v_cvt_pk_f32_fp8_e32 v[142:143], v125
	v_cvt_pk_f32_fp8_sdwa v[124:125], v125 src0_sel:WORD_1
	v_cvt_pk_f32_fp8_e32 v[144:145], v126
	v_cvt_pk_f32_fp8_sdwa v[146:147], v126 src0_sel:WORD_1
	v_cvt_pk_f32_fp8_e32 v[148:149], v127
	v_cvt_pk_f32_fp8_sdwa v[126:127], v127 src0_sel:WORD_1
	v_cvt_pk_f32_fp8_e32 v[150:151], v120
	v_cvt_pk_f32_fp8_sdwa v[152:153], v120 src0_sel:WORD_1
	v_cvt_pk_f32_fp8_e32 v[154:155], v121
	v_cvt_pk_f32_fp8_sdwa v[120:121], v121 src0_sel:WORD_1
	v_cvt_pk_f32_fp8_e32 v[156:157], v122
	v_cvt_pk_f32_fp8_sdwa v[158:159], v122 src0_sel:WORD_1
	v_cvt_pk_f32_fp8_e32 v[160:161], v123
	v_cvt_pk_f32_fp8_sdwa v[122:123], v123 src0_sel:WORD_1
	v_pk_fma_f32 v[138:139], v[138:139], v[28:29], 0 op_sel_hi:[1,0,0]
	v_pk_fma_f32 v[140:141], v[140:141], v[28:29], 0 op_sel_hi:[1,0,0]
	v_pk_fma_f32 v[142:143], v[142:143], v[28:29], 0 op_sel_hi:[1,0,0]
	v_pk_fma_f32 v[124:125], v[124:125], v[28:29], 0 op_sel_hi:[1,0,0]
	v_pk_fma_f32 v[144:145], v[144:145], v[28:29], 0 op_sel_hi:[1,0,0]
	v_pk_fma_f32 v[146:147], v[146:147], v[28:29], 0 op_sel_hi:[1,0,0]
	v_pk_fma_f32 v[148:149], v[148:149], v[28:29], 0 op_sel_hi:[1,0,0]
	v_pk_fma_f32 v[126:127], v[126:127], v[28:29], 0 op_sel_hi:[1,0,0]
	v_pk_fma_f32 v[138:139], v[150:151], v[28:29], v[138:139] op_sel:[0,1,0]
	v_pk_fma_f32 v[140:141], v[152:153], v[28:29], v[140:141] op_sel:[0,1,0]
	v_pk_fma_f32 v[142:143], v[154:155], v[28:29], v[142:143] op_sel:[0,1,0]
	v_pk_fma_f32 v[120:121], v[120:121], v[28:29], v[124:125] op_sel:[0,1,0]
	v_pk_fma_f32 v[124:125], v[156:157], v[28:29], v[144:145] op_sel:[0,1,0]
	v_pk_fma_f32 v[144:145], v[158:159], v[28:29], v[146:147] op_sel:[0,1,0]
	v_pk_fma_f32 v[146:147], v[160:161], v[28:29], v[148:149] op_sel:[0,1,0]
	v_pk_fma_f32 v[122:123], v[122:123], v[28:29], v[126:127] op_sel:[0,1,0]
	v_cvt_pk_f32_fp8_e32 v[126:127], v116
	v_cvt_pk_f32_fp8_sdwa v[148:149], v116 src0_sel:WORD_1
	v_cvt_pk_f32_fp8_e32 v[150:151], v117
	v_cvt_pk_f32_fp8_sdwa v[116:117], v117 src0_sel:WORD_1
	v_cvt_pk_f32_fp8_e32 v[152:153], v118
	v_cvt_pk_f32_fp8_sdwa v[154:155], v118 src0_sel:WORD_1
	v_cvt_pk_f32_fp8_e32 v[156:157], v119
	v_cvt_pk_f32_fp8_sdwa v[118:119], v119 src0_sel:WORD_1
	v_pk_fma_f32 v[126:127], v[126:127], v[30:31], v[138:139] op_sel_hi:[1,0,1]
	v_pk_fma_f32 v[138:139], v[148:149], v[30:31], v[140:141] op_sel_hi:[1,0,1]
	v_pk_fma_f32 v[140:141], v[150:151], v[30:31], v[142:143] op_sel_hi:[1,0,1]
	v_pk_fma_f32 v[116:117], v[116:117], v[30:31], v[120:121] op_sel_hi:[1,0,1]
	v_pk_fma_f32 v[120:121], v[152:153], v[30:31], v[124:125] op_sel_hi:[1,0,1]
	v_pk_fma_f32 v[124:125], v[154:155], v[30:31], v[144:145] op_sel_hi:[1,0,1]
	v_pk_fma_f32 v[142:143], v[156:157], v[30:31], v[146:147] op_sel_hi:[1,0,1]
	v_pk_fma_f32 v[118:119], v[118:119], v[30:31], v[122:123] op_sel_hi:[1,0,1]
	v_cvt_pk_f32_fp8_e32 v[122:123], v112
	v_cvt_pk_f32_fp8_sdwa v[144:145], v112 src0_sel:WORD_1
	v_cvt_pk_f32_fp8_e32 v[146:147], v113
	v_cvt_pk_f32_fp8_sdwa v[112:113], v113 src0_sel:WORD_1
	v_cvt_pk_f32_fp8_e32 v[148:149], v114
	v_cvt_pk_f32_fp8_sdwa v[150:151], v114 src0_sel:WORD_1
	v_cvt_pk_f32_fp8_e32 v[152:153], v115
	v_cvt_pk_f32_fp8_sdwa v[114:115], v115 src0_sel:WORD_1
	v_mov_b32_e32 v128, v31
	v_pk_fma_f32 v[122:123], v[122:123], v[128:129], v[126:127] op_sel_hi:[1,0,1]
	v_pk_fma_f32 v[126:127], v[144:145], v[128:129], v[138:139] op_sel_hi:[1,0,1]
	v_pk_fma_f32 v[138:139], v[146:147], v[128:129], v[140:141] op_sel_hi:[1,0,1]
	v_pk_fma_f32 v[112:113], v[112:113], v[128:129], v[116:117] op_sel_hi:[1,0,1]
	v_pk_fma_f32 v[116:117], v[148:149], v[128:129], v[120:121] op_sel_hi:[1,0,1]
	v_pk_fma_f32 v[120:121], v[150:151], v[128:129], v[124:125] op_sel_hi:[1,0,1]
	v_pk_fma_f32 v[124:125], v[152:153], v[128:129], v[142:143] op_sel_hi:[1,0,1]
	v_pk_fma_f32 v[114:115], v[114:115], v[128:129], v[118:119] op_sel_hi:[1,0,1]
	v_cvt_pk_f32_fp8_e32 v[118:119], v108
	v_cvt_pk_f32_fp8_sdwa v[140:141], v108 src0_sel:WORD_1
	v_cvt_pk_f32_fp8_e32 v[142:143], v109
	v_cvt_pk_f32_fp8_sdwa v[108:109], v109 src0_sel:WORD_1
	v_cvt_pk_f32_fp8_e32 v[144:145], v110
	v_cvt_pk_f32_fp8_sdwa v[146:147], v110 src0_sel:WORD_1
	v_cvt_pk_f32_fp8_e32 v[148:149], v111
	v_cvt_pk_f32_fp8_sdwa v[110:111], v111 src0_sel:WORD_1
	v_pk_fma_f32 v[118:119], v[118:119], v[24:25], v[122:123] op_sel_hi:[1,0,1]
	v_pk_fma_f32 v[122:123], v[140:141], v[24:25], v[126:127] op_sel_hi:[1,0,1]
	v_pk_fma_f32 v[126:127], v[142:143], v[24:25], v[138:139] op_sel_hi:[1,0,1]
	v_pk_fma_f32 v[108:109], v[108:109], v[24:25], v[112:113] op_sel_hi:[1,0,1]
	v_pk_fma_f32 v[112:113], v[144:145], v[24:25], v[116:117] op_sel_hi:[1,0,1]
	v_pk_fma_f32 v[116:117], v[146:147], v[24:25], v[120:121] op_sel_hi:[1,0,1]
	v_pk_fma_f32 v[120:121], v[148:149], v[24:25], v[124:125] op_sel_hi:[1,0,1]
	v_pk_fma_f32 v[110:111], v[110:111], v[24:25], v[114:115] op_sel_hi:[1,0,1]
	v_cvt_pk_f32_fp8_e32 v[114:115], v104
	v_cvt_pk_f32_fp8_sdwa v[124:125], v104 src0_sel:WORD_1
	v_cvt_pk_f32_fp8_e32 v[138:139], v105
	v_cvt_pk_f32_fp8_sdwa v[104:105], v105 src0_sel:WORD_1
	v_cvt_pk_f32_fp8_e32 v[140:141], v106
	v_cvt_pk_f32_fp8_sdwa v[142:143], v106 src0_sel:WORD_1
	v_cvt_pk_f32_fp8_e32 v[144:145], v107
	v_cvt_pk_f32_fp8_sdwa v[106:107], v107 src0_sel:WORD_1
	v_pk_fma_f32 v[114:115], v[114:115], v[24:25], v[118:119] op_sel:[0,1,0]
	v_pk_fma_f32 v[118:119], v[124:125], v[24:25], v[122:123] op_sel:[0,1,0]
	v_pk_fma_f32 v[122:123], v[138:139], v[24:25], v[126:127] op_sel:[0,1,0]
	v_pk_fma_f32 v[104:105], v[104:105], v[24:25], v[108:109] op_sel:[0,1,0]
	v_pk_fma_f32 v[108:109], v[140:141], v[24:25], v[112:113] op_sel:[0,1,0]
	v_pk_fma_f32 v[112:113], v[142:143], v[24:25], v[116:117] op_sel:[0,1,0]
	v_pk_fma_f32 v[116:117], v[144:145], v[24:25], v[120:121] op_sel:[0,1,0]
	v_pk_fma_f32 v[106:107], v[106:107], v[24:25], v[110:111] op_sel:[0,1,0]
	v_cvt_pk_f32_fp8_e32 v[110:111], v100
	v_cvt_pk_f32_fp8_sdwa v[120:121], v100 src0_sel:WORD_1
	v_cvt_pk_f32_fp8_e32 v[124:125], v101
	v_cvt_pk_f32_fp8_sdwa v[100:101], v101 src0_sel:WORD_1
	v_cvt_pk_f32_fp8_e32 v[126:127], v102
	v_cvt_pk_f32_fp8_sdwa v[138:139], v102 src0_sel:WORD_1
	v_cvt_pk_f32_fp8_e32 v[140:141], v103
	v_cvt_pk_f32_fp8_sdwa v[102:103], v103 src0_sel:WORD_1
	v_pk_fma_f32 v[110:111], v[110:111], v[26:27], v[114:115] op_sel_hi:[1,0,1]
	v_pk_fma_f32 v[114:115], v[120:121], v[26:27], v[118:119] op_sel_hi:[1,0,1]
	v_pk_fma_f32 v[118:119], v[124:125], v[26:27], v[122:123] op_sel_hi:[1,0,1]
	v_pk_fma_f32 v[100:101], v[100:101], v[26:27], v[104:105] op_sel_hi:[1,0,1]
	v_pk_fma_f32 v[104:105], v[126:127], v[26:27], v[108:109] op_sel_hi:[1,0,1]
	v_pk_fma_f32 v[108:109], v[138:139], v[26:27], v[112:113] op_sel_hi:[1,0,1]
	v_pk_fma_f32 v[112:113], v[140:141], v[26:27], v[116:117] op_sel_hi:[1,0,1]
	v_pk_fma_f32 v[102:103], v[102:103], v[26:27], v[106:107] op_sel_hi:[1,0,1]
	v_cvt_pk_f32_fp8_e32 v[106:107], v96
	v_cvt_pk_f32_fp8_sdwa v[116:117], v96 src0_sel:WORD_1
	v_cvt_pk_f32_fp8_e32 v[120:121], v97
	v_cvt_pk_f32_fp8_sdwa v[96:97], v97 src0_sel:WORD_1
	v_cvt_pk_f32_fp8_e32 v[122:123], v98
	v_cvt_pk_f32_fp8_sdwa v[124:125], v98 src0_sel:WORD_1
	v_cvt_pk_f32_fp8_e32 v[126:127], v99
	v_cvt_pk_f32_fp8_sdwa v[98:99], v99 src0_sel:WORD_1
	v_mov_b32_e32 v128, v27
	v_pk_fma_f32 v[106:107], v[106:107], v[128:129], v[110:111] op_sel_hi:[1,0,1]
	v_pk_fma_f32 v[110:111], v[116:117], v[128:129], v[114:115] op_sel_hi:[1,0,1]
	v_pk_fma_f32 v[114:115], v[120:121], v[128:129], v[118:119] op_sel_hi:[1,0,1]
	v_pk_fma_f32 v[96:97], v[96:97], v[128:129], v[100:101] op_sel_hi:[1,0,1]
	v_pk_fma_f32 v[100:101], v[122:123], v[128:129], v[104:105] op_sel_hi:[1,0,1]
	v_pk_fma_f32 v[104:105], v[124:125], v[128:129], v[108:109] op_sel_hi:[1,0,1]
	v_pk_fma_f32 v[108:109], v[126:127], v[128:129], v[112:113] op_sel_hi:[1,0,1]
	v_lshl_or_b32 v12, v12, 7, v136
	global_load_dwordx4 v[124:127], v12, s[4:5] sc0
	v_pk_fma_f32 v[98:99], v[98:99], v[128:129], v[102:103] op_sel_hi:[1,0,1]
	v_cvt_pk_f32_fp8_e32 v[102:103], v92
	v_cvt_pk_f32_fp8_sdwa v[112:113], v92 src0_sel:WORD_1
	v_cvt_pk_f32_fp8_e32 v[116:117], v93
	v_cvt_pk_f32_fp8_sdwa v[92:93], v93 src0_sel:WORD_1
	v_cvt_pk_f32_fp8_e32 v[118:119], v94
	v_cvt_pk_f32_fp8_sdwa v[120:121], v94 src0_sel:WORD_1
	v_cvt_pk_f32_fp8_e32 v[122:123], v95
	v_cvt_pk_f32_fp8_sdwa v[94:95], v95 src0_sel:WORD_1
	v_pk_fma_f32 v[102:103], v[102:103], v[20:21], v[106:107] op_sel_hi:[1,0,1]
	v_pk_fma_f32 v[106:107], v[112:113], v[20:21], v[110:111] op_sel_hi:[1,0,1]
	v_pk_fma_f32 v[110:111], v[116:117], v[20:21], v[114:115] op_sel_hi:[1,0,1]
	v_pk_fma_f32 v[92:93], v[92:93], v[20:21], v[96:97] op_sel_hi:[1,0,1]
	v_pk_fma_f32 v[96:97], v[118:119], v[20:21], v[100:101] op_sel_hi:[1,0,1]
	v_pk_fma_f32 v[100:101], v[120:121], v[20:21], v[104:105] op_sel_hi:[1,0,1]
	v_pk_fma_f32 v[104:105], v[122:123], v[20:21], v[108:109] op_sel_hi:[1,0,1]
	v_lshl_or_b32 v13, v13, 7, v136
	global_load_dwordx4 v[120:123], v13, s[4:5] sc0
	v_pk_fma_f32 v[94:95], v[94:95], v[20:21], v[98:99] op_sel_hi:[1,0,1]
	v_cvt_pk_f32_fp8_e32 v[98:99], v88
	v_cvt_pk_f32_fp8_sdwa v[108:109], v88 src0_sel:WORD_1
	v_cvt_pk_f32_fp8_e32 v[112:113], v89
	v_cvt_pk_f32_fp8_sdwa v[88:89], v89 src0_sel:WORD_1
	v_cvt_pk_f32_fp8_e32 v[114:115], v90
	v_cvt_pk_f32_fp8_sdwa v[116:117], v90 src0_sel:WORD_1
	v_cvt_pk_f32_fp8_e32 v[118:119], v91
	v_cvt_pk_f32_fp8_sdwa v[90:91], v91 src0_sel:WORD_1
	v_pk_fma_f32 v[98:99], v[98:99], v[20:21], v[102:103] op_sel:[0,1,0]
	v_pk_fma_f32 v[102:103], v[108:109], v[20:21], v[106:107] op_sel:[0,1,0]
	v_pk_fma_f32 v[106:107], v[112:113], v[20:21], v[110:111] op_sel:[0,1,0]
	v_pk_fma_f32 v[88:89], v[88:89], v[20:21], v[92:93] op_sel:[0,1,0]
	v_pk_fma_f32 v[92:93], v[114:115], v[20:21], v[96:97] op_sel:[0,1,0]
	v_pk_fma_f32 v[96:97], v[116:117], v[20:21], v[100:101] op_sel:[0,1,0]
	v_pk_fma_f32 v[100:101], v[118:119], v[20:21], v[104:105] op_sel:[0,1,0]
	v_lshl_or_b32 v14, v14, 7, v136
	global_load_dwordx4 v[116:119], v14, s[4:5] sc0
	v_pk_fma_f32 v[90:91], v[90:91], v[20:21], v[94:95] op_sel:[0,1,0]
	v_cvt_pk_f32_fp8_e32 v[94:95], v84
	v_cvt_pk_f32_fp8_sdwa v[104:105], v84 src0_sel:WORD_1
	v_cvt_pk_f32_fp8_e32 v[108:109], v85
	v_cvt_pk_f32_fp8_sdwa v[84:85], v85 src0_sel:WORD_1
	v_cvt_pk_f32_fp8_e32 v[110:111], v86
	v_cvt_pk_f32_fp8_sdwa v[112:113], v86 src0_sel:WORD_1
	v_cvt_pk_f32_fp8_e32 v[114:115], v87
	v_cvt_pk_f32_fp8_sdwa v[86:87], v87 src0_sel:WORD_1
	v_pk_fma_f32 v[94:95], v[94:95], v[22:23], v[98:99] op_sel_hi:[1,0,1]
	v_pk_fma_f32 v[98:99], v[104:105], v[22:23], v[102:103] op_sel_hi:[1,0,1]
	v_pk_fma_f32 v[102:103], v[108:109], v[22:23], v[106:107] op_sel_hi:[1,0,1]
	v_pk_fma_f32 v[84:85], v[84:85], v[22:23], v[88:89] op_sel_hi:[1,0,1]
	v_pk_fma_f32 v[88:89], v[110:111], v[22:23], v[92:93] op_sel_hi:[1,0,1]
	v_pk_fma_f32 v[92:93], v[112:113], v[22:23], v[96:97] op_sel_hi:[1,0,1]
	v_pk_fma_f32 v[96:97], v[114:115], v[22:23], v[100:101] op_sel_hi:[1,0,1]
	v_pk_fma_f32 v[86:87], v[86:87], v[22:23], v[90:91] op_sel_hi:[1,0,1]
	v_cvt_pk_f32_fp8_e32 v[90:91], v80
	v_cvt_pk_f32_fp8_sdwa v[100:101], v80 src0_sel:WORD_1
	v_cvt_pk_f32_fp8_e32 v[104:105], v81
	v_cvt_pk_f32_fp8_sdwa v[80:81], v81 src0_sel:WORD_1
	v_cvt_pk_f32_fp8_e32 v[106:107], v82
	v_cvt_pk_f32_fp8_sdwa v[108:109], v82 src0_sel:WORD_1
	v_cvt_pk_f32_fp8_e32 v[110:111], v83
	v_cvt_pk_f32_fp8_sdwa v[82:83], v83 src0_sel:WORD_1
	v_mov_b32_e32 v112, v23
	v_pk_fma_f32 v[90:91], v[90:91], v[112:113], v[94:95] op_sel_hi:[1,0,1]
	v_pk_fma_f32 v[94:95], v[100:101], v[112:113], v[98:99] op_sel_hi:[1,0,1]
	v_pk_fma_f32 v[98:99], v[104:105], v[112:113], v[102:103] op_sel_hi:[1,0,1]
	v_pk_fma_f32 v[80:81], v[80:81], v[112:113], v[84:85] op_sel_hi:[1,0,1]
	v_pk_fma_f32 v[84:85], v[106:107], v[112:113], v[88:89] op_sel_hi:[1,0,1]
	v_pk_fma_f32 v[88:89], v[108:109], v[112:113], v[92:93] op_sel_hi:[1,0,1]
	v_pk_fma_f32 v[92:93], v[110:111], v[112:113], v[96:97] op_sel_hi:[1,0,1]
	v_lshl_or_b32 v8, v8, 7, v136
	global_load_dwordx4 v[108:111], v8, s[4:5] sc0
	v_pk_fma_f32 v[82:83], v[82:83], v[112:113], v[86:87] op_sel_hi:[1,0,1]
	v_lshl_or_b32 v15, v15, 7, v136
	global_load_dwordx4 v[112:115], v15, s[4:5] sc0
	v_cvt_pk_f32_fp8_e32 v[86:87], v76
	v_cvt_pk_f32_fp8_sdwa v[96:97], v76 src0_sel:WORD_1
	v_cvt_pk_f32_fp8_e32 v[100:101], v77
	v_cvt_pk_f32_fp8_sdwa v[76:77], v77 src0_sel:WORD_1
	v_cvt_pk_f32_fp8_e32 v[102:103], v78
	v_cvt_pk_f32_fp8_sdwa v[104:105], v78 src0_sel:WORD_1
	v_cvt_pk_f32_fp8_e32 v[106:107], v79
	v_cvt_pk_f32_fp8_sdwa v[78:79], v79 src0_sel:WORD_1
	v_pk_fma_f32 v[86:87], v[86:87], v[16:17], v[90:91] op_sel_hi:[1,0,1]
	v_pk_fma_f32 v[90:91], v[96:97], v[16:17], v[94:95] op_sel_hi:[1,0,1]
	v_pk_fma_f32 v[94:95], v[100:101], v[16:17], v[98:99] op_sel_hi:[1,0,1]
	v_pk_fma_f32 v[76:77], v[76:77], v[16:17], v[80:81] op_sel_hi:[1,0,1]
	v_pk_fma_f32 v[80:81], v[102:103], v[16:17], v[84:85] op_sel_hi:[1,0,1]
	v_pk_fma_f32 v[84:85], v[104:105], v[16:17], v[88:89] op_sel_hi:[1,0,1]
	v_pk_fma_f32 v[88:89], v[106:107], v[16:17], v[92:93] op_sel_hi:[1,0,1]
	v_lshl_or_b32 v9, v9, 7, v136
	global_load_dwordx4 v[104:107], v9, s[4:5] sc0
	v_pk_fma_f32 v[78:79], v[78:79], v[16:17], v[82:83] op_sel_hi:[1,0,1]
	v_cvt_pk_f32_fp8_e32 v[82:83], v72
	v_cvt_pk_f32_fp8_sdwa v[92:93], v72 src0_sel:WORD_1
	v_cvt_pk_f32_fp8_e32 v[96:97], v73
	v_cvt_pk_f32_fp8_sdwa v[72:73], v73 src0_sel:WORD_1
	v_cvt_pk_f32_fp8_e32 v[98:99], v74
	v_cvt_pk_f32_fp8_sdwa v[100:101], v74 src0_sel:WORD_1
	v_cvt_pk_f32_fp8_e32 v[102:103], v75
	v_cvt_pk_f32_fp8_sdwa v[74:75], v75 src0_sel:WORD_1
	v_pk_fma_f32 v[82:83], v[82:83], v[16:17], v[86:87] op_sel:[0,1,0]
	v_pk_fma_f32 v[86:87], v[92:93], v[16:17], v[90:91] op_sel:[0,1,0]
	v_pk_fma_f32 v[90:91], v[96:97], v[16:17], v[94:95] op_sel:[0,1,0]
	v_pk_fma_f32 v[72:73], v[72:73], v[16:17], v[76:77] op_sel:[0,1,0]
	v_pk_fma_f32 v[76:77], v[98:99], v[16:17], v[80:81] op_sel:[0,1,0]
	v_pk_fma_f32 v[80:81], v[100:101], v[16:17], v[84:85] op_sel:[0,1,0]
	v_pk_fma_f32 v[84:85], v[102:103], v[16:17], v[88:89] op_sel:[0,1,0]
	v_lshl_or_b32 v10, v10, 7, v136
	global_load_dwordx4 v[100:103], v10, s[4:5] sc0
	v_pk_fma_f32 v[74:75], v[74:75], v[16:17], v[78:79] op_sel:[0,1,0]
	v_cvt_pk_f32_fp8_e32 v[78:79], v68
	v_cvt_pk_f32_fp8_sdwa v[88:89], v68 src0_sel:WORD_1
	v_cvt_pk_f32_fp8_e32 v[92:93], v69
	v_cvt_pk_f32_fp8_sdwa v[68:69], v69 src0_sel:WORD_1
	v_cvt_pk_f32_fp8_e32 v[94:95], v70
	v_cvt_pk_f32_fp8_sdwa v[96:97], v70 src0_sel:WORD_1
	v_cvt_pk_f32_fp8_e32 v[98:99], v71
	v_cvt_pk_f32_fp8_sdwa v[70:71], v71 src0_sel:WORD_1
	v_pk_fma_f32 v[78:79], v[78:79], v[18:19], v[82:83] op_sel_hi:[1,0,1]
	v_pk_fma_f32 v[82:83], v[88:89], v[18:19], v[86:87] op_sel_hi:[1,0,1]
	v_pk_fma_f32 v[86:87], v[92:93], v[18:19], v[90:91] op_sel_hi:[1,0,1]
	v_pk_fma_f32 v[68:69], v[68:69], v[18:19], v[72:73] op_sel_hi:[1,0,1]
	v_pk_fma_f32 v[72:73], v[94:95], v[18:19], v[76:77] op_sel_hi:[1,0,1]
	v_pk_fma_f32 v[76:77], v[96:97], v[18:19], v[80:81] op_sel_hi:[1,0,1]
	v_pk_fma_f32 v[80:81], v[98:99], v[18:19], v[84:85] op_sel_hi:[1,0,1]
	v_pk_fma_f32 v[70:71], v[70:71], v[18:19], v[74:75] op_sel_hi:[1,0,1]
	v_cvt_pk_f32_fp8_e32 v[74:75], v64
	v_cvt_pk_f32_fp8_sdwa v[84:85], v64 src0_sel:WORD_1
	v_cvt_pk_f32_fp8_e32 v[88:89], v65
	v_cvt_pk_f32_fp8_sdwa v[64:65], v65 src0_sel:WORD_1
	v_cvt_pk_f32_fp8_e32 v[90:91], v66
	v_cvt_pk_f32_fp8_sdwa v[92:93], v66 src0_sel:WORD_1
	v_cvt_pk_f32_fp8_e32 v[94:95], v67
	v_cvt_pk_f32_fp8_sdwa v[66:67], v67 src0_sel:WORD_1
	v_mov_b32_e32 v96, v19
	v_pk_fma_f32 v[74:75], v[74:75], v[96:97], v[78:79] op_sel_hi:[1,0,1]
	v_pk_fma_f32 v[78:79], v[84:85], v[96:97], v[82:83] op_sel_hi:[1,0,1]
	v_pk_fma_f32 v[82:83], v[88:89], v[96:97], v[86:87] op_sel_hi:[1,0,1]
	v_lshl_or_b32 v6, v6, 7, v136
	global_load_dwordx4 v[84:87], v6, s[4:5] sc0
	v_pk_fma_f32 v[64:65], v[64:65], v[96:97], v[68:69] op_sel_hi:[1,0,1]
	v_pk_fma_f32 v[68:69], v[90:91], v[96:97], v[72:73] op_sel_hi:[1,0,1]
	v_lshl_or_b32 v5, v5, 7, v136
	global_load_dwordx4 v[88:91], v5, s[4:5] sc0
	v_pk_fma_f32 v[72:73], v[92:93], v[96:97], v[76:77] op_sel_hi:[1,0,1]
	v_pk_fma_f32 v[76:77], v[94:95], v[96:97], v[80:81] op_sel_hi:[1,0,1]
	v_lshl_or_b32 v4, v4, 7, v136
	global_load_dwordx4 v[92:95], v4, s[4:5] sc0
	v_pk_fma_f32 v[66:67], v[66:67], v[96:97], v[70:71] op_sel_hi:[1,0,1]
	v_lshl_or_b32 v11, v11, 7, v136
	global_load_dwordx4 v[96:99], v11, s[4:5] sc0
	v_permlane32_swap_b32_e32 v74, v68
	v_permlane32_swap_b32_e32 v75, v69
	v_permlane32_swap_b32_e32 v78, v72
	v_permlane32_swap_b32_e32 v79, v73
	v_permlane32_swap_b32_e32 v82, v76
	v_permlane32_swap_b32_e32 v83, v77
	v_permlane32_swap_b32_e32 v64, v66
	v_permlane32_swap_b32_e32 v65, v67
	v_add_f32_e32 v68, v74, v68
	v_add_f32_e32 v69, v75, v69
	v_add_f32_e32 v70, v78, v72
	v_add_f32_e32 v71, v79, v73
	v_add_f32_e32 v72, v82, v76
	v_add_f32_e32 v73, v83, v77
	v_lshl_or_b32 v7, v7, 7, v136
	global_load_dwordx4 v[80:83], v7, s[4:5] sc0
	v_lshl_or_b32 v0, v0, 7, v136
	global_load_dwordx4 v[76:79], v0, s[4:5] sc0
	v_add_f32_e32 v64, v64, v66
	v_add_f32_e32 v65, v65, v67
	v_permlane16_swap_b32_e32 v68, v72
	v_permlane16_swap_b32_e32 v69, v73
	v_permlane16_swap_b32_e32 v70, v64
	v_permlane16_swap_b32_e32 v71, v65
	v_pk_add_f32 v[66:67], v[68:69], v[72:73]
	v_lshl_or_b32 v1, v1, 7, v136
	global_load_dwordx4 v[72:75], v1, s[4:5] sc0
	v_pk_add_f32 v[64:65], v[70:71], v[64:65]
	s_ashr_i32 s9, s8, 31
	v_cndmask_b32_e64 v68, v66, v64, s[0:1]
	v_cndmask_b32_e64 v70, v64, v66, s[0:1]
	v_cndmask_b32_e64 v64, v67, v65, s[0:1]
	v_mov_b32_dpp v68, v68 row_ror:8 row_mask:0xf bank_mask:0xf bound_ctrl:1
	v_cndmask_b32_e64 v71, v65, v67, s[0:1]
	v_mov_b32_dpp v69, v64 row_ror:8 row_mask:0xf bank_mask:0xf bound_ctrl:1
	v_pk_add_f32 v[66:67], v[70:71], v[68:69]
	s_lshl_b64 s[10:11], s[8:9], 11
	v_pk_mul_f32 v[64:65], v[66:67], v[66:67]
	v_cvt_pk_bf16_f32 v68, v66, v67
	v_add_f32_e32 v64, v64, v65
	v_lshl_add_u64 v[66:67], v[130:131], 0, s[10:11]
	global_store_dword v[66:67], v68, off
	v_add_f32_dpp v64, v64, v64 quad_perm:[1,0,3,2] row_mask:0xf bank_mask:0xf bound_ctrl:1
	s_nop 1
	v_add_f32_dpp v64, v64, v64 quad_perm:[2,3,0,1] row_mask:0xf bank_mask:0xf bound_ctrl:1
	s_nop 1
	v_add_f32_dpp v64, v64, v64 row_half_mirror row_mask:0xf bank_mask:0xf bound_ctrl:1
	s_nop 1
	v_add_f32_dpp v64, v64, v64 row_ror:8 row_mask:0xf bank_mask:0xf bound_ctrl:1
	v_mov_b32_e32 v65, v64
	s_nop 1
	v_permlane16_swap_b32_e32 v64, v65
	v_add_f32_e32 v64, v64, v65
	v_mov_b32_e32 v65, v64
	s_nop 1
	v_permlane32_swap_b32_e32 v64, v65
	s_and_saveexec_b64 s[10:11], s[2:3]
	s_lshl_b64 s[16:17], s[8:9], 2
	s_add_u32 s16, s12, s16
	v_add_f32_e32 v64, v64, v65
	s_addc_u32 s17, s13, s17
	global_store_dword v129, v64, s[16:17]
	s_or_b64 exec, exec, s[10:11]
	v_lshl_or_b32 v2, v2, 7, v136
	global_load_dwordx4 v[68:71], v2, s[4:5] sc0
	v_lshl_or_b32 v3, v3, 7, v136
	global_load_dwordx4 v[64:67], v3, s[4:5] sc0
	s_add_u32 s22, s20, 0x200
	s_lshl_b32 s22, s22, 9
	v_lshl_add_u64 v[28:29], v[134:135], 0, s[22:23]
	global_load_dwordx4 v[16:19], v[28:29], off offset:48
	global_load_dwordx4 v[20:23], v[28:29], off offset:32
	global_load_dwordx4 v[24:27], v[28:29], off offset:16
	s_nop 0
	global_load_dwordx4 v[28:31], v[28:29], off
	s_add_u32 s6, s20, 0x100
	s_waitcnt vmcnt(22)
	v_cvt_pk_f32_fp8_e32 v[138:139], v240
	v_cvt_pk_f32_fp8_sdwa v[140:141], v240 src0_sel:WORD_1
	v_cvt_pk_f32_fp8_e32 v[142:143], v241
	v_cvt_pk_f32_fp8_sdwa v[240:241], v241 src0_sel:WORD_1
	v_cvt_pk_f32_fp8_e32 v[144:145], v242
	v_cvt_pk_f32_fp8_sdwa v[146:147], v242 src0_sel:WORD_1
	v_cvt_pk_f32_fp8_e32 v[148:149], v243
	v_cvt_pk_f32_fp8_sdwa v[242:243], v243 src0_sel:WORD_1
	v_cvt_pk_f32_fp8_e32 v[150:151], v236
	v_cvt_pk_f32_fp8_sdwa v[152:153], v236 src0_sel:WORD_1
	v_cvt_pk_f32_fp8_e32 v[154:155], v237
	v_cvt_pk_f32_fp8_sdwa v[236:237], v237 src0_sel:WORD_1
	v_cvt_pk_f32_fp8_e32 v[156:157], v238
	v_cvt_pk_f32_fp8_sdwa v[158:159], v238 src0_sel:WORD_1
	v_cvt_pk_f32_fp8_e32 v[160:161], v239
	v_cvt_pk_f32_fp8_sdwa v[238:239], v239 src0_sel:WORD_1
	v_pk_fma_f32 v[138:139], v[138:139], v[48:49], 0 op_sel_hi:[1,0,0]
	v_pk_fma_f32 v[140:141], v[140:141], v[48:49], 0 op_sel_hi:[1,0,0]
	v_pk_fma_f32 v[142:143], v[142:143], v[48:49], 0 op_sel_hi:[1,0,0]
	v_pk_fma_f32 v[240:241], v[240:241], v[48:49], 0 op_sel_hi:[1,0,0]
	v_pk_fma_f32 v[144:145], v[144:145], v[48:49], 0 op_sel_hi:[1,0,0]
	v_pk_fma_f32 v[146:147], v[146:147], v[48:49], 0 op_sel_hi:[1,0,0]
	v_pk_fma_f32 v[148:149], v[148:149], v[48:49], 0 op_sel_hi:[1,0,0]
	v_pk_fma_f32 v[242:243], v[242:243], v[48:49], 0 op_sel_hi:[1,0,0]
	v_pk_fma_f32 v[138:139], v[150:151], v[48:49], v[138:139] op_sel:[0,1,0]
	v_pk_fma_f32 v[140:141], v[152:153], v[48:49], v[140:141] op_sel:[0,1,0]
	v_pk_fma_f32 v[142:143], v[154:155], v[48:49], v[142:143] op_sel:[0,1,0]
	v_pk_fma_f32 v[236:237], v[236:237], v[48:49], v[240:241] op_sel:[0,1,0]
	v_pk_fma_f32 v[240:241], v[156:157], v[48:49], v[144:145] op_sel:[0,1,0]
	v_pk_fma_f32 v[144:145], v[158:159], v[48:49], v[146:147] op_sel:[0,1,0]
	v_pk_fma_f32 v[146:147], v[160:161], v[48:49], v[148:149] op_sel:[0,1,0]
	v_pk_fma_f32 v[238:239], v[238:239], v[48:49], v[242:243] op_sel:[0,1,0]
	v_cvt_pk_f32_fp8_e32 v[242:243], v232
	v_cvt_pk_f32_fp8_sdwa v[148:149], v232 src0_sel:WORD_1
	v_cvt_pk_f32_fp8_e32 v[150:151], v233
	v_cvt_pk_f32_fp8_sdwa v[232:233], v233 src0_sel:WORD_1
	v_cvt_pk_f32_fp8_e32 v[152:153], v234
	v_cvt_pk_f32_fp8_sdwa v[154:155], v234 src0_sel:WORD_1
	v_cvt_pk_f32_fp8_e32 v[156:157], v235
	v_cvt_pk_f32_fp8_sdwa v[234:235], v235 src0_sel:WORD_1
	v_pk_fma_f32 v[242:243], v[242:243], v[50:51], v[138:139] op_sel_hi:[1,0,1]
	v_pk_fma_f32 v[138:139], v[148:149], v[50:51], v[140:141] op_sel_hi:[1,0,1]
	v_pk_fma_f32 v[140:141], v[150:151], v[50:51], v[142:143] op_sel_hi:[1,0,1]
	v_pk_fma_f32 v[232:233], v[232:233], v[50:51], v[236:237] op_sel_hi:[1,0,1]
	v_pk_fma_f32 v[236:237], v[152:153], v[50:51], v[240:241] op_sel_hi:[1,0,1]
	v_pk_fma_f32 v[240:241], v[154:155], v[50:51], v[144:145] op_sel_hi:[1,0,1]
	v_pk_fma_f32 v[142:143], v[156:157], v[50:51], v[146:147] op_sel_hi:[1,0,1]
	v_pk_fma_f32 v[234:235], v[234:235], v[50:51], v[238:239] op_sel_hi:[1,0,1]
	v_cvt_pk_f32_fp8_e32 v[238:239], v228
	v_cvt_pk_f32_fp8_sdwa v[144:145], v228 src0_sel:WORD_1
	v_cvt_pk_f32_fp8_e32 v[146:147], v229
	v_cvt_pk_f32_fp8_sdwa v[228:229], v229 src0_sel:WORD_1
	v_cvt_pk_f32_fp8_e32 v[148:149], v230
	v_cvt_pk_f32_fp8_sdwa v[150:151], v230 src0_sel:WORD_1
	v_cvt_pk_f32_fp8_e32 v[152:153], v231
	v_cvt_pk_f32_fp8_sdwa v[230:231], v231 src0_sel:WORD_1
	v_mov_b32_e32 v128, v51
	v_pk_fma_f32 v[238:239], v[238:239], v[128:129], v[242:243] op_sel_hi:[1,0,1]
	v_pk_fma_f32 v[242:243], v[144:145], v[128:129], v[138:139] op_sel_hi:[1,0,1]
	v_pk_fma_f32 v[138:139], v[146:147], v[128:129], v[140:141] op_sel_hi:[1,0,1]
	v_pk_fma_f32 v[228:229], v[228:229], v[128:129], v[232:233] op_sel_hi:[1,0,1]
	v_pk_fma_f32 v[232:233], v[148:149], v[128:129], v[236:237] op_sel_hi:[1,0,1]
	v_pk_fma_f32 v[236:237], v[150:151], v[128:129], v[240:241] op_sel_hi:[1,0,1]
	v_pk_fma_f32 v[240:241], v[152:153], v[128:129], v[142:143] op_sel_hi:[1,0,1]
	v_pk_fma_f32 v[230:231], v[230:231], v[128:129], v[234:235] op_sel_hi:[1,0,1]
	v_cvt_pk_f32_fp8_e32 v[234:235], v224
	v_cvt_pk_f32_fp8_sdwa v[140:141], v224 src0_sel:WORD_1
	v_cvt_pk_f32_fp8_e32 v[142:143], v225
	v_cvt_pk_f32_fp8_sdwa v[224:225], v225 src0_sel:WORD_1
	v_cvt_pk_f32_fp8_e32 v[144:145], v226
	v_cvt_pk_f32_fp8_sdwa v[146:147], v226 src0_sel:WORD_1
	v_cvt_pk_f32_fp8_e32 v[148:149], v227
	v_cvt_pk_f32_fp8_sdwa v[226:227], v227 src0_sel:WORD_1
	v_pk_fma_f32 v[234:235], v[234:235], v[52:53], v[238:239] op_sel_hi:[1,0,1]
	v_pk_fma_f32 v[238:239], v[140:141], v[52:53], v[242:243] op_sel_hi:[1,0,1]
	v_pk_fma_f32 v[242:243], v[142:143], v[52:53], v[138:139] op_sel_hi:[1,0,1]
	v_pk_fma_f32 v[224:225], v[224:225], v[52:53], v[228:229] op_sel_hi:[1,0,1]
	v_pk_fma_f32 v[228:229], v[144:145], v[52:53], v[232:233] op_sel_hi:[1,0,1]
	v_pk_fma_f32 v[232:233], v[146:147], v[52:53], v[236:237] op_sel_hi:[1,0,1]
	v_pk_fma_f32 v[236:237], v[148:149], v[52:53], v[240:241] op_sel_hi:[1,0,1]
	v_pk_fma_f32 v[226:227], v[226:227], v[52:53], v[230:231] op_sel_hi:[1,0,1]
	v_cvt_pk_f32_fp8_e32 v[230:231], v220
	v_cvt_pk_f32_fp8_sdwa v[240:241], v220 src0_sel:WORD_1
	v_cvt_pk_f32_fp8_e32 v[138:139], v221
	v_cvt_pk_f32_fp8_sdwa v[220:221], v221 src0_sel:WORD_1
	v_cvt_pk_f32_fp8_e32 v[140:141], v222
	v_cvt_pk_f32_fp8_sdwa v[142:143], v222 src0_sel:WORD_1
	v_cvt_pk_f32_fp8_e32 v[144:145], v223
	v_cvt_pk_f32_fp8_sdwa v[222:223], v223 src0_sel:WORD_1
	v_pk_fma_f32 v[230:231], v[230:231], v[52:53], v[234:235] op_sel:[0,1,0]
	v_pk_fma_f32 v[234:235], v[240:241], v[52:53], v[238:239] op_sel:[0,1,0]
	v_pk_fma_f32 v[238:239], v[138:139], v[52:53], v[242:243] op_sel:[0,1,0]
	v_pk_fma_f32 v[220:221], v[220:221], v[52:53], v[224:225] op_sel:[0,1,0]
	v_pk_fma_f32 v[224:225], v[140:141], v[52:53], v[228:229] op_sel:[0,1,0]
	v_pk_fma_f32 v[228:229], v[142:143], v[52:53], v[232:233] op_sel:[0,1,0]
	v_pk_fma_f32 v[232:233], v[144:145], v[52:53], v[236:237] op_sel:[0,1,0]
	v_pk_fma_f32 v[222:223], v[222:223], v[52:53], v[226:227] op_sel:[0,1,0]
	v_cvt_pk_f32_fp8_e32 v[226:227], v216
	v_cvt_pk_f32_fp8_sdwa v[236:237], v216 src0_sel:WORD_1
	v_cvt_pk_f32_fp8_e32 v[240:241], v217
	v_cvt_pk_f32_fp8_sdwa v[216:217], v217 src0_sel:WORD_1
	v_cvt_pk_f32_fp8_e32 v[242:243], v218
	v_cvt_pk_f32_fp8_sdwa v[138:139], v218 src0_sel:WORD_1
	v_cvt_pk_f32_fp8_e32 v[140:141], v219
	v_cvt_pk_f32_fp8_sdwa v[218:219], v219 src0_sel:WORD_1
	v_pk_fma_f32 v[226:227], v[226:227], v[54:55], v[230:231] op_sel_hi:[1,0,1]
	v_pk_fma_f32 v[230:231], v[236:237], v[54:55], v[234:235] op_sel_hi:[1,0,1]
	v_pk_fma_f32 v[234:235], v[240:241], v[54:55], v[238:239] op_sel_hi:[1,0,1]
	v_pk_fma_f32 v[216:217], v[216:217], v[54:55], v[220:221] op_sel_hi:[1,0,1]
	v_pk_fma_f32 v[220:221], v[242:243], v[54:55], v[224:225] op_sel_hi:[1,0,1]
	v_pk_fma_f32 v[224:225], v[138:139], v[54:55], v[228:229] op_sel_hi:[1,0,1]
	v_pk_fma_f32 v[228:229], v[140:141], v[54:55], v[232:233] op_sel_hi:[1,0,1]
	v_pk_fma_f32 v[218:219], v[218:219], v[54:55], v[222:223] op_sel_hi:[1,0,1]
	v_cvt_pk_f32_fp8_e32 v[222:223], v212
	v_cvt_pk_f32_fp8_sdwa v[232:233], v212 src0_sel:WORD_1
	v_cvt_pk_f32_fp8_e32 v[236:237], v213
	v_cvt_pk_f32_fp8_sdwa v[212:213], v213 src0_sel:WORD_1
	v_cvt_pk_f32_fp8_e32 v[238:239], v214
	v_cvt_pk_f32_fp8_sdwa v[240:241], v214 src0_sel:WORD_1
	v_cvt_pk_f32_fp8_e32 v[242:243], v215
	v_cvt_pk_f32_fp8_sdwa v[214:215], v215 src0_sel:WORD_1
	v_mov_b32_e32 v128, v55
	v_pk_fma_f32 v[222:223], v[222:223], v[128:129], v[226:227] op_sel_hi:[1,0,1]
	v_pk_fma_f32 v[226:227], v[232:233], v[128:129], v[230:231] op_sel_hi:[1,0,1]
	v_pk_fma_f32 v[230:231], v[236:237], v[128:129], v[234:235] op_sel_hi:[1,0,1]
	v_pk_fma_f32 v[212:213], v[212:213], v[128:129], v[216:217] op_sel_hi:[1,0,1]
	v_pk_fma_f32 v[216:217], v[238:239], v[128:129], v[220:221] op_sel_hi:[1,0,1]
	v_pk_fma_f32 v[220:221], v[240:241], v[128:129], v[224:225] op_sel_hi:[1,0,1]
	v_pk_fma_f32 v[224:225], v[242:243], v[128:129], v[228:229] op_sel_hi:[1,0,1]
	v_lshl_or_b32 v32, v32, 7, v136
	global_load_dwordx4 v[240:243], v32, s[4:5] sc0
	v_pk_fma_f32 v[214:215], v[214:215], v[128:129], v[218:219] op_sel_hi:[1,0,1]
	v_cvt_pk_f32_fp8_e32 v[218:219], v200
	v_cvt_pk_f32_fp8_sdwa v[228:229], v200 src0_sel:WORD_1
	v_cvt_pk_f32_fp8_e32 v[232:233], v201
	v_cvt_pk_f32_fp8_sdwa v[200:201], v201 src0_sel:WORD_1
	v_cvt_pk_f32_fp8_e32 v[234:235], v202
	v_cvt_pk_f32_fp8_sdwa v[236:237], v202 src0_sel:WORD_1
	v_cvt_pk_f32_fp8_e32 v[238:239], v203
	v_cvt_pk_f32_fp8_sdwa v[202:203], v203 src0_sel:WORD_1
	v_pk_fma_f32 v[218:219], v[218:219], v[56:57], v[222:223] op_sel_hi:[1,0,1]
	v_pk_fma_f32 v[222:223], v[228:229], v[56:57], v[226:227] op_sel_hi:[1,0,1]
	v_pk_fma_f32 v[226:227], v[232:233], v[56:57], v[230:231] op_sel_hi:[1,0,1]
	v_pk_fma_f32 v[200:201], v[200:201], v[56:57], v[212:213] op_sel_hi:[1,0,1]
	v_pk_fma_f32 v[212:213], v[234:235], v[56:57], v[216:217] op_sel_hi:[1,0,1]
	v_pk_fma_f32 v[216:217], v[236:237], v[56:57], v[220:221] op_sel_hi:[1,0,1]
	v_pk_fma_f32 v[220:221], v[238:239], v[56:57], v[224:225] op_sel_hi:[1,0,1]
	v_lshl_or_b32 v33, v33, 7, v136
	global_load_dwordx4 v[236:239], v33, s[4:5] sc0
	v_pk_fma_f32 v[202:203], v[202:203], v[56:57], v[214:215] op_sel_hi:[1,0,1]
	v_cvt_pk_f32_fp8_e32 v[214:215], v196
	v_cvt_pk_f32_fp8_sdwa v[224:225], v196 src0_sel:WORD_1
	v_cvt_pk_f32_fp8_e32 v[228:229], v197
	v_cvt_pk_f32_fp8_sdwa v[196:197], v197 src0_sel:WORD_1
	v_cvt_pk_f32_fp8_e32 v[230:231], v198
	v_cvt_pk_f32_fp8_sdwa v[232:233], v198 src0_sel:WORD_1
	v_cvt_pk_f32_fp8_e32 v[234:235], v199
	v_cvt_pk_f32_fp8_sdwa v[198:199], v199 src0_sel:WORD_1
	v_pk_fma_f32 v[214:215], v[214:215], v[56:57], v[218:219] op_sel:[0,1,0]
	v_pk_fma_f32 v[218:219], v[224:225], v[56:57], v[222:223] op_sel:[0,1,0]
	v_pk_fma_f32 v[222:223], v[228:229], v[56:57], v[226:227] op_sel:[0,1,0]
	v_pk_fma_f32 v[196:197], v[196:197], v[56:57], v[200:201] op_sel:[0,1,0]
	v_pk_fma_f32 v[200:201], v[230:231], v[56:57], v[212:213] op_sel:[0,1,0]
	v_pk_fma_f32 v[212:213], v[232:233], v[56:57], v[216:217] op_sel:[0,1,0]
	v_pk_fma_f32 v[216:217], v[234:235], v[56:57], v[220:221] op_sel:[0,1,0]
	v_lshl_or_b32 v34, v34, 7, v136
	global_load_dwordx4 v[232:235], v34, s[4:5] sc0
	v_pk_fma_f32 v[198:199], v[198:199], v[56:57], v[202:203] op_sel:[0,1,0]
	v_cvt_pk_f32_fp8_e32 v[202:203], v192
	v_cvt_pk_f32_fp8_sdwa v[220:221], v192 src0_sel:WORD_1
	v_cvt_pk_f32_fp8_e32 v[224:225], v193
	v_cvt_pk_f32_fp8_sdwa v[192:193], v193 src0_sel:WORD_1
	v_cvt_pk_f32_fp8_e32 v[226:227], v194
	v_cvt_pk_f32_fp8_sdwa v[228:229], v194 src0_sel:WORD_1
	v_cvt_pk_f32_fp8_e32 v[230:231], v195
	v_cvt_pk_f32_fp8_sdwa v[194:195], v195 src0_sel:WORD_1
	v_pk_fma_f32 v[202:203], v[202:203], v[58:59], v[214:215] op_sel_hi:[1,0,1]
	v_pk_fma_f32 v[214:215], v[220:221], v[58:59], v[218:219] op_sel_hi:[1,0,1]
	v_pk_fma_f32 v[218:219], v[224:225], v[58:59], v[222:223] op_sel_hi:[1,0,1]
	v_pk_fma_f32 v[192:193], v[192:193], v[58:59], v[196:197] op_sel_hi:[1,0,1]
	v_pk_fma_f32 v[196:197], v[226:227], v[58:59], v[200:201] op_sel_hi:[1,0,1]
	v_pk_fma_f32 v[200:201], v[228:229], v[58:59], v[212:213] op_sel_hi:[1,0,1]
	v_pk_fma_f32 v[212:213], v[230:231], v[58:59], v[216:217] op_sel_hi:[1,0,1]
	v_pk_fma_f32 v[194:195], v[194:195], v[58:59], v[198:199] op_sel_hi:[1,0,1]
	v_cvt_pk_f32_fp8_e32 v[198:199], v184
	v_cvt_pk_f32_fp8_sdwa v[216:217], v184 src0_sel:WORD_1
	v_cvt_pk_f32_fp8_e32 v[220:221], v185
	v_cvt_pk_f32_fp8_sdwa v[184:185], v185 src0_sel:WORD_1
	v_cvt_pk_f32_fp8_e32 v[222:223], v186
	v_cvt_pk_f32_fp8_sdwa v[224:225], v186 src0_sel:WORD_1
	v_cvt_pk_f32_fp8_e32 v[226:227], v187
	v_cvt_pk_f32_fp8_sdwa v[186:187], v187 src0_sel:WORD_1
	v_mov_b32_e32 v228, v59
	v_pk_fma_f32 v[198:199], v[198:199], v[228:229], v[202:203] op_sel_hi:[1,0,1]
	v_pk_fma_f32 v[202:203], v[216:217], v[228:229], v[214:215] op_sel_hi:[1,0,1]
	v_pk_fma_f32 v[214:215], v[220:221], v[228:229], v[218:219] op_sel_hi:[1,0,1]
	v_pk_fma_f32 v[184:185], v[184:185], v[228:229], v[192:193] op_sel_hi:[1,0,1]
	v_pk_fma_f32 v[192:193], v[222:223], v[228:229], v[196:197] op_sel_hi:[1,0,1]
	v_pk_fma_f32 v[196:197], v[224:225], v[228:229], v[200:201] op_sel_hi:[1,0,1]
	v_pk_fma_f32 v[200:201], v[226:227], v[228:229], v[212:213] op_sel_hi:[1,0,1]
	v_lshl_or_b32 v36, v36, 7, v136
	global_load_dwordx4 v[224:227], v36, s[4:5] sc0
	v_pk_fma_f32 v[186:187], v[186:187], v[228:229], v[194:195] op_sel_hi:[1,0,1]
	v_lshl_or_b32 v35, v35, 7, v136
	global_load_dwordx4 v[228:231], v35, s[4:5] sc0
	v_cvt_pk_f32_fp8_e32 v[194:195], v180
	v_cvt_pk_f32_fp8_sdwa v[212:213], v180 src0_sel:WORD_1
	v_cvt_pk_f32_fp8_e32 v[216:217], v181
	v_cvt_pk_f32_fp8_sdwa v[180:181], v181 src0_sel:WORD_1
	v_cvt_pk_f32_fp8_e32 v[218:219], v182
	v_cvt_pk_f32_fp8_sdwa v[220:221], v182 src0_sel:WORD_1
	v_cvt_pk_f32_fp8_e32 v[222:223], v183
	v_cvt_pk_f32_fp8_sdwa v[182:183], v183 src0_sel:WORD_1
	v_pk_fma_f32 v[194:195], v[194:195], v[60:61], v[198:199] op_sel_hi:[1,0,1]
	v_pk_fma_f32 v[198:199], v[212:213], v[60:61], v[202:203] op_sel_hi:[1,0,1]
	v_pk_fma_f32 v[202:203], v[216:217], v[60:61], v[214:215] op_sel_hi:[1,0,1]
	v_pk_fma_f32 v[180:181], v[180:181], v[60:61], v[184:185] op_sel_hi:[1,0,1]
	v_pk_fma_f32 v[184:185], v[218:219], v[60:61], v[192:193] op_sel_hi:[1,0,1]
	v_pk_fma_f32 v[192:193], v[220:221], v[60:61], v[196:197] op_sel_hi:[1,0,1]
	v_pk_fma_f32 v[196:197], v[222:223], v[60:61], v[200:201] op_sel_hi:[1,0,1]
	v_lshl_or_b32 v37, v37, 7, v136
	global_load_dwordx4 v[220:223], v37, s[4:5] sc0
	v_pk_fma_f32 v[182:183], v[182:183], v[60:61], v[186:187] op_sel_hi:[1,0,1]
	v_cvt_pk_f32_fp8_e32 v[186:187], v172
	v_cvt_pk_f32_fp8_sdwa v[200:201], v172 src0_sel:WORD_1
	v_cvt_pk_f32_fp8_e32 v[212:213], v173
	v_cvt_pk_f32_fp8_sdwa v[172:173], v173 src0_sel:WORD_1
	v_cvt_pk_f32_fp8_e32 v[214:215], v174
	v_cvt_pk_f32_fp8_sdwa v[216:217], v174 src0_sel:WORD_1
	v_cvt_pk_f32_fp8_e32 v[218:219], v175
	v_cvt_pk_f32_fp8_sdwa v[174:175], v175 src0_sel:WORD_1
	v_pk_fma_f32 v[186:187], v[186:187], v[60:61], v[194:195] op_sel:[0,1,0]
	v_pk_fma_f32 v[194:195], v[200:201], v[60:61], v[198:199] op_sel:[0,1,0]
	v_pk_fma_f32 v[198:199], v[212:213], v[60:61], v[202:203] op_sel:[0,1,0]
	v_pk_fma_f32 v[172:173], v[172:173], v[60:61], v[180:181] op_sel:[0,1,0]
	v_pk_fma_f32 v[180:181], v[214:215], v[60:61], v[184:185] op_sel:[0,1,0]
	v_pk_fma_f32 v[184:185], v[216:217], v[60:61], v[192:193] op_sel:[0,1,0]
	v_pk_fma_f32 v[192:193], v[218:219], v[60:61], v[196:197] op_sel:[0,1,0]
	v_lshl_or_b32 v38, v38, 7, v136
	global_load_dwordx4 v[216:219], v38, s[4:5] sc0
	v_pk_fma_f32 v[174:175], v[174:175], v[60:61], v[182:183] op_sel:[0,1,0]
	v_cvt_pk_f32_fp8_e32 v[182:183], v168
	v_cvt_pk_f32_fp8_sdwa v[196:197], v168 src0_sel:WORD_1
	v_cvt_pk_f32_fp8_e32 v[200:201], v169
	v_cvt_pk_f32_fp8_sdwa v[168:169], v169 src0_sel:WORD_1
	v_cvt_pk_f32_fp8_e32 v[202:203], v170
	v_cvt_pk_f32_fp8_sdwa v[212:213], v170 src0_sel:WORD_1
	v_cvt_pk_f32_fp8_e32 v[214:215], v171
	v_cvt_pk_f32_fp8_sdwa v[170:171], v171 src0_sel:WORD_1
	v_pk_fma_f32 v[182:183], v[182:183], v[62:63], v[186:187] op_sel_hi:[1,0,1]
	v_pk_fma_f32 v[186:187], v[196:197], v[62:63], v[194:195] op_sel_hi:[1,0,1]
	v_pk_fma_f32 v[194:195], v[200:201], v[62:63], v[198:199] op_sel_hi:[1,0,1]
	v_pk_fma_f32 v[168:169], v[168:169], v[62:63], v[172:173] op_sel_hi:[1,0,1]
	v_pk_fma_f32 v[172:173], v[202:203], v[62:63], v[180:181] op_sel_hi:[1,0,1]
	v_pk_fma_f32 v[180:181], v[212:213], v[62:63], v[184:185] op_sel_hi:[1,0,1]
	v_pk_fma_f32 v[184:185], v[214:215], v[62:63], v[192:193] op_sel_hi:[1,0,1]
	v_pk_fma_f32 v[170:171], v[170:171], v[62:63], v[174:175] op_sel_hi:[1,0,1]
	v_cvt_pk_f32_fp8_e32 v[174:175], v164
	v_cvt_pk_f32_fp8_sdwa v[192:193], v164 src0_sel:WORD_1
	v_cvt_pk_f32_fp8_e32 v[196:197], v165
	v_cvt_pk_f32_fp8_sdwa v[164:165], v165 src0_sel:WORD_1
	v_cvt_pk_f32_fp8_e32 v[198:199], v166
	v_cvt_pk_f32_fp8_sdwa v[200:201], v166 src0_sel:WORD_1
	v_cvt_pk_f32_fp8_e32 v[202:203], v167
	v_cvt_pk_f32_fp8_sdwa v[166:167], v167 src0_sel:WORD_1
	v_mov_b32_e32 v212, v63
	v_pk_fma_f32 v[174:175], v[174:175], v[212:213], v[182:183] op_sel_hi:[1,0,1]
	v_pk_fma_f32 v[182:183], v[192:193], v[212:213], v[186:187] op_sel_hi:[1,0,1]
	v_pk_fma_f32 v[186:187], v[196:197], v[212:213], v[194:195] op_sel_hi:[1,0,1]
	v_lshl_or_b32 v42, v42, 7, v136
	global_load_dwordx4 v[192:195], v42, s[4:5] sc0
	v_pk_fma_f32 v[164:165], v[164:165], v[212:213], v[168:169] op_sel_hi:[1,0,1]
	v_pk_fma_f32 v[168:169], v[198:199], v[212:213], v[172:173] op_sel_hi:[1,0,1]
	v_lshl_or_b32 v41, v41, 7, v136
	global_load_dwordx4 v[196:199], v41, s[4:5] sc0
	v_pk_fma_f32 v[172:173], v[200:201], v[212:213], v[180:181] op_sel_hi:[1,0,1]
	v_pk_fma_f32 v[180:181], v[202:203], v[212:213], v[184:185] op_sel_hi:[1,0,1]
	v_lshl_or_b32 v40, v40, 7, v136
	global_load_dwordx4 v[200:203], v40, s[4:5] sc0
	v_pk_fma_f32 v[166:167], v[166:167], v[212:213], v[170:171] op_sel_hi:[1,0,1]
	v_lshl_or_b32 v39, v39, 7, v136
	global_load_dwordx4 v[212:215], v39, s[4:5] sc0
	v_permlane32_swap_b32_e32 v174, v168
	v_permlane32_swap_b32_e32 v175, v169
	v_permlane32_swap_b32_e32 v182, v172
	v_permlane32_swap_b32_e32 v183, v173
	v_permlane32_swap_b32_e32 v186, v180
	v_permlane32_swap_b32_e32 v187, v181
	v_permlane32_swap_b32_e32 v164, v166
	v_permlane32_swap_b32_e32 v165, v167
	v_add_f32_e32 v168, v174, v168
	v_add_f32_e32 v169, v175, v169
	v_add_f32_e32 v170, v182, v172
	v_add_f32_e32 v171, v183, v173
	v_add_f32_e32 v172, v186, v180
	v_add_f32_e32 v173, v187, v181
	v_lshl_or_b32 v43, v43, 7, v136
	global_load_dwordx4 v[184:187], v43, s[4:5] sc0
	v_lshl_or_b32 v44, v44, 7, v136
	global_load_dwordx4 v[180:183], v44, s[4:5] sc0
	v_add_f32_e32 v164, v164, v166
	v_add_f32_e32 v165, v165, v167
	v_permlane16_swap_b32_e32 v168, v172
	v_permlane16_swap_b32_e32 v169, v173
	v_permlane16_swap_b32_e32 v170, v164
	v_permlane16_swap_b32_e32 v171, v165
	v_pk_add_f32 v[166:167], v[168:169], v[172:173]
	v_lshl_or_b32 v45, v45, 7, v136
	global_load_dwordx4 v[172:175], v45, s[4:5] sc0
	v_pk_add_f32 v[164:165], v[170:171], v[164:165]
	s_ashr_i32 s7, s6, 31
	v_cndmask_b32_e64 v168, v166, v164, s[0:1]
	v_cndmask_b32_e64 v170, v164, v166, s[0:1]
	v_cndmask_b32_e64 v164, v167, v165, s[0:1]
	v_mov_b32_dpp v168, v168 row_ror:8 row_mask:0xf bank_mask:0xf bound_ctrl:1
	v_cndmask_b32_e64 v171, v165, v167, s[0:1]
	v_mov_b32_dpp v169, v164 row_ror:8 row_mask:0xf bank_mask:0xf bound_ctrl:1
	v_pk_add_f32 v[166:167], v[170:171], v[168:169]
	s_lshl_b64 s[8:9], s[6:7], 11
	v_pk_mul_f32 v[164:165], v[166:167], v[166:167]
	v_cvt_pk_bf16_f32 v168, v166, v167
	v_add_f32_e32 v164, v164, v165
	v_lshl_add_u64 v[166:167], v[130:131], 0, s[8:9]
	global_store_dword v[166:167], v168, off
	v_add_f32_dpp v164, v164, v164 quad_perm:[1,0,3,2] row_mask:0xf bank_mask:0xf bound_ctrl:1
	s_nop 1
	v_add_f32_dpp v164, v164, v164 quad_perm:[2,3,0,1] row_mask:0xf bank_mask:0xf bound_ctrl:1
	s_nop 1
	v_add_f32_dpp v164, v164, v164 row_half_mirror row_mask:0xf bank_mask:0xf bound_ctrl:1
	s_nop 1
	v_add_f32_dpp v164, v164, v164 row_ror:8 row_mask:0xf bank_mask:0xf bound_ctrl:1
	v_mov_b32_e32 v165, v164
	s_nop 1
	v_permlane16_swap_b32_e32 v164, v165
	v_add_f32_e32 v164, v164, v165
	v_mov_b32_e32 v165, v164
	s_nop 1
	v_permlane32_swap_b32_e32 v164, v165
	s_and_saveexec_b64 s[8:9], s[2:3]
	s_lshl_b64 s[10:11], s[6:7], 2
	s_add_u32 s10, s12, s10
	v_add_f32_e32 v164, v164, v165
	s_addc_u32 s11, s13, s11
	global_store_dword v129, v164, s[10:11]
	s_or_b64 exec, exec, s[8:9]
	v_lshl_or_b32 v46, v46, 7, v136
	global_load_dwordx4 v[168:171], v46, s[4:5] sc0
	v_lshl_or_b32 v47, v47, 7, v136
	global_load_dwordx4 v[164:167], v47, s[4:5] sc0
	s_add_u32 s22, s20, 0x300
	s_lshl_b32 s22, s22, 9
	v_lshl_add_u64 v[48:49], v[134:135], 0, s[22:23]
	global_load_dwordx4 v[60:63], v[48:49], off offset:48
	global_load_dwordx4 v[56:59], v[48:49], off offset:32
	global_load_dwordx4 v[52:55], v[48:49], off offset:16
	s_nop 0
	global_load_dwordx4 v[48:51], v[48:49], off
	s_add_u32 s20, s20, 0x200
	s_mov_b32 s8, s20
	s_waitcnt vmcnt(22)
	v_cvt_pk_f32_fp8_e32 v[138:139], v124
	v_cvt_pk_f32_fp8_sdwa v[140:141], v124 src0_sel:WORD_1
	v_cvt_pk_f32_fp8_e32 v[142:143], v125
	v_cvt_pk_f32_fp8_sdwa v[124:125], v125 src0_sel:WORD_1
	v_cvt_pk_f32_fp8_e32 v[144:145], v126
	v_cvt_pk_f32_fp8_sdwa v[146:147], v126 src0_sel:WORD_1
	v_cvt_pk_f32_fp8_e32 v[148:149], v127
	v_cvt_pk_f32_fp8_sdwa v[126:127], v127 src0_sel:WORD_1
	v_cvt_pk_f32_fp8_e32 v[150:151], v120
	v_cvt_pk_f32_fp8_sdwa v[152:153], v120 src0_sel:WORD_1
	v_cvt_pk_f32_fp8_e32 v[154:155], v121
	v_cvt_pk_f32_fp8_sdwa v[120:121], v121 src0_sel:WORD_1
	v_cvt_pk_f32_fp8_e32 v[156:157], v122
	v_cvt_pk_f32_fp8_sdwa v[158:159], v122 src0_sel:WORD_1
	v_cvt_pk_f32_fp8_e32 v[160:161], v123
	v_cvt_pk_f32_fp8_sdwa v[122:123], v123 src0_sel:WORD_1
	v_pk_fma_f32 v[138:139], v[138:139], v[28:29], 0 op_sel_hi:[1,0,0]
	v_pk_fma_f32 v[140:141], v[140:141], v[28:29], 0 op_sel_hi:[1,0,0]
	v_pk_fma_f32 v[142:143], v[142:143], v[28:29], 0 op_sel_hi:[1,0,0]
	v_pk_fma_f32 v[124:125], v[124:125], v[28:29], 0 op_sel_hi:[1,0,0]
	v_pk_fma_f32 v[144:145], v[144:145], v[28:29], 0 op_sel_hi:[1,0,0]
	v_pk_fma_f32 v[146:147], v[146:147], v[28:29], 0 op_sel_hi:[1,0,0]
	v_pk_fma_f32 v[148:149], v[148:149], v[28:29], 0 op_sel_hi:[1,0,0]
	v_pk_fma_f32 v[126:127], v[126:127], v[28:29], 0 op_sel_hi:[1,0,0]
	v_pk_fma_f32 v[138:139], v[150:151], v[28:29], v[138:139] op_sel:[0,1,0]
	v_pk_fma_f32 v[140:141], v[152:153], v[28:29], v[140:141] op_sel:[0,1,0]
	v_pk_fma_f32 v[142:143], v[154:155], v[28:29], v[142:143] op_sel:[0,1,0]
	v_pk_fma_f32 v[120:121], v[120:121], v[28:29], v[124:125] op_sel:[0,1,0]
	v_pk_fma_f32 v[124:125], v[156:157], v[28:29], v[144:145] op_sel:[0,1,0]
	v_pk_fma_f32 v[144:145], v[158:159], v[28:29], v[146:147] op_sel:[0,1,0]
	v_pk_fma_f32 v[146:147], v[160:161], v[28:29], v[148:149] op_sel:[0,1,0]
	v_pk_fma_f32 v[122:123], v[122:123], v[28:29], v[126:127] op_sel:[0,1,0]
	v_cvt_pk_f32_fp8_e32 v[126:127], v116
	v_cvt_pk_f32_fp8_sdwa v[148:149], v116 src0_sel:WORD_1
	v_cvt_pk_f32_fp8_e32 v[150:151], v117
	v_cvt_pk_f32_fp8_sdwa v[116:117], v117 src0_sel:WORD_1
	v_cvt_pk_f32_fp8_e32 v[152:153], v118
	v_cvt_pk_f32_fp8_sdwa v[154:155], v118 src0_sel:WORD_1
	v_cvt_pk_f32_fp8_e32 v[156:157], v119
	v_cvt_pk_f32_fp8_sdwa v[118:119], v119 src0_sel:WORD_1
	v_pk_fma_f32 v[126:127], v[126:127], v[30:31], v[138:139] op_sel_hi:[1,0,1]
	v_pk_fma_f32 v[138:139], v[148:149], v[30:31], v[140:141] op_sel_hi:[1,0,1]
	v_pk_fma_f32 v[140:141], v[150:151], v[30:31], v[142:143] op_sel_hi:[1,0,1]
	v_pk_fma_f32 v[116:117], v[116:117], v[30:31], v[120:121] op_sel_hi:[1,0,1]
	v_pk_fma_f32 v[120:121], v[152:153], v[30:31], v[124:125] op_sel_hi:[1,0,1]
	v_pk_fma_f32 v[124:125], v[154:155], v[30:31], v[144:145] op_sel_hi:[1,0,1]
	v_pk_fma_f32 v[142:143], v[156:157], v[30:31], v[146:147] op_sel_hi:[1,0,1]
	v_pk_fma_f32 v[118:119], v[118:119], v[30:31], v[122:123] op_sel_hi:[1,0,1]
	v_cvt_pk_f32_fp8_e32 v[122:123], v112
	v_cvt_pk_f32_fp8_sdwa v[144:145], v112 src0_sel:WORD_1
	v_cvt_pk_f32_fp8_e32 v[146:147], v113
	v_cvt_pk_f32_fp8_sdwa v[112:113], v113 src0_sel:WORD_1
	v_cvt_pk_f32_fp8_e32 v[148:149], v114
	v_cvt_pk_f32_fp8_sdwa v[150:151], v114 src0_sel:WORD_1
	v_cvt_pk_f32_fp8_e32 v[152:153], v115
	v_cvt_pk_f32_fp8_sdwa v[114:115], v115 src0_sel:WORD_1
	v_mov_b32_e32 v128, v31
	v_pk_fma_f32 v[122:123], v[122:123], v[128:129], v[126:127] op_sel_hi:[1,0,1]
	v_pk_fma_f32 v[126:127], v[144:145], v[128:129], v[138:139] op_sel_hi:[1,0,1]
	v_pk_fma_f32 v[138:139], v[146:147], v[128:129], v[140:141] op_sel_hi:[1,0,1]
	v_pk_fma_f32 v[112:113], v[112:113], v[128:129], v[116:117] op_sel_hi:[1,0,1]
	v_pk_fma_f32 v[116:117], v[148:149], v[128:129], v[120:121] op_sel_hi:[1,0,1]
	v_pk_fma_f32 v[120:121], v[150:151], v[128:129], v[124:125] op_sel_hi:[1,0,1]
	v_pk_fma_f32 v[124:125], v[152:153], v[128:129], v[142:143] op_sel_hi:[1,0,1]
	v_pk_fma_f32 v[114:115], v[114:115], v[128:129], v[118:119] op_sel_hi:[1,0,1]
	v_cvt_pk_f32_fp8_e32 v[118:119], v108
	v_cvt_pk_f32_fp8_sdwa v[140:141], v108 src0_sel:WORD_1
	v_cvt_pk_f32_fp8_e32 v[142:143], v109
	v_cvt_pk_f32_fp8_sdwa v[108:109], v109 src0_sel:WORD_1
	v_cvt_pk_f32_fp8_e32 v[144:145], v110
	v_cvt_pk_f32_fp8_sdwa v[146:147], v110 src0_sel:WORD_1
	v_cvt_pk_f32_fp8_e32 v[148:149], v111
	v_cvt_pk_f32_fp8_sdwa v[110:111], v111 src0_sel:WORD_1
	v_pk_fma_f32 v[118:119], v[118:119], v[24:25], v[122:123] op_sel_hi:[1,0,1]
	v_pk_fma_f32 v[122:123], v[140:141], v[24:25], v[126:127] op_sel_hi:[1,0,1]
	v_pk_fma_f32 v[126:127], v[142:143], v[24:25], v[138:139] op_sel_hi:[1,0,1]
	v_pk_fma_f32 v[108:109], v[108:109], v[24:25], v[112:113] op_sel_hi:[1,0,1]
	v_pk_fma_f32 v[112:113], v[144:145], v[24:25], v[116:117] op_sel_hi:[1,0,1]
	v_pk_fma_f32 v[116:117], v[146:147], v[24:25], v[120:121] op_sel_hi:[1,0,1]
	v_pk_fma_f32 v[120:121], v[148:149], v[24:25], v[124:125] op_sel_hi:[1,0,1]
	v_pk_fma_f32 v[110:111], v[110:111], v[24:25], v[114:115] op_sel_hi:[1,0,1]
	v_cvt_pk_f32_fp8_e32 v[114:115], v104
	v_cvt_pk_f32_fp8_sdwa v[124:125], v104 src0_sel:WORD_1
	v_cvt_pk_f32_fp8_e32 v[138:139], v105
	v_cvt_pk_f32_fp8_sdwa v[104:105], v105 src0_sel:WORD_1
	v_cvt_pk_f32_fp8_e32 v[140:141], v106
	v_cvt_pk_f32_fp8_sdwa v[142:143], v106 src0_sel:WORD_1
	v_cvt_pk_f32_fp8_e32 v[144:145], v107
	v_cvt_pk_f32_fp8_sdwa v[106:107], v107 src0_sel:WORD_1
	v_pk_fma_f32 v[114:115], v[114:115], v[24:25], v[118:119] op_sel:[0,1,0]
	v_pk_fma_f32 v[118:119], v[124:125], v[24:25], v[122:123] op_sel:[0,1,0]
	v_pk_fma_f32 v[122:123], v[138:139], v[24:25], v[126:127] op_sel:[0,1,0]
	v_pk_fma_f32 v[104:105], v[104:105], v[24:25], v[108:109] op_sel:[0,1,0]
	v_pk_fma_f32 v[108:109], v[140:141], v[24:25], v[112:113] op_sel:[0,1,0]
	v_pk_fma_f32 v[112:113], v[142:143], v[24:25], v[116:117] op_sel:[0,1,0]
	v_pk_fma_f32 v[116:117], v[144:145], v[24:25], v[120:121] op_sel:[0,1,0]
	v_pk_fma_f32 v[106:107], v[106:107], v[24:25], v[110:111] op_sel:[0,1,0]
	v_cvt_pk_f32_fp8_e32 v[110:111], v100
	v_cvt_pk_f32_fp8_sdwa v[120:121], v100 src0_sel:WORD_1
	v_cvt_pk_f32_fp8_e32 v[124:125], v101
	v_cvt_pk_f32_fp8_sdwa v[100:101], v101 src0_sel:WORD_1
	v_cvt_pk_f32_fp8_e32 v[126:127], v102
	v_cvt_pk_f32_fp8_sdwa v[138:139], v102 src0_sel:WORD_1
	v_cvt_pk_f32_fp8_e32 v[140:141], v103
	v_cvt_pk_f32_fp8_sdwa v[102:103], v103 src0_sel:WORD_1
	v_pk_fma_f32 v[110:111], v[110:111], v[26:27], v[114:115] op_sel_hi:[1,0,1]
	v_pk_fma_f32 v[114:115], v[120:121], v[26:27], v[118:119] op_sel_hi:[1,0,1]
	v_pk_fma_f32 v[118:119], v[124:125], v[26:27], v[122:123] op_sel_hi:[1,0,1]
	v_pk_fma_f32 v[100:101], v[100:101], v[26:27], v[104:105] op_sel_hi:[1,0,1]
	v_pk_fma_f32 v[104:105], v[126:127], v[26:27], v[108:109] op_sel_hi:[1,0,1]
	v_pk_fma_f32 v[108:109], v[138:139], v[26:27], v[112:113] op_sel_hi:[1,0,1]
	v_pk_fma_f32 v[112:113], v[140:141], v[26:27], v[116:117] op_sel_hi:[1,0,1]
	v_pk_fma_f32 v[102:103], v[102:103], v[26:27], v[106:107] op_sel_hi:[1,0,1]
	v_cvt_pk_f32_fp8_e32 v[106:107], v96
	v_cvt_pk_f32_fp8_sdwa v[116:117], v96 src0_sel:WORD_1
	v_cvt_pk_f32_fp8_e32 v[120:121], v97
	v_cvt_pk_f32_fp8_sdwa v[96:97], v97 src0_sel:WORD_1
	v_cvt_pk_f32_fp8_e32 v[122:123], v98
	v_cvt_pk_f32_fp8_sdwa v[124:125], v98 src0_sel:WORD_1
	v_cvt_pk_f32_fp8_e32 v[126:127], v99
	v_cvt_pk_f32_fp8_sdwa v[98:99], v99 src0_sel:WORD_1
	v_mov_b32_e32 v128, v27
	v_pk_fma_f32 v[106:107], v[106:107], v[128:129], v[110:111] op_sel_hi:[1,0,1]
	v_pk_fma_f32 v[110:111], v[116:117], v[128:129], v[114:115] op_sel_hi:[1,0,1]
	v_pk_fma_f32 v[114:115], v[120:121], v[128:129], v[118:119] op_sel_hi:[1,0,1]
	v_pk_fma_f32 v[96:97], v[96:97], v[128:129], v[100:101] op_sel_hi:[1,0,1]
	v_pk_fma_f32 v[100:101], v[122:123], v[128:129], v[104:105] op_sel_hi:[1,0,1]
	v_pk_fma_f32 v[104:105], v[124:125], v[128:129], v[108:109] op_sel_hi:[1,0,1]
	v_pk_fma_f32 v[108:109], v[126:127], v[128:129], v[112:113] op_sel_hi:[1,0,1]
	v_pk_fma_f32 v[98:99], v[98:99], v[128:129], v[102:103] op_sel_hi:[1,0,1]
	v_cvt_pk_f32_fp8_e32 v[102:103], v92
	v_cvt_pk_f32_fp8_sdwa v[112:113], v92 src0_sel:WORD_1
	v_cvt_pk_f32_fp8_e32 v[116:117], v93
	v_cvt_pk_f32_fp8_sdwa v[92:93], v93 src0_sel:WORD_1
	v_cvt_pk_f32_fp8_e32 v[118:119], v94
	v_cvt_pk_f32_fp8_sdwa v[120:121], v94 src0_sel:WORD_1
	v_cvt_pk_f32_fp8_e32 v[122:123], v95
	v_cvt_pk_f32_fp8_sdwa v[94:95], v95 src0_sel:WORD_1
	v_pk_fma_f32 v[102:103], v[102:103], v[20:21], v[106:107] op_sel_hi:[1,0,1]
	v_pk_fma_f32 v[106:107], v[112:113], v[20:21], v[110:111] op_sel_hi:[1,0,1]
	v_pk_fma_f32 v[110:111], v[116:117], v[20:21], v[114:115] op_sel_hi:[1,0,1]
	v_pk_fma_f32 v[92:93], v[92:93], v[20:21], v[96:97] op_sel_hi:[1,0,1]
	v_pk_fma_f32 v[96:97], v[118:119], v[20:21], v[100:101] op_sel_hi:[1,0,1]
	v_pk_fma_f32 v[100:101], v[120:121], v[20:21], v[104:105] op_sel_hi:[1,0,1]
	v_pk_fma_f32 v[104:105], v[122:123], v[20:21], v[108:109] op_sel_hi:[1,0,1]
	v_pk_fma_f32 v[94:95], v[94:95], v[20:21], v[98:99] op_sel_hi:[1,0,1]
	v_cvt_pk_f32_fp8_e32 v[98:99], v88
	v_cvt_pk_f32_fp8_sdwa v[108:109], v88 src0_sel:WORD_1
	v_cvt_pk_f32_fp8_e32 v[112:113], v89
	v_cvt_pk_f32_fp8_sdwa v[88:89], v89 src0_sel:WORD_1
	v_cvt_pk_f32_fp8_e32 v[114:115], v90
	v_cvt_pk_f32_fp8_sdwa v[116:117], v90 src0_sel:WORD_1
	v_cvt_pk_f32_fp8_e32 v[118:119], v91
	v_cvt_pk_f32_fp8_sdwa v[90:91], v91 src0_sel:WORD_1
	v_pk_fma_f32 v[98:99], v[98:99], v[20:21], v[102:103] op_sel:[0,1,0]
	v_pk_fma_f32 v[102:103], v[108:109], v[20:21], v[106:107] op_sel:[0,1,0]
	v_pk_fma_f32 v[106:107], v[112:113], v[20:21], v[110:111] op_sel:[0,1,0]
	v_pk_fma_f32 v[88:89], v[88:89], v[20:21], v[92:93] op_sel:[0,1,0]
	v_pk_fma_f32 v[92:93], v[114:115], v[20:21], v[96:97] op_sel:[0,1,0]
	v_pk_fma_f32 v[96:97], v[116:117], v[20:21], v[100:101] op_sel:[0,1,0]
	v_pk_fma_f32 v[100:101], v[118:119], v[20:21], v[104:105] op_sel:[0,1,0]
	v_pk_fma_f32 v[90:91], v[90:91], v[20:21], v[94:95] op_sel:[0,1,0]
	v_cvt_pk_f32_fp8_e32 v[94:95], v84
	v_cvt_pk_f32_fp8_sdwa v[104:105], v84 src0_sel:WORD_1
	v_cvt_pk_f32_fp8_e32 v[108:109], v85
	v_cvt_pk_f32_fp8_sdwa v[84:85], v85 src0_sel:WORD_1
	v_cvt_pk_f32_fp8_e32 v[110:111], v86
	v_cvt_pk_f32_fp8_sdwa v[112:113], v86 src0_sel:WORD_1
	v_cvt_pk_f32_fp8_e32 v[114:115], v87
	v_cvt_pk_f32_fp8_sdwa v[86:87], v87 src0_sel:WORD_1
	v_pk_fma_f32 v[94:95], v[94:95], v[22:23], v[98:99] op_sel_hi:[1,0,1]
	v_pk_fma_f32 v[98:99], v[104:105], v[22:23], v[102:103] op_sel_hi:[1,0,1]
	v_pk_fma_f32 v[102:103], v[108:109], v[22:23], v[106:107] op_sel_hi:[1,0,1]
	v_pk_fma_f32 v[84:85], v[84:85], v[22:23], v[88:89] op_sel_hi:[1,0,1]
	v_pk_fma_f32 v[88:89], v[110:111], v[22:23], v[92:93] op_sel_hi:[1,0,1]
	v_pk_fma_f32 v[92:93], v[112:113], v[22:23], v[96:97] op_sel_hi:[1,0,1]
	v_pk_fma_f32 v[96:97], v[114:115], v[22:23], v[100:101] op_sel_hi:[1,0,1]
	v_pk_fma_f32 v[86:87], v[86:87], v[22:23], v[90:91] op_sel_hi:[1,0,1]
	v_cvt_pk_f32_fp8_e32 v[90:91], v80
	v_cvt_pk_f32_fp8_sdwa v[100:101], v80 src0_sel:WORD_1
	v_cvt_pk_f32_fp8_e32 v[104:105], v81
	v_cvt_pk_f32_fp8_sdwa v[80:81], v81 src0_sel:WORD_1
	v_cvt_pk_f32_fp8_e32 v[106:107], v82
	v_cvt_pk_f32_fp8_sdwa v[108:109], v82 src0_sel:WORD_1
	v_cvt_pk_f32_fp8_e32 v[110:111], v83
	v_cvt_pk_f32_fp8_sdwa v[82:83], v83 src0_sel:WORD_1
	v_mov_b32_e32 v112, v23
	v_pk_fma_f32 v[90:91], v[90:91], v[112:113], v[94:95] op_sel_hi:[1,0,1]
	v_pk_fma_f32 v[94:95], v[100:101], v[112:113], v[98:99] op_sel_hi:[1,0,1]
	v_pk_fma_f32 v[98:99], v[104:105], v[112:113], v[102:103] op_sel_hi:[1,0,1]
	v_pk_fma_f32 v[80:81], v[80:81], v[112:113], v[84:85] op_sel_hi:[1,0,1]
	v_pk_fma_f32 v[84:85], v[106:107], v[112:113], v[88:89] op_sel_hi:[1,0,1]
	v_pk_fma_f32 v[88:89], v[108:109], v[112:113], v[92:93] op_sel_hi:[1,0,1]
	v_pk_fma_f32 v[92:93], v[110:111], v[112:113], v[96:97] op_sel_hi:[1,0,1]
	v_pk_fma_f32 v[82:83], v[82:83], v[112:113], v[86:87] op_sel_hi:[1,0,1]
	v_cvt_pk_f32_fp8_e32 v[86:87], v76
	v_cvt_pk_f32_fp8_sdwa v[96:97], v76 src0_sel:WORD_1
	v_cvt_pk_f32_fp8_e32 v[100:101], v77
	v_cvt_pk_f32_fp8_sdwa v[76:77], v77 src0_sel:WORD_1
	v_cvt_pk_f32_fp8_e32 v[102:103], v78
	v_cvt_pk_f32_fp8_sdwa v[104:105], v78 src0_sel:WORD_1
	v_cvt_pk_f32_fp8_e32 v[106:107], v79
	v_cvt_pk_f32_fp8_sdwa v[78:79], v79 src0_sel:WORD_1
	v_pk_fma_f32 v[86:87], v[86:87], v[16:17], v[90:91] op_sel_hi:[1,0,1]
	v_pk_fma_f32 v[90:91], v[96:97], v[16:17], v[94:95] op_sel_hi:[1,0,1]
	v_pk_fma_f32 v[94:95], v[100:101], v[16:17], v[98:99] op_sel_hi:[1,0,1]
	v_pk_fma_f32 v[76:77], v[76:77], v[16:17], v[80:81] op_sel_hi:[1,0,1]
	v_pk_fma_f32 v[80:81], v[102:103], v[16:17], v[84:85] op_sel_hi:[1,0,1]
	v_pk_fma_f32 v[84:85], v[104:105], v[16:17], v[88:89] op_sel_hi:[1,0,1]
	v_pk_fma_f32 v[88:89], v[106:107], v[16:17], v[92:93] op_sel_hi:[1,0,1]
	v_pk_fma_f32 v[78:79], v[78:79], v[16:17], v[82:83] op_sel_hi:[1,0,1]
	v_cvt_pk_f32_fp8_e32 v[82:83], v72
	v_cvt_pk_f32_fp8_sdwa v[92:93], v72 src0_sel:WORD_1
	v_cvt_pk_f32_fp8_e32 v[96:97], v73
	v_cvt_pk_f32_fp8_sdwa v[72:73], v73 src0_sel:WORD_1
	v_cvt_pk_f32_fp8_e32 v[98:99], v74
	v_cvt_pk_f32_fp8_sdwa v[100:101], v74 src0_sel:WORD_1
	v_cvt_pk_f32_fp8_e32 v[102:103], v75
	v_cvt_pk_f32_fp8_sdwa v[74:75], v75 src0_sel:WORD_1
	v_pk_fma_f32 v[82:83], v[82:83], v[16:17], v[86:87] op_sel:[0,1,0]
	v_pk_fma_f32 v[86:87], v[92:93], v[16:17], v[90:91] op_sel:[0,1,0]
	v_pk_fma_f32 v[90:91], v[96:97], v[16:17], v[94:95] op_sel:[0,1,0]
	v_pk_fma_f32 v[72:73], v[72:73], v[16:17], v[76:77] op_sel:[0,1,0]
	v_pk_fma_f32 v[76:77], v[98:99], v[16:17], v[80:81] op_sel:[0,1,0]
	v_pk_fma_f32 v[80:81], v[100:101], v[16:17], v[84:85] op_sel:[0,1,0]
	v_pk_fma_f32 v[84:85], v[102:103], v[16:17], v[88:89] op_sel:[0,1,0]
	v_pk_fma_f32 v[74:75], v[74:75], v[16:17], v[78:79] op_sel:[0,1,0]
	v_cvt_pk_f32_fp8_e32 v[78:79], v68
	v_cvt_pk_f32_fp8_sdwa v[88:89], v68 src0_sel:WORD_1
	v_cvt_pk_f32_fp8_e32 v[92:93], v69
	v_cvt_pk_f32_fp8_sdwa v[68:69], v69 src0_sel:WORD_1
	v_cvt_pk_f32_fp8_e32 v[94:95], v70
	v_cvt_pk_f32_fp8_sdwa v[96:97], v70 src0_sel:WORD_1
	v_cvt_pk_f32_fp8_e32 v[98:99], v71
	v_cvt_pk_f32_fp8_sdwa v[70:71], v71 src0_sel:WORD_1
	v_pk_fma_f32 v[78:79], v[78:79], v[18:19], v[82:83] op_sel_hi:[1,0,1]
	v_pk_fma_f32 v[82:83], v[88:89], v[18:19], v[86:87] op_sel_hi:[1,0,1]
	v_pk_fma_f32 v[86:87], v[92:93], v[18:19], v[90:91] op_sel_hi:[1,0,1]
	v_pk_fma_f32 v[68:69], v[68:69], v[18:19], v[72:73] op_sel_hi:[1,0,1]
	v_pk_fma_f32 v[72:73], v[94:95], v[18:19], v[76:77] op_sel_hi:[1,0,1]
	v_pk_fma_f32 v[76:77], v[96:97], v[18:19], v[80:81] op_sel_hi:[1,0,1]
	v_pk_fma_f32 v[80:81], v[98:99], v[18:19], v[84:85] op_sel_hi:[1,0,1]
	v_pk_fma_f32 v[70:71], v[70:71], v[18:19], v[74:75] op_sel_hi:[1,0,1]
	v_cvt_pk_f32_fp8_e32 v[74:75], v64
	v_cvt_pk_f32_fp8_sdwa v[84:85], v64 src0_sel:WORD_1
	v_cvt_pk_f32_fp8_e32 v[88:89], v65
	v_cvt_pk_f32_fp8_sdwa v[64:65], v65 src0_sel:WORD_1
	v_cvt_pk_f32_fp8_e32 v[90:91], v66
	v_cvt_pk_f32_fp8_sdwa v[92:93], v66 src0_sel:WORD_1
	v_cvt_pk_f32_fp8_e32 v[94:95], v67
	v_cvt_pk_f32_fp8_sdwa v[66:67], v67 src0_sel:WORD_1
	v_mov_b32_e32 v96, v19
	v_pk_fma_f32 v[74:75], v[74:75], v[96:97], v[78:79] op_sel_hi:[1,0,1]
	v_pk_fma_f32 v[78:79], v[84:85], v[96:97], v[82:83] op_sel_hi:[1,0,1]
	v_pk_fma_f32 v[82:83], v[88:89], v[96:97], v[86:87] op_sel_hi:[1,0,1]
	v_pk_fma_f32 v[64:65], v[64:65], v[96:97], v[68:69] op_sel_hi:[1,0,1]
	v_pk_fma_f32 v[68:69], v[90:91], v[96:97], v[72:73] op_sel_hi:[1,0,1]
	v_pk_fma_f32 v[72:73], v[92:93], v[96:97], v[76:77] op_sel_hi:[1,0,1]
	v_pk_fma_f32 v[76:77], v[94:95], v[96:97], v[80:81] op_sel_hi:[1,0,1]
	v_pk_fma_f32 v[66:67], v[66:67], v[96:97], v[70:71] op_sel_hi:[1,0,1]
	v_permlane32_swap_b32_e32 v74, v68
	v_permlane32_swap_b32_e32 v75, v69
	v_permlane32_swap_b32_e32 v78, v72
	v_permlane32_swap_b32_e32 v79, v73
	v_permlane32_swap_b32_e32 v82, v76
	v_permlane32_swap_b32_e32 v83, v77
	v_permlane32_swap_b32_e32 v64, v66
	v_permlane32_swap_b32_e32 v65, v67
	v_add_f32_e32 v68, v74, v68
	v_add_f32_e32 v69, v75, v69
	v_add_f32_e32 v70, v78, v72
	v_add_f32_e32 v71, v79, v73
	v_add_f32_e32 v72, v82, v76
	v_add_f32_e32 v73, v83, v77
	v_add_f32_e32 v64, v64, v66
	v_add_f32_e32 v65, v65, v67
	v_permlane16_swap_b32_e32 v68, v72
	v_permlane16_swap_b32_e32 v69, v73
	v_permlane16_swap_b32_e32 v70, v64
	v_permlane16_swap_b32_e32 v71, v65
	v_pk_add_f32 v[66:67], v[68:69], v[72:73]
	v_pk_add_f32 v[64:65], v[70:71], v[64:65]
	s_ashr_i32 s9, s8, 31
	v_cndmask_b32_e64 v68, v66, v64, s[0:1]
	v_cndmask_b32_e64 v70, v64, v66, s[0:1]
	v_cndmask_b32_e64 v64, v67, v65, s[0:1]
	v_mov_b32_dpp v68, v68 row_ror:8 row_mask:0xf bank_mask:0xf bound_ctrl:1
	v_cndmask_b32_e64 v71, v65, v67, s[0:1]
	v_mov_b32_dpp v69, v64 row_ror:8 row_mask:0xf bank_mask:0xf bound_ctrl:1
	v_pk_add_f32 v[66:67], v[70:71], v[68:69]
	s_lshl_b64 s[10:11], s[8:9], 11
	v_pk_mul_f32 v[64:65], v[66:67], v[66:67]
	v_cvt_pk_bf16_f32 v68, v66, v67
	v_add_f32_e32 v64, v64, v65
	v_lshl_add_u64 v[66:67], v[130:131], 0, s[10:11]
	global_store_dword v[66:67], v68, off
	v_add_f32_dpp v64, v64, v64 quad_perm:[1,0,3,2] row_mask:0xf bank_mask:0xf bound_ctrl:1
	s_nop 1
	v_add_f32_dpp v64, v64, v64 quad_perm:[2,3,0,1] row_mask:0xf bank_mask:0xf bound_ctrl:1
	s_nop 1
	v_add_f32_dpp v64, v64, v64 row_half_mirror row_mask:0xf bank_mask:0xf bound_ctrl:1
	s_nop 1
	v_add_f32_dpp v64, v64, v64 row_ror:8 row_mask:0xf bank_mask:0xf bound_ctrl:1
	v_mov_b32_e32 v65, v64
	s_nop 1
	v_permlane16_swap_b32_e32 v64, v65
	v_add_f32_e32 v64, v64, v65
	v_mov_b32_e32 v65, v64
	s_nop 1
	v_permlane32_swap_b32_e32 v64, v65
	s_and_saveexec_b64 s[10:11], s[2:3]
	s_lshl_b64 s[16:17], s[8:9], 2
	s_add_u32 s16, s12, s16
	v_add_f32_e32 v64, v64, v65
	s_addc_u32 s17, s13, s17
	global_store_dword v129, v64, s[16:17]
	s_or_b64 exec, exec, s[10:11]
	s_add_u32 s6, s20, 0x100
	s_waitcnt vmcnt(2)
	v_cvt_pk_f32_fp8_e32 v[138:139], v240
	v_cvt_pk_f32_fp8_sdwa v[140:141], v240 src0_sel:WORD_1
	v_cvt_pk_f32_fp8_e32 v[142:143], v241
	v_cvt_pk_f32_fp8_sdwa v[240:241], v241 src0_sel:WORD_1
	v_cvt_pk_f32_fp8_e32 v[144:145], v242
	v_cvt_pk_f32_fp8_sdwa v[146:147], v242 src0_sel:WORD_1
	v_cvt_pk_f32_fp8_e32 v[148:149], v243
	v_cvt_pk_f32_fp8_sdwa v[242:243], v243 src0_sel:WORD_1
	v_cvt_pk_f32_fp8_e32 v[150:151], v236
	v_cvt_pk_f32_fp8_sdwa v[152:153], v236 src0_sel:WORD_1
	v_cvt_pk_f32_fp8_e32 v[154:155], v237
	v_cvt_pk_f32_fp8_sdwa v[236:237], v237 src0_sel:WORD_1
	v_cvt_pk_f32_fp8_e32 v[156:157], v238
	v_cvt_pk_f32_fp8_sdwa v[158:159], v238 src0_sel:WORD_1
	v_cvt_pk_f32_fp8_e32 v[160:161], v239
	v_cvt_pk_f32_fp8_sdwa v[238:239], v239 src0_sel:WORD_1
	v_pk_fma_f32 v[138:139], v[138:139], v[48:49], 0 op_sel_hi:[1,0,0]
	v_pk_fma_f32 v[140:141], v[140:141], v[48:49], 0 op_sel_hi:[1,0,0]
	v_pk_fma_f32 v[142:143], v[142:143], v[48:49], 0 op_sel_hi:[1,0,0]
	v_pk_fma_f32 v[240:241], v[240:241], v[48:49], 0 op_sel_hi:[1,0,0]
	v_pk_fma_f32 v[144:145], v[144:145], v[48:49], 0 op_sel_hi:[1,0,0]
	v_pk_fma_f32 v[146:147], v[146:147], v[48:49], 0 op_sel_hi:[1,0,0]
	v_pk_fma_f32 v[148:149], v[148:149], v[48:49], 0 op_sel_hi:[1,0,0]
	v_pk_fma_f32 v[242:243], v[242:243], v[48:49], 0 op_sel_hi:[1,0,0]
	v_pk_fma_f32 v[138:139], v[150:151], v[48:49], v[138:139] op_sel:[0,1,0]
	v_pk_fma_f32 v[140:141], v[152:153], v[48:49], v[140:141] op_sel:[0,1,0]
	v_pk_fma_f32 v[142:143], v[154:155], v[48:49], v[142:143] op_sel:[0,1,0]
	v_pk_fma_f32 v[236:237], v[236:237], v[48:49], v[240:241] op_sel:[0,1,0]
	v_pk_fma_f32 v[240:241], v[156:157], v[48:49], v[144:145] op_sel:[0,1,0]
	v_pk_fma_f32 v[144:145], v[158:159], v[48:49], v[146:147] op_sel:[0,1,0]
	v_pk_fma_f32 v[146:147], v[160:161], v[48:49], v[148:149] op_sel:[0,1,0]
	v_pk_fma_f32 v[238:239], v[238:239], v[48:49], v[242:243] op_sel:[0,1,0]
	v_cvt_pk_f32_fp8_e32 v[242:243], v232
	v_cvt_pk_f32_fp8_sdwa v[148:149], v232 src0_sel:WORD_1
	v_cvt_pk_f32_fp8_e32 v[150:151], v233
	v_cvt_pk_f32_fp8_sdwa v[232:233], v233 src0_sel:WORD_1
	v_cvt_pk_f32_fp8_e32 v[152:153], v234
	v_cvt_pk_f32_fp8_sdwa v[154:155], v234 src0_sel:WORD_1
	v_cvt_pk_f32_fp8_e32 v[156:157], v235
	v_cvt_pk_f32_fp8_sdwa v[234:235], v235 src0_sel:WORD_1
	v_pk_fma_f32 v[242:243], v[242:243], v[50:51], v[138:139] op_sel_hi:[1,0,1]
	v_pk_fma_f32 v[138:139], v[148:149], v[50:51], v[140:141] op_sel_hi:[1,0,1]
	v_pk_fma_f32 v[140:141], v[150:151], v[50:51], v[142:143] op_sel_hi:[1,0,1]
	v_pk_fma_f32 v[232:233], v[232:233], v[50:51], v[236:237] op_sel_hi:[1,0,1]
	v_pk_fma_f32 v[236:237], v[152:153], v[50:51], v[240:241] op_sel_hi:[1,0,1]
	v_pk_fma_f32 v[240:241], v[154:155], v[50:51], v[144:145] op_sel_hi:[1,0,1]
	v_pk_fma_f32 v[142:143], v[156:157], v[50:51], v[146:147] op_sel_hi:[1,0,1]
	v_pk_fma_f32 v[234:235], v[234:235], v[50:51], v[238:239] op_sel_hi:[1,0,1]
	v_cvt_pk_f32_fp8_e32 v[238:239], v228
	v_cvt_pk_f32_fp8_sdwa v[144:145], v228 src0_sel:WORD_1
	v_cvt_pk_f32_fp8_e32 v[146:147], v229
	v_cvt_pk_f32_fp8_sdwa v[228:229], v229 src0_sel:WORD_1
	v_cvt_pk_f32_fp8_e32 v[148:149], v230
	v_cvt_pk_f32_fp8_sdwa v[150:151], v230 src0_sel:WORD_1
	v_cvt_pk_f32_fp8_e32 v[152:153], v231
	v_cvt_pk_f32_fp8_sdwa v[230:231], v231 src0_sel:WORD_1
	v_mov_b32_e32 v128, v51
	v_pk_fma_f32 v[238:239], v[238:239], v[128:129], v[242:243] op_sel_hi:[1,0,1]
	v_pk_fma_f32 v[242:243], v[144:145], v[128:129], v[138:139] op_sel_hi:[1,0,1]
	v_pk_fma_f32 v[138:139], v[146:147], v[128:129], v[140:141] op_sel_hi:[1,0,1]
	v_pk_fma_f32 v[228:229], v[228:229], v[128:129], v[232:233] op_sel_hi:[1,0,1]
	v_pk_fma_f32 v[232:233], v[148:149], v[128:129], v[236:237] op_sel_hi:[1,0,1]
	v_pk_fma_f32 v[236:237], v[150:151], v[128:129], v[240:241] op_sel_hi:[1,0,1]
	v_pk_fma_f32 v[240:241], v[152:153], v[128:129], v[142:143] op_sel_hi:[1,0,1]
	v_pk_fma_f32 v[230:231], v[230:231], v[128:129], v[234:235] op_sel_hi:[1,0,1]
	v_cvt_pk_f32_fp8_e32 v[234:235], v224
	v_cvt_pk_f32_fp8_sdwa v[140:141], v224 src0_sel:WORD_1
	v_cvt_pk_f32_fp8_e32 v[142:143], v225
	v_cvt_pk_f32_fp8_sdwa v[224:225], v225 src0_sel:WORD_1
	v_cvt_pk_f32_fp8_e32 v[144:145], v226
	v_cvt_pk_f32_fp8_sdwa v[146:147], v226 src0_sel:WORD_1
	v_cvt_pk_f32_fp8_e32 v[148:149], v227
	v_cvt_pk_f32_fp8_sdwa v[226:227], v227 src0_sel:WORD_1
	v_pk_fma_f32 v[234:235], v[234:235], v[52:53], v[238:239] op_sel_hi:[1,0,1]
	v_pk_fma_f32 v[238:239], v[140:141], v[52:53], v[242:243] op_sel_hi:[1,0,1]
	v_pk_fma_f32 v[242:243], v[142:143], v[52:53], v[138:139] op_sel_hi:[1,0,1]
	v_pk_fma_f32 v[224:225], v[224:225], v[52:53], v[228:229] op_sel_hi:[1,0,1]
	v_pk_fma_f32 v[228:229], v[144:145], v[52:53], v[232:233] op_sel_hi:[1,0,1]
	v_pk_fma_f32 v[232:233], v[146:147], v[52:53], v[236:237] op_sel_hi:[1,0,1]
	v_pk_fma_f32 v[236:237], v[148:149], v[52:53], v[240:241] op_sel_hi:[1,0,1]
	v_pk_fma_f32 v[226:227], v[226:227], v[52:53], v[230:231] op_sel_hi:[1,0,1]
	v_cvt_pk_f32_fp8_e32 v[230:231], v220
	v_cvt_pk_f32_fp8_sdwa v[240:241], v220 src0_sel:WORD_1
	v_cvt_pk_f32_fp8_e32 v[138:139], v221
	v_cvt_pk_f32_fp8_sdwa v[220:221], v221 src0_sel:WORD_1
	v_cvt_pk_f32_fp8_e32 v[140:141], v222
	v_cvt_pk_f32_fp8_sdwa v[142:143], v222 src0_sel:WORD_1
	v_cvt_pk_f32_fp8_e32 v[144:145], v223
	v_cvt_pk_f32_fp8_sdwa v[222:223], v223 src0_sel:WORD_1
	v_pk_fma_f32 v[230:231], v[230:231], v[52:53], v[234:235] op_sel:[0,1,0]
	v_pk_fma_f32 v[234:235], v[240:241], v[52:53], v[238:239] op_sel:[0,1,0]
	v_pk_fma_f32 v[238:239], v[138:139], v[52:53], v[242:243] op_sel:[0,1,0]
	v_pk_fma_f32 v[220:221], v[220:221], v[52:53], v[224:225] op_sel:[0,1,0]
	v_pk_fma_f32 v[224:225], v[140:141], v[52:53], v[228:229] op_sel:[0,1,0]
	v_pk_fma_f32 v[228:229], v[142:143], v[52:53], v[232:233] op_sel:[0,1,0]
	v_pk_fma_f32 v[232:233], v[144:145], v[52:53], v[236:237] op_sel:[0,1,0]
	v_pk_fma_f32 v[222:223], v[222:223], v[52:53], v[226:227] op_sel:[0,1,0]
	v_cvt_pk_f32_fp8_e32 v[226:227], v216
	v_cvt_pk_f32_fp8_sdwa v[236:237], v216 src0_sel:WORD_1
	v_cvt_pk_f32_fp8_e32 v[240:241], v217
	v_cvt_pk_f32_fp8_sdwa v[216:217], v217 src0_sel:WORD_1
	v_cvt_pk_f32_fp8_e32 v[242:243], v218
	v_cvt_pk_f32_fp8_sdwa v[138:139], v218 src0_sel:WORD_1
	v_cvt_pk_f32_fp8_e32 v[140:141], v219
	v_cvt_pk_f32_fp8_sdwa v[218:219], v219 src0_sel:WORD_1
	v_pk_fma_f32 v[226:227], v[226:227], v[54:55], v[230:231] op_sel_hi:[1,0,1]
	v_pk_fma_f32 v[230:231], v[236:237], v[54:55], v[234:235] op_sel_hi:[1,0,1]
	v_pk_fma_f32 v[234:235], v[240:241], v[54:55], v[238:239] op_sel_hi:[1,0,1]
	v_pk_fma_f32 v[216:217], v[216:217], v[54:55], v[220:221] op_sel_hi:[1,0,1]
	v_pk_fma_f32 v[220:221], v[242:243], v[54:55], v[224:225] op_sel_hi:[1,0,1]
	v_pk_fma_f32 v[224:225], v[138:139], v[54:55], v[228:229] op_sel_hi:[1,0,1]
	v_pk_fma_f32 v[228:229], v[140:141], v[54:55], v[232:233] op_sel_hi:[1,0,1]
	v_pk_fma_f32 v[218:219], v[218:219], v[54:55], v[222:223] op_sel_hi:[1,0,1]
	v_cvt_pk_f32_fp8_e32 v[222:223], v212
	v_cvt_pk_f32_fp8_sdwa v[232:233], v212 src0_sel:WORD_1
	v_cvt_pk_f32_fp8_e32 v[236:237], v213
	v_cvt_pk_f32_fp8_sdwa v[212:213], v213 src0_sel:WORD_1
	v_cvt_pk_f32_fp8_e32 v[238:239], v214
	v_cvt_pk_f32_fp8_sdwa v[240:241], v214 src0_sel:WORD_1
	v_cvt_pk_f32_fp8_e32 v[242:243], v215
	v_cvt_pk_f32_fp8_sdwa v[214:215], v215 src0_sel:WORD_1
	v_mov_b32_e32 v128, v55
	v_pk_fma_f32 v[222:223], v[222:223], v[128:129], v[226:227] op_sel_hi:[1,0,1]
	v_pk_fma_f32 v[226:227], v[232:233], v[128:129], v[230:231] op_sel_hi:[1,0,1]
	v_pk_fma_f32 v[230:231], v[236:237], v[128:129], v[234:235] op_sel_hi:[1,0,1]
	v_pk_fma_f32 v[212:213], v[212:213], v[128:129], v[216:217] op_sel_hi:[1,0,1]
	v_pk_fma_f32 v[216:217], v[238:239], v[128:129], v[220:221] op_sel_hi:[1,0,1]
	v_pk_fma_f32 v[220:221], v[240:241], v[128:129], v[224:225] op_sel_hi:[1,0,1]
	v_pk_fma_f32 v[224:225], v[242:243], v[128:129], v[228:229] op_sel_hi:[1,0,1]
	v_pk_fma_f32 v[214:215], v[214:215], v[128:129], v[218:219] op_sel_hi:[1,0,1]
	v_cvt_pk_f32_fp8_e32 v[218:219], v200
	v_cvt_pk_f32_fp8_sdwa v[228:229], v200 src0_sel:WORD_1
	v_cvt_pk_f32_fp8_e32 v[232:233], v201
	v_cvt_pk_f32_fp8_sdwa v[200:201], v201 src0_sel:WORD_1
	v_cvt_pk_f32_fp8_e32 v[234:235], v202
	v_cvt_pk_f32_fp8_sdwa v[236:237], v202 src0_sel:WORD_1
	v_cvt_pk_f32_fp8_e32 v[238:239], v203
	v_cvt_pk_f32_fp8_sdwa v[202:203], v203 src0_sel:WORD_1
	v_pk_fma_f32 v[218:219], v[218:219], v[56:57], v[222:223] op_sel_hi:[1,0,1]
	v_pk_fma_f32 v[222:223], v[228:229], v[56:57], v[226:227] op_sel_hi:[1,0,1]
	v_pk_fma_f32 v[226:227], v[232:233], v[56:57], v[230:231] op_sel_hi:[1,0,1]
	v_pk_fma_f32 v[200:201], v[200:201], v[56:57], v[212:213] op_sel_hi:[1,0,1]
	v_pk_fma_f32 v[212:213], v[234:235], v[56:57], v[216:217] op_sel_hi:[1,0,1]
	v_pk_fma_f32 v[216:217], v[236:237], v[56:57], v[220:221] op_sel_hi:[1,0,1]
	v_pk_fma_f32 v[220:221], v[238:239], v[56:57], v[224:225] op_sel_hi:[1,0,1]
	v_pk_fma_f32 v[202:203], v[202:203], v[56:57], v[214:215] op_sel_hi:[1,0,1]
	v_cvt_pk_f32_fp8_e32 v[214:215], v196
	v_cvt_pk_f32_fp8_sdwa v[224:225], v196 src0_sel:WORD_1
	v_cvt_pk_f32_fp8_e32 v[228:229], v197
	v_cvt_pk_f32_fp8_sdwa v[196:197], v197 src0_sel:WORD_1
	v_cvt_pk_f32_fp8_e32 v[230:231], v198
	v_cvt_pk_f32_fp8_sdwa v[232:233], v198 src0_sel:WORD_1
	v_cvt_pk_f32_fp8_e32 v[234:235], v199
	v_cvt_pk_f32_fp8_sdwa v[198:199], v199 src0_sel:WORD_1
	v_pk_fma_f32 v[214:215], v[214:215], v[56:57], v[218:219] op_sel:[0,1,0]
	v_pk_fma_f32 v[218:219], v[224:225], v[56:57], v[222:223] op_sel:[0,1,0]
	v_pk_fma_f32 v[222:223], v[228:229], v[56:57], v[226:227] op_sel:[0,1,0]
	v_pk_fma_f32 v[196:197], v[196:197], v[56:57], v[200:201] op_sel:[0,1,0]
	v_pk_fma_f32 v[200:201], v[230:231], v[56:57], v[212:213] op_sel:[0,1,0]
	v_pk_fma_f32 v[212:213], v[232:233], v[56:57], v[216:217] op_sel:[0,1,0]
	v_pk_fma_f32 v[216:217], v[234:235], v[56:57], v[220:221] op_sel:[0,1,0]
	v_pk_fma_f32 v[198:199], v[198:199], v[56:57], v[202:203] op_sel:[0,1,0]
	v_cvt_pk_f32_fp8_e32 v[202:203], v192
	v_cvt_pk_f32_fp8_sdwa v[220:221], v192 src0_sel:WORD_1
	v_cvt_pk_f32_fp8_e32 v[224:225], v193
	v_cvt_pk_f32_fp8_sdwa v[192:193], v193 src0_sel:WORD_1
	v_cvt_pk_f32_fp8_e32 v[226:227], v194
	v_cvt_pk_f32_fp8_sdwa v[228:229], v194 src0_sel:WORD_1
	v_cvt_pk_f32_fp8_e32 v[230:231], v195
	v_cvt_pk_f32_fp8_sdwa v[194:195], v195 src0_sel:WORD_1
	v_pk_fma_f32 v[202:203], v[202:203], v[58:59], v[214:215] op_sel_hi:[1,0,1]
	v_pk_fma_f32 v[214:215], v[220:221], v[58:59], v[218:219] op_sel_hi:[1,0,1]
	v_pk_fma_f32 v[218:219], v[224:225], v[58:59], v[222:223] op_sel_hi:[1,0,1]
	v_pk_fma_f32 v[192:193], v[192:193], v[58:59], v[196:197] op_sel_hi:[1,0,1]
	v_pk_fma_f32 v[196:197], v[226:227], v[58:59], v[200:201] op_sel_hi:[1,0,1]
	v_pk_fma_f32 v[200:201], v[228:229], v[58:59], v[212:213] op_sel_hi:[1,0,1]
	v_pk_fma_f32 v[212:213], v[230:231], v[58:59], v[216:217] op_sel_hi:[1,0,1]
	v_pk_fma_f32 v[194:195], v[194:195], v[58:59], v[198:199] op_sel_hi:[1,0,1]
	v_cvt_pk_f32_fp8_e32 v[198:199], v184
	v_cvt_pk_f32_fp8_sdwa v[216:217], v184 src0_sel:WORD_1
	v_cvt_pk_f32_fp8_e32 v[220:221], v185
	v_cvt_pk_f32_fp8_sdwa v[184:185], v185 src0_sel:WORD_1
	v_cvt_pk_f32_fp8_e32 v[222:223], v186
	v_cvt_pk_f32_fp8_sdwa v[224:225], v186 src0_sel:WORD_1
	v_cvt_pk_f32_fp8_e32 v[226:227], v187
	v_cvt_pk_f32_fp8_sdwa v[186:187], v187 src0_sel:WORD_1
	v_mov_b32_e32 v228, v59
	v_pk_fma_f32 v[198:199], v[198:199], v[228:229], v[202:203] op_sel_hi:[1,0,1]
	v_pk_fma_f32 v[202:203], v[216:217], v[228:229], v[214:215] op_sel_hi:[1,0,1]
	v_pk_fma_f32 v[214:215], v[220:221], v[228:229], v[218:219] op_sel_hi:[1,0,1]
	v_pk_fma_f32 v[184:185], v[184:185], v[228:229], v[192:193] op_sel_hi:[1,0,1]
	v_pk_fma_f32 v[192:193], v[222:223], v[228:229], v[196:197] op_sel_hi:[1,0,1]
	v_pk_fma_f32 v[196:197], v[224:225], v[228:229], v[200:201] op_sel_hi:[1,0,1]
	v_pk_fma_f32 v[200:201], v[226:227], v[228:229], v[212:213] op_sel_hi:[1,0,1]
	v_pk_fma_f32 v[186:187], v[186:187], v[228:229], v[194:195] op_sel_hi:[1,0,1]
	v_cvt_pk_f32_fp8_e32 v[194:195], v180
	v_cvt_pk_f32_fp8_sdwa v[212:213], v180 src0_sel:WORD_1
	v_cvt_pk_f32_fp8_e32 v[216:217], v181
	v_cvt_pk_f32_fp8_sdwa v[180:181], v181 src0_sel:WORD_1
	v_cvt_pk_f32_fp8_e32 v[218:219], v182
	v_cvt_pk_f32_fp8_sdwa v[220:221], v182 src0_sel:WORD_1
	v_cvt_pk_f32_fp8_e32 v[222:223], v183
	v_cvt_pk_f32_fp8_sdwa v[182:183], v183 src0_sel:WORD_1
	v_pk_fma_f32 v[194:195], v[194:195], v[60:61], v[198:199] op_sel_hi:[1,0,1]
	v_pk_fma_f32 v[198:199], v[212:213], v[60:61], v[202:203] op_sel_hi:[1,0,1]
	v_pk_fma_f32 v[202:203], v[216:217], v[60:61], v[214:215] op_sel_hi:[1,0,1]
	v_pk_fma_f32 v[180:181], v[180:181], v[60:61], v[184:185] op_sel_hi:[1,0,1]
	v_pk_fma_f32 v[184:185], v[218:219], v[60:61], v[192:193] op_sel_hi:[1,0,1]
	v_pk_fma_f32 v[192:193], v[220:221], v[60:61], v[196:197] op_sel_hi:[1,0,1]
	v_pk_fma_f32 v[196:197], v[222:223], v[60:61], v[200:201] op_sel_hi:[1,0,1]
	v_pk_fma_f32 v[182:183], v[182:183], v[60:61], v[186:187] op_sel_hi:[1,0,1]
	v_cvt_pk_f32_fp8_e32 v[186:187], v172
	v_cvt_pk_f32_fp8_sdwa v[200:201], v172 src0_sel:WORD_1
	v_cvt_pk_f32_fp8_e32 v[212:213], v173
	v_cvt_pk_f32_fp8_sdwa v[172:173], v173 src0_sel:WORD_1
	v_cvt_pk_f32_fp8_e32 v[214:215], v174
	v_cvt_pk_f32_fp8_sdwa v[216:217], v174 src0_sel:WORD_1
	v_cvt_pk_f32_fp8_e32 v[218:219], v175
	v_cvt_pk_f32_fp8_sdwa v[174:175], v175 src0_sel:WORD_1
	v_pk_fma_f32 v[186:187], v[186:187], v[60:61], v[194:195] op_sel:[0,1,0]
	v_pk_fma_f32 v[194:195], v[200:201], v[60:61], v[198:199] op_sel:[0,1,0]
	v_pk_fma_f32 v[198:199], v[212:213], v[60:61], v[202:203] op_sel:[0,1,0]
	v_pk_fma_f32 v[172:173], v[172:173], v[60:61], v[180:181] op_sel:[0,1,0]
	v_pk_fma_f32 v[180:181], v[214:215], v[60:61], v[184:185] op_sel:[0,1,0]
	v_pk_fma_f32 v[184:185], v[216:217], v[60:61], v[192:193] op_sel:[0,1,0]
	v_pk_fma_f32 v[192:193], v[218:219], v[60:61], v[196:197] op_sel:[0,1,0]
	v_pk_fma_f32 v[174:175], v[174:175], v[60:61], v[182:183] op_sel:[0,1,0]
	v_cvt_pk_f32_fp8_e32 v[182:183], v168
	v_cvt_pk_f32_fp8_sdwa v[196:197], v168 src0_sel:WORD_1
	v_cvt_pk_f32_fp8_e32 v[200:201], v169
	v_cvt_pk_f32_fp8_sdwa v[168:169], v169 src0_sel:WORD_1
	v_cvt_pk_f32_fp8_e32 v[202:203], v170
	v_cvt_pk_f32_fp8_sdwa v[212:213], v170 src0_sel:WORD_1
	v_cvt_pk_f32_fp8_e32 v[214:215], v171
	v_cvt_pk_f32_fp8_sdwa v[170:171], v171 src0_sel:WORD_1
	v_pk_fma_f32 v[182:183], v[182:183], v[62:63], v[186:187] op_sel_hi:[1,0,1]
	v_pk_fma_f32 v[186:187], v[196:197], v[62:63], v[194:195] op_sel_hi:[1,0,1]
	v_pk_fma_f32 v[194:195], v[200:201], v[62:63], v[198:199] op_sel_hi:[1,0,1]
	v_pk_fma_f32 v[168:169], v[168:169], v[62:63], v[172:173] op_sel_hi:[1,0,1]
	v_pk_fma_f32 v[172:173], v[202:203], v[62:63], v[180:181] op_sel_hi:[1,0,1]
	v_pk_fma_f32 v[180:181], v[212:213], v[62:63], v[184:185] op_sel_hi:[1,0,1]
	v_pk_fma_f32 v[184:185], v[214:215], v[62:63], v[192:193] op_sel_hi:[1,0,1]
	v_pk_fma_f32 v[170:171], v[170:171], v[62:63], v[174:175] op_sel_hi:[1,0,1]
	v_cvt_pk_f32_fp8_e32 v[174:175], v164
	v_cvt_pk_f32_fp8_sdwa v[192:193], v164 src0_sel:WORD_1
	v_cvt_pk_f32_fp8_e32 v[196:197], v165
	v_cvt_pk_f32_fp8_sdwa v[164:165], v165 src0_sel:WORD_1
	v_cvt_pk_f32_fp8_e32 v[198:199], v166
	v_cvt_pk_f32_fp8_sdwa v[200:201], v166 src0_sel:WORD_1
	v_cvt_pk_f32_fp8_e32 v[202:203], v167
	v_cvt_pk_f32_fp8_sdwa v[166:167], v167 src0_sel:WORD_1
	v_mov_b32_e32 v212, v63
	v_pk_fma_f32 v[174:175], v[174:175], v[212:213], v[182:183] op_sel_hi:[1,0,1]
	v_pk_fma_f32 v[182:183], v[192:193], v[212:213], v[186:187] op_sel_hi:[1,0,1]
	v_pk_fma_f32 v[186:187], v[196:197], v[212:213], v[194:195] op_sel_hi:[1,0,1]
	v_pk_fma_f32 v[164:165], v[164:165], v[212:213], v[168:169] op_sel_hi:[1,0,1]
	v_pk_fma_f32 v[168:169], v[198:199], v[212:213], v[172:173] op_sel_hi:[1,0,1]
	v_pk_fma_f32 v[172:173], v[200:201], v[212:213], v[180:181] op_sel_hi:[1,0,1]
	v_pk_fma_f32 v[180:181], v[202:203], v[212:213], v[184:185] op_sel_hi:[1,0,1]
	v_pk_fma_f32 v[166:167], v[166:167], v[212:213], v[170:171] op_sel_hi:[1,0,1]
	v_permlane32_swap_b32_e32 v174, v168
	v_permlane32_swap_b32_e32 v175, v169
	v_permlane32_swap_b32_e32 v182, v172
	v_permlane32_swap_b32_e32 v183, v173
	v_permlane32_swap_b32_e32 v186, v180
	v_permlane32_swap_b32_e32 v187, v181
	v_permlane32_swap_b32_e32 v164, v166
	v_permlane32_swap_b32_e32 v165, v167
	v_add_f32_e32 v168, v174, v168
	v_add_f32_e32 v169, v175, v169
	v_add_f32_e32 v170, v182, v172
	v_add_f32_e32 v171, v183, v173
	v_add_f32_e32 v172, v186, v180
	v_add_f32_e32 v173, v187, v181
	v_add_f32_e32 v164, v164, v166
	v_add_f32_e32 v165, v165, v167
	v_permlane16_swap_b32_e32 v168, v172
	v_permlane16_swap_b32_e32 v169, v173
	v_permlane16_swap_b32_e32 v170, v164
	v_permlane16_swap_b32_e32 v171, v165
	v_pk_add_f32 v[166:167], v[168:169], v[172:173]
	v_pk_add_f32 v[164:165], v[170:171], v[164:165]
	s_ashr_i32 s7, s6, 31
	v_cndmask_b32_e64 v168, v166, v164, s[0:1]
	v_cndmask_b32_e64 v170, v164, v166, s[0:1]
	v_cndmask_b32_e64 v164, v167, v165, s[0:1]
	v_mov_b32_dpp v168, v168 row_ror:8 row_mask:0xf bank_mask:0xf bound_ctrl:1
	v_cndmask_b32_e64 v171, v165, v167, s[0:1]
	v_mov_b32_dpp v169, v164 row_ror:8 row_mask:0xf bank_mask:0xf bound_ctrl:1
	v_pk_add_f32 v[166:167], v[170:171], v[168:169]
	s_lshl_b64 s[8:9], s[6:7], 11
	v_pk_mul_f32 v[164:165], v[166:167], v[166:167]
	v_cvt_pk_bf16_f32 v168, v166, v167
	v_add_f32_e32 v164, v164, v165
	v_lshl_add_u64 v[166:167], v[130:131], 0, s[8:9]
	global_store_dword v[166:167], v168, off
	v_add_f32_dpp v164, v164, v164 quad_perm:[1,0,3,2] row_mask:0xf bank_mask:0xf bound_ctrl:1
	s_nop 1
	v_add_f32_dpp v164, v164, v164 quad_perm:[2,3,0,1] row_mask:0xf bank_mask:0xf bound_ctrl:1
	s_nop 1
	v_add_f32_dpp v164, v164, v164 row_half_mirror row_mask:0xf bank_mask:0xf bound_ctrl:1
	s_nop 1
	v_add_f32_dpp v164, v164, v164 row_ror:8 row_mask:0xf bank_mask:0xf bound_ctrl:1
	v_mov_b32_e32 v165, v164
	s_nop 1
	v_permlane16_swap_b32_e32 v164, v165
	v_add_f32_e32 v164, v164, v165
	v_mov_b32_e32 v165, v164
	s_nop 1
	v_permlane32_swap_b32_e32 v164, v165
	s_and_saveexec_b64 s[8:9], s[2:3]
	s_lshl_b64 s[10:11], s[6:7], 2
	s_add_u32 s10, s12, s10
	v_add_f32_e32 v164, v164, v165
	s_addc_u32 s11, s13, s11
	global_store_dword v129, v164, s[10:11]
	s_or_b64 exec, exec, s[8:9]
